# write-through (sc1) on all plain 16-byte output stores so the grid barrier's L2 writeback has less to flush; on top of v20
# baseline (speedup 1.0000x reference)
; __device__ __forceinline__ float dot4(f32x4 a, f32x4 b) { return (a.x * b.x + a.y * b.y) + (a.z * b.z + a.w * b.w); }
;     __device__ __forceinline__ void epi(const f32x4 (&acc)[2][2][4][2], const Unit& u, int wr, int wc, int fr, int fq) const {
;     ...
;         } else if (wc < 2) {
;             float* kd = KR + rowt * 64; float* sq = SSQ + rowt * 16 + 12 + wc;
; #pragma unroll
;             for (int ai = 0; ai < 2; ++ai)
; #pragma unroll
;                 for (int m = 0; m < 4; ++m) { const size_t ro = (size_t)(ai * 128 + m * 16);
;                     *(f32x4*)((char*)kd + (ro * 64 + lrow * 64u + lcol) * 4) = acc[ai][0][m][0]; *(f32x4*)((char*)kd + (ro * 64 + lrow * 64u + lcol + 4) * 4) = acc[ai][0][m][1];
;                     float ss = dot4(acc[ai][0][m][0], acc[ai][0][m][0]) + dot4(acc[ai][0][m][1], acc[ai][0][m][1]);
;                     ss += __shfl_xor(ss, 16); ss += __shfl_xor(ss, 32);
;                     if (fq == 0) *(float*)((char*)sq + (ro * 16 + lrow * 16u) * 4) = ss; }
.LBB0_266:
	s_ashr_i32 s25, s24, 31
	v_mov_b32_e32 v156, v152
	v_mov_b32_e32 v142, v154
	s_cmp_gt_i32 s22, 10
	s_mov_b64 s[26:27], -1
	s_cbranch_scc0 .LBB0_286
	s_andn2_b64 vcc, exec, s[10:11]
	s_cbranch_vccnz .LBB0_285
	v_mul_f32_e32 v144, v127, v127
	v_mul_f32_e32 v145, v129, v129
	v_lshlrev_b32_e32 v146, 6, v156
	v_mov_b32_e32 v143, v147
	v_fmac_f32_e32 v144, v126, v126
	v_fmac_f32_e32 v145, v128, v128
	v_lshl_add_u64 v[148:149], v[146:147], 0, v[142:143]
	v_add_f32_e32 v144, v144, v145
	v_mul_f32_e32 v145, v123, v123
	v_mul_f32_e32 v146, v125, v125
	v_cmp_lt_i32_e32 vcc, v220, v215
	v_fmac_f32_e32 v145, v122, v122
	v_fmac_f32_e32 v146, v124, v124
	v_cndmask_b32_e32 v143, v210, v220, vcc
	v_add_f32_e32 v145, v145, v146
	v_lshlrev_b32_e32 v143, 2, v143
	v_add_f32_e32 v144, v145, v144
	s_lshl_b64 s[26:27], s[24:25], 16
	ds_bpermute_b32 v145, v143, v144
	s_add_u32 s26, s58, s26
	s_addc_u32 s27, s59, s27
	s_lshl_b64 s[42:43], s[24:25], 14
	v_cmp_lt_i32_e32 vcc, v221, v215
	s_add_u32 s42, s66, s42
	s_addc_u32 s43, s67, s43
	v_cndmask_b32_e32 v146, v210, v221, vcc
	v_lshlrev_b32_e32 v157, 2, v146
	v_lshlrev_b32_e32 v146, 4, v156
	v_lshl_add_u64 v[150:151], v[146:147], 2, s[42:43]
	s_waitcnt lgkmcnt(0)
	v_add_f32_e32 v146, v144, v145
	ds_bpermute_b32 v158, v157, v146
	v_lshl_add_u64 v[144:145], v[150:151], 0, 48
	v_lshl_add_u64 v[148:149], v[148:149], 2, s[26:27]
	global_store_dwordx4 v[148:149], v[126:129], off sc1
	global_store_dwordx4 v[148:149], v[122:125], off offset:16 sc1
	s_and_saveexec_b64 s[26:27], s[38:39]
	s_cbranch_execz .LBB0_270
	s_waitcnt lgkmcnt(0)
	v_add_f32_e32 v146, v146, v158
	global_store_dword v[144:145], v146, off
.LBB0_270:
	s_or_b64 exec, exec, s[26:27]
	v_mul_f32_e32 v146, v111, v111
	s_waitcnt lgkmcnt(0)
	v_mul_f32_e32 v158, v113, v113
	v_fmac_f32_e32 v146, v110, v110
	v_fmac_f32_e32 v158, v112, v112
	v_add_f32_e32 v146, v146, v158
	v_mul_f32_e32 v158, v107, v107
	v_mul_f32_e32 v159, v109, v109
	v_fmac_f32_e32 v158, v106, v106
	v_fmac_f32_e32 v159, v108, v108
	v_add_f32_e32 v158, v158, v159
	v_add_f32_e32 v146, v158, v146
	ds_bpermute_b32 v158, v143, v146
	v_add_co_u32_e32 v160, vcc, 0x1000, v148
	s_waitcnt lgkmcnt(0)
	v_add_f32_e32 v146, v146, v158
	ds_bpermute_b32 v158, v157, v146
	v_addc_co_u32_e32 v161, vcc, 0, v149, vcc
	global_store_dwordx4 v[160:161], v[110:113], off sc1
	global_store_dwordx4 v[160:161], v[106:109], off offset:16 sc1
	s_and_saveexec_b64 s[26:27], s[38:39]
	s_cbranch_execz .LBB0_272
	s_waitcnt lgkmcnt(0)
	v_add_f32_e32 v146, v146, v158
	global_store_dword v[150:151], v146, off offset:1072
.LBB0_272:
	s_or_b64 exec, exec, s[26:27]
	v_mul_f32_e32 v146, v95, v95
	s_waitcnt lgkmcnt(0)
	v_mul_f32_e32 v158, v97, v97
	v_fmac_f32_e32 v146, v94, v94
	v_fmac_f32_e32 v158, v96, v96
	v_add_f32_e32 v146, v146, v158
	v_mul_f32_e32 v158, v91, v91
	v_mul_f32_e32 v159, v93, v93
	v_fmac_f32_e32 v158, v90, v90
	v_fmac_f32_e32 v159, v92, v92
	v_add_f32_e32 v158, v158, v159
	v_add_f32_e32 v146, v158, v146
	ds_bpermute_b32 v158, v143, v146
	v_add_co_u32_e32 v160, vcc, 0x2000, v148
	s_waitcnt lgkmcnt(0)
	v_add_f32_e32 v146, v146, v158
	ds_bpermute_b32 v158, v157, v146
	v_addc_co_u32_e32 v161, vcc, 0, v149, vcc
	global_store_dwordx4 v[160:161], v[94:97], off sc1
	global_store_dwordx4 v[160:161], v[90:93], off offset:16 sc1
	s_and_saveexec_b64 s[26:27], s[38:39]
	s_cbranch_execz .LBB0_274
	s_waitcnt lgkmcnt(0)
	v_add_f32_e32 v146, v146, v158
	global_store_dword v[150:151], v146, off offset:2096
.LBB0_274:
	s_or_b64 exec, exec, s[26:27]
	v_mul_f32_e32 v146, v79, v79
	s_waitcnt lgkmcnt(0)
	v_mul_f32_e32 v158, v81, v81
	v_fmac_f32_e32 v146, v78, v78
	v_fmac_f32_e32 v158, v80, v80
	v_add_f32_e32 v146, v146, v158
	v_mul_f32_e32 v158, v75, v75
	v_mul_f32_e32 v159, v77, v77
	v_fmac_f32_e32 v158, v74, v74
	v_fmac_f32_e32 v159, v76, v76
	v_add_f32_e32 v158, v158, v159
	v_add_f32_e32 v146, v158, v146
	ds_bpermute_b32 v158, v143, v146
	v_add_co_u32_e32 v160, vcc, 0x3000, v148
	s_waitcnt lgkmcnt(0)
	v_add_f32_e32 v146, v146, v158
	ds_bpermute_b32 v158, v157, v146
	v_addc_co_u32_e32 v161, vcc, 0, v149, vcc
	global_store_dwordx4 v[160:161], v[78:81], off sc1
	global_store_dwordx4 v[160:161], v[74:77], off offset:16 sc1
	s_and_saveexec_b64 s[26:27], s[38:39]
	s_cbranch_execz .LBB0_276
	s_waitcnt lgkmcnt(0)
	v_add_f32_e32 v146, v146, v158
	global_store_dword v[150:151], v146, off offset:3120
; __device__ __forceinline__ float dot4(f32x4 a, f32x4 b) { return (a.x * b.x + a.y * b.y) + (a.z * b.z + a.w * b.w); }
;     __device__ __forceinline__ void epi(const f32x4 (&acc)[2][2][4][2], const Unit& u, int wr, int wc, int fr, int fq) const {
;     ...
;         } else if (wc < 2) {
;             float* kd = KR + rowt * 64; float* sq = SSQ + rowt * 16 + 12 + wc;
; #pragma unroll
;             for (int ai = 0; ai < 2; ++ai)
; #pragma unroll
;                 for (int m = 0; m < 4; ++m) { const size_t ro = (size_t)(ai * 128 + m * 16);
;                     *(f32x4*)((char*)kd + (ro * 64 + lrow * 64u + lcol) * 4) = acc[ai][0][m][0]; *(f32x4*)((char*)kd + (ro * 64 + lrow * 64u + lcol + 4) * 4) = acc[ai][0][m][1];
;                     float ss = dot4(acc[ai][0][m][0], acc[ai][0][m][0]) + dot4(acc[ai][0][m][1], acc[ai][0][m][1]);
;                     ss += __shfl_xor(ss, 16); ss += __shfl_xor(ss, 32);
;                     if (fq == 0) *(float*)((char*)sq + (ro * 16 + lrow * 16u) * 4) = ss; }
.LBB0_276:
	s_or_b64 exec, exec, s[26:27]
	v_mul_f32_e32 v146, v63, v63
	v_mul_f32_e32 v150, v65, v65
	v_fmac_f32_e32 v146, v62, v62
	v_fmac_f32_e32 v150, v64, v64
	v_add_f32_e32 v146, v146, v150
	v_mul_f32_e32 v150, v59, v59
	v_mul_f32_e32 v151, v61, v61
	v_fmac_f32_e32 v150, v58, v58
	v_fmac_f32_e32 v151, v60, v60
	v_add_f32_e32 v150, v150, v151
	v_add_f32_e32 v146, v150, v146
	ds_bpermute_b32 v150, v143, v146
	s_waitcnt lgkmcnt(0)
	v_add_co_u32_e32 v158, vcc, 0x8000, v148
	v_add_f32_e32 v146, v146, v150
	ds_bpermute_b32 v150, v157, v146
	v_addc_co_u32_e32 v159, vcc, 0, v149, vcc
	global_store_dwordx4 v[158:159], v[62:65], off sc1
	global_store_dwordx4 v[158:159], v[58:61], off offset:16 sc1
	s_and_saveexec_b64 s[26:27], s[38:39]
	s_cbranch_execz .LBB0_278
	s_waitcnt lgkmcnt(0)
	v_add_f32_e32 v146, v146, v150
	v_add_co_u32_e32 v150, vcc, 0x2000, v144
	s_nop 1
	v_addc_co_u32_e32 v151, vcc, 0, v145, vcc
	global_store_dword v[150:151], v146, off
.LBB0_278:
	s_or_b64 exec, exec, s[26:27]
	v_mul_f32_e32 v146, v47, v47
	s_waitcnt lgkmcnt(0)
	v_mul_f32_e32 v150, v49, v49
	v_fmac_f32_e32 v146, v46, v46
	v_fmac_f32_e32 v150, v48, v48
	v_add_f32_e32 v146, v146, v150
	v_mul_f32_e32 v150, v43, v43
	v_mul_f32_e32 v151, v45, v45
	v_fmac_f32_e32 v150, v42, v42
	v_fmac_f32_e32 v151, v44, v44
	v_add_f32_e32 v150, v150, v151
	v_add_f32_e32 v146, v150, v146
	ds_bpermute_b32 v150, v143, v146
	v_add_co_u32_e32 v158, vcc, 0x9000, v148
	s_waitcnt lgkmcnt(0)
	v_add_f32_e32 v146, v146, v150
	ds_bpermute_b32 v150, v157, v146
	v_addc_co_u32_e32 v159, vcc, 0, v149, vcc
	global_store_dwordx4 v[158:159], v[46:49], off sc1
	global_store_dwordx4 v[158:159], v[42:45], off offset:16 sc1
	s_and_saveexec_b64 s[26:27], s[38:39]
	s_cbranch_execz .LBB0_280
	s_waitcnt lgkmcnt(0)
	v_add_f32_e32 v146, v146, v150
	v_add_co_u32_e32 v150, vcc, 0x2000, v144
	s_nop 1
	v_addc_co_u32_e32 v151, vcc, 0, v145, vcc
	global_store_dword v[150:151], v146, off offset:1024
.LBB0_280:
	s_or_b64 exec, exec, s[26:27]
	v_mul_f32_e32 v146, v31, v31
	s_waitcnt lgkmcnt(0)
	v_mul_f32_e32 v150, v33, v33
	v_fmac_f32_e32 v146, v30, v30
	v_fmac_f32_e32 v150, v32, v32
	v_add_f32_e32 v146, v146, v150
	v_mul_f32_e32 v150, v27, v27
	v_mul_f32_e32 v151, v29, v29
	v_fmac_f32_e32 v150, v26, v26
	v_fmac_f32_e32 v151, v28, v28
	v_add_f32_e32 v150, v150, v151
	v_add_f32_e32 v146, v150, v146
	ds_bpermute_b32 v150, v143, v146
	v_add_co_u32_e32 v158, vcc, 0xa000, v148
	s_waitcnt lgkmcnt(0)
	v_add_f32_e32 v146, v146, v150
	ds_bpermute_b32 v150, v157, v146
	v_addc_co_u32_e32 v159, vcc, 0, v149, vcc
	global_store_dwordx4 v[158:159], v[30:33], off sc1
	global_store_dwordx4 v[158:159], v[26:29], off offset:16 sc1
	s_and_saveexec_b64 s[26:27], s[38:39]
	s_cbranch_execz .LBB0_282
	s_waitcnt lgkmcnt(0)
	v_add_f32_e32 v146, v146, v150
	v_add_co_u32_e32 v150, vcc, 0x2000, v144
	s_nop 1
	v_addc_co_u32_e32 v151, vcc, 0, v145, vcc
	global_store_dword v[150:151], v146, off offset:2048
.LBB0_282:
	s_or_b64 exec, exec, s[26:27]
	v_add_co_u32_e32 v148, vcc, 0xb000, v148
	v_mul_f32_e32 v146, v15, v15
	s_nop 0
	v_addc_co_u32_e32 v149, vcc, 0, v149, vcc
	global_store_dwordx4 v[148:149], v[14:17], off sc1
	global_store_dwordx4 v[148:149], v[10:13], off offset:16 sc1
	v_mul_f32_e32 v148, v17, v17
	v_fmac_f32_e32 v146, v14, v14
	v_fmac_f32_e32 v148, v16, v16
	v_add_f32_e32 v146, v146, v148
	v_mul_f32_e32 v148, v11, v11
	v_mul_f32_e32 v149, v13, v13
	v_fmac_f32_e32 v148, v10, v10
	v_fmac_f32_e32 v149, v12, v12
	v_add_f32_e32 v148, v148, v149
	v_add_f32_e32 v146, v148, v146
	ds_bpermute_b32 v143, v143, v146
	s_waitcnt lgkmcnt(0)
	v_add_f32_e32 v143, v146, v143
	ds_bpermute_b32 v146, v157, v143
	s_and_saveexec_b64 s[26:27], s[38:39]
	s_cbranch_execz .LBB0_284
	v_add_co_u32_e32 v144, vcc, 0x2000, v144
	s_waitcnt lgkmcnt(0)
	v_add_f32_e32 v143, v143, v146
	v_addc_co_u32_e32 v145, vcc, 0, v145, vcc
	global_store_dword v[144:145], v143, off offset:3072

; __device__ __forceinline__ unsigned pk2(float lo, float hi) { return f2bf(lo) | (f2bf(hi) << 16); }
; __device__ __forceinline__ float dot4(f32x4 a, f32x4 b) { return (a.x * b.x + a.y * b.y) + (a.z * b.z + a.w * b.w); }
;     __device__ __forceinline__ void epi(const f32x4 (&acc)[2][2][4][2], const Unit& u, int wr, int wc, int fr, int fq) const {
;     ...
;         if (pn < 11) {
;             bf16* dst; int ld;
;             if (pn < 4) { dst = XR + rowt * 1024 + pn * 256; ld = 1024; } else if (pn < 8) { dst = GR + rowt * 1024 + (pn - 4) * 256; ld = 1024; }
;             else if (pn < 10) { dst = CQ + rowt * 512 + (pn - 8) * 256; ld = 512; } else { dst = CKV + rowt * 256; ld = 256; }
;             const unsigned loff = (lrow * (unsigned)ld + lcol) * 2u;
; #pragma unroll
;             for (int ai = 0; ai < 2; ++ai)
; #pragma unroll
;                 for (int m = 0; m < 4; ++m) {
; #pragma unroll
;                     for (int bj = 0; bj < 2; ++bj) { const f32x4 v0 = acc[ai][bj][m][0], v1 = acc[ai][bj][m][1];
;                         u32x4 w; w.x = pk2(v0[0], v0[1]); w.y = pk2(v0[2], v0[3]); w.z = pk2(v1[0], v1[1]); w.w = pk2(v1[2], v1[3]);
;                         *(u32x4*)((char*)dst + ((size_t)(ai * 128 + m * 16) * ld + bj * 128) * 2 + loff) = w; } }
;             if (pn >= 8) {
;                 float* sq = SSQ + rowt * 16 + (pn < 10 ? (pn - 8) * 4 : 8) + wc;
; #pragma unroll
;                 for (int ai = 0; ai < 2; ++ai)
; #pragma unroll
;                     for (int m = 0; m < 4; ++m) { float ss = 0.f;
; #pragma unroll
;                         for (int bj = 0; bj < 2; ++bj)
; #pragma unroll
;                             for (int n = 0; n < 2; ++n) ss += dot4(acc[ai][bj][m][n], acc[ai][bj][m][n]);
;                         ss += __shfl_xor(ss, 16); ss += __shfl_xor(ss, 32);
;                         if (fq == 0) *(float*)((char*)sq + ((size_t)(ai * 128 + m * 16) * 16 + lrow * 16u) * 4) = ss; } }
.LBB0_299:
	v_cvt_pk_bf16_f32 v148, v126, v127
	v_cvt_pk_bf16_f32 v149, v128, v129
	v_cvt_pk_bf16_f32 v150, v122, v123
	v_cvt_pk_bf16_f32 v151, v124, v125
	v_mul_lo_u32 v143, s15, v156
	s_waitcnt lgkmcnt(0)
	v_add_lshl_u32 v146, v143, v142, 1
	global_store_dwordx4 v146, v[148:151], s[26:27] sc1
	v_lshl_add_u64 v[142:143], s[26:27], 0, v[146:147]
	s_lshl_b32 s12, s15, 5
	v_cvt_pk_bf16_f32 v148, v118, v119
	v_cvt_pk_bf16_f32 v149, v120, v121
	v_cvt_pk_bf16_f32 v150, v114, v115
	v_cvt_pk_bf16_f32 v151, v116, v117
	global_store_dwordx4 v146, v[148:151], s[26:27] offset:256 sc1
	s_nop 1
	v_cvt_pk_bf16_f32 v148, v110, v111
	v_cvt_pk_bf16_f32 v149, v112, v113
	v_cvt_pk_bf16_f32 v150, v106, v107
	v_cvt_pk_bf16_f32 v151, v108, v109
	v_lshl_add_u64 v[144:145], v[142:143], 0, s[12:13]
	global_store_dwordx4 v[144:145], v[148:151], off sc1
	s_lshl_b32 s12, s15, 6
	s_nop 0
	v_cvt_pk_bf16_f32 v148, v102, v103
	v_cvt_pk_bf16_f32 v149, v104, v105
	v_cvt_pk_bf16_f32 v150, v98, v99
	v_cvt_pk_bf16_f32 v151, v100, v101
	global_store_dwordx4 v[144:145], v[148:151], off offset:256 sc1
	s_nop 1
	v_cvt_pk_bf16_f32 v148, v94, v95
	v_cvt_pk_bf16_f32 v149, v96, v97
	v_cvt_pk_bf16_f32 v150, v90, v91
	v_cvt_pk_bf16_f32 v151, v92, v93
	v_lshl_add_u64 v[144:145], v[142:143], 0, s[12:13]
	global_store_dwordx4 v[144:145], v[148:151], off sc1
	s_nop 1
	v_cvt_pk_bf16_f32 v148, v86, v87
	v_cvt_pk_bf16_f32 v149, v88, v89
	v_cvt_pk_bf16_f32 v150, v82, v83
	v_cvt_pk_bf16_f32 v151, v84, v85
	global_store_dwordx4 v[144:145], v[148:151], off offset:256 sc1
	s_nop 1
	v_cvt_pk_bf16_f32 v148, v78, v79
	v_cvt_pk_bf16_f32 v149, v80, v81
	v_cvt_pk_bf16_f32 v150, v74, v75
	s_mul_i32 s12, s15, 0x60
	v_cvt_pk_bf16_f32 v151, v76, v77
	v_lshl_add_u64 v[144:145], v[142:143], 0, s[12:13]
	global_store_dwordx4 v[144:145], v[148:151], off sc1
	s_nop 1
	v_cvt_pk_bf16_f32 v148, v70, v71
	v_cvt_pk_bf16_f32 v149, v72, v73
	v_cvt_pk_bf16_f32 v150, v66, v67
	v_cvt_pk_bf16_f32 v151, v68, v69
	global_store_dwordx4 v[144:145], v[148:151], off offset:256 sc1
	s_nop 1
	v_cvt_pk_bf16_f32 v148, v62, v63
	v_cvt_pk_bf16_f32 v149, v64, v65
	v_cvt_pk_bf16_f32 v150, v58, v59
	s_lshl_b32 s12, s15, 8
	v_cvt_pk_bf16_f32 v151, v60, v61
	v_lshl_add_u64 v[144:145], v[142:143], 0, s[12:13]
	global_store_dwordx4 v[144:145], v[148:151], off sc1
	s_nop 1
	v_cvt_pk_bf16_f32 v148, v54, v55
	v_cvt_pk_bf16_f32 v149, v56, v57
	v_cvt_pk_bf16_f32 v150, v50, v51
	v_cvt_pk_bf16_f32 v151, v52, v53
	global_store_dwordx4 v[144:145], v[148:151], off offset:256 sc1
	s_nop 1
	v_cvt_pk_bf16_f32 v148, v46, v47
	v_cvt_pk_bf16_f32 v149, v48, v49
	v_cvt_pk_bf16_f32 v150, v42, v43
	s_mul_i32 s12, s15, 0x120
	v_cvt_pk_bf16_f32 v151, v44, v45
	v_lshl_add_u64 v[144:145], v[142:143], 0, s[12:13]
	global_store_dwordx4 v[144:145], v[148:151], off sc1
	s_nop 1
	v_cvt_pk_bf16_f32 v148, v38, v39
	v_cvt_pk_bf16_f32 v149, v40, v41
	v_cvt_pk_bf16_f32 v150, v34, v35
	v_cvt_pk_bf16_f32 v151, v36, v37
	global_store_dwordx4 v[144:145], v[148:151], off offset:256 sc1
	s_nop 1
	v_cvt_pk_bf16_f32 v148, v30, v31
	v_cvt_pk_bf16_f32 v149, v32, v33
	v_cvt_pk_bf16_f32 v150, v26, v27
	s_mul_i32 s12, s15, 0x140
	v_cvt_pk_bf16_f32 v151, v28, v29
	v_lshl_add_u64 v[144:145], v[142:143], 0, s[12:13]
	global_store_dwordx4 v[144:145], v[148:151], off sc1
	s_nop 1
	v_cvt_pk_bf16_f32 v148, v22, v23
	v_cvt_pk_bf16_f32 v149, v24, v25
	v_cvt_pk_bf16_f32 v150, v18, v19
	v_cvt_pk_bf16_f32 v151, v20, v21
	global_store_dwordx4 v[144:145], v[148:151], off offset:256 sc1
	s_nop 1
	v_cvt_pk_bf16_f32 v148, v14, v15
	v_cvt_pk_bf16_f32 v149, v16, v17
	s_mul_i32 s12, s15, 0x160
	v_lshl_add_u64 v[158:159], v[142:143], 0, s[12:13]
	v_cvt_pk_bf16_f32 v150, v10, v11
	v_cvt_pk_bf16_f32 v142, v6, v7
	v_cvt_pk_bf16_f32 v151, v12, v13
	v_cvt_pk_bf16_f32 v143, v8, v9
	v_cvt_pk_bf16_f32 v144, v2, v3
	v_cvt_pk_bf16_f32 v145, v4, v5
	s_cmp_lt_i32 s22, 8
	global_store_dwordx4 v[158:159], v[148:151], off sc1
	global_store_dwordx4 v[158:159], v[142:145], off offset:256 sc1
	s_cbranch_scc1 .LBB0_317
	v_mul_f32_e32 v127, v127, v127
	v_mul_f32_e32 v123, v123, v123
	v_fmac_f32_e32 v127, v126, v126
	v_mul_f32_e32 v126, v129, v129
	v_fmac_f32_e32 v123, v122, v122
	v_mul_f32_e32 v122, v125, v125
	v_mul_f32_e32 v119, v119, v119
	v_fmac_f32_e32 v126, v128, v128
	v_fmac_f32_e32 v122, v124, v124
	v_fmac_f32_e32 v119, v118, v118
	v_mul_f32_e32 v118, v121, v121
	v_mul_f32_e32 v115, v115, v115
	v_add_f32_e32 v126, v127, v126
	v_add_f32_e32 v122, v123, v122
	v_fmac_f32_e32 v118, v120, v120
	v_fmac_f32_e32 v115, v114, v114
	v_mul_f32_e32 v114, v117, v117
	v_cmp_lt_i32_e32 vcc, v220, v215
	v_add_f32_e32 v122, v122, v126
	v_add_f32_e32 v118, v119, v118
	v_fmac_f32_e32 v114, v116, v116
	v_cndmask_b32_e32 v142, v210, v220, vcc
	v_add_f32_e32 v118, v118, v122
	v_add_f32_e32 v114, v115, v114
	v_lshlrev_b32_e32 v142, 2, v142
	v_add_f32_e32 v114, v114, v118
	ds_bpermute_b32 v115, v142, v114
	s_lshl_b64 s[24:25], s[24:25], 14
	s_add_u32 s15, s60, s24
	v_cmp_lt_i32_e32 vcc, v221, v215
	s_addc_u32 s17, s61, s25
	s_lshl_b32 s12, s22, 2
	v_cndmask_b32_e32 v116, v210, v221, vcc
	s_lshl_b64 s[22:23], s[12:13], 2
	v_lshlrev_b32_e32 v116, 2, v116
	s_waitcnt lgkmcnt(0)
	v_add_f32_e32 v117, v114, v115
	s_add_u32 s12, s15, s22
	ds_bpermute_b32 v118, v116, v117
	s_addc_u32 s15, s17, s23
	s_add_u32 s22, s12, s68
	s_addc_u32 s23, s15, 0
	v_lshlrev_b32_e32 v146, 4, v156
	v_lshl_add_u64 v[114:115], v[146:147], 2, s[22:23]
	s_and_saveexec_b64 s[22:23], s[38:39]
	s_cbranch_execz .LBB0_302
	s_waitcnt lgkmcnt(0)
	v_add_f32_e32 v117, v117, v118
	global_store_dword v[114:115], v117, off offset:-128

; __device__ __forceinline__ unsigned pk2(float lo, float hi) { return f2bf(lo) | (f2bf(hi) << 16); }
; __device__ __forceinline__ void phase_conv(const Args& a, const Ctx& c0, int l) {
;     ...
;     for (int it = c.bid; it < NB * NCHUNK; it += c.G) {
;         const int b = it / NCHUNK, cc = it - b * NCHUNK; const bool isc = cc < 4;
;         const int seg0 = isc ? NL + b * CTXL : b * SEQ, T = isc ? CTXL : SEQ, t0 = (isc ? cc : cc - 4) * 64 + rg * 16;
;         u32x4 x[19];
; #pragma unroll
;         for (int i = 0; i < 19; ++i) { const int t = t0 - 2 + i; x[i] = (t >= 0 && t < T) ? *(const u32x4*)(XR + (size_t)(seg0 + t) * RW + ch) : (u32x4){0u, 0u, 0u, 0u}; }
; #pragma unroll
;         for (int r = 0; r < 16; ++r) { float o[8];
; #pragma unroll
;             for (int e = 0; e < 8; ++e) o[e] = bias[e];
; #pragma unroll
;             for (int k = 0; k < 4; ++k) { const u32x4 xv = x[r + k];
;                 o[0] = fmaf(bflo(xv.x), w[k][0], o[0]); o[1] = fmaf(bfhi(xv.x), w[k][1], o[1]); o[2] = fmaf(bflo(xv.y), w[k][2], o[2]); o[3] = fmaf(bfhi(xv.y), w[k][3], o[3]);
;                 o[4] = fmaf(bflo(xv.z), w[k][4], o[4]); o[5] = fmaf(bfhi(xv.z), w[k][5], o[5]); o[6] = fmaf(bflo(xv.w), w[k][6], o[6]); o[7] = fmaf(bfhi(xv.w), w[k][7], o[7]); }
;             u32x4 wv; wv.x = pk2(o[0], o[1]); wv.y = pk2(o[2], o[3]); wv.z = pk2(o[4], o[5]); wv.w = pk2(o[6], o[7]);
;             *(u32x4*)(U + (size_t)(seg0 + t0 + r) * RW + ch) = wv; }
;     }
.LBB0_378:
	s_or_b64 exec, exec, s[2:3]
	s_waitcnt vmcnt(0)
	v_lshlrev_b32_e32 v135, 16, v103
	v_lshlrev_b32_e32 v134, 16, v102
	v_and_b32_e32 v103, 0xffff0000, v103
	v_and_b32_e32 v102, 0xffff0000, v102
	v_lshlrev_b32_e32 v37, 16, v101
	v_lshlrev_b32_e32 v36, 16, v100
	v_and_b32_e32 v101, 0xffff0000, v101
	v_and_b32_e32 v100, 0xffff0000, v100
	v_pk_fma_f32 v[102:103], v[102:103], v[20:21], v[8:9]
	v_and_b32_e32 v139, 0xffff0000, v99
	v_and_b32_e32 v138, 0xffff0000, v98
	v_pk_fma_f32 v[36:37], v[36:37], v[18:19], v[6:7]
	v_pk_fma_f32 v[100:101], v[100:101], v[4:5], v[120:121]
	v_lshlrev_b32_e32 v129, 16, v97
	v_lshlrev_b32_e32 v128, 16, v96
	v_and_b32_e32 v131, 0xffff0000, v97
	v_and_b32_e32 v130, 0xffff0000, v96
	v_lshlrev_b32_e32 v137, 16, v99
	v_lshlrev_b32_e32 v136, 16, v98
	v_pk_fma_f32 v[98:99], v[138:139], v[28:29], v[102:103]
	v_lshlrev_b32_e32 v103, 16, v115
	v_lshlrev_b32_e32 v102, 16, v114
	v_and_b32_e32 v115, 0xffff0000, v115
	v_and_b32_e32 v114, 0xffff0000, v114
	v_pk_fma_f32 v[36:37], v[128:129], v[26:27], v[36:37]
	v_pk_fma_f32 v[96:97], v[130:131], v[124:125], v[100:101]
	v_lshlrev_b32_e32 v101, 16, v113
	v_lshlrev_b32_e32 v100, 16, v112
	v_and_b32_e32 v113, 0xffff0000, v113
	v_and_b32_e32 v112, 0xffff0000, v112
	v_pk_fma_f32 v[134:135], v[134:135], v[14:15], v[2:3]
	v_pk_fma_f32 v[98:99], v[114:115], v[24:25], v[98:99]
	v_lshlrev_b32_e32 v141, 16, v107
	v_lshlrev_b32_e32 v140, 16, v106
	v_and_b32_e32 v107, 0xffff0000, v107
	v_and_b32_e32 v106, 0xffff0000, v106
	v_pk_fma_f32 v[36:37], v[100:101], v[22:23], v[36:37]
	v_pk_fma_f32 v[96:97], v[112:113], v[122:123], v[96:97]
	v_lshlrev_b32_e32 v133, 16, v105
	v_lshlrev_b32_e32 v132, 16, v104
	v_and_b32_e32 v105, 0xffff0000, v105
	v_and_b32_e32 v104, 0xffff0000, v104
	v_pk_fma_f32 v[134:135], v[136:137], v[38:39], v[134:135]
	v_pk_fma_f32 v[98:99], v[106:107], v[12:13], v[98:99]
	v_pk_fma_f32 v[36:37], v[132:133], v[10:11], v[36:37]
	v_pk_fma_f32 v[96:97], v[104:105], v[16:17], v[96:97]
	v_pk_fma_f32 v[134:135], v[102:103], v[34:35], v[134:135]
	v_bfe_u32 v127, v99, 16, 1
	v_bfe_u32 v142, v98, 16, 1
	v_pk_fma_f32 v[134:135], v[140:141], v[30:31], v[134:135]
	v_bfe_u32 v143, v97, 16, 1
	v_bfe_u32 v144, v96, 16, 1
	v_add3_u32 v98, v98, v142, s37
	v_add3_u32 v99, v99, v127, s37
	v_bfe_u32 v127, v36, 16, 1
	v_bfe_u32 v142, v37, 16, 1
	v_add3_u32 v96, v96, v144, s37
	v_add3_u32 v97, v97, v143, s37
	v_bfe_u32 v143, v134, 16, 1
	v_bfe_u32 v144, v135, 16, 1
	v_add3_u32 v37, v37, v142, s37
	v_add3_u32 v36, v36, v127, s37
	v_add3_u32 v135, v135, v144, s37
	v_add3_u32 v134, v134, v143, s37
	v_lshrrev_b32_e32 v36, 16, v36
	v_lshrrev_b32_e32 v37, 16, v37
	v_lshrrev_b32_e32 v127, 16, v134
	v_lshrrev_b32_e32 v134, 16, v135
	v_and_or_b32 v97, v97, s33, v37
	v_and_or_b32 v96, v96, s33, v36
	v_lshlrev_b64 v[36:37], 11, v[32:33]
	v_and_or_b32 v99, v99, s33, v134
	v_and_or_b32 v98, v98, s33, v127
	v_lshl_add_u64 v[36:37], v[118:119], 0, v[36:37]
	global_store_dwordx4 v[36:37], v[96:99], off sc1
	v_pk_fma_f32 v[36:37], v[128:129], v[18:19], v[6:7]
	v_lshlrev_b32_e32 v135, 16, v111
	v_pk_fma_f32 v[96:97], v[130:131], v[4:5], v[120:121]
	v_pk_fma_f32 v[130:131], v[138:139], v[20:21], v[8:9]
	v_pk_fma_f32 v[36:37], v[100:101], v[26:27], v[36:37]
	v_pk_fma_f32 v[130:131], v[114:115], v[28:29], v[130:131]
	v_lshlrev_b32_e32 v134, 16, v110
	v_pk_fma_f32 v[130:131], v[106:107], v[24:25], v[130:131]
	v_and_b32_e32 v111, 0xffff0000, v111
	v_and_b32_e32 v110, 0xffff0000, v110
	v_pk_fma_f32 v[96:97], v[112:113], v[124:125], v[96:97]
	v_pk_fma_f32 v[36:37], v[132:133], v[22:23], v[36:37]
	v_lshlrev_b32_e32 v129, 16, v109
	v_lshlrev_b32_e32 v128, 16, v108
	v_pk_fma_f32 v[130:131], v[110:111], v[12:13], v[130:131]
	v_pk_fma_f32 v[96:97], v[104:105], v[122:123], v[96:97]
	v_pk_fma_f32 v[36:37], v[128:129], v[10:11], v[36:37]
	v_and_b32_e32 v109, 0xffff0000, v109
	v_and_b32_e32 v108, 0xffff0000, v108
	v_pk_fma_f32 v[98:99], v[136:137], v[14:15], v[2:3]
	v_bfe_u32 v127, v130, 16, 1
	v_pk_fma_f32 v[96:97], v[108:109], v[16:17], v[96:97]
	v_pk_fma_f32 v[98:99], v[102:103], v[38:39], v[98:99]
	v_bfe_u32 v33, v131, 16, 1
	v_add3_u32 v127, v130, v127, s37
	v_bfe_u32 v130, v36, 16, 1
	v_pk_fma_f32 v[98:99], v[140:141], v[34:35], v[98:99]
	v_bfe_u32 v137, v96, 16, 1
	v_add3_u32 v33, v131, v33, s37
	v_bfe_u32 v131, v37, 16, 1
	v_add3_u32 v36, v36, v130, s37
	v_pk_fma_f32 v[98:99], v[134:135], v[30:31], v[98:99]
	v_bfe_u32 v136, v97, 16, 1
	v_add3_u32 v96, v96, v137, s37
	v_add3_u32 v37, v37, v131, s37
	v_lshrrev_b32_e32 v36, 16, v36
	v_add3_u32 v97, v97, v136, s37
	v_bfe_u32 v136, v98, 16, 1
	v_bfe_u32 v137, v99, 16, 1
	v_lshrrev_b32_e32 v37, 16, v37
	v_and_or_b32 v96, v96, s33, v36
	v_or_b32_e32 v36, 1, v32
	v_add3_u32 v99, v99, v137, s37
	v_add3_u32 v98, v98, v136, s37
	v_and_or_b32 v97, v97, s33, v37
	v_ashrrev_i32_e32 v37, 31, v36
	v_lshrrev_b32_e32 v98, 16, v98
	v_lshrrev_b32_e32 v99, 16, v99
	v_lshlrev_b64 v[36:37], 11, v[36:37]
	v_and_or_b32 v99, v33, s33, v99
	v_and_or_b32 v98, v127, s33, v98
	v_lshl_add_u64 v[36:37], v[118:119], 0, v[36:37]
	global_store_dwordx4 v[36:37], v[96:99], off sc1
	v_pk_fma_f32 v[36:37], v[100:101], v[18:19], v[6:7]
	v_and_b32_e32 v101, 0xffff0000, v89
	v_pk_fma_f32 v[96:97], v[112:113], v[4:5], v[120:121]
	v_and_b32_e32 v100, 0xffff0000, v88
	v_pk_fma_f32 v[96:97], v[104:105], v[124:125], v[96:97]
	v_lshlrev_b32_e32 v99, 16, v89
	v_pk_fma_f32 v[96:97], v[108:109], v[122:123], v[96:97]
	v_lshlrev_b32_e32 v98, 16, v88
	v_pk_fma_f32 v[88:89], v[100:101], v[16:17], v[96:97]
	v_pk_fma_f32 v[96:97], v[102:103], v[14:15], v[2:3]
	v_pk_fma_f32 v[102:103], v[114:115], v[20:21], v[8:9]
; __device__ __forceinline__ unsigned pk2(float lo, float hi) { return f2bf(lo) | (f2bf(hi) << 16); }
; __device__ __forceinline__ void phase_conv(const Args& a, const Ctx& c0, int l) {
;     ...
;     for (int it = c.bid; it < NB * NCHUNK; it += c.G) {
;         const int b = it / NCHUNK, cc = it - b * NCHUNK; const bool isc = cc < 4;
;         const int seg0 = isc ? NL + b * CTXL : b * SEQ, T = isc ? CTXL : SEQ, t0 = (isc ? cc : cc - 4) * 64 + rg * 16;
;         u32x4 x[19];
; #pragma unroll
;         for (int i = 0; i < 19; ++i) { const int t = t0 - 2 + i; x[i] = (t >= 0 && t < T) ? *(const u32x4*)(XR + (size_t)(seg0 + t) * RW + ch) : (u32x4){0u, 0u, 0u, 0u}; }
; #pragma unroll
;         for (int r = 0; r < 16; ++r) { float o[8];
; #pragma unroll
;             for (int e = 0; e < 8; ++e) o[e] = bias[e];
; #pragma unroll
;             for (int k = 0; k < 4; ++k) { const u32x4 xv = x[r + k];
;                 o[0] = fmaf(bflo(xv.x), w[k][0], o[0]); o[1] = fmaf(bfhi(xv.x), w[k][1], o[1]); o[2] = fmaf(bflo(xv.y), w[k][2], o[2]); o[3] = fmaf(bfhi(xv.y), w[k][3], o[3]);
;                 o[4] = fmaf(bflo(xv.z), w[k][4], o[4]); o[5] = fmaf(bfhi(xv.z), w[k][5], o[5]); o[6] = fmaf(bflo(xv.w), w[k][6], o[6]); o[7] = fmaf(bfhi(xv.w), w[k][7], o[7]); }
;             u32x4 wv; wv.x = pk2(o[0], o[1]); wv.y = pk2(o[2], o[3]); wv.z = pk2(o[4], o[5]); wv.w = pk2(o[6], o[7]);
;             *(u32x4*)(U + (size_t)(seg0 + t0 + r) * RW + ch) = wv; }
;     }
	v_pk_fma_f32 v[36:37], v[132:133], v[26:27], v[36:37]
	v_pk_fma_f32 v[102:103], v[106:107], v[28:29], v[102:103]
	v_and_b32_e32 v115, 0xffff0000, v91
	v_pk_fma_f32 v[102:103], v[110:111], v[24:25], v[102:103]
	v_and_b32_e32 v114, 0xffff0000, v90
	v_pk_fma_f32 v[36:37], v[128:129], v[22:23], v[36:37]
	v_lshlrev_b32_e32 v113, 16, v91
	v_lshlrev_b32_e32 v112, 16, v90
	v_pk_fma_f32 v[90:91], v[114:115], v[12:13], v[102:103]
	v_pk_fma_f32 v[36:37], v[98:99], v[10:11], v[36:37]
	v_bfe_u32 v33, v91, 16, 1
	v_pk_fma_f32 v[96:97], v[140:141], v[38:39], v[96:97]
	v_bfe_u32 v102, v90, 16, 1
	v_add3_u32 v33, v91, v33, s37
	v_bfe_u32 v91, v36, 16, 1
	v_pk_fma_f32 v[96:97], v[134:135], v[34:35], v[96:97]
	v_bfe_u32 v127, v88, 16, 1
	v_add3_u32 v90, v90, v102, s37
	v_bfe_u32 v102, v37, 16, 1
	v_add3_u32 v36, v36, v91, s37
	v_pk_fma_f32 v[96:97], v[112:113], v[30:31], v[96:97]
	v_bfe_u32 v103, v89, 16, 1
	v_add3_u32 v88, v88, v127, s37
	v_add3_u32 v37, v37, v102, s37
	v_lshrrev_b32_e32 v36, 16, v36
	v_add3_u32 v89, v89, v103, s37
	v_bfe_u32 v103, v96, 16, 1
	v_bfe_u32 v127, v97, 16, 1
	v_lshrrev_b32_e32 v37, 16, v37
	v_and_or_b32 v88, v88, s33, v36
	v_or_b32_e32 v36, 2, v32
	v_add3_u32 v97, v97, v127, s37
	v_add3_u32 v96, v96, v103, s37
	v_and_or_b32 v89, v89, s33, v37
	v_ashrrev_i32_e32 v37, 31, v36
	v_lshrrev_b32_e32 v96, 16, v96
	v_lshrrev_b32_e32 v91, 16, v97
	v_lshlrev_b64 v[36:37], 11, v[36:37]
	v_and_or_b32 v91, v33, s33, v91
	v_and_or_b32 v90, v90, s33, v96
	v_lshl_add_u64 v[36:37], v[118:119], 0, v[36:37]
	v_pk_fma_f32 v[102:103], v[106:107], v[20:21], v[8:9]
	global_store_dwordx4 v[36:37], v[88:91], off sc1
	v_pk_fma_f32 v[36:37], v[132:133], v[18:19], v[6:7]
	v_pk_fma_f32 v[102:103], v[110:111], v[28:29], v[102:103]
	v_pk_fma_f32 v[88:89], v[104:105], v[4:5], v[120:121]
	v_pk_fma_f32 v[36:37], v[128:129], v[26:27], v[36:37]
	v_pk_fma_f32 v[102:103], v[114:115], v[24:25], v[102:103]
	v_lshlrev_b32_e32 v105, 16, v95
	v_lshlrev_b32_e32 v104, 16, v94
	v_and_b32_e32 v95, 0xffff0000, v95
	v_and_b32_e32 v94, 0xffff0000, v94
	v_pk_fma_f32 v[88:89], v[108:109], v[124:125], v[88:89]
	v_pk_fma_f32 v[36:37], v[98:99], v[22:23], v[36:37]
	v_lshlrev_b32_e32 v97, 16, v93
	v_lshlrev_b32_e32 v96, 16, v92
	v_pk_fma_f32 v[102:103], v[94:95], v[12:13], v[102:103]
	v_pk_fma_f32 v[88:89], v[100:101], v[122:123], v[88:89]
	v_pk_fma_f32 v[36:37], v[96:97], v[10:11], v[36:37]
	v_and_b32_e32 v93, 0xffff0000, v93
	v_and_b32_e32 v92, 0xffff0000, v92
	v_pk_fma_f32 v[90:91], v[140:141], v[14:15], v[2:3]
	v_bfe_u32 v33, v103, 16, 1
	v_pk_fma_f32 v[88:89], v[92:93], v[16:17], v[88:89]
	v_pk_fma_f32 v[90:91], v[134:135], v[38:39], v[90:91]
	v_bfe_u32 v106, v102, 16, 1
	v_add3_u32 v33, v103, v33, s37
	v_bfe_u32 v103, v36, 16, 1
	v_pk_fma_f32 v[90:91], v[112:113], v[34:35], v[90:91]
	v_bfe_u32 v127, v88, 16, 1
	v_add3_u32 v102, v102, v106, s37
	v_bfe_u32 v106, v37, 16, 1
	v_add3_u32 v36, v36, v103, s37
	v_pk_fma_f32 v[90:91], v[104:105], v[30:31], v[90:91]
	v_bfe_u32 v107, v89, 16, 1
	v_add3_u32 v88, v88, v127, s37
	v_add3_u32 v37, v37, v106, s37
	v_lshrrev_b32_e32 v36, 16, v36
	v_add3_u32 v89, v89, v107, s37
	v_bfe_u32 v107, v90, 16, 1
	v_bfe_u32 v127, v91, 16, 1
	v_lshrrev_b32_e32 v37, 16, v37
	v_and_or_b32 v88, v88, s33, v36
	v_or_b32_e32 v36, 3, v32
	v_add3_u32 v91, v91, v127, s37
	v_add3_u32 v90, v90, v107, s37
	v_and_or_b32 v89, v89, s33, v37
	v_ashrrev_i32_e32 v37, 31, v36
	v_lshrrev_b32_e32 v90, 16, v90
	v_lshrrev_b32_e32 v91, 16, v91
	v_lshlrev_b64 v[36:37], 11, v[36:37]
	v_and_or_b32 v91, v33, s33, v91
	v_and_or_b32 v90, v102, s33, v90
	v_lshl_add_u64 v[36:37], v[118:119], 0, v[36:37]
	v_pk_fma_f32 v[106:107], v[110:111], v[20:21], v[8:9]
	global_store_dwordx4 v[36:37], v[88:91], off sc1
	v_pk_fma_f32 v[36:37], v[128:129], v[18:19], v[6:7]
	v_pk_fma_f32 v[106:107], v[114:115], v[28:29], v[106:107]
	v_pk_fma_f32 v[88:89], v[108:109], v[4:5], v[120:121]
	v_pk_fma_f32 v[36:37], v[98:99], v[26:27], v[36:37]
	v_pk_fma_f32 v[88:89], v[100:101], v[124:125], v[88:89]
	v_pk_fma_f32 v[106:107], v[94:95], v[24:25], v[106:107]
	v_and_b32_e32 v111, 0xffff0000, v83
	v_and_b32_e32 v110, 0xffff0000, v82
	v_pk_fma_f32 v[36:37], v[96:97], v[22:23], v[36:37]
	v_pk_fma_f32 v[88:89], v[92:93], v[122:123], v[88:89]
	v_lshlrev_b32_e32 v91, 16, v81
	v_lshlrev_b32_e32 v90, 16, v80
	v_and_b32_e32 v103, 0xffff0000, v81
	v_and_b32_e32 v102, 0xffff0000, v80
	v_lshlrev_b32_e32 v109, 16, v83
	v_lshlrev_b32_e32 v108, 16, v82
	v_pk_fma_f32 v[82:83], v[110:111], v[12:13], v[106:107]
	v_pk_fma_f32 v[36:37], v[90:91], v[10:11], v[36:37]
	v_pk_fma_f32 v[80:81], v[102:103], v[16:17], v[88:89]
	v_pk_fma_f32 v[88:89], v[134:135], v[14:15], v[2:3]
	v_bfe_u32 v33, v83, 16, 1
	v_pk_fma_f32 v[88:89], v[112:113], v[38:39], v[88:89]
	v_bfe_u32 v106, v82, 16, 1
	v_add3_u32 v33, v83, v33, s37
	v_bfe_u32 v83, v36, 16, 1
	v_pk_fma_f32 v[88:89], v[104:105], v[34:35], v[88:89]
	v_bfe_u32 v127, v80, 16, 1
	v_add3_u32 v82, v82, v106, s37
	v_bfe_u32 v106, v37, 16, 1
	v_add3_u32 v36, v36, v83, s37
	v_pk_fma_f32 v[88:89], v[108:109], v[30:31], v[88:89]
	v_bfe_u32 v107, v81, 16, 1
	v_add3_u32 v80, v80, v127, s37
	v_add3_u32 v37, v37, v106, s37
	v_lshrrev_b32_e32 v36, 16, v36
	v_add3_u32 v81, v81, v107, s37
	v_bfe_u32 v107, v88, 16, 1
	v_bfe_u32 v127, v89, 16, 1
	v_lshrrev_b32_e32 v37, 16, v37
	v_and_or_b32 v80, v80, s33, v36
	v_or_b32_e32 v36, 4, v32
	v_add3_u32 v89, v89, v127, s37
	v_add3_u32 v88, v88, v107, s37
	v_and_or_b32 v81, v81, s33, v37
	v_ashrrev_i32_e32 v37, 31, v36
	v_lshrrev_b32_e32 v88, 16, v88
	v_lshrrev_b32_e32 v83, 16, v89
	v_lshlrev_b64 v[36:37], 11, v[36:37]
	v_and_or_b32 v83, v33, s33, v83
; __device__ __forceinline__ unsigned pk2(float lo, float hi) { return f2bf(lo) | (f2bf(hi) << 16); }
; __device__ __forceinline__ void phase_conv(const Args& a, const Ctx& c0, int l) {
;     ...
;     for (int it = c.bid; it < NB * NCHUNK; it += c.G) {
;         const int b = it / NCHUNK, cc = it - b * NCHUNK; const bool isc = cc < 4;
;         const int seg0 = isc ? NL + b * CTXL : b * SEQ, T = isc ? CTXL : SEQ, t0 = (isc ? cc : cc - 4) * 64 + rg * 16;
;         u32x4 x[19];
; #pragma unroll
;         for (int i = 0; i < 19; ++i) { const int t = t0 - 2 + i; x[i] = (t >= 0 && t < T) ? *(const u32x4*)(XR + (size_t)(seg0 + t) * RW + ch) : (u32x4){0u, 0u, 0u, 0u}; }
; #pragma unroll
;         for (int r = 0; r < 16; ++r) { float o[8];
; #pragma unroll
;             for (int e = 0; e < 8; ++e) o[e] = bias[e];
; #pragma unroll
;             for (int k = 0; k < 4; ++k) { const u32x4 xv = x[r + k];
;                 o[0] = fmaf(bflo(xv.x), w[k][0], o[0]); o[1] = fmaf(bfhi(xv.x), w[k][1], o[1]); o[2] = fmaf(bflo(xv.y), w[k][2], o[2]); o[3] = fmaf(bfhi(xv.y), w[k][3], o[3]);
;                 o[4] = fmaf(bflo(xv.z), w[k][4], o[4]); o[5] = fmaf(bfhi(xv.z), w[k][5], o[5]); o[6] = fmaf(bflo(xv.w), w[k][6], o[6]); o[7] = fmaf(bfhi(xv.w), w[k][7], o[7]); }
;             u32x4 wv; wv.x = pk2(o[0], o[1]); wv.y = pk2(o[2], o[3]); wv.z = pk2(o[4], o[5]); wv.w = pk2(o[6], o[7]);
;             *(u32x4*)(U + (size_t)(seg0 + t0 + r) * RW + ch) = wv; }
;     }
	v_and_or_b32 v82, v82, s33, v88
	v_lshl_add_u64 v[36:37], v[118:119], 0, v[36:37]
	global_store_dwordx4 v[36:37], v[80:83], off sc1
	v_pk_fma_f32 v[36:37], v[98:99], v[18:19], v[6:7]
	v_pk_fma_f32 v[98:99], v[114:115], v[20:21], v[8:9]
	v_pk_fma_f32 v[80:81], v[100:101], v[4:5], v[120:121]
	v_pk_fma_f32 v[98:99], v[94:95], v[28:29], v[98:99]
	v_pk_fma_f32 v[36:37], v[96:97], v[26:27], v[36:37]
	v_pk_fma_f32 v[98:99], v[110:111], v[24:25], v[98:99]
	v_lshlrev_b32_e32 v101, 16, v87
	v_lshlrev_b32_e32 v100, 16, v86
	v_and_b32_e32 v87, 0xffff0000, v87
	v_and_b32_e32 v86, 0xffff0000, v86
	v_pk_fma_f32 v[80:81], v[92:93], v[124:125], v[80:81]
	v_pk_fma_f32 v[36:37], v[90:91], v[22:23], v[36:37]
	v_lshlrev_b32_e32 v89, 16, v85
	v_lshlrev_b32_e32 v88, 16, v84
	v_pk_fma_f32 v[98:99], v[86:87], v[12:13], v[98:99]
	v_pk_fma_f32 v[80:81], v[102:103], v[122:123], v[80:81]
	v_pk_fma_f32 v[36:37], v[88:89], v[10:11], v[36:37]
	v_and_b32_e32 v85, 0xffff0000, v85
	v_and_b32_e32 v84, 0xffff0000, v84
	v_pk_fma_f32 v[82:83], v[112:113], v[14:15], v[2:3]
	v_bfe_u32 v33, v99, 16, 1
	v_pk_fma_f32 v[80:81], v[84:85], v[16:17], v[80:81]
	v_pk_fma_f32 v[82:83], v[104:105], v[38:39], v[82:83]
	v_bfe_u32 v106, v98, 16, 1
	v_add3_u32 v33, v99, v33, s37
	v_bfe_u32 v99, v36, 16, 1
	v_pk_fma_f32 v[82:83], v[108:109], v[34:35], v[82:83]
	v_bfe_u32 v112, v80, 16, 1
	v_add3_u32 v98, v98, v106, s37
	v_bfe_u32 v106, v37, 16, 1
	v_add3_u32 v36, v36, v99, s37
	v_pk_fma_f32 v[82:83], v[100:101], v[30:31], v[82:83]
	v_bfe_u32 v107, v81, 16, 1
	v_add3_u32 v80, v80, v112, s37
	v_add3_u32 v37, v37, v106, s37
	v_lshrrev_b32_e32 v36, 16, v36
	v_add3_u32 v81, v81, v107, s37
	v_bfe_u32 v107, v82, 16, 1
	v_bfe_u32 v112, v83, 16, 1
	v_lshrrev_b32_e32 v37, 16, v37
	v_and_or_b32 v80, v80, s33, v36
	v_or_b32_e32 v36, 5, v32
	v_add3_u32 v83, v83, v112, s37
	v_add3_u32 v82, v82, v107, s37
	v_and_or_b32 v81, v81, s33, v37
	v_ashrrev_i32_e32 v37, 31, v36
	v_lshrrev_b32_e32 v82, 16, v82
	v_lshrrev_b32_e32 v83, 16, v83
	v_lshlrev_b64 v[36:37], 11, v[36:37]
	v_and_or_b32 v83, v33, s33, v83
	v_and_or_b32 v82, v98, s33, v82
	v_lshl_add_u64 v[36:37], v[118:119], 0, v[36:37]
	v_pk_fma_f32 v[94:95], v[94:95], v[20:21], v[8:9]
	global_store_dwordx4 v[36:37], v[80:83], off sc1
	v_pk_fma_f32 v[36:37], v[96:97], v[18:19], v[6:7]
	v_pk_fma_f32 v[94:95], v[110:111], v[28:29], v[94:95]
	v_pk_fma_f32 v[80:81], v[92:93], v[4:5], v[120:121]
	v_pk_fma_f32 v[36:37], v[90:91], v[26:27], v[36:37]
	v_pk_fma_f32 v[80:81], v[102:103], v[124:125], v[80:81]
	v_pk_fma_f32 v[94:95], v[86:87], v[24:25], v[94:95]
	v_and_b32_e32 v99, 0xffff0000, v75
	v_and_b32_e32 v98, 0xffff0000, v74
	v_pk_fma_f32 v[36:37], v[88:89], v[22:23], v[36:37]
	v_pk_fma_f32 v[80:81], v[84:85], v[122:123], v[80:81]
	v_lshlrev_b32_e32 v83, 16, v73
	v_lshlrev_b32_e32 v82, 16, v72
	v_and_b32_e32 v93, 0xffff0000, v73
	v_and_b32_e32 v92, 0xffff0000, v72
	v_lshlrev_b32_e32 v97, 16, v75
	v_lshlrev_b32_e32 v96, 16, v74
	v_pk_fma_f32 v[74:75], v[98:99], v[12:13], v[94:95]
	v_pk_fma_f32 v[36:37], v[82:83], v[10:11], v[36:37]
	v_pk_fma_f32 v[72:73], v[92:93], v[16:17], v[80:81]
	v_pk_fma_f32 v[80:81], v[104:105], v[14:15], v[2:3]
	v_bfe_u32 v33, v75, 16, 1
	v_pk_fma_f32 v[80:81], v[108:109], v[38:39], v[80:81]
	v_bfe_u32 v94, v74, 16, 1
	v_add3_u32 v33, v75, v33, s37
	v_bfe_u32 v75, v36, 16, 1
	v_pk_fma_f32 v[80:81], v[100:101], v[34:35], v[80:81]
	v_bfe_u32 v104, v72, 16, 1
	v_add3_u32 v74, v74, v94, s37
	v_bfe_u32 v94, v37, 16, 1
	v_add3_u32 v36, v36, v75, s37
	v_pk_fma_f32 v[80:81], v[96:97], v[30:31], v[80:81]
	v_bfe_u32 v95, v73, 16, 1
	v_add3_u32 v72, v72, v104, s37
	v_add3_u32 v37, v37, v94, s37
	v_lshrrev_b32_e32 v36, 16, v36
	v_add3_u32 v73, v73, v95, s37
	v_bfe_u32 v95, v80, 16, 1
	v_bfe_u32 v104, v81, 16, 1
	v_lshrrev_b32_e32 v37, 16, v37
	v_and_or_b32 v72, v72, s33, v36
	v_or_b32_e32 v36, 6, v32
	v_add3_u32 v81, v81, v104, s37
	v_add3_u32 v80, v80, v95, s37
	v_and_or_b32 v73, v73, s33, v37
	v_ashrrev_i32_e32 v37, 31, v36
	v_lshrrev_b32_e32 v80, 16, v80
	v_lshrrev_b32_e32 v75, 16, v81
	v_lshlrev_b64 v[36:37], 11, v[36:37]
	v_and_or_b32 v75, v33, s33, v75
	v_and_or_b32 v74, v74, s33, v80
	v_lshl_add_u64 v[36:37], v[118:119], 0, v[36:37]
	global_store_dwordx4 v[36:37], v[72:75], off sc1
	v_pk_fma_f32 v[36:37], v[90:91], v[18:19], v[6:7]
	v_pk_fma_f32 v[90:91], v[110:111], v[20:21], v[8:9]
	v_pk_fma_f32 v[72:73], v[102:103], v[4:5], v[120:121]
	v_pk_fma_f32 v[90:91], v[86:87], v[28:29], v[90:91]
	v_pk_fma_f32 v[36:37], v[88:89], v[26:27], v[36:37]
	v_pk_fma_f32 v[90:91], v[98:99], v[24:25], v[90:91]
	v_lshlrev_b32_e32 v95, 16, v79
	v_lshlrev_b32_e32 v94, 16, v78
	v_and_b32_e32 v79, 0xffff0000, v79
	v_and_b32_e32 v78, 0xffff0000, v78
	v_pk_fma_f32 v[72:73], v[84:85], v[124:125], v[72:73]
	v_pk_fma_f32 v[36:37], v[82:83], v[22:23], v[36:37]
	v_lshlrev_b32_e32 v81, 16, v77
	v_lshlrev_b32_e32 v80, 16, v76
	v_pk_fma_f32 v[90:91], v[78:79], v[12:13], v[90:91]
	v_pk_fma_f32 v[72:73], v[92:93], v[122:123], v[72:73]
	v_pk_fma_f32 v[36:37], v[80:81], v[10:11], v[36:37]
	v_and_b32_e32 v77, 0xffff0000, v77
	v_and_b32_e32 v76, 0xffff0000, v76
	v_pk_fma_f32 v[74:75], v[108:109], v[14:15], v[2:3]
	v_bfe_u32 v33, v91, 16, 1
	v_pk_fma_f32 v[72:73], v[76:77], v[16:17], v[72:73]
	v_pk_fma_f32 v[74:75], v[100:101], v[38:39], v[74:75]
	v_bfe_u32 v102, v90, 16, 1
	v_add3_u32 v33, v91, v33, s37
	v_bfe_u32 v91, v36, 16, 1
	v_pk_fma_f32 v[74:75], v[96:97], v[34:35], v[74:75]
	v_bfe_u32 v104, v72, 16, 1
	v_add3_u32 v90, v90, v102, s37
	v_bfe_u32 v102, v37, 16, 1
	v_add3_u32 v36, v36, v91, s37
	v_pk_fma_f32 v[74:75], v[94:95], v[30:31], v[74:75]
	v_bfe_u32 v103, v73, 16, 1
; __device__ __forceinline__ unsigned pk2(float lo, float hi) { return f2bf(lo) | (f2bf(hi) << 16); }
; __device__ __forceinline__ void phase_conv(const Args& a, const Ctx& c0, int l) {
;     ...
;     for (int it = c.bid; it < NB * NCHUNK; it += c.G) {
;         const int b = it / NCHUNK, cc = it - b * NCHUNK; const bool isc = cc < 4;
;         const int seg0 = isc ? NL + b * CTXL : b * SEQ, T = isc ? CTXL : SEQ, t0 = (isc ? cc : cc - 4) * 64 + rg * 16;
;         u32x4 x[19];
; #pragma unroll
;         for (int i = 0; i < 19; ++i) { const int t = t0 - 2 + i; x[i] = (t >= 0 && t < T) ? *(const u32x4*)(XR + (size_t)(seg0 + t) * RW + ch) : (u32x4){0u, 0u, 0u, 0u}; }
; #pragma unroll
;         for (int r = 0; r < 16; ++r) { float o[8];
; #pragma unroll
;             for (int e = 0; e < 8; ++e) o[e] = bias[e];
; #pragma unroll
;             for (int k = 0; k < 4; ++k) { const u32x4 xv = x[r + k];
;                 o[0] = fmaf(bflo(xv.x), w[k][0], o[0]); o[1] = fmaf(bfhi(xv.x), w[k][1], o[1]); o[2] = fmaf(bflo(xv.y), w[k][2], o[2]); o[3] = fmaf(bfhi(xv.y), w[k][3], o[3]);
;                 o[4] = fmaf(bflo(xv.z), w[k][4], o[4]); o[5] = fmaf(bfhi(xv.z), w[k][5], o[5]); o[6] = fmaf(bflo(xv.w), w[k][6], o[6]); o[7] = fmaf(bfhi(xv.w), w[k][7], o[7]); }
;             u32x4 wv; wv.x = pk2(o[0], o[1]); wv.y = pk2(o[2], o[3]); wv.z = pk2(o[4], o[5]); wv.w = pk2(o[6], o[7]);
;             *(u32x4*)(U + (size_t)(seg0 + t0 + r) * RW + ch) = wv; }
;     }
	v_add3_u32 v72, v72, v104, s37
	v_add3_u32 v37, v37, v102, s37
	v_lshrrev_b32_e32 v36, 16, v36
	v_add3_u32 v73, v73, v103, s37
	v_bfe_u32 v103, v74, 16, 1
	v_bfe_u32 v104, v75, 16, 1
	v_lshrrev_b32_e32 v37, 16, v37
	v_and_or_b32 v72, v72, s33, v36
	v_or_b32_e32 v36, 7, v32
	v_add3_u32 v75, v75, v104, s37
	v_add3_u32 v74, v74, v103, s37
	v_and_or_b32 v73, v73, s33, v37
	v_ashrrev_i32_e32 v37, 31, v36
	v_lshrrev_b32_e32 v74, 16, v74
	v_lshrrev_b32_e32 v75, 16, v75
	v_lshlrev_b64 v[36:37], 11, v[36:37]
	v_and_or_b32 v75, v33, s33, v75
	v_and_or_b32 v74, v90, s33, v74
	v_lshl_add_u64 v[36:37], v[118:119], 0, v[36:37]
	v_pk_fma_f32 v[86:87], v[86:87], v[20:21], v[8:9]
	global_store_dwordx4 v[36:37], v[72:75], off sc1
	v_pk_fma_f32 v[36:37], v[88:89], v[18:19], v[6:7]
	v_pk_fma_f32 v[86:87], v[98:99], v[28:29], v[86:87]
	v_pk_fma_f32 v[72:73], v[84:85], v[4:5], v[120:121]
	v_pk_fma_f32 v[36:37], v[82:83], v[26:27], v[36:37]
	v_pk_fma_f32 v[72:73], v[92:93], v[124:125], v[72:73]
	v_pk_fma_f32 v[86:87], v[78:79], v[24:25], v[86:87]
	v_and_b32_e32 v91, 0xffff0000, v67
	v_and_b32_e32 v90, 0xffff0000, v66
	v_pk_fma_f32 v[36:37], v[80:81], v[22:23], v[36:37]
	v_pk_fma_f32 v[72:73], v[76:77], v[122:123], v[72:73]
	v_lshlrev_b32_e32 v75, 16, v65
	v_lshlrev_b32_e32 v74, 16, v64
	v_and_b32_e32 v85, 0xffff0000, v65
	v_and_b32_e32 v84, 0xffff0000, v64
	v_lshlrev_b32_e32 v89, 16, v67
	v_lshlrev_b32_e32 v88, 16, v66
	v_pk_fma_f32 v[66:67], v[90:91], v[12:13], v[86:87]
	v_pk_fma_f32 v[36:37], v[74:75], v[10:11], v[36:37]
	v_pk_fma_f32 v[64:65], v[84:85], v[16:17], v[72:73]
	v_pk_fma_f32 v[72:73], v[100:101], v[14:15], v[2:3]
	v_bfe_u32 v33, v67, 16, 1
	v_pk_fma_f32 v[72:73], v[96:97], v[38:39], v[72:73]
	v_bfe_u32 v86, v66, 16, 1
	v_add3_u32 v33, v67, v33, s37
	v_bfe_u32 v67, v36, 16, 1
	v_pk_fma_f32 v[72:73], v[94:95], v[34:35], v[72:73]
	v_bfe_u32 v100, v64, 16, 1
	v_add3_u32 v66, v66, v86, s37
	v_bfe_u32 v86, v37, 16, 1
	v_add3_u32 v36, v36, v67, s37
	v_pk_fma_f32 v[72:73], v[88:89], v[30:31], v[72:73]
	v_bfe_u32 v87, v65, 16, 1
	v_add3_u32 v64, v64, v100, s37
	v_add3_u32 v37, v37, v86, s37
	v_lshrrev_b32_e32 v36, 16, v36
	v_add3_u32 v65, v65, v87, s37
	v_bfe_u32 v87, v72, 16, 1
	v_bfe_u32 v100, v73, 16, 1
	v_lshrrev_b32_e32 v37, 16, v37
	v_and_or_b32 v64, v64, s33, v36
	v_or_b32_e32 v36, 8, v32
	v_add3_u32 v73, v73, v100, s37
	v_add3_u32 v72, v72, v87, s37
	v_and_or_b32 v65, v65, s33, v37
	v_ashrrev_i32_e32 v37, 31, v36
	v_lshrrev_b32_e32 v72, 16, v72
	v_lshrrev_b32_e32 v67, 16, v73
	v_lshlrev_b64 v[36:37], 11, v[36:37]
	v_and_or_b32 v67, v33, s33, v67
	v_and_or_b32 v66, v66, s33, v72
	v_lshl_add_u64 v[36:37], v[118:119], 0, v[36:37]
	global_store_dwordx4 v[36:37], v[64:67], off sc1
	v_pk_fma_f32 v[36:37], v[82:83], v[18:19], v[6:7]
	v_pk_fma_f32 v[82:83], v[98:99], v[20:21], v[8:9]
	v_pk_fma_f32 v[64:65], v[92:93], v[4:5], v[120:121]
	v_pk_fma_f32 v[82:83], v[78:79], v[28:29], v[82:83]
	v_pk_fma_f32 v[36:37], v[80:81], v[26:27], v[36:37]
	v_pk_fma_f32 v[82:83], v[90:91], v[24:25], v[82:83]
	v_lshlrev_b32_e32 v87, 16, v71
	v_lshlrev_b32_e32 v86, 16, v70
	v_and_b32_e32 v71, 0xffff0000, v71
	v_and_b32_e32 v70, 0xffff0000, v70
	v_pk_fma_f32 v[64:65], v[76:77], v[124:125], v[64:65]
	v_pk_fma_f32 v[36:37], v[74:75], v[22:23], v[36:37]
	v_lshlrev_b32_e32 v73, 16, v69
	v_lshlrev_b32_e32 v72, 16, v68
	v_pk_fma_f32 v[82:83], v[70:71], v[12:13], v[82:83]
	v_pk_fma_f32 v[64:65], v[84:85], v[122:123], v[64:65]
	v_pk_fma_f32 v[36:37], v[72:73], v[10:11], v[36:37]
	v_and_b32_e32 v69, 0xffff0000, v69
	v_and_b32_e32 v68, 0xffff0000, v68
	v_pk_fma_f32 v[66:67], v[96:97], v[14:15], v[2:3]
	v_bfe_u32 v33, v83, 16, 1
	v_pk_fma_f32 v[64:65], v[68:69], v[16:17], v[64:65]
	v_pk_fma_f32 v[66:67], v[94:95], v[38:39], v[66:67]
	v_bfe_u32 v92, v82, 16, 1
	v_add3_u32 v33, v83, v33, s37
	v_bfe_u32 v83, v36, 16, 1
	v_pk_fma_f32 v[66:67], v[88:89], v[34:35], v[66:67]
	v_bfe_u32 v96, v64, 16, 1
	v_add3_u32 v82, v82, v92, s37
	v_bfe_u32 v92, v37, 16, 1
	v_add3_u32 v36, v36, v83, s37
	v_pk_fma_f32 v[66:67], v[86:87], v[30:31], v[66:67]
	v_bfe_u32 v93, v65, 16, 1
	v_add3_u32 v64, v64, v96, s37
	v_add3_u32 v37, v37, v92, s37
	v_lshrrev_b32_e32 v36, 16, v36
	v_add3_u32 v65, v65, v93, s37
	v_bfe_u32 v93, v66, 16, 1
	v_bfe_u32 v96, v67, 16, 1
	v_lshrrev_b32_e32 v37, 16, v37
	v_and_or_b32 v64, v64, s33, v36
	v_or_b32_e32 v36, 9, v32
	v_add3_u32 v67, v67, v96, s37
	v_add3_u32 v66, v66, v93, s37
	v_and_or_b32 v65, v65, s33, v37
	v_ashrrev_i32_e32 v37, 31, v36
	v_lshrrev_b32_e32 v66, 16, v66
	v_lshrrev_b32_e32 v67, 16, v67
	v_lshlrev_b64 v[36:37], 11, v[36:37]
	v_and_or_b32 v67, v33, s33, v67
	v_and_or_b32 v66, v82, s33, v66
	v_lshl_add_u64 v[36:37], v[118:119], 0, v[36:37]
	v_pk_fma_f32 v[78:79], v[78:79], v[20:21], v[8:9]
	global_store_dwordx4 v[36:37], v[64:67], off sc1
	v_pk_fma_f32 v[36:37], v[80:81], v[18:19], v[6:7]
	v_pk_fma_f32 v[78:79], v[90:91], v[28:29], v[78:79]
	v_pk_fma_f32 v[64:65], v[76:77], v[4:5], v[120:121]
	v_pk_fma_f32 v[36:37], v[74:75], v[26:27], v[36:37]
	v_pk_fma_f32 v[64:65], v[84:85], v[124:125], v[64:65]
	v_pk_fma_f32 v[78:79], v[70:71], v[24:25], v[78:79]
	v_and_b32_e32 v83, 0xffff0000, v59
	v_and_b32_e32 v82, 0xffff0000, v58
	v_pk_fma_f32 v[36:37], v[72:73], v[22:23], v[36:37]
	v_pk_fma_f32 v[64:65], v[68:69], v[122:123], v[64:65]
	v_lshlrev_b32_e32 v67, 16, v57
	v_lshlrev_b32_e32 v66, 16, v56
	v_and_b32_e32 v77, 0xffff0000, v57
	v_and_b32_e32 v76, 0xffff0000, v56
	v_lshlrev_b32_e32 v81, 16, v59
	v_lshlrev_b32_e32 v80, 16, v58
	v_pk_fma_f32 v[58:59], v[82:83], v[12:13], v[78:79]
	v_pk_fma_f32 v[36:37], v[66:67], v[10:11], v[36:37]
	v_pk_fma_f32 v[56:57], v[76:77], v[16:17], v[64:65]
; __device__ __forceinline__ unsigned pk2(float lo, float hi) { return f2bf(lo) | (f2bf(hi) << 16); }
; __device__ __forceinline__ void phase_conv(const Args& a, const Ctx& c0, int l) {
;     ...
;     for (int it = c.bid; it < NB * NCHUNK; it += c.G) {
;         const int b = it / NCHUNK, cc = it - b * NCHUNK; const bool isc = cc < 4;
;         const int seg0 = isc ? NL + b * CTXL : b * SEQ, T = isc ? CTXL : SEQ, t0 = (isc ? cc : cc - 4) * 64 + rg * 16;
;         u32x4 x[19];
; #pragma unroll
;         for (int i = 0; i < 19; ++i) { const int t = t0 - 2 + i; x[i] = (t >= 0 && t < T) ? *(const u32x4*)(XR + (size_t)(seg0 + t) * RW + ch) : (u32x4){0u, 0u, 0u, 0u}; }
; #pragma unroll
;         for (int r = 0; r < 16; ++r) { float o[8];
; #pragma unroll
;             for (int e = 0; e < 8; ++e) o[e] = bias[e];
; #pragma unroll
;             for (int k = 0; k < 4; ++k) { const u32x4 xv = x[r + k];
;                 o[0] = fmaf(bflo(xv.x), w[k][0], o[0]); o[1] = fmaf(bfhi(xv.x), w[k][1], o[1]); o[2] = fmaf(bflo(xv.y), w[k][2], o[2]); o[3] = fmaf(bfhi(xv.y), w[k][3], o[3]);
;                 o[4] = fmaf(bflo(xv.z), w[k][4], o[4]); o[5] = fmaf(bfhi(xv.z), w[k][5], o[5]); o[6] = fmaf(bflo(xv.w), w[k][6], o[6]); o[7] = fmaf(bfhi(xv.w), w[k][7], o[7]); }
;             u32x4 wv; wv.x = pk2(o[0], o[1]); wv.y = pk2(o[2], o[3]); wv.z = pk2(o[4], o[5]); wv.w = pk2(o[6], o[7]);
;             *(u32x4*)(U + (size_t)(seg0 + t0 + r) * RW + ch) = wv; }
;     }
	v_pk_fma_f32 v[64:65], v[94:95], v[14:15], v[2:3]
	v_bfe_u32 v33, v59, 16, 1
	v_pk_fma_f32 v[64:65], v[88:89], v[38:39], v[64:65]
	v_bfe_u32 v78, v58, 16, 1
	v_add3_u32 v33, v59, v33, s37
	v_bfe_u32 v59, v36, 16, 1
	v_pk_fma_f32 v[64:65], v[86:87], v[34:35], v[64:65]
	v_bfe_u32 v92, v56, 16, 1
	v_add3_u32 v58, v58, v78, s37
	v_bfe_u32 v78, v37, 16, 1
	v_add3_u32 v36, v36, v59, s37
	v_pk_fma_f32 v[64:65], v[80:81], v[30:31], v[64:65]
	v_bfe_u32 v79, v57, 16, 1
	v_add3_u32 v56, v56, v92, s37
	v_add3_u32 v37, v37, v78, s37
	v_lshrrev_b32_e32 v36, 16, v36
	v_add3_u32 v57, v57, v79, s37
	v_bfe_u32 v79, v64, 16, 1
	v_bfe_u32 v92, v65, 16, 1
	v_lshrrev_b32_e32 v37, 16, v37
	v_and_or_b32 v56, v56, s33, v36
	v_or_b32_e32 v36, 10, v32
	v_add3_u32 v65, v65, v92, s37
	v_add3_u32 v64, v64, v79, s37
	v_and_or_b32 v57, v57, s33, v37
	v_ashrrev_i32_e32 v37, 31, v36
	v_lshrrev_b32_e32 v64, 16, v64
	v_lshrrev_b32_e32 v59, 16, v65
	v_lshlrev_b64 v[36:37], 11, v[36:37]
	v_and_or_b32 v59, v33, s33, v59
	v_and_or_b32 v58, v58, s33, v64
	v_lshl_add_u64 v[36:37], v[118:119], 0, v[36:37]
	global_store_dwordx4 v[36:37], v[56:59], off sc1
	v_pk_fma_f32 v[36:37], v[74:75], v[18:19], v[6:7]
	v_pk_fma_f32 v[74:75], v[90:91], v[20:21], v[8:9]
	v_pk_fma_f32 v[56:57], v[84:85], v[4:5], v[120:121]
	v_pk_fma_f32 v[74:75], v[70:71], v[28:29], v[74:75]
	v_pk_fma_f32 v[36:37], v[72:73], v[26:27], v[36:37]
	v_pk_fma_f32 v[74:75], v[82:83], v[24:25], v[74:75]
	v_lshlrev_b32_e32 v79, 16, v63
	v_lshlrev_b32_e32 v78, 16, v62
	v_and_b32_e32 v63, 0xffff0000, v63
	v_and_b32_e32 v62, 0xffff0000, v62
	v_pk_fma_f32 v[56:57], v[68:69], v[124:125], v[56:57]
	v_pk_fma_f32 v[36:37], v[66:67], v[22:23], v[36:37]
	v_lshlrev_b32_e32 v65, 16, v61
	v_lshlrev_b32_e32 v64, 16, v60
	v_pk_fma_f32 v[74:75], v[62:63], v[12:13], v[74:75]
	v_pk_fma_f32 v[56:57], v[76:77], v[122:123], v[56:57]
	v_pk_fma_f32 v[36:37], v[64:65], v[10:11], v[36:37]
	v_and_b32_e32 v61, 0xffff0000, v61
	v_and_b32_e32 v60, 0xffff0000, v60
	v_pk_fma_f32 v[58:59], v[88:89], v[14:15], v[2:3]
	v_bfe_u32 v33, v75, 16, 1
	v_pk_fma_f32 v[56:57], v[60:61], v[16:17], v[56:57]
	v_pk_fma_f32 v[58:59], v[86:87], v[38:39], v[58:59]
	v_bfe_u32 v84, v74, 16, 1
	v_add3_u32 v33, v75, v33, s37
	v_bfe_u32 v75, v36, 16, 1
	v_pk_fma_f32 v[58:59], v[80:81], v[34:35], v[58:59]
	v_bfe_u32 v88, v56, 16, 1
	v_add3_u32 v74, v74, v84, s37
	v_bfe_u32 v84, v37, 16, 1
	v_add3_u32 v36, v36, v75, s37
	v_pk_fma_f32 v[58:59], v[78:79], v[30:31], v[58:59]
	v_bfe_u32 v85, v57, 16, 1
	v_add3_u32 v56, v56, v88, s37
	v_add3_u32 v37, v37, v84, s37
	v_lshrrev_b32_e32 v36, 16, v36
	v_add3_u32 v57, v57, v85, s37
	v_bfe_u32 v85, v58, 16, 1
	v_bfe_u32 v88, v59, 16, 1
	v_lshrrev_b32_e32 v37, 16, v37
	v_and_or_b32 v56, v56, s33, v36
	v_or_b32_e32 v36, 11, v32
	v_add3_u32 v59, v59, v88, s37
	v_add3_u32 v58, v58, v85, s37
	v_and_or_b32 v57, v57, s33, v37
	v_ashrrev_i32_e32 v37, 31, v36
	v_lshrrev_b32_e32 v58, 16, v58
	v_lshrrev_b32_e32 v59, 16, v59
	v_lshlrev_b64 v[36:37], 11, v[36:37]
	v_and_or_b32 v59, v33, s33, v59
	v_and_or_b32 v58, v74, s33, v58
	v_lshl_add_u64 v[36:37], v[118:119], 0, v[36:37]
	v_pk_fma_f32 v[70:71], v[70:71], v[20:21], v[8:9]
	global_store_dwordx4 v[36:37], v[56:59], off sc1
	v_pk_fma_f32 v[36:37], v[72:73], v[18:19], v[6:7]
	v_pk_fma_f32 v[70:71], v[82:83], v[28:29], v[70:71]
	v_pk_fma_f32 v[56:57], v[68:69], v[4:5], v[120:121]
	v_pk_fma_f32 v[36:37], v[66:67], v[26:27], v[36:37]
	v_pk_fma_f32 v[56:57], v[76:77], v[124:125], v[56:57]
	v_pk_fma_f32 v[70:71], v[62:63], v[24:25], v[70:71]
	v_and_b32_e32 v75, 0xffff0000, v51
	v_and_b32_e32 v74, 0xffff0000, v50
	v_pk_fma_f32 v[36:37], v[64:65], v[22:23], v[36:37]
	v_pk_fma_f32 v[56:57], v[60:61], v[122:123], v[56:57]
	v_lshlrev_b32_e32 v59, 16, v49
	v_lshlrev_b32_e32 v58, 16, v48
	v_and_b32_e32 v69, 0xffff0000, v49
	v_and_b32_e32 v68, 0xffff0000, v48
	v_lshlrev_b32_e32 v73, 16, v51
	v_lshlrev_b32_e32 v72, 16, v50
	v_pk_fma_f32 v[50:51], v[74:75], v[12:13], v[70:71]
	v_pk_fma_f32 v[36:37], v[58:59], v[10:11], v[36:37]
	v_pk_fma_f32 v[48:49], v[68:69], v[16:17], v[56:57]
	v_pk_fma_f32 v[56:57], v[86:87], v[14:15], v[2:3]
	v_bfe_u32 v33, v51, 16, 1
	v_pk_fma_f32 v[56:57], v[80:81], v[38:39], v[56:57]
	v_bfe_u32 v70, v50, 16, 1
	v_add3_u32 v33, v51, v33, s37
	v_bfe_u32 v51, v36, 16, 1
	v_pk_fma_f32 v[56:57], v[78:79], v[34:35], v[56:57]
	v_bfe_u32 v84, v48, 16, 1
	v_add3_u32 v50, v50, v70, s37
	v_bfe_u32 v70, v37, 16, 1
	v_add3_u32 v36, v36, v51, s37
	v_pk_fma_f32 v[56:57], v[72:73], v[30:31], v[56:57]
	v_bfe_u32 v71, v49, 16, 1
	v_add3_u32 v48, v48, v84, s37
	v_add3_u32 v37, v37, v70, s37
	v_lshrrev_b32_e32 v36, 16, v36
	v_add3_u32 v49, v49, v71, s37
	v_bfe_u32 v71, v56, 16, 1
	v_bfe_u32 v84, v57, 16, 1
	v_lshrrev_b32_e32 v37, 16, v37
	v_and_or_b32 v48, v48, s33, v36
	v_or_b32_e32 v36, 12, v32
	v_add3_u32 v57, v57, v84, s37
	v_add3_u32 v56, v56, v71, s37
	v_and_or_b32 v49, v49, s33, v37
	v_ashrrev_i32_e32 v37, 31, v36
	v_lshrrev_b32_e32 v56, 16, v56
	v_lshrrev_b32_e32 v51, 16, v57
	v_lshlrev_b64 v[36:37], 11, v[36:37]
	v_and_or_b32 v51, v33, s33, v51
	v_and_or_b32 v50, v50, s33, v56
	v_lshl_add_u64 v[36:37], v[118:119], 0, v[36:37]
	global_store_dwordx4 v[36:37], v[48:51], off sc1
	v_pk_fma_f32 v[36:37], v[66:67], v[18:19], v[6:7]
	v_pk_fma_f32 v[66:67], v[82:83], v[20:21], v[8:9]
	v_pk_fma_f32 v[48:49], v[76:77], v[4:5], v[120:121]
	v_pk_fma_f32 v[66:67], v[62:63], v[28:29], v[66:67]
	v_pk_fma_f32 v[36:37], v[64:65], v[26:27], v[36:37]
	v_pk_fma_f32 v[66:67], v[74:75], v[24:25], v[66:67]
	v_lshlrev_b32_e32 v71, 16, v55
	v_lshlrev_b32_e32 v70, 16, v54
	v_and_b32_e32 v55, 0xffff0000, v55
; __device__ __forceinline__ unsigned pk2(float lo, float hi) { return f2bf(lo) | (f2bf(hi) << 16); }
; __device__ __forceinline__ void phase_conv(const Args& a, const Ctx& c0, int l) {
;     ...
;     for (int it = c.bid; it < NB * NCHUNK; it += c.G) {
;         const int b = it / NCHUNK, cc = it - b * NCHUNK; const bool isc = cc < 4;
;         const int seg0 = isc ? NL + b * CTXL : b * SEQ, T = isc ? CTXL : SEQ, t0 = (isc ? cc : cc - 4) * 64 + rg * 16;
;         u32x4 x[19];
; #pragma unroll
;         for (int i = 0; i < 19; ++i) { const int t = t0 - 2 + i; x[i] = (t >= 0 && t < T) ? *(const u32x4*)(XR + (size_t)(seg0 + t) * RW + ch) : (u32x4){0u, 0u, 0u, 0u}; }
; #pragma unroll
;         for (int r = 0; r < 16; ++r) { float o[8];
; #pragma unroll
;             for (int e = 0; e < 8; ++e) o[e] = bias[e];
; #pragma unroll
;             for (int k = 0; k < 4; ++k) { const u32x4 xv = x[r + k];
;                 o[0] = fmaf(bflo(xv.x), w[k][0], o[0]); o[1] = fmaf(bfhi(xv.x), w[k][1], o[1]); o[2] = fmaf(bflo(xv.y), w[k][2], o[2]); o[3] = fmaf(bfhi(xv.y), w[k][3], o[3]);
;                 o[4] = fmaf(bflo(xv.z), w[k][4], o[4]); o[5] = fmaf(bfhi(xv.z), w[k][5], o[5]); o[6] = fmaf(bflo(xv.w), w[k][6], o[6]); o[7] = fmaf(bfhi(xv.w), w[k][7], o[7]); }
;             u32x4 wv; wv.x = pk2(o[0], o[1]); wv.y = pk2(o[2], o[3]); wv.z = pk2(o[4], o[5]); wv.w = pk2(o[6], o[7]);
;             *(u32x4*)(U + (size_t)(seg0 + t0 + r) * RW + ch) = wv; }
;     }
	v_and_b32_e32 v54, 0xffff0000, v54
	v_pk_fma_f32 v[48:49], v[60:61], v[124:125], v[48:49]
	v_pk_fma_f32 v[36:37], v[58:59], v[22:23], v[36:37]
	v_lshlrev_b32_e32 v57, 16, v53
	v_lshlrev_b32_e32 v56, 16, v52
	v_pk_fma_f32 v[66:67], v[54:55], v[12:13], v[66:67]
	v_pk_fma_f32 v[48:49], v[68:69], v[122:123], v[48:49]
	v_pk_fma_f32 v[36:37], v[56:57], v[10:11], v[36:37]
	v_and_b32_e32 v53, 0xffff0000, v53
	v_and_b32_e32 v52, 0xffff0000, v52
	v_pk_fma_f32 v[50:51], v[80:81], v[14:15], v[2:3]
	v_bfe_u32 v33, v67, 16, 1
	v_pk_fma_f32 v[48:49], v[52:53], v[16:17], v[48:49]
	v_pk_fma_f32 v[50:51], v[78:79], v[38:39], v[50:51]
	v_bfe_u32 v76, v66, 16, 1
	v_add3_u32 v33, v67, v33, s37
	v_bfe_u32 v67, v36, 16, 1
	v_pk_fma_f32 v[50:51], v[72:73], v[34:35], v[50:51]
	v_bfe_u32 v80, v48, 16, 1
	v_add3_u32 v66, v66, v76, s37
	v_bfe_u32 v76, v37, 16, 1
	v_add3_u32 v36, v36, v67, s37
	v_pk_fma_f32 v[50:51], v[70:71], v[30:31], v[50:51]
	v_bfe_u32 v77, v49, 16, 1
	v_add3_u32 v48, v48, v80, s37
	v_add3_u32 v37, v37, v76, s37
	v_lshrrev_b32_e32 v36, 16, v36
	v_add3_u32 v49, v49, v77, s37
	v_bfe_u32 v77, v50, 16, 1
	v_bfe_u32 v80, v51, 16, 1
	v_lshrrev_b32_e32 v37, 16, v37
	v_and_or_b32 v48, v48, s33, v36
	v_or_b32_e32 v36, 13, v32
	v_add3_u32 v51, v51, v80, s37
	v_add3_u32 v50, v50, v77, s37
	v_and_or_b32 v49, v49, s33, v37
	v_ashrrev_i32_e32 v37, 31, v36
	v_lshrrev_b32_e32 v50, 16, v50
	v_lshrrev_b32_e32 v51, 16, v51
	v_lshlrev_b64 v[36:37], 11, v[36:37]
	v_and_or_b32 v51, v33, s33, v51
	v_and_or_b32 v50, v66, s33, v50
	v_lshl_add_u64 v[36:37], v[118:119], 0, v[36:37]
	v_pk_fma_f32 v[62:63], v[62:63], v[20:21], v[8:9]
	global_store_dwordx4 v[36:37], v[48:51], off sc1
	v_pk_fma_f32 v[36:37], v[64:65], v[18:19], v[6:7]
	v_pk_fma_f32 v[62:63], v[74:75], v[28:29], v[62:63]
	v_pk_fma_f32 v[48:49], v[60:61], v[4:5], v[120:121]
	v_pk_fma_f32 v[36:37], v[58:59], v[26:27], v[36:37]
	v_pk_fma_f32 v[48:49], v[68:69], v[124:125], v[48:49]
	v_pk_fma_f32 v[62:63], v[54:55], v[24:25], v[62:63]
	v_and_b32_e32 v67, 0xffff0000, v43
	v_and_b32_e32 v66, 0xffff0000, v42
	v_pk_fma_f32 v[36:37], v[56:57], v[22:23], v[36:37]
	v_pk_fma_f32 v[48:49], v[52:53], v[122:123], v[48:49]
	v_lshlrev_b32_e32 v51, 16, v41
	v_lshlrev_b32_e32 v50, 16, v40
	v_and_b32_e32 v61, 0xffff0000, v41
	v_and_b32_e32 v60, 0xffff0000, v40
	v_lshlrev_b32_e32 v65, 16, v43
	v_lshlrev_b32_e32 v64, 16, v42
	v_pk_fma_f32 v[42:43], v[66:67], v[12:13], v[62:63]
	v_pk_fma_f32 v[36:37], v[50:51], v[10:11], v[36:37]
	v_pk_fma_f32 v[40:41], v[60:61], v[16:17], v[48:49]
	v_pk_fma_f32 v[48:49], v[78:79], v[14:15], v[2:3]
	v_bfe_u32 v33, v43, 16, 1
	v_pk_fma_f32 v[48:49], v[72:73], v[38:39], v[48:49]
	v_bfe_u32 v62, v42, 16, 1
	v_add3_u32 v33, v43, v33, s37
	v_bfe_u32 v43, v36, 16, 1
	v_pk_fma_f32 v[48:49], v[70:71], v[34:35], v[48:49]
	v_bfe_u32 v76, v40, 16, 1
	v_add3_u32 v42, v42, v62, s37
	v_bfe_u32 v62, v37, 16, 1
	v_add3_u32 v36, v36, v43, s37
	v_pk_fma_f32 v[48:49], v[64:65], v[30:31], v[48:49]
	v_bfe_u32 v63, v41, 16, 1
	v_add3_u32 v40, v40, v76, s37
	v_add3_u32 v37, v37, v62, s37
	v_lshrrev_b32_e32 v36, 16, v36
	v_add3_u32 v41, v41, v63, s37
	v_bfe_u32 v63, v48, 16, 1
	v_bfe_u32 v76, v49, 16, 1
	v_lshrrev_b32_e32 v37, 16, v37
	v_and_or_b32 v40, v40, s33, v36
	v_or_b32_e32 v36, 14, v32
	v_add3_u32 v49, v49, v76, s37
	v_add3_u32 v48, v48, v63, s37
	v_and_or_b32 v41, v41, s33, v37
	v_ashrrev_i32_e32 v37, 31, v36
	v_lshrrev_b32_e32 v48, 16, v48
	v_lshrrev_b32_e32 v43, 16, v49
	v_lshlrev_b64 v[36:37], 11, v[36:37]
	v_and_or_b32 v43, v33, s33, v43
	v_and_or_b32 v42, v42, s33, v48
	v_lshl_add_u64 v[36:37], v[118:119], 0, v[36:37]
	global_store_dwordx4 v[36:37], v[40:43], off sc1
	v_pk_fma_f32 v[36:37], v[58:59], v[18:19], v[6:7]
	v_lshlrev_b32_e32 v49, 16, v47
	v_pk_fma_f32 v[40:41], v[68:69], v[4:5], v[120:121]
	v_pk_fma_f32 v[36:37], v[56:57], v[26:27], v[36:37]
	v_pk_fma_f32 v[40:41], v[52:53], v[124:125], v[40:41]
	v_pk_fma_f32 v[36:37], v[50:51], v[22:23], v[36:37]
	v_lshlrev_b32_e32 v43, 16, v45
	v_lshlrev_b32_e32 v42, 16, v44
	v_pk_fma_f32 v[40:41], v[60:61], v[122:123], v[40:41]
	v_pk_fma_f32 v[36:37], v[42:43], v[10:11], v[36:37]
	v_and_b32_e32 v43, 0xffff0000, v45
	v_and_b32_e32 v42, 0xffff0000, v44
	v_pk_fma_f32 v[40:41], v[42:43], v[16:17], v[40:41]
	v_pk_fma_f32 v[42:43], v[72:73], v[14:15], v[2:3]
	v_pk_fma_f32 v[44:45], v[74:75], v[20:21], v[8:9]
	v_pk_fma_f32 v[42:43], v[70:71], v[38:39], v[42:43]
	v_pk_fma_f32 v[44:45], v[54:55], v[28:29], v[44:45]
	v_pk_fma_f32 v[42:43], v[64:65], v[34:35], v[42:43]
	v_lshlrev_b32_e32 v48, 16, v46
	v_pk_fma_f32 v[44:45], v[66:67], v[24:25], v[44:45]
	v_pk_fma_f32 v[42:43], v[48:49], v[30:31], v[42:43]
	v_and_b32_e32 v47, 0xffff0000, v47
	v_and_b32_e32 v46, 0xffff0000, v46
	v_bfe_u32 v48, v40, 16, 1
	v_pk_fma_f32 v[44:45], v[46:47], v[12:13], v[44:45]
	v_add3_u32 v40, v40, v48, s37
	v_bfe_u32 v48, v43, 16, 1
	v_bfe_u32 v33, v45, 16, 1
	v_bfe_u32 v46, v44, 16, 1
	v_bfe_u32 v47, v41, 16, 1
	v_add3_u32 v43, v43, v48, s37
	v_add3_u32 v41, v41, v47, s37
	v_add3_u32 v44, v44, v46, s37
	v_add3_u32 v33, v45, v33, s37
	v_bfe_u32 v45, v36, 16, 1
	v_bfe_u32 v46, v37, 16, 1
	v_bfe_u32 v47, v42, 16, 1
	v_lshrrev_b32_e32 v43, 16, v43
	v_or_b32_e32 v32, 15, v32
	v_add3_u32 v42, v42, v47, s37
	v_add3_u32 v37, v37, v46, s37
	v_add3_u32 v36, v36, v45, s37
	v_and_or_b32 v43, v33, s33, v43
	v_ashrrev_i32_e32 v33, 31, v32
	v_readlane_b32 s2, v253, 43
	v_lshrrev_b32_e32 v36, 16, v36
	v_lshrrev_b32_e32 v37, 16, v37
	v_lshrrev_b32_e32 v42, 16, v42
	v_lshlrev_b64 v[32:33], 11, v[32:33]
	s_add_i32 s5, s5, s91
	s_add_i32 s4, s4, s2
	v_and_or_b32 v42, v44, s33, v42
	v_and_or_b32 v41, v41, s33, v37
	v_and_or_b32 v40, v40, s33, v36
	v_lshl_add_u64 v[32:33], v[118:119], 0, v[32:33]
	s_cmpk_lt_i32 s5, 0x110
	global_store_dwordx4 v[32:33], v[40:43], off sc1
	s_cbranch_scc0 .LBB0_417

; __device__ __forceinline__ unsigned pk2(float lo, float hi) { return f2bf(lo) | (f2bf(hi) << 16); }
;     __device__ __forceinline__ void epi(const f32x4 (&acc)[2][2][4][2], const Unit& u, int wr, int wc, int fr, int fq) const {
;         unsigned loff = (unsigned)((wr * 64 + fr) * 1536 + wc * 32 + 8 * fq) * 2u; asm volatile("" : "+v"(loff));
;         char* base = (char*)(O + (size_t)u.pm * 256 * 1536 + (size_t)u.pn * 256);
; #pragma unroll
;         for (int ai = 0; ai < 2; ++ai)
; #pragma unroll
;             for (int m = 0; m < 4; ++m)
; #pragma unroll
;                 for (int bj = 0; bj < 2; ++bj) { const f32x4 v0 = acc[ai][bj][m][0], v1 = acc[ai][bj][m][1];
;                     u32x4 w; w.x = pk2(v0[0], v0[1]); w.y = pk2(v0[2], v0[3]); w.z = pk2(v1[0], v1[1]); w.w = pk2(v1[2], v1[3]);
;                     *(u32x4*)(base + ((size_t)(ai * 128 + m * 16) * 1536 + bj * 128) * 2 + loff) = w; }
;     }
.LBB0_484:
	v_bfe_u32 v149, v126, 16, 1
	v_add3_u32 v126, v126, v149, s37
	v_bfe_u32 v149, v127, 16, 1
	v_lshrrev_b32_e32 v126, 16, v126
	v_add3_u32 v127, v127, v149, s37
	v_and_or_b32 v126, v127, s33, v126
	v_bfe_u32 v127, v128, 16, 1
	v_add3_u32 v127, v128, v127, s37
	v_bfe_u32 v128, v129, 16, 1
	v_lshrrev_b32_e32 v127, 16, v127
	v_add3_u32 v128, v129, v128, s37
	v_and_or_b32 v127, v128, s33, v127
	v_bfe_u32 v128, v122, 16, 1
	v_add3_u32 v122, v122, v128, s37
	v_bfe_u32 v128, v123, 16, 1
	v_lshrrev_b32_e32 v122, 16, v122
	v_add3_u32 v123, v123, v128, s37
	v_and_or_b32 v128, v123, s33, v122
	v_cvt_pk_bf16_f32 v129, v124, v125
	v_bfe_u32 v122, v118, 16, 1
	v_add3_u32 v118, v118, v122, s37
	v_bfe_u32 v122, v119, 16, 1
	v_lshrrev_b32_e32 v118, 16, v118
	v_add3_u32 v119, v119, v122, s37
	v_and_or_b32 v118, v119, s33, v118
	v_bfe_u32 v119, v120, 16, 1
	v_add3_u32 v119, v120, v119, s37
	v_bfe_u32 v120, v121, 16, 1
	v_lshrrev_b32_e32 v119, 16, v119
	v_add3_u32 v120, v121, v120, s37
	v_and_or_b32 v119, v120, s33, v119
	v_bfe_u32 v120, v114, 16, 1
	v_add3_u32 v114, v114, v120, s37
	v_bfe_u32 v120, v115, 16, 1
	v_lshrrev_b32_e32 v114, 16, v114
	v_add3_u32 v115, v115, v120, s37
	v_and_or_b32 v120, v115, s33, v114
	v_cvt_pk_bf16_f32 v121, v116, v117
	v_bfe_u32 v114, v110, 16, 1
	v_add3_u32 v110, v110, v114, s37
	v_bfe_u32 v114, v111, 16, 1
	v_lshrrev_b32_e32 v110, 16, v110
	v_add3_u32 v111, v111, v114, s37
	v_and_or_b32 v110, v111, s33, v110
	v_bfe_u32 v111, v112, 16, 1
	v_add3_u32 v111, v112, v111, s37
	v_bfe_u32 v112, v113, 16, 1
	v_lshrrev_b32_e32 v111, 16, v111
	v_add3_u32 v112, v113, v112, s37
	v_and_or_b32 v111, v112, s33, v111
	v_bfe_u32 v112, v106, 16, 1
	v_add3_u32 v106, v106, v112, s37
	v_bfe_u32 v112, v107, 16, 1
	v_lshrrev_b32_e32 v106, 16, v106
	v_add3_u32 v107, v107, v112, s37
	v_and_or_b32 v112, v107, s33, v106
	v_bfe_u32 v106, v108, 16, 1
	v_add3_u32 v106, v108, v106, s37
	v_bfe_u32 v108, v102, 16, 1
	v_add3_u32 v102, v102, v108, s37
	v_bfe_u32 v108, v103, 16, 1
	v_lshrrev_b32_e32 v102, 16, v102
	v_add3_u32 v103, v103, v108, s37
	v_and_or_b32 v102, v103, s33, v102
	v_bfe_u32 v103, v104, 16, 1
	v_add3_u32 v103, v104, v103, s37
	v_bfe_u32 v104, v105, 16, 1
	v_lshrrev_b32_e32 v103, 16, v103
	v_add3_u32 v104, v105, v104, s37
	v_and_or_b32 v103, v104, s33, v103
	v_bfe_u32 v104, v98, 16, 1
	v_add3_u32 v98, v98, v104, s37
	v_bfe_u32 v104, v99, 16, 1
	v_lshrrev_b32_e32 v98, 16, v98
	v_add3_u32 v99, v99, v104, s37
	v_and_or_b32 v104, v99, s33, v98
	v_cvt_pk_bf16_f32 v105, v100, v101
	v_bfe_u32 v98, v94, 16, 1
	v_add3_u32 v94, v94, v98, s37
	v_bfe_u32 v98, v95, 16, 1
	v_lshrrev_b32_e32 v94, 16, v94
	v_add3_u32 v95, v95, v98, s37
	v_and_or_b32 v94, v95, s33, v94
	v_bfe_u32 v95, v96, 16, 1
	v_add3_u32 v95, v96, v95, s37
	v_bfe_u32 v96, v97, 16, 1
	v_lshrrev_b32_e32 v95, 16, v95
	v_add3_u32 v96, v97, v96, s37
	v_and_or_b32 v95, v96, s33, v95
	v_bfe_u32 v96, v90, 16, 1
	v_add3_u32 v90, v90, v96, s37
	v_bfe_u32 v96, v91, 16, 1
	v_lshrrev_b32_e32 v90, 16, v90
	v_add3_u32 v91, v91, v96, s37
	v_and_or_b32 v96, v91, s33, v90
	v_bfe_u32 v90, v92, 16, 1
	v_add3_u32 v90, v92, v90, s37
	v_bfe_u32 v92, v86, 16, 1
	v_add3_u32 v86, v86, v92, s37
	v_bfe_u32 v92, v87, 16, 1
	v_lshrrev_b32_e32 v86, 16, v86
	v_add3_u32 v87, v87, v92, s37
	v_and_or_b32 v86, v87, s33, v86
	v_bfe_u32 v87, v88, 16, 1
	v_add3_u32 v87, v88, v87, s37
	v_bfe_u32 v88, v89, 16, 1
	v_lshrrev_b32_e32 v87, 16, v87
	v_add3_u32 v88, v89, v88, s37
	v_and_or_b32 v87, v88, s33, v87
	v_bfe_u32 v88, v82, 16, 1
	v_add3_u32 v82, v82, v88, s37
	v_bfe_u32 v88, v83, 16, 1
	v_lshrrev_b32_e32 v82, 16, v82
	v_add3_u32 v83, v83, v88, s37
	v_and_or_b32 v88, v83, s33, v82
	v_cvt_pk_bf16_f32 v89, v84, v85
	v_bfe_u32 v82, v78, 16, 1
	v_add3_u32 v78, v78, v82, s37
	v_bfe_u32 v82, v79, 16, 1
	v_lshrrev_b32_e32 v78, 16, v78
	v_add3_u32 v79, v79, v82, s37
	v_and_or_b32 v78, v79, s33, v78
	v_bfe_u32 v79, v80, 16, 1
	v_add3_u32 v79, v80, v79, s37
	v_bfe_u32 v80, v81, 16, 1
	v_lshrrev_b32_e32 v79, 16, v79
	v_add3_u32 v80, v81, v80, s37
	v_and_or_b32 v79, v80, s33, v79
	v_bfe_u32 v80, v74, 16, 1
	v_add3_u32 v74, v74, v80, s37
	v_bfe_u32 v80, v75, 16, 1
	v_lshrrev_b32_e32 v74, 16, v74
	v_add3_u32 v75, v75, v80, s37
	v_and_or_b32 v80, v75, s33, v74
	v_bfe_u32 v74, v76, 16, 1
	v_add3_u32 v74, v76, v74, s37
	v_bfe_u32 v76, v70, 16, 1
	v_add3_u32 v70, v70, v76, s37
	v_bfe_u32 v76, v71, 16, 1
	v_lshrrev_b32_e32 v70, 16, v70
	v_add3_u32 v71, v71, v76, s37
	v_and_or_b32 v70, v71, s33, v70
	v_bfe_u32 v71, v72, 16, 1
	v_add3_u32 v71, v72, v71, s37
	v_bfe_u32 v72, v73, 16, 1
	v_lshrrev_b32_e32 v71, 16, v71
	v_add3_u32 v72, v73, v72, s37
	v_and_or_b32 v71, v72, s33, v71
	v_bfe_u32 v72, v66, 16, 1
	v_add3_u32 v66, v66, v72, s37
	v_bfe_u32 v72, v67, 16, 1
	v_lshrrev_b32_e32 v66, 16, v66
	v_add3_u32 v67, v67, v72, s37
	v_and_or_b32 v72, v67, s33, v66
	v_cvt_pk_bf16_f32 v73, v68, v69
	v_bfe_u32 v66, v62, 16, 1
	v_add3_u32 v62, v62, v66, s37
	v_bfe_u32 v66, v63, 16, 1
	v_lshrrev_b32_e32 v62, 16, v62
	v_add3_u32 v63, v63, v66, s37
	v_and_or_b32 v62, v63, s33, v62
	v_bfe_u32 v63, v64, 16, 1
	v_add3_u32 v63, v64, v63, s37
	v_bfe_u32 v64, v65, 16, 1
	v_lshrrev_b32_e32 v63, 16, v63
	v_add3_u32 v64, v65, v64, s37
	v_and_or_b32 v63, v64, s33, v63
	v_bfe_u32 v64, v58, 16, 1
	v_add3_u32 v58, v58, v64, s37
	v_bfe_u32 v64, v59, 16, 1
	v_lshrrev_b32_e32 v58, 16, v58
	v_add3_u32 v59, v59, v64, s37
	v_and_or_b32 v64, v59, s33, v58
	v_bfe_u32 v58, v60, 16, 1
	v_add3_u32 v58, v60, v58, s37
	v_bfe_u32 v60, v54, 16, 1
	v_add3_u32 v54, v54, v60, s37
	v_bfe_u32 v60, v55, 16, 1
	v_lshrrev_b32_e32 v54, 16, v54
	v_add3_u32 v55, v55, v60, s37
; __device__ __forceinline__ unsigned pk2(float lo, float hi) { return f2bf(lo) | (f2bf(hi) << 16); }
; #define PG8_BAR __builtin_amdgcn_s_barrier()
; template <class P>
; __device__ __forceinline__ void gemm_phase(LAS unsigned char* lds, const P& p) {
;     ...
;         cur = nxt; cA = nA; cB = nB; ++ui;
;         if (wr == 1) PG8_BAR;
;     __device__ __forceinline__ void epi(const f32x4 (&acc)[2][2][4][2], const Unit& u, int wr, int wc, int fr, int fq) const {
;         unsigned loff = (unsigned)((wr * 64 + fr) * 1536 + wc * 32 + 8 * fq) * 2u; asm volatile("" : "+v"(loff));
;         char* base = (char*)(O + (size_t)u.pm * 256 * 1536 + (size_t)u.pn * 256);
; #pragma unroll
;         for (int ai = 0; ai < 2; ++ai)
; #pragma unroll
;             for (int m = 0; m < 4; ++m)
; #pragma unroll
;                 for (int bj = 0; bj < 2; ++bj) { const f32x4 v0 = acc[ai][bj][m][0], v1 = acc[ai][bj][m][1];
;                     u32x4 w; w.x = pk2(v0[0], v0[1]); w.y = pk2(v0[2], v0[3]); w.z = pk2(v1[0], v1[1]); w.w = pk2(v1[2], v1[3]);
;                     *(u32x4*)(base + ((size_t)(ai * 128 + m * 16) * 1536 + bj * 128) * 2 + loff) = w; }
;     }
	v_and_or_b32 v54, v55, s33, v54
	v_bfe_u32 v55, v56, 16, 1
	v_add3_u32 v55, v56, v55, s37
	v_bfe_u32 v56, v57, 16, 1
	v_lshrrev_b32_e32 v55, 16, v55
	v_add3_u32 v56, v57, v56, s37
	v_and_or_b32 v55, v56, s33, v55
	v_bfe_u32 v56, v50, 16, 1
	v_add3_u32 v50, v50, v56, s37
	v_bfe_u32 v56, v51, 16, 1
	v_lshrrev_b32_e32 v50, 16, v50
	v_add3_u32 v51, v51, v56, s37
	v_and_or_b32 v56, v51, s33, v50
	v_cvt_pk_bf16_f32 v57, v52, v53
	v_bfe_u32 v50, v46, 16, 1
	v_add3_u32 v46, v46, v50, s37
	v_bfe_u32 v50, v47, 16, 1
	v_lshrrev_b32_e32 v46, 16, v46
	v_add3_u32 v47, v47, v50, s37
	v_and_or_b32 v46, v47, s33, v46
	v_bfe_u32 v47, v48, 16, 1
	v_add3_u32 v47, v48, v47, s37
	v_bfe_u32 v48, v49, 16, 1
	v_lshrrev_b32_e32 v47, 16, v47
	v_add3_u32 v48, v49, v48, s37
	v_and_or_b32 v47, v48, s33, v47
	v_bfe_u32 v48, v42, 16, 1
	v_add3_u32 v42, v42, v48, s37
	v_bfe_u32 v48, v43, 16, 1
	v_lshrrev_b32_e32 v42, 16, v42
	v_add3_u32 v43, v43, v48, s37
	v_and_or_b32 v48, v43, s33, v42
	v_bfe_u32 v42, v44, 16, 1
	v_add3_u32 v42, v44, v42, s37
	v_bfe_u32 v44, v38, 16, 1
	v_add3_u32 v38, v38, v44, s37
	v_bfe_u32 v44, v39, 16, 1
	v_lshrrev_b32_e32 v38, 16, v38
	v_add3_u32 v39, v39, v44, s37
	v_and_or_b32 v38, v39, s33, v38
	v_bfe_u32 v39, v40, 16, 1
	v_add3_u32 v39, v40, v39, s37
	v_bfe_u32 v40, v41, 16, 1
	v_lshrrev_b32_e32 v39, 16, v39
	v_add3_u32 v40, v41, v40, s37
	v_and_or_b32 v39, v40, s33, v39
	v_bfe_u32 v40, v34, 16, 1
	v_add3_u32 v34, v34, v40, s37
	v_bfe_u32 v40, v35, 16, 1
	v_lshrrev_b32_e32 v34, 16, v34
	v_add3_u32 v35, v35, v40, s37
	v_and_or_b32 v40, v35, s33, v34
	v_cvt_pk_bf16_f32 v41, v36, v37
	v_bfe_u32 v34, v30, 16, 1
	v_add3_u32 v30, v30, v34, s37
	v_bfe_u32 v34, v31, 16, 1
	v_lshrrev_b32_e32 v30, 16, v30
	v_add3_u32 v31, v31, v34, s37
	v_and_or_b32 v30, v31, s33, v30
	v_bfe_u32 v31, v32, 16, 1
	v_add3_u32 v31, v32, v31, s37
	v_bfe_u32 v32, v33, 16, 1
	v_lshrrev_b32_e32 v31, 16, v31
	v_add3_u32 v32, v33, v32, s37
	v_and_or_b32 v31, v32, s33, v31
	v_bfe_u32 v32, v26, 16, 1
	v_add3_u32 v26, v26, v32, s37
	v_bfe_u32 v32, v27, 16, 1
	v_lshrrev_b32_e32 v26, 16, v26
	v_add3_u32 v27, v27, v32, s37
	v_and_or_b32 v32, v27, s33, v26
	v_bfe_u32 v26, v28, 16, 1
	v_add3_u32 v26, v28, v26, s37
	v_bfe_u32 v28, v22, 16, 1
	v_add3_u32 v22, v22, v28, s37
	v_bfe_u32 v28, v23, 16, 1
	v_lshrrev_b32_e32 v22, 16, v22
	v_add3_u32 v23, v23, v28, s37
	v_and_or_b32 v22, v23, s33, v22
	v_bfe_u32 v23, v24, 16, 1
	v_add3_u32 v23, v24, v23, s37
	v_bfe_u32 v24, v25, 16, 1
	v_lshrrev_b32_e32 v23, 16, v23
	v_add3_u32 v24, v25, v24, s37
	v_and_or_b32 v23, v24, s33, v23
	v_bfe_u32 v24, v18, 16, 1
	v_add3_u32 v18, v18, v24, s37
	v_bfe_u32 v24, v19, 16, 1
	v_lshrrev_b32_e32 v18, 16, v18
	v_add3_u32 v19, v19, v24, s37
	v_and_or_b32 v24, v19, s33, v18
	v_cvt_pk_bf16_f32 v25, v20, v21
	v_bfe_u32 v18, v14, 16, 1
	s_mul_i32 s11, s20, 0xc0000
	v_add3_u32 v14, v14, v18, s37
	v_bfe_u32 v18, v15, 16, 1
	s_mul_hi_i32 s9, s20, 0xc0000
	s_add_u32 s11, s57, s11
	v_lshrrev_b32_e32 v14, 16, v14
	v_add3_u32 v15, v15, v18, s37
	s_addc_u32 s9, s58, s9
	s_ashr_i32 s23, s22, 31
	v_and_or_b32 v14, v15, s33, v14
	v_bfe_u32 v15, v16, 16, 1
	s_lshl_b64 s[20:21], s[22:23], 9
	v_add3_u32 v15, v16, v15, s37
	v_bfe_u32 v16, v17, 16, 1
	s_add_u32 s20, s11, s20
	v_lshrrev_b32_e32 v15, 16, v15
	v_add3_u32 v16, v17, v16, s37
	v_mov_b32_e32 v146, v145
	s_addc_u32 s21, s9, s21
	v_bfe_u32 v107, v109, 16, 1
	v_and_or_b32 v15, v16, s33, v15
	v_bfe_u32 v16, v10, 16, 1
	v_lshrrev_b32_e32 v106, 16, v106
	v_lshl_add_u64 v[142:143], s[20:21], 0, v[146:147]
	v_add3_u32 v107, v109, v107, s37
	v_add3_u32 v10, v10, v16, s37
	v_bfe_u32 v16, v11, 16, 1
	v_and_or_b32 v113, v107, s33, v106
	v_add_co_u32_e32 v106, vcc, s86, v142
	v_bfe_u32 v91, v93, 16, 1
	v_lshrrev_b32_e32 v10, 16, v10
	v_add3_u32 v11, v11, v16, s37
	v_addc_co_u32_e32 v107, vcc, 0, v143, vcc
	v_lshrrev_b32_e32 v90, 16, v90
	v_add3_u32 v91, v93, v91, s37
	v_and_or_b32 v16, v11, s33, v10
	v_bfe_u32 v10, v12, 16, 1
	v_and_or_b32 v97, v91, s33, v90
	v_add_co_u32_e32 v90, vcc, s82, v142
	v_bfe_u32 v75, v77, 16, 1
	v_add3_u32 v10, v12, v10, s37
	v_bfe_u32 v12, v6, 16, 1
	v_addc_co_u32_e32 v91, vcc, 0, v143, vcc
	v_lshrrev_b32_e32 v74, 16, v74
	v_add3_u32 v75, v77, v75, s37
	s_mov_b32 s9, 0x24000
	v_add3_u32 v6, v6, v12, s37
	v_bfe_u32 v12, v7, 16, 1
	v_and_or_b32 v81, v75, s33, v74
	v_add_co_u32_e32 v74, vcc, s9, v142
	v_bfe_u32 v59, v61, 16, 1
	v_lshrrev_b32_e32 v6, 16, v6
	v_add3_u32 v7, v7, v12, s37
	v_addc_co_u32_e32 v75, vcc, 0, v143, vcc
	v_lshrrev_b32_e32 v58, 16, v58
	v_add3_u32 v59, v61, v59, s37
	s_mov_b32 s9, 0x60000
	v_and_or_b32 v6, v7, s33, v6
	v_bfe_u32 v7, v8, 16, 1
	v_and_or_b32 v65, v59, s33, v58
	v_add_co_u32_e32 v58, vcc, s9, v142
	v_bfe_u32 v43, v45, 16, 1
	v_add3_u32 v7, v8, v7, s37
	v_bfe_u32 v8, v9, 16, 1
	v_addc_co_u32_e32 v59, vcc, 0, v143, vcc
	v_lshrrev_b32_e32 v42, 16, v42
	v_add3_u32 v43, v45, v43, s37
	s_mov_b32 s9, 0x6c000
	v_lshrrev_b32_e32 v7, 16, v7
	v_add3_u32 v8, v9, v8, s37
	v_and_or_b32 v49, v43, s33, v42
	v_add_co_u32_e32 v42, vcc, s9, v142
	v_bfe_u32 v27, v29, 16, 1
	v_and_or_b32 v7, v8, s33, v7
	v_bfe_u32 v8, v2, 16, 1
	v_addc_co_u32_e32 v43, vcc, 0, v143, vcc
	v_lshrrev_b32_e32 v26, 16, v26
	v_add3_u32 v27, v29, v27, s37
	s_mov_b32 s9, 0x78000
	v_add3_u32 v2, v2, v8, s37
	v_bfe_u32 v8, v3, 16, 1
	v_and_or_b32 v33, v27, s33, v26
	v_add_co_u32_e32 v26, vcc, s9, v142
	v_bfe_u32 v11, v13, 16, 1
	v_lshrrev_b32_e32 v2, 16, v2
	v_add3_u32 v3, v3, v8, s37
	v_addc_co_u32_e32 v27, vcc, 0, v143, vcc
	v_lshrrev_b32_e32 v10, 16, v10
	v_add3_u32 v11, v13, v11, s37
	s_mov_b32 s9, 0x84000
	v_and_or_b32 v8, v3, s33, v2
	v_and_or_b32 v17, v11, s33, v10
	v_add_co_u32_e32 v10, vcc, s9, v142
	v_addc_co_u32_e32 v11, vcc, 0, v143, vcc
	global_store_dwordx4 v146, v[126:129], s[20:21] sc1
	global_store_dwordx4 v146, v[118:121], s[20:21] offset:256 sc1
	v_cvt_pk_bf16_f32 v9, v4, v5
	s_andn2_b64 vcc, exec, s[40:41]
	s_mov_b64 s[20:21], -1
	global_store_dwordx4 v[106:107], v[110:113], off sc1
	global_store_dwordx4 v[106:107], v[102:105], off offset:256 sc1
	global_store_dwordx4 v[90:91], v[94:97], off sc1
	global_store_dwordx4 v[90:91], v[86:89], off offset:256 sc1
	global_store_dwordx4 v[74:75], v[78:81], off sc1
	global_store_dwordx4 v[74:75], v[70:73], off offset:256 sc1
	global_store_dwordx4 v[58:59], v[62:65], off sc1
	global_store_dwordx4 v[58:59], v[54:57], off offset:256 sc1
	global_store_dwordx4 v[42:43], v[46:49], off sc1
	global_store_dwordx4 v[42:43], v[38:41], off offset:256 sc1
	global_store_dwordx4 v[26:27], v[30:33], off sc1
	global_store_dwordx4 v[26:27], v[22:25], off offset:256 sc1
	global_store_dwordx4 v[10:11], v[14:17], off sc1
	global_store_dwordx4 v[10:11], v[6:9], off offset:256 sc1
	s_cbranch_vccnz .LBB0_476
	s_andn2_b64 vcc, exec, s[2:3]
	s_cbranch_vccnz .LBB0_475
	s_barrier
	s_branch .LBB0_475

; #define LAS __attribute__((address_space(3)))
; __device__ __forceinline__ unsigned pk2(float lo, float hi) { return f2bf(lo) | (f2bf(hi) << 16); }
;     __device__ __forceinline__ void epi(const f32x4 (&acc)[2][2][4][2], const Unit& u, int wr, int wc, int fr, int fq) const {
;     ...
;         asm volatile("s_waitcnt lgkmcnt(0)" ::: "memory"); __builtin_amdgcn_s_barrier(); asm volatile("" ::: "memory");
;         const f32x4 g0 = *(const f32x4*)((const char*)kn + lcol * 4), g1 = *(const f32x4*)((const char*)kn + lcol * 4 + 16);
;         const unsigned koff = (lrow * (unsigned)DQK + lcol) * 2u, voff = (lrow * (unsigned)DVH + lcol) * 2u;
;         char* kb = (char*)(Ko + hrow0 * DQK); char* vb = (char*)(Vo + hrow0 * DVH);
; #pragma unroll
;         for (int ai = 0; ai < 2; ++ai)
; #pragma unroll
;             for (int m = 0; m < 4; ++m) { const f32x4 pt = *(const LAS f32x4*)(part + (ai * 128 + m * 16 + lrow) * 4);
;                 const float tot = ((pt.x + pt.y) + (pt.z + pt.w)) + kr2[ai][m]; const float rk = rsqrtf(tot * (1.f / DQK) + EPS); const float f = sc[ai][m] * rk;
;                 const f32x4 k0 = acc[ai][0][m][0] * f * g0, k1 = acc[ai][0][m][1] * f * g1, v0 = acc[ai][1][m][0] * sc[ai][m], v1 = acc[ai][1][m][1] * sc[ai][m];
;                 u32x4 w; w.x = pk2(k0[0], k0[1]); w.y = pk2(k0[2], k0[3]); w.z = pk2(k1[0], k1[1]); w.w = pk2(k1[2], k1[3]);
;                 *(u32x4*)(kb + (size_t)(ai * 128 + m * 16) * DQK * 2 + koff) = w;
;                 w.x = pk2(v0[0], v0[1]); w.y = pk2(v0[2], v0[3]); w.z = pk2(v1[0], v1[1]); w.w = pk2(v1[2], v1[3]);
;                 *(u32x4*)(vb + (size_t)(ai * 128 + m * 16) * DVH * 2 + voff) = w;
;                 if (wc == 0 && fq == 0) RSTDK[(size_t)(rowt + ai * 128 + m * 16 + lrow) * 8 + h] = rk; }
.LBB0_520:
	s_or_b64 exec, exec, s[48:49]
	s_waitcnt lgkmcnt(0)
	s_barrier
	v_lshlrev_b32_e32 v130, 2, v155
	global_load_dwordx4 v[134:137], v130, s[8:9]
	s_waitcnt lgkmcnt(0)
	global_load_dwordx4 v[130:133], v130, s[8:9] offset:16
	s_movk_i32 s27, 0xc0
	v_lshlrev_b32_e32 v163, 1, v155
	v_add_u32_e32 v167, 0, v146
	v_mov_b32_e32 v183, v182
	v_mul_lo_u32 v159, v153, s27
	v_add_u32_e32 v186, s46, v153
	v_add_f32_e32 v173, v184, v185
	v_mov_b32_e32 v194, v182
	v_mov_b32_e32 v195, v182
	v_lshl_add_u32 v184, v153, 8, v163
	v_add_u32_e32 v153, 0x20000, v167
	v_pk_mul_f32 v[128:129], v[128:129], v[194:195]
	v_pk_mul_f32 v[194:195], v[124:125], v[194:195]
	v_pk_mul_f32 v[196:197], v[122:123], v[182:183]
	ds_read_b128 v[122:125], v153
	s_add_i32 s19, s46, 0xffffc000
	s_and_b32 s21, s46, 0xf00
	s_ashr_i32 s5, s26, 4
	s_lshr_b32 s19, s19, 8
	s_waitcnt lgkmcnt(0)
	v_mov_b32_e32 v198, v123
	v_mov_b32_e32 v199, v124
	v_mov_b32_e32 v123, v125
	v_pk_add_f32 v[122:123], v[198:199], v[122:123]
	s_addk_i32 s21, 0x100
	v_add_f32_e32 v122, v122, v123
	v_add_f32_e32 v122, v173, v122
	v_fmamk_f32 v122, v122, 0x3baaaaab, v180
	v_mul_f32_e32 v123, 0x4b800000, v122
	v_cmp_gt_f32_e32 vcc, s79, v122
	s_cmp_lt_i32 s26, 64
	s_cselect_b32 s5, s5, s19
	v_cndmask_b32_e32 v122, v122, v123, vcc
	v_rsq_f32_e32 v122, v122
	s_cselect_b32 s19, s21, 0
	s_lshl_b32 s5, s5, 3
	s_add_i32 s5, s5, s4
	v_mul_f32_e32 v123, 0x45800000, v122
	v_cndmask_b32_e32 v122, v122, v123, vcc
	v_mul_f32_e32 v124, v182, v122
	v_pk_mul_f32 v[118:119], v[118:119], v[124:125] op_sel_hi:[1,0]
	v_pk_mul_f32 v[120:121], v[120:121], v[124:125] op_sel_hi:[1,0]
	v_pk_mul_f32 v[114:115], v[114:115], v[124:125] op_sel_hi:[1,0]
	v_pk_mul_f32 v[116:117], v[116:117], v[124:125] op_sel_hi:[1,0]
	s_mul_hi_i32 s21, s5, 0x1100
	s_mulk_i32 s5, 0x1100
	v_add_lshl_u32 v188, v159, v155, 1
	s_add_u32 s46, s5, s19
	s_addc_u32 s47, s21, 0
	s_mul_hi_u32 s5, s46, 0x180
	s_mul_i32 s21, s47, 0x180
	s_mul_i32 s19, s46, 0x180
	s_add_i32 s5, s5, s21
	s_add_u32 s26, s63, s19
	v_pk_mul_f32 v[126:127], v[126:127], v[182:183]
	s_addc_u32 s27, s64, s5
	s_lshl_b64 s[46:47], s[46:47], 8
	s_add_u32 s46, s65, s46
	s_addc_u32 s47, s66, s47
	s_ashr_i32 s5, s4, 31
	s_waitcnt vmcnt(1)
	v_pk_mul_f32 v[118:119], v[134:135], v[118:119]
	v_pk_mul_f32 v[120:121], v[136:137], v[120:121]
	s_waitcnt vmcnt(0)
	v_pk_mul_f32 v[124:125], v[132:133], v[116:117]
	v_pk_mul_f32 v[114:115], v[130:131], v[114:115]
	v_bfe_u32 v116, v118, 16, 1
	v_bfe_u32 v117, v119, 16, 1
	v_bfe_u32 v123, v120, 16, 1
	v_bfe_u32 v155, v114, 16, 1
	v_bfe_u32 v159, v115, 16, 1
	v_add3_u32 v116, v118, v116, s37
	v_bfe_u32 v153, v121, 16, 1
	v_add3_u32 v117, v119, v117, s37
	v_add3_u32 v118, v120, v123, s37
	v_add3_u32 v114, v114, v155, s37
	v_add3_u32 v120, v115, v159, s37
	v_lshrrev_b32_e32 v115, 16, v116
	v_add3_u32 v119, v121, v153, s37
	v_lshrrev_b32_e32 v116, 16, v118
	v_lshrrev_b32_e32 v118, 16, v114
	v_and_or_b32 v114, v117, s33, v115
	v_and_or_b32 v115, v119, s33, v116
	v_and_or_b32 v116, v120, s33, v118
	v_cvt_pk_bf16_f32 v117, v124, v125
	global_store_dwordx4 v188, v[114:117], s[26:27] sc1
	s_nop 1
	v_cvt_pk_bf16_f32 v114, v126, v127
	v_cvt_pk_bf16_f32 v115, v128, v129
	v_cvt_pk_bf16_f32 v116, v196, v197
	v_cvt_pk_bf16_f32 v117, v194, v195
	global_store_dwordx4 v184, v[114:117], s[46:47] sc1
	s_and_saveexec_b64 s[48:49], s[42:43]
	s_cbranch_execz .LBB0_522
	v_mov_b32_e32 v187, v147
	v_lshlrev_b64 v[114:115], 5, v[186:187]
	v_lshl_add_u64 v[114:115], s[6:7], 0, v[114:115]
	v_lshl_add_u64 v[114:115], s[4:5], 2, v[114:115]
	global_store_dword v[114:115], v122, off
.LBB0_522:
	s_or_b64 exec, exec, s[48:49]
	s_add_i32 s19, 0, 0x20000
	v_add_u32_e32 v118, s19, v146
	ds_read_b128 v[120:123], v118 offset:256
	v_mov_b32_e32 v177, v176
	v_mov_b32_e32 v189, v147
	v_lshl_add_u64 v[116:117], s[26:27], 0, v[188:189]
	v_pk_mul_f32 v[102:103], v[102:103], v[176:177]
	s_waitcnt lgkmcnt(0)
	v_mov_b32_e32 v124, v121
	v_mov_b32_e32 v125, v122
	v_mov_b32_e32 v121, v123
	v_pk_add_f32 v[120:121], v[124:125], v[120:121]
	v_pk_mul_f32 v[122:123], v[98:99], v[176:177]
	v_add_f32_e32 v119, v120, v121
	v_add_f32_e32 v120, v178, v179
	v_add_f32_e32 v119, v120, v119
	v_fmamk_f32 v119, v119, 0x3baaaaab, v180
	v_cmp_gt_f32_e32 vcc, s79, v119
	v_mul_f32_e32 v120, 0x4b800000, v119
	v_mov_b32_e32 v185, v147
	v_cndmask_b32_e32 v119, v119, v120, vcc
	v_rsq_f32_e32 v119, v119
	v_lshl_add_u64 v[114:115], s[46:47], 0, v[184:185]
	v_mul_f32_e32 v120, 0x45800000, v119
	v_cndmask_b32_e32 v119, v119, v120, vcc
	v_mul_f32_e32 v120, v176, v119
	v_pk_mul_f32 v[110:111], v[110:111], v[120:121] op_sel_hi:[1,0]
	v_pk_mul_f32 v[112:113], v[112:113], v[120:121] op_sel_hi:[1,0]
	v_pk_mul_f32 v[110:111], v[134:135], v[110:111]
	v_pk_mul_f32 v[112:113], v[136:137], v[112:113]
	v_pk_mul_f32 v[106:107], v[106:107], v[120:121] op_sel_hi:[1,0]
	v_pk_mul_f32 v[108:109], v[108:109], v[120:121] op_sel_hi:[1,0]
	v_mov_b32_e32 v120, v176
	v_mov_b32_e32 v121, v176
	v_cvt_pk_bf16_f32 v98, v110, v111
	v_pk_mul_f32 v[104:105], v[104:105], v[120:121]
	v_pk_mul_f32 v[120:121], v[100:101], v[120:121]
	v_pk_mul_f32 v[106:107], v[130:131], v[106:107]
	v_cvt_pk_bf16_f32 v99, v112, v113
	v_pk_mul_f32 v[108:109], v[132:133], v[108:109]
	v_cvt_pk_bf16_f32 v100, v106, v107
	v_cvt_pk_bf16_f32 v101, v108, v109
	v_add_co_u32_e32 v106, vcc, s87, v116
	s_nop 1
	v_addc_co_u32_e32 v107, vcc, 0, v117, vcc
	global_store_dwordx4 v[106:107], v[98:101], off offset:2048 sc1
	s_nop 1
	v_cvt_pk_bf16_f32 v98, v102, v103
	v_cvt_pk_bf16_f32 v99, v104, v105
	v_cvt_pk_bf16_f32 v100, v122, v123
	v_cvt_pk_bf16_f32 v101, v120, v121
	v_add_co_u32_e32 v102, vcc, 0x1000, v114
	s_nop 1
	v_addc_co_u32_e32 v103, vcc, 0, v115, vcc
	global_store_dwordx4 v[102:103], v[98:101], off sc1
	s_and_saveexec_b64 s[26:27], s[42:43]
	s_cbranch_execz .LBB0_524
	v_add_u32_e32 v146, 16, v186
	v_lshlrev_b64 v[98:99], 5, v[146:147]
	v_lshl_add_u64 v[98:99], s[6:7], 0, v[98:99]
	v_lshl_add_u64 v[98:99], s[4:5], 2, v[98:99]
	global_store_dword v[98:99], v119, off
; #define LAS __attribute__((address_space(3)))
; __device__ __forceinline__ unsigned pk2(float lo, float hi) { return f2bf(lo) | (f2bf(hi) << 16); }
;     __device__ __forceinline__ void epi(const f32x4 (&acc)[2][2][4][2], const Unit& u, int wr, int wc, int fr, int fq) const {
;     ...
;         asm volatile("s_waitcnt lgkmcnt(0)" ::: "memory"); __builtin_amdgcn_s_barrier(); asm volatile("" ::: "memory");
;         const f32x4 g0 = *(const f32x4*)((const char*)kn + lcol * 4), g1 = *(const f32x4*)((const char*)kn + lcol * 4 + 16);
;         const unsigned koff = (lrow * (unsigned)DQK + lcol) * 2u, voff = (lrow * (unsigned)DVH + lcol) * 2u;
;         char* kb = (char*)(Ko + hrow0 * DQK); char* vb = (char*)(Vo + hrow0 * DVH);
; #pragma unroll
;         for (int ai = 0; ai < 2; ++ai)
; #pragma unroll
;             for (int m = 0; m < 4; ++m) { const f32x4 pt = *(const LAS f32x4*)(part + (ai * 128 + m * 16 + lrow) * 4);
;                 const float tot = ((pt.x + pt.y) + (pt.z + pt.w)) + kr2[ai][m]; const float rk = rsqrtf(tot * (1.f / DQK) + EPS); const float f = sc[ai][m] * rk;
;                 const f32x4 k0 = acc[ai][0][m][0] * f * g0, k1 = acc[ai][0][m][1] * f * g1, v0 = acc[ai][1][m][0] * sc[ai][m], v1 = acc[ai][1][m][1] * sc[ai][m];
;                 u32x4 w; w.x = pk2(k0[0], k0[1]); w.y = pk2(k0[2], k0[3]); w.z = pk2(k1[0], k1[1]); w.w = pk2(k1[2], k1[3]);
;                 *(u32x4*)(kb + (size_t)(ai * 128 + m * 16) * DQK * 2 + koff) = w;
;                 w.x = pk2(v0[0], v0[1]); w.y = pk2(v0[2], v0[3]); w.z = pk2(v1[0], v1[1]); w.w = pk2(v1[2], v1[3]);
;                 *(u32x4*)(vb + (size_t)(ai * 128 + m * 16) * DVH * 2 + voff) = w;
;                 if (wc == 0 && fq == 0) RSTDK[(size_t)(rowt + ai * 128 + m * 16 + lrow) * 8 + h] = rk; }
.LBB0_524:
	s_or_b64 exec, exec, s[26:27]
	ds_read_b128 v[98:101], v118 offset:512
	v_add_f32_e32 v104, v174, v175
	v_mov_b32_e32 v173, v172
	s_movk_i32 s19, 0x3000
	v_pk_mul_f32 v[86:87], v[86:87], v[172:173]
	s_waitcnt lgkmcnt(0)
	v_mov_b32_e32 v102, v99
	v_mov_b32_e32 v103, v100
	v_mov_b32_e32 v99, v101
	v_pk_add_f32 v[98:99], v[102:103], v[98:99]
	v_pk_mul_f32 v[102:103], v[82:83], v[172:173]
	v_add_f32_e32 v98, v98, v99
	v_add_f32_e32 v98, v104, v98
	v_fmamk_f32 v98, v98, 0x3baaaaab, v180
	v_mul_f32_e32 v99, 0x4b800000, v98
	v_cmp_gt_f32_e32 vcc, s79, v98
	s_nop 1
	v_cndmask_b32_e32 v98, v98, v99, vcc
	v_rsq_f32_e32 v98, v98
	s_nop 0
	v_mul_f32_e32 v99, 0x45800000, v98
	v_cndmask_b32_e32 v98, v98, v99, vcc
	v_mul_f32_e32 v100, v172, v98
	v_pk_mul_f32 v[94:95], v[94:95], v[100:101] op_sel_hi:[1,0]
	v_pk_mul_f32 v[96:97], v[96:97], v[100:101] op_sel_hi:[1,0]
	v_pk_mul_f32 v[94:95], v[134:135], v[94:95]
	v_pk_mul_f32 v[96:97], v[136:137], v[96:97]
	v_pk_mul_f32 v[90:91], v[90:91], v[100:101] op_sel_hi:[1,0]
	v_pk_mul_f32 v[92:93], v[92:93], v[100:101] op_sel_hi:[1,0]
	v_mov_b32_e32 v100, v172
	v_mov_b32_e32 v101, v172
	v_cvt_pk_bf16_f32 v82, v94, v95
	v_pk_mul_f32 v[88:89], v[88:89], v[100:101]
	v_pk_mul_f32 v[100:101], v[84:85], v[100:101]
	v_pk_mul_f32 v[90:91], v[130:131], v[90:91]
	v_cvt_pk_bf16_f32 v83, v96, v97
	v_pk_mul_f32 v[92:93], v[132:133], v[92:93]
	v_cvt_pk_bf16_f32 v84, v90, v91
	v_cvt_pk_bf16_f32 v85, v92, v93
	v_add_co_u32_e32 v90, vcc, s19, v116
	s_nop 1
	v_addc_co_u32_e32 v91, vcc, 0, v117, vcc
	global_store_dwordx4 v[90:91], v[82:85], off sc1
	s_nop 1
	v_cvt_pk_bf16_f32 v82, v86, v87
	v_cvt_pk_bf16_f32 v83, v88, v89
	v_cvt_pk_bf16_f32 v84, v102, v103
	v_cvt_pk_bf16_f32 v85, v100, v101
	v_add_co_u32_e32 v86, vcc, 0x2000, v114
	s_nop 1
	v_addc_co_u32_e32 v87, vcc, 0, v115, vcc
	global_store_dwordx4 v[86:87], v[82:85], off sc1
	s_and_saveexec_b64 s[26:27], s[42:43]
	s_cbranch_execz .LBB0_526
	v_add_u32_e32 v146, 32, v186
	v_lshlrev_b64 v[82:83], 5, v[146:147]
	v_lshl_add_u64 v[82:83], s[6:7], 0, v[82:83]
	v_lshl_add_u64 v[82:83], s[4:5], 2, v[82:83]
	global_store_dword v[82:83], v98, off
.LBB0_526:
	s_or_b64 exec, exec, s[26:27]
	ds_read_b128 v[82:85], v118 offset:768
	v_add_f32_e32 v88, v170, v171
	v_mov_b32_e32 v167, v166
	s_movk_i32 s19, 0x4000
	v_pk_mul_f32 v[70:71], v[70:71], v[166:167]
	s_waitcnt lgkmcnt(0)
	v_mov_b32_e32 v86, v83
	v_mov_b32_e32 v87, v84
	v_mov_b32_e32 v83, v85
	v_pk_add_f32 v[82:83], v[86:87], v[82:83]
	v_pk_mul_f32 v[86:87], v[66:67], v[166:167]
	v_add_f32_e32 v82, v82, v83
	v_add_f32_e32 v82, v88, v82
	v_fmamk_f32 v82, v82, 0x3baaaaab, v180
	v_mul_f32_e32 v83, 0x4b800000, v82
	v_cmp_gt_f32_e32 vcc, s79, v82
	s_nop 1
	v_cndmask_b32_e32 v82, v82, v83, vcc
	v_rsq_f32_e32 v82, v82
	s_nop 0
	v_mul_f32_e32 v83, 0x45800000, v82
	v_cndmask_b32_e32 v82, v82, v83, vcc
	v_mul_f32_e32 v84, v166, v82
	v_pk_mul_f32 v[78:79], v[78:79], v[84:85] op_sel_hi:[1,0]
	v_pk_mul_f32 v[80:81], v[80:81], v[84:85] op_sel_hi:[1,0]
	v_pk_mul_f32 v[78:79], v[134:135], v[78:79]
	v_pk_mul_f32 v[80:81], v[136:137], v[80:81]
	v_pk_mul_f32 v[74:75], v[74:75], v[84:85] op_sel_hi:[1,0]
	v_pk_mul_f32 v[76:77], v[76:77], v[84:85] op_sel_hi:[1,0]
	v_mov_b32_e32 v84, v166
	v_mov_b32_e32 v85, v166
	v_cvt_pk_bf16_f32 v66, v78, v79
	v_pk_mul_f32 v[72:73], v[72:73], v[84:85]
	v_pk_mul_f32 v[84:85], v[68:69], v[84:85]
	v_pk_mul_f32 v[74:75], v[130:131], v[74:75]
	v_cvt_pk_bf16_f32 v67, v80, v81
	v_pk_mul_f32 v[76:77], v[132:133], v[76:77]
	v_cvt_pk_bf16_f32 v68, v74, v75
	v_cvt_pk_bf16_f32 v69, v76, v77
	v_add_co_u32_e32 v74, vcc, s19, v116
	s_nop 1
	v_addc_co_u32_e32 v75, vcc, 0, v117, vcc
	global_store_dwordx4 v[74:75], v[66:69], off offset:2048 sc1
	s_nop 1
	v_cvt_pk_bf16_f32 v66, v70, v71
	v_cvt_pk_bf16_f32 v67, v72, v73
	v_cvt_pk_bf16_f32 v68, v86, v87
	v_cvt_pk_bf16_f32 v69, v84, v85
	v_add_co_u32_e32 v70, vcc, 0x3000, v114
	s_nop 1
	v_addc_co_u32_e32 v71, vcc, 0, v115, vcc
	global_store_dwordx4 v[70:71], v[66:69], off sc1
	s_and_saveexec_b64 s[26:27], s[42:43]
	s_cbranch_execz .LBB0_528
	v_add_u32_e32 v146, 48, v186
	v_lshlrev_b64 v[66:67], 5, v[146:147]
	v_lshl_add_u64 v[66:67], s[6:7], 0, v[66:67]
	v_lshl_add_u64 v[66:67], s[4:5], 2, v[66:67]
	global_store_dword v[66:67], v82, off
.LBB0_528:
	s_or_b64 exec, exec, s[26:27]
	ds_read_b128 v[66:69], v118 offset:2048
	v_add_f32_e32 v72, v168, v169
	v_mov_b32_e32 v163, v162
	v_pk_mul_f32 v[54:55], v[54:55], v[162:163]
	v_add_u32_e32 v146, 0x80, v186
	s_waitcnt lgkmcnt(0)
	v_mov_b32_e32 v70, v67
	v_mov_b32_e32 v71, v68
	v_mov_b32_e32 v67, v69
	v_pk_add_f32 v[66:67], v[70:71], v[66:67]
	v_pk_mul_f32 v[70:71], v[50:51], v[162:163]
	v_add_f32_e32 v66, v66, v67
	v_add_f32_e32 v66, v72, v66
	v_fmamk_f32 v66, v66, 0x3baaaaab, v180
	v_mul_f32_e32 v67, 0x4b800000, v66
	v_cmp_gt_f32_e32 vcc, s79, v66
	s_nop 1
	v_cndmask_b32_e32 v66, v66, v67, vcc
	v_rsq_f32_e32 v66, v66
	s_nop 0
	v_mul_f32_e32 v67, 0x45800000, v66
	v_cndmask_b32_e32 v66, v66, v67, vcc
	v_mul_f32_e32 v68, v162, v66
	v_pk_mul_f32 v[62:63], v[62:63], v[68:69] op_sel_hi:[1,0]
	v_pk_mul_f32 v[64:65], v[64:65], v[68:69] op_sel_hi:[1,0]
	v_pk_mul_f32 v[62:63], v[134:135], v[62:63]
	v_pk_mul_f32 v[64:65], v[136:137], v[64:65]
	v_pk_mul_f32 v[58:59], v[58:59], v[68:69] op_sel_hi:[1,0]
	v_pk_mul_f32 v[60:61], v[60:61], v[68:69] op_sel_hi:[1,0]
	v_mov_b32_e32 v68, v162
	v_mov_b32_e32 v69, v162
	v_cvt_pk_bf16_f32 v50, v62, v63
	v_pk_mul_f32 v[56:57], v[56:57], v[68:69]
	v_pk_mul_f32 v[68:69], v[52:53], v[68:69]
	v_pk_mul_f32 v[58:59], v[130:131], v[58:59]
	v_cvt_pk_bf16_f32 v51, v64, v65
	v_pk_mul_f32 v[60:61], v[132:133], v[60:61]
	v_cvt_pk_bf16_f32 v52, v58, v59
	v_cvt_pk_bf16_f32 v53, v60, v61
	v_add_co_u32_e32 v58, vcc, s86, v116
	s_nop 1
	v_addc_co_u32_e32 v59, vcc, 0, v117, vcc
	global_store_dwordx4 v[58:59], v[50:53], off sc1
	s_nop 1
	v_cvt_pk_bf16_f32 v50, v54, v55
	v_cvt_pk_bf16_f32 v51, v56, v57
	v_cvt_pk_bf16_f32 v52, v70, v71
	v_cvt_pk_bf16_f32 v53, v68, v69
	v_add_co_u32_e32 v54, vcc, 0x8000, v114
	s_nop 1
	v_addc_co_u32_e32 v55, vcc, 0, v115, vcc
	global_store_dwordx4 v[54:55], v[50:53], off sc1
	s_and_saveexec_b64 s[26:27], s[42:43]
	s_cbranch_execz .LBB0_530
	v_lshlrev_b64 v[50:51], 5, v[146:147]
	v_lshl_add_u64 v[50:51], s[6:7], 0, v[50:51]
	v_lshl_add_u64 v[50:51], s[4:5], 2, v[50:51]
	global_store_dword v[50:51], v66, off
; #define LAS __attribute__((address_space(3)))
; __device__ __forceinline__ unsigned pk2(float lo, float hi) { return f2bf(lo) | (f2bf(hi) << 16); }
;     __device__ __forceinline__ void epi(const f32x4 (&acc)[2][2][4][2], const Unit& u, int wr, int wc, int fr, int fq) const {
;     ...
;         asm volatile("s_waitcnt lgkmcnt(0)" ::: "memory"); __builtin_amdgcn_s_barrier(); asm volatile("" ::: "memory");
;         const f32x4 g0 = *(const f32x4*)((const char*)kn + lcol * 4), g1 = *(const f32x4*)((const char*)kn + lcol * 4 + 16);
;         const unsigned koff = (lrow * (unsigned)DQK + lcol) * 2u, voff = (lrow * (unsigned)DVH + lcol) * 2u;
;         char* kb = (char*)(Ko + hrow0 * DQK); char* vb = (char*)(Vo + hrow0 * DVH);
; #pragma unroll
;         for (int ai = 0; ai < 2; ++ai)
; #pragma unroll
;             for (int m = 0; m < 4; ++m) { const f32x4 pt = *(const LAS f32x4*)(part + (ai * 128 + m * 16 + lrow) * 4);
;                 const float tot = ((pt.x + pt.y) + (pt.z + pt.w)) + kr2[ai][m]; const float rk = rsqrtf(tot * (1.f / DQK) + EPS); const float f = sc[ai][m] * rk;
;                 const f32x4 k0 = acc[ai][0][m][0] * f * g0, k1 = acc[ai][0][m][1] * f * g1, v0 = acc[ai][1][m][0] * sc[ai][m], v1 = acc[ai][1][m][1] * sc[ai][m];
;                 u32x4 w; w.x = pk2(k0[0], k0[1]); w.y = pk2(k0[2], k0[3]); w.z = pk2(k1[0], k1[1]); w.w = pk2(k1[2], k1[3]);
;                 *(u32x4*)(kb + (size_t)(ai * 128 + m * 16) * DQK * 2 + koff) = w;
;                 w.x = pk2(v0[0], v0[1]); w.y = pk2(v0[2], v0[3]); w.z = pk2(v1[0], v1[1]); w.w = pk2(v1[2], v1[3]);
;                 *(u32x4*)(vb + (size_t)(ai * 128 + m * 16) * DVH * 2 + voff) = w;
;                 if (wc == 0 && fq == 0) RSTDK[(size_t)(rowt + ai * 128 + m * 16 + lrow) * 8 + h] = rk; }
.LBB0_530:
	s_or_b64 exec, exec, s[26:27]
	ds_read_b128 v[50:53], v118 offset:2304
	v_add_f32_e32 v56, v164, v165
	v_mov_b32_e32 v159, v158
	s_mov_b32 s19, 0xd000
	v_pk_mul_f32 v[38:39], v[38:39], v[158:159]
	s_waitcnt lgkmcnt(0)
	v_mov_b32_e32 v54, v51
	v_mov_b32_e32 v55, v52
	v_mov_b32_e32 v51, v53
	v_pk_add_f32 v[50:51], v[54:55], v[50:51]
	v_pk_mul_f32 v[54:55], v[34:35], v[158:159]
	v_add_f32_e32 v50, v50, v51
	v_add_f32_e32 v50, v56, v50
	v_fmamk_f32 v50, v50, 0x3baaaaab, v180
	v_mul_f32_e32 v51, 0x4b800000, v50
	v_cmp_gt_f32_e32 vcc, s79, v50
	s_nop 1
	v_cndmask_b32_e32 v50, v50, v51, vcc
	v_rsq_f32_e32 v50, v50
	s_nop 0
	v_mul_f32_e32 v51, 0x45800000, v50
	v_cndmask_b32_e32 v50, v50, v51, vcc
	v_mul_f32_e32 v52, v158, v50
	v_pk_mul_f32 v[46:47], v[46:47], v[52:53] op_sel_hi:[1,0]
	v_pk_mul_f32 v[48:49], v[48:49], v[52:53] op_sel_hi:[1,0]
	v_pk_mul_f32 v[46:47], v[134:135], v[46:47]
	v_pk_mul_f32 v[48:49], v[136:137], v[48:49]
	v_pk_mul_f32 v[42:43], v[42:43], v[52:53] op_sel_hi:[1,0]
	v_pk_mul_f32 v[44:45], v[44:45], v[52:53] op_sel_hi:[1,0]
	v_mov_b32_e32 v52, v158
	v_mov_b32_e32 v53, v158
	v_cvt_pk_bf16_f32 v34, v46, v47
	v_pk_mul_f32 v[40:41], v[40:41], v[52:53]
	v_pk_mul_f32 v[52:53], v[36:37], v[52:53]
	v_pk_mul_f32 v[42:43], v[130:131], v[42:43]
	v_cvt_pk_bf16_f32 v35, v48, v49
	v_pk_mul_f32 v[44:45], v[132:133], v[44:45]
	v_cvt_pk_bf16_f32 v36, v42, v43
	v_cvt_pk_bf16_f32 v37, v44, v45
	v_add_co_u32_e32 v42, vcc, s19, v116
	s_nop 1
	v_addc_co_u32_e32 v43, vcc, 0, v117, vcc
	global_store_dwordx4 v[42:43], v[34:37], off offset:2048 sc1
	s_nop 1
	v_cvt_pk_bf16_f32 v34, v38, v39
	v_cvt_pk_bf16_f32 v35, v40, v41
	v_cvt_pk_bf16_f32 v36, v54, v55
	v_cvt_pk_bf16_f32 v37, v52, v53
	v_add_co_u32_e32 v38, vcc, 0x9000, v114
	s_nop 1
	v_addc_co_u32_e32 v39, vcc, 0, v115, vcc
	global_store_dwordx4 v[38:39], v[34:37], off sc1
	s_and_saveexec_b64 s[26:27], s[42:43]
	s_cbranch_execz .LBB0_532
	v_add_u32_e32 v34, 16, v146
	v_mov_b32_e32 v35, v147
	v_lshlrev_b64 v[34:35], 5, v[34:35]
	v_lshl_add_u64 v[34:35], s[6:7], 0, v[34:35]
	v_lshl_add_u64 v[34:35], s[4:5], 2, v[34:35]
	global_store_dword v[34:35], v50, off
.LBB0_532:
	s_or_b64 exec, exec, s[26:27]
	ds_read_b128 v[34:37], v118 offset:2560
	v_add_f32_e32 v40, v160, v161
	v_mov_b32_e32 v155, v154
	s_mov_b32 s19, 0xf000
	v_pk_mul_f32 v[22:23], v[22:23], v[154:155]
	s_waitcnt lgkmcnt(0)
	v_mov_b32_e32 v38, v35
	v_mov_b32_e32 v39, v36
	v_mov_b32_e32 v35, v37
	v_pk_add_f32 v[34:35], v[38:39], v[34:35]
	v_pk_mul_f32 v[38:39], v[18:19], v[154:155]
	v_add_f32_e32 v34, v34, v35
	v_add_f32_e32 v34, v40, v34
	v_fmamk_f32 v34, v34, 0x3baaaaab, v180
	v_mul_f32_e32 v35, 0x4b800000, v34
	v_cmp_gt_f32_e32 vcc, s79, v34
	s_nop 1
	v_cndmask_b32_e32 v34, v34, v35, vcc
	v_rsq_f32_e32 v34, v34
	s_nop 0
	v_mul_f32_e32 v35, 0x45800000, v34
	v_cndmask_b32_e32 v34, v34, v35, vcc
	v_mul_f32_e32 v36, v154, v34
	v_pk_mul_f32 v[30:31], v[30:31], v[36:37] op_sel_hi:[1,0]
	v_pk_mul_f32 v[32:33], v[32:33], v[36:37] op_sel_hi:[1,0]
	v_pk_mul_f32 v[30:31], v[134:135], v[30:31]
	v_pk_mul_f32 v[32:33], v[136:137], v[32:33]
	v_pk_mul_f32 v[26:27], v[26:27], v[36:37] op_sel_hi:[1,0]
	v_pk_mul_f32 v[28:29], v[28:29], v[36:37] op_sel_hi:[1,0]
	v_mov_b32_e32 v36, v154
	v_mov_b32_e32 v37, v154
	v_cvt_pk_bf16_f32 v18, v30, v31
	v_pk_mul_f32 v[24:25], v[24:25], v[36:37]
	v_pk_mul_f32 v[36:37], v[20:21], v[36:37]
	v_pk_mul_f32 v[26:27], v[130:131], v[26:27]
	v_cvt_pk_bf16_f32 v19, v32, v33
	v_pk_mul_f32 v[28:29], v[132:133], v[28:29]
	v_cvt_pk_bf16_f32 v20, v26, v27
	v_cvt_pk_bf16_f32 v21, v28, v29
	v_add_co_u32_e32 v26, vcc, s19, v116
	s_nop 1
	v_addc_co_u32_e32 v27, vcc, 0, v117, vcc
	global_store_dwordx4 v[26:27], v[18:21], off sc1
	s_nop 1
	v_cvt_pk_bf16_f32 v18, v22, v23
	v_cvt_pk_bf16_f32 v19, v24, v25
	v_cvt_pk_bf16_f32 v20, v38, v39
	v_cvt_pk_bf16_f32 v21, v36, v37
	v_add_co_u32_e32 v22, vcc, 0xa000, v114
	s_nop 1
	v_addc_co_u32_e32 v23, vcc, 0, v115, vcc
	global_store_dwordx4 v[22:23], v[18:21], off sc1
	s_and_saveexec_b64 s[26:27], s[42:43]
	s_cbranch_execz .LBB0_534
	v_add_u32_e32 v18, 32, v146
	v_mov_b32_e32 v19, v147
	v_lshlrev_b64 v[18:19], 5, v[18:19]
	v_lshl_add_u64 v[18:19], s[6:7], 0, v[18:19]
	v_lshl_add_u64 v[18:19], s[4:5], 2, v[18:19]
	global_store_dword v[18:19], v34, off
.LBB0_534:
	s_or_b64 exec, exec, s[26:27]
	ds_read_b128 v[18:21], v118 offset:2816
	v_add_f32_e32 v24, v156, v157
	v_mov_b32_e32 v153, v152
	v_pk_mul_f32 v[6:7], v[6:7], v[152:153]
	s_waitcnt lgkmcnt(0)
	v_mov_b32_e32 v22, v19
	v_mov_b32_e32 v23, v20
	v_mov_b32_e32 v19, v21
	v_pk_add_f32 v[18:19], v[22:23], v[18:19]
	v_pk_mul_f32 v[22:23], v[2:3], v[152:153]
	v_add_f32_e32 v18, v18, v19
	v_add_f32_e32 v18, v24, v18
	v_fmamk_f32 v18, v18, 0x3baaaaab, v180
	v_mul_f32_e32 v19, 0x4b800000, v18
	v_cmp_gt_f32_e32 vcc, s79, v18
	s_nop 1
	v_cndmask_b32_e32 v18, v18, v19, vcc
	v_rsq_f32_e32 v18, v18
	s_nop 0
	v_mul_f32_e32 v19, 0x45800000, v18
	v_cndmask_b32_e32 v18, v18, v19, vcc
	v_mul_f32_e32 v20, v152, v18
	v_pk_mul_f32 v[14:15], v[14:15], v[20:21] op_sel_hi:[1,0]
	v_pk_mul_f32 v[16:17], v[16:17], v[20:21] op_sel_hi:[1,0]
	v_pk_mul_f32 v[14:15], v[134:135], v[14:15]
	v_pk_mul_f32 v[16:17], v[136:137], v[16:17]
	v_pk_mul_f32 v[10:11], v[10:11], v[20:21] op_sel_hi:[1,0]
	v_pk_mul_f32 v[12:13], v[12:13], v[20:21] op_sel_hi:[1,0]
	v_mov_b32_e32 v20, v152
	v_mov_b32_e32 v21, v152
	v_cvt_pk_bf16_f32 v2, v14, v15
	v_pk_mul_f32 v[8:9], v[8:9], v[20:21]
	v_pk_mul_f32 v[20:21], v[4:5], v[20:21]
	v_pk_mul_f32 v[10:11], v[130:131], v[10:11]
	v_cvt_pk_bf16_f32 v3, v16, v17
	v_pk_mul_f32 v[12:13], v[132:133], v[12:13]
	v_cvt_pk_bf16_f32 v4, v10, v11
	v_cvt_pk_bf16_f32 v5, v12, v13
	v_add_co_u32_e32 v10, vcc, s81, v116
	s_nop 1
	v_addc_co_u32_e32 v11, vcc, 0, v117, vcc
	global_store_dwordx4 v[10:11], v[2:5], off offset:2048 sc1
	s_nop 1
	v_cvt_pk_bf16_f32 v2, v6, v7
	v_cvt_pk_bf16_f32 v3, v8, v9
	v_cvt_pk_bf16_f32 v4, v22, v23
	v_cvt_pk_bf16_f32 v5, v20, v21
	v_add_co_u32_e32 v6, vcc, 0xb000, v114
	s_nop 1
	v_addc_co_u32_e32 v7, vcc, 0, v115, vcc
	global_store_dwordx4 v[6:7], v[2:5], off sc1
	s_and_saveexec_b64 s[26:27], s[42:43]
	s_cbranch_execz .LBB0_536
	v_add_u32_e32 v146, 48, v146
	v_lshlrev_b64 v[2:3], 5, v[146:147]
	v_lshl_add_u64 v[2:3], s[6:7], 0, v[2:3]
	v_lshl_add_u64 v[2:3], s[4:5], 2, v[2:3]
	global_store_dword v[2:3], v18, off

; __device__ __forceinline__ float sigmoid_fast(float x) { return __builtin_amdgcn_rcpf(1.f + __expf(-x)); }
;     template <bool BWD>
;     __device__ __forceinline__ void epi_dir(const f32x4 (&acc)[2][2][4][2], const Unit& u, int wr, int wc, int fr, int fq) const {
;         const int dir = BWD ? 1 : 0, gblk = u.pn & 7;
;         unsigned coff = (unsigned)(wc * 32 + 4 * fq) * 4u;
;         unsigned loffu = (unsigned)((wr * 64 + fr) * 1024 + wc * 32 + 4 * fq) * 2u;
;         asm volatile("" : "+v"(coff), "+v"(loffu));
;         const unsigned loffh = loffu * 2u;
;         const size_t ubase = ((size_t)u.pm * 256 * 1024 + (size_t)gblk * 128);
;         const char* Ub = U + ubase * 2;
;         char* Hb = HP + ((size_t)dir * NR * 1024 + ubase) * 4;
;         const char* bap = (const char*)(ba + dir * 1024 + gblk * 128); const char* bxp = (const char*)(bx + dir * 1024 + gblk * 128); const char* lmp = (const char*)(lam + dir * 1024 + gblk * 128);
;         const int rowt = u.pm * 256; const int lane = fq * 16 + fr;
;         const int bsel = (lane & 48) | (BWD ? 0 : 15);
; #pragma unroll
;         for (int ai = 0; ai < 2; ++ai) {
;             const int r64 = rowt + ai * 128 + wr * 64; const int chunk = r64 < NL ? (r64 >> 12) * NCHUNK + 4 + ((r64 & (SEQ - 1)) >> 6) : ((r64 - NL) >> 8) * NCHUNK + (((r64 - NL) & (CTXL - 1)) >> 6);
; #pragma unroll
;             for (int n = 0; n < 2; ++n) {
;                 f32x4 A[4], H[4];
;                 const f32x4 bav = *(const f32x4*)(bap + n * 64 + coff), bxv = *(const f32x4*)(bxp + n * 64 + coff), lsl = *(const f32x4*)(lmp + n * 64 + coff);
; #pragma unroll
;                 for (int m = 0; m < 4; ++m) {
;                     const u32x2 uw = *(const u32x2*)(Ub + ((size_t)(ai * 128 + m * 16) * 1024 + n * 16) * 2 + loffu);
;                     const float uv[4] = {bflo(uw.x), bfhi(uw.x), bflo(uw.y), bfhi(uw.y)};
; #pragma unroll
;                     for (int j = 0; j < 4; ++j) { const float r = sigmoid_fast(acc[ai][0][m][n][j] + bav[j]), ig = sigmoid_fast(acc[ai][1][m][n][j] + bxv[j]);
;                         const float la = r * lsl[j]; A[m][j] = __expf(la); H[m][j] = __builtin_amdgcn_sqrtf(one_minus_exp(2.f * la)) * (ig * uv[j]); } }
.Lge_chunk:
	s_and_b32 s27, s48, 7
	s_lshl_b32 s12, s27, 9
	v_add_u32_e32 v186, s12, v228
	s_lshl_b32 s19, s21, 12
	s_add_i32 s19, s19, s12
	v_add_u32_e32 v187, s19, v228
	v_add_u32_e32 v188, 0x2000, v187
	s_lshl_b32 s19, s27, 8
	v_add_u32_e32 v190, s19, v229
	v_add_u32_e32 v191, 0x8000, v190
	v_add_u32_e32 v192, 0x10000, v190
	v_add_u32_e32 v193, 0x18000, v190
	v_lshl_add_u32 v194, v229, 1, s12
	v_add_u32_e32 v195, 0x10000, v194
	v_add_u32_e32 v196, 0x20000, v194
	v_add_u32_e32 v197, 0x30000, v194
	s_lshl_b32 s19, s26, 19
	s_add_u32 s50, s65, s19
	s_addc_u32 s51, s66, 0
	s_add_u32 s52, s50, 0x40000
	s_addc_u32 s53, s51, 0
	s_lshl_b32 s19, s26, 20
	s_add_u32 s54, s74, s19
	s_addc_u32 s55, s75, 0
	s_mov_b32 s49, 0xbdcccccd
	s_cmp_gt_u32 s48, 7
	s_cbranch_scc0 .Lge_fwd
	s_add_u32 s54, s54, 0x4400000
	s_addc_u32 s55, s55, 0
	s_add_u32 s56, s54, 0x80000
	s_addc_u32 s57, s55, 0
	s_add_u32 s26, s83, s12
	s_addc_u32 s27, s84, 0
	global_load_dwordx4 v[130:133], v228, s[26:27]
	s_add_u32 s26, s85, s12
	s_addc_u32 s27, s86, 0
	global_load_dwordx4 v[134:137], v228, s[26:27]
	s_add_u32 s26, s92, s12
	s_addc_u32 s27, s93, 0
	global_load_dwordx4 v[138:141], v228, s[26:27]
	global_load_dwordx2 v[168:169], v190, s[50:51]
	global_load_dwordx2 v[170:171], v191, s[50:51]
	global_load_dwordx2 v[172:173], v192, s[50:51]
	global_load_dwordx2 v[174:175], v193, s[50:51]
	global_load_dwordx2 v[176:177], v190, s[52:53]
	global_load_dwordx2 v[178:179], v191, s[52:53]
	global_load_dwordx2 v[182:183], v192, s[52:53]
	global_load_dwordx2 v[184:185], v193, s[52:53]
	s_waitcnt vmcnt(4)
	v_add_f32_e32 v126, v126, v130
	v_add_f32_e32 v127, v127, v131
	v_add_f32_e32 v128, v128, v132
	v_add_f32_e32 v129, v129, v133
	v_add_f32_e32 v122, v122, v130
	v_add_f32_e32 v123, v123, v131
	v_add_f32_e32 v124, v124, v132
	v_add_f32_e32 v125, v125, v133
	v_mul_f32_e32 v126, 0xbfb8aa3b, v126
	v_mul_f32_e32 v127, 0xbfb8aa3b, v127
	v_mul_f32_e32 v128, 0xbfb8aa3b, v128
	v_mul_f32_e32 v129, 0xbfb8aa3b, v129
	v_mul_f32_e32 v122, 0xbfb8aa3b, v122
	v_mul_f32_e32 v123, 0xbfb8aa3b, v123
	v_mul_f32_e32 v124, 0xbfb8aa3b, v124
	v_mul_f32_e32 v125, 0xbfb8aa3b, v125
	v_exp_f32_e32 v126, v126
	v_exp_f32_e32 v127, v127
	v_exp_f32_e32 v128, v128
	v_exp_f32_e32 v129, v129
	v_exp_f32_e32 v122, v122
	v_exp_f32_e32 v123, v123
	v_exp_f32_e32 v124, v124
	v_exp_f32_e32 v125, v125
	v_add_f32_e32 v126, 1.0, v126
	v_add_f32_e32 v127, 1.0, v127
	v_add_f32_e32 v128, 1.0, v128
	v_add_f32_e32 v129, 1.0, v129
	v_add_f32_e32 v122, 1.0, v122
	v_add_f32_e32 v123, 1.0, v123
	v_add_f32_e32 v124, 1.0, v124
	v_add_f32_e32 v125, 1.0, v125
	v_rcp_f32_e32 v126, v126
	v_rcp_f32_e32 v127, v127
	v_rcp_f32_e32 v128, v128
	v_rcp_f32_e32 v129, v129
	v_rcp_f32_e32 v122, v122
	v_rcp_f32_e32 v123, v123
	v_rcp_f32_e32 v124, v124
	v_rcp_f32_e32 v125, v125
	v_mul_f32_e32 v126, v138, v126
	v_mul_f32_e32 v127, v139, v127
	v_mul_f32_e32 v128, v140, v128
	v_mul_f32_e32 v129, v141, v129
	v_mul_f32_e32 v122, v138, v122
	v_mul_f32_e32 v123, v139, v123
	v_mul_f32_e32 v124, v140, v124
	v_mul_f32_e32 v125, v141, v125
	v_add_f32_e32 v198, v126, v126
	v_add_f32_e32 v201, v127, v127
	v_add_f32_e32 v204, v128, v128
	v_add_f32_e32 v207, v129, v129
	v_add_f32_e32 v216, v122, v122
	v_add_f32_e32 v219, v123, v123
	v_add_f32_e32 v240, v124, v124
	v_add_f32_e32 v243, v125, v125
	v_mul_f32_e32 v199, 0x3fb8aa3b, v198
	v_mul_f32_e32 v202, 0x3fb8aa3b, v201
	v_mul_f32_e32 v205, 0x3fb8aa3b, v204
	v_mul_f32_e32 v208, 0x3fb8aa3b, v207
	v_mul_f32_e32 v217, 0x3fb8aa3b, v216
	v_mul_f32_e32 v238, 0x3fb8aa3b, v219
	v_mul_f32_e32 v241, 0x3fb8aa3b, v240
	v_mul_f32_e32 v244, 0x3fb8aa3b, v243
	v_exp_f32_e32 v199, v199
	v_exp_f32_e32 v202, v202
	v_exp_f32_e32 v205, v205
	v_exp_f32_e32 v208, v208
	v_exp_f32_e32 v217, v217
	v_exp_f32_e32 v238, v238
	v_exp_f32_e32 v241, v241
	v_exp_f32_e32 v244, v244
	v_fmamk_f32 v200, v198, 0x3c088889, v211
	v_fmamk_f32 v203, v201, 0x3c088889, v211
	v_fmamk_f32 v206, v204, 0x3c088889, v211
	v_fmamk_f32 v209, v207, 0x3c088889, v211
	v_fmamk_f32 v218, v216, 0x3c088889, v211
	v_fmamk_f32 v239, v219, 0x3c088889, v211
	v_fmamk_f32 v242, v240, 0x3c088889, v211
	v_fmamk_f32 v245, v243, 0x3c088889, v211
	v_sub_f32_e32 v199, 1.0, v199
	v_sub_f32_e32 v202, 1.0, v202
	v_sub_f32_e32 v205, 1.0, v205
	v_sub_f32_e32 v208, 1.0, v208
	v_sub_f32_e32 v217, 1.0, v217
	v_sub_f32_e32 v238, 1.0, v238
	v_sub_f32_e32 v241, 1.0, v241
	v_sub_f32_e32 v244, 1.0, v244
	v_fmaak_f32 v200, v198, v200, 0x3e2aaaab
	v_fmaak_f32 v203, v201, v203, 0x3e2aaaab
	v_fmaak_f32 v206, v204, v206, 0x3e2aaaab
	v_fmaak_f32 v209, v207, v209, 0x3e2aaaab
	v_fmaak_f32 v218, v216, v218, 0x3e2aaaab
	v_fmaak_f32 v239, v219, v239, 0x3e2aaaab
	v_fmaak_f32 v242, v240, v242, 0x3e2aaaab
	v_fmaak_f32 v245, v243, v245, 0x3e2aaaab
	v_fma_f32 v200, v198, v200, 0.5
	v_fma_f32 v203, v201, v203, 0.5
	v_fma_f32 v206, v204, v206, 0.5
	v_fma_f32 v209, v207, v209, 0.5
	v_fma_f32 v218, v216, v218, 0.5
	v_fma_f32 v239, v219, v239, 0.5
	v_fma_f32 v242, v240, v242, 0.5
	v_fma_f32 v245, v243, v245, 0.5
	v_fma_f32 v200, v198, v200, 1.0
	v_fma_f32 v203, v201, v203, 1.0
	v_fma_f32 v206, v204, v206, 1.0
	v_fma_f32 v209, v207, v209, 1.0
	v_fma_f32 v218, v216, v218, 1.0
	v_fma_f32 v239, v219, v239, 1.0
	v_fma_f32 v242, v240, v242, 1.0
	v_fma_f32 v245, v243, v245, 1.0
	v_mul_f32_e64 v200, v200, -v198
	v_mul_f32_e64 v203, v203, -v201
	v_mul_f32_e64 v206, v206, -v204
	v_mul_f32_e64 v209, v209, -v207
	v_mul_f32_e64 v218, v218, -v216
	v_mul_f32_e64 v239, v239, -v219
	v_mul_f32_e64 v242, v242, -v240
	v_mul_f32_e64 v245, v245, -v243
	v_cmp_nlt_f32_e32 vcc, s49, v198
	v_add_f32_e32 v98, v98, v134
	v_mul_f32_e32 v98, 0xbfb8aa3b, v98
; __device__ __forceinline__ float sigmoid_fast(float x) { return __builtin_amdgcn_rcpf(1.f + __expf(-x)); }
; __device__ __forceinline__ float one_minus_exp(float x) { const float p = -x * (1.f + x * (0.5f + x * (0.16666667f + x * (0.041666668f + x * 0.0083333338f)))); return x > -0.1f ? p : 1.f - __expf(x); }
;     template <bool BWD>
;     __device__ __forceinline__ void epi_dir(const f32x4 (&acc)[2][2][4][2], const Unit& u, int wr, int wc, int fr, int fq) const {
;     ...
;                 const f32x4 bav = *(const f32x4*)(bap + n * 64 + coff), bxv = *(const f32x4*)(bxp + n * 64 + coff), lsl = *(const f32x4*)(lmp + n * 64 + coff);
; #pragma unroll
;                 for (int m = 0; m < 4; ++m) {
;                     const u32x2 uw = *(const u32x2*)(Ub + ((size_t)(ai * 128 + m * 16) * 1024 + n * 16) * 2 + loffu);
;                     const float uv[4] = {bflo(uw.x), bfhi(uw.x), bflo(uw.y), bfhi(uw.y)};
; #pragma unroll
;                     for (int j = 0; j < 4; ++j) { const float r = sigmoid_fast(acc[ai][0][m][n][j] + bav[j]), ig = sigmoid_fast(acc[ai][1][m][n][j] + bxv[j]);
;                         const float la = r * lsl[j]; A[m][j] = __expf(la); H[m][j] = __builtin_amdgcn_sqrtf(one_minus_exp(2.f * la)) * (ig * uv[j]); } }
	v_cndmask_b32_e32 v199, v200, v199, vcc
	v_cmp_nlt_f32_e32 vcc, s49, v201
	v_add_f32_e32 v99, v99, v135
	v_mul_f32_e32 v99, 0xbfb8aa3b, v99
	v_cndmask_b32_e32 v202, v203, v202, vcc
	v_cmp_nlt_f32_e32 vcc, s49, v204
	v_add_f32_e32 v100, v100, v136
	v_mul_f32_e32 v100, 0xbfb8aa3b, v100
	v_cndmask_b32_e32 v205, v206, v205, vcc
	v_cmp_nlt_f32_e32 vcc, s49, v207
	v_add_f32_e32 v101, v101, v137
	v_mul_f32_e32 v101, 0xbfb8aa3b, v101
	v_cndmask_b32_e32 v208, v209, v208, vcc
	v_cmp_nlt_f32_e32 vcc, s49, v216
	v_add_f32_e32 v102, v102, v134
	v_mul_f32_e32 v102, 0xbfb8aa3b, v102
	v_cndmask_b32_e32 v217, v218, v217, vcc
	v_cmp_nlt_f32_e32 vcc, s49, v219
	v_add_f32_e32 v103, v103, v135
	v_mul_f32_e32 v103, 0xbfb8aa3b, v103
	v_cndmask_b32_e32 v238, v239, v238, vcc
	v_cmp_nlt_f32_e32 vcc, s49, v240
	v_add_f32_e32 v104, v104, v136
	v_mul_f32_e32 v104, 0xbfb8aa3b, v104
	v_cndmask_b32_e32 v241, v242, v241, vcc
	v_cmp_nlt_f32_e32 vcc, s49, v243
	v_add_f32_e32 v105, v105, v137
	v_mul_f32_e32 v105, 0xbfb8aa3b, v105
	v_cndmask_b32_e32 v244, v245, v244, vcc
	v_exp_f32_e32 v98, v98
	v_exp_f32_e32 v99, v99
	v_exp_f32_e32 v100, v100
	v_exp_f32_e32 v101, v101
	v_exp_f32_e32 v102, v102
	v_exp_f32_e32 v103, v103
	v_exp_f32_e32 v104, v104
	v_exp_f32_e32 v105, v105
	v_sqrt_f32_e32 v199, v199
	v_sqrt_f32_e32 v202, v202
	v_sqrt_f32_e32 v205, v205
	v_sqrt_f32_e32 v208, v208
	v_sqrt_f32_e32 v217, v217
	v_sqrt_f32_e32 v238, v238
	v_sqrt_f32_e32 v241, v241
	v_sqrt_f32_e32 v244, v244
	v_add_f32_e32 v98, 1.0, v98
	v_add_f32_e32 v99, 1.0, v99
	v_add_f32_e32 v100, 1.0, v100
	v_add_f32_e32 v101, 1.0, v101
	v_add_f32_e32 v102, 1.0, v102
	v_add_f32_e32 v103, 1.0, v103
	v_add_f32_e32 v104, 1.0, v104
	v_add_f32_e32 v105, 1.0, v105
	v_lshlrev_b32_e32 v200, 16, v168
	v_and_b32_e32 v203, 0xffff0000, v168
	v_lshlrev_b32_e32 v206, 16, v169
	v_and_b32_e32 v209, 0xffff0000, v169
	v_lshlrev_b32_e32 v218, 16, v170
	v_and_b32_e32 v239, 0xffff0000, v170
	v_lshlrev_b32_e32 v242, 16, v171
	v_and_b32_e32 v245, 0xffff0000, v171
	v_rcp_f32_e32 v98, v98
	v_rcp_f32_e32 v99, v99
	v_rcp_f32_e32 v100, v100
	v_rcp_f32_e32 v101, v101
	v_rcp_f32_e32 v102, v102
	v_rcp_f32_e32 v103, v103
	v_rcp_f32_e32 v104, v104
	v_rcp_f32_e32 v105, v105
	v_mul_f32_e32 v126, 0x3fb8aa3b, v126
	v_mul_f32_e32 v127, 0x3fb8aa3b, v127
	v_mul_f32_e32 v128, 0x3fb8aa3b, v128
	v_mul_f32_e32 v129, 0x3fb8aa3b, v129
	v_mul_f32_e32 v122, 0x3fb8aa3b, v122
	v_mul_f32_e32 v123, 0x3fb8aa3b, v123
	v_mul_f32_e32 v124, 0x3fb8aa3b, v124
	v_mul_f32_e32 v125, 0x3fb8aa3b, v125
	v_mul_f32_e32 v98, v98, v200
	v_mul_f32_e32 v99, v99, v203
	v_mul_f32_e32 v100, v100, v206
	v_mul_f32_e32 v101, v101, v209
	v_mul_f32_e32 v102, v102, v218
	v_mul_f32_e32 v103, v103, v239
	v_mul_f32_e32 v104, v104, v242
	v_mul_f32_e32 v105, v105, v245
	v_exp_f32_e32 v126, v126
	v_exp_f32_e32 v127, v127
	v_exp_f32_e32 v128, v128
	v_exp_f32_e32 v129, v129
	v_exp_f32_e32 v122, v122
	v_exp_f32_e32 v123, v123
	v_exp_f32_e32 v124, v124
	v_exp_f32_e32 v125, v125
	v_mul_f32_e32 v98, v98, v199
	v_mul_f32_e32 v99, v99, v202
	v_mul_f32_e32 v100, v100, v205
	v_mul_f32_e32 v101, v101, v208
	v_mul_f32_e32 v102, v102, v217
	v_mul_f32_e32 v103, v103, v238
	v_mul_f32_e32 v104, v104, v241
	v_mul_f32_e32 v105, v105, v244
	v_add_f32_e32 v118, v118, v130
	v_add_f32_e32 v119, v119, v131
	v_add_f32_e32 v120, v120, v132
	v_add_f32_e32 v121, v121, v133
	v_add_f32_e32 v114, v114, v130
	v_add_f32_e32 v115, v115, v131
	v_add_f32_e32 v116, v116, v132
	v_add_f32_e32 v117, v117, v133
	v_mul_f32_e32 v118, 0xbfb8aa3b, v118
	v_mul_f32_e32 v119, 0xbfb8aa3b, v119
	v_mul_f32_e32 v120, 0xbfb8aa3b, v120
	v_mul_f32_e32 v121, 0xbfb8aa3b, v121
	v_mul_f32_e32 v114, 0xbfb8aa3b, v114
	v_mul_f32_e32 v115, 0xbfb8aa3b, v115
	v_mul_f32_e32 v116, 0xbfb8aa3b, v116
	v_mul_f32_e32 v117, 0xbfb8aa3b, v117
	v_exp_f32_e32 v118, v118
	v_exp_f32_e32 v119, v119
	v_exp_f32_e32 v120, v120
	v_exp_f32_e32 v121, v121
	v_exp_f32_e32 v114, v114
	v_exp_f32_e32 v115, v115
	v_exp_f32_e32 v116, v116
	v_exp_f32_e32 v117, v117
	v_add_f32_e32 v118, 1.0, v118
	v_add_f32_e32 v119, 1.0, v119
	v_add_f32_e32 v120, 1.0, v120
	v_add_f32_e32 v121, 1.0, v121
	v_add_f32_e32 v114, 1.0, v114
	v_add_f32_e32 v115, 1.0, v115
	v_add_f32_e32 v116, 1.0, v116
	v_add_f32_e32 v117, 1.0, v117
	v_rcp_f32_e32 v118, v118
	v_rcp_f32_e32 v119, v119
	v_rcp_f32_e32 v120, v120
	v_rcp_f32_e32 v121, v121
	v_rcp_f32_e32 v114, v114
	v_rcp_f32_e32 v115, v115
	v_rcp_f32_e32 v116, v116
	v_rcp_f32_e32 v117, v117
	v_mul_f32_e32 v118, v138, v118
	v_mul_f32_e32 v119, v139, v119
	v_mul_f32_e32 v120, v140, v120
	v_mul_f32_e32 v121, v141, v121
	v_mul_f32_e32 v114, v138, v114
	v_mul_f32_e32 v115, v139, v115
	v_mul_f32_e32 v116, v140, v116
	v_mul_f32_e32 v117, v141, v117
	v_add_f32_e32 v198, v118, v118
	v_add_f32_e32 v201, v119, v119
	v_add_f32_e32 v204, v120, v120
	v_add_f32_e32 v207, v121, v121
	v_add_f32_e32 v216, v114, v114
	v_add_f32_e32 v219, v115, v115
	v_add_f32_e32 v240, v116, v116
	v_add_f32_e32 v243, v117, v117
	v_mul_f32_e32 v199, 0x3fb8aa3b, v198
	v_mul_f32_e32 v202, 0x3fb8aa3b, v201
	v_mul_f32_e32 v205, 0x3fb8aa3b, v204
	v_mul_f32_e32 v208, 0x3fb8aa3b, v207
	v_mul_f32_e32 v217, 0x3fb8aa3b, v216
	v_mul_f32_e32 v238, 0x3fb8aa3b, v219
	v_mul_f32_e32 v241, 0x3fb8aa3b, v240
	v_mul_f32_e32 v244, 0x3fb8aa3b, v243
	v_exp_f32_e32 v199, v199
	v_exp_f32_e32 v202, v202
	v_exp_f32_e32 v205, v205
	v_exp_f32_e32 v208, v208
	v_exp_f32_e32 v217, v217
	v_exp_f32_e32 v238, v238
	v_exp_f32_e32 v241, v241
	v_exp_f32_e32 v244, v244
	v_fmamk_f32 v200, v198, 0x3c088889, v211
	v_fmamk_f32 v203, v201, 0x3c088889, v211
	v_fmamk_f32 v206, v204, 0x3c088889, v211
	v_fmamk_f32 v209, v207, 0x3c088889, v211
; __device__ __forceinline__ float sigmoid_fast(float x) { return __builtin_amdgcn_rcpf(1.f + __expf(-x)); }
; __device__ __forceinline__ float one_minus_exp(float x) { const float p = -x * (1.f + x * (0.5f + x * (0.16666667f + x * (0.041666668f + x * 0.0083333338f)))); return x > -0.1f ? p : 1.f - __expf(x); }
; #define SCAN_STEP(D) { const float ap = dppf<(BWD ? 0x100 : 0x110) + D>(1.f, av), hp = dppf<(BWD ? 0x100 : 0x110) + D>(0.f, hv); hv = fmaf(av, hp, hv); av = av * ap; }
;     template <bool BWD>
;     __device__ __forceinline__ void epi_dir(const f32x4 (&acc)[2][2][4][2], const Unit& u, int wr, int wc, int fr, int fq) const {
;     ...
;                     const u32x2 uw = *(const u32x2*)(Ub + ((size_t)(ai * 128 + m * 16) * 1024 + n * 16) * 2 + loffu);
;                     const float uv[4] = {bflo(uw.x), bfhi(uw.x), bflo(uw.y), bfhi(uw.y)};
; #pragma unroll
;                     for (int j = 0; j < 4; ++j) { const float r = sigmoid_fast(acc[ai][0][m][n][j] + bav[j]), ig = sigmoid_fast(acc[ai][1][m][n][j] + bxv[j]);
;                         const float la = r * lsl[j]; A[m][j] = __expf(la); H[m][j] = __builtin_amdgcn_sqrtf(one_minus_exp(2.f * la)) * (ig * uv[j]); } }
; #pragma unroll
;                 for (int m = 0; m < 4; ++m)
; #pragma unroll
;                     for (int j = 0; j < 4; ++j) { float av = A[m][j], hv = H[m][j];
;     ...
;                         SCAN_STEP(1) SCAN_STEP(2) SCAN_STEP(4) SCAN_STEP(8)
	v_fmamk_f32 v218, v216, 0x3c088889, v211
	v_fmamk_f32 v239, v219, 0x3c088889, v211
	v_fmamk_f32 v242, v240, 0x3c088889, v211
	v_fmamk_f32 v245, v243, 0x3c088889, v211
	v_sub_f32_e32 v199, 1.0, v199
	v_sub_f32_e32 v202, 1.0, v202
	v_sub_f32_e32 v205, 1.0, v205
	v_sub_f32_e32 v208, 1.0, v208
	v_sub_f32_e32 v217, 1.0, v217
	v_sub_f32_e32 v238, 1.0, v238
	v_sub_f32_e32 v241, 1.0, v241
	v_sub_f32_e32 v244, 1.0, v244
	v_fmaak_f32 v200, v198, v200, 0x3e2aaaab
	v_fmaak_f32 v203, v201, v203, 0x3e2aaaab
	v_fmaak_f32 v206, v204, v206, 0x3e2aaaab
	v_fmaak_f32 v209, v207, v209, 0x3e2aaaab
	v_fmaak_f32 v218, v216, v218, 0x3e2aaaab
	v_fmaak_f32 v239, v219, v239, 0x3e2aaaab
	v_fmaak_f32 v242, v240, v242, 0x3e2aaaab
	v_fmaak_f32 v245, v243, v245, 0x3e2aaaab
	v_fma_f32 v200, v198, v200, 0.5
	v_fma_f32 v203, v201, v203, 0.5
	v_fma_f32 v206, v204, v206, 0.5
	v_fma_f32 v209, v207, v209, 0.5
	v_fma_f32 v218, v216, v218, 0.5
	v_fma_f32 v239, v219, v239, 0.5
	v_fma_f32 v242, v240, v242, 0.5
	v_fma_f32 v245, v243, v245, 0.5
	v_fma_f32 v200, v198, v200, 1.0
	v_fma_f32 v203, v201, v203, 1.0
	v_fma_f32 v206, v204, v206, 1.0
	v_fma_f32 v209, v207, v209, 1.0
	v_fma_f32 v218, v216, v218, 1.0
	v_fma_f32 v239, v219, v239, 1.0
	v_fma_f32 v242, v240, v242, 1.0
	v_fma_f32 v245, v243, v245, 1.0
	v_mul_f32_e64 v200, v200, -v198
	v_mul_f32_e64 v203, v203, -v201
	v_mul_f32_e64 v206, v206, -v204
	v_mul_f32_e64 v209, v209, -v207
	v_mul_f32_e64 v218, v218, -v216
	v_mul_f32_e64 v239, v239, -v219
	v_mul_f32_e64 v242, v242, -v240
	v_mul_f32_e64 v245, v245, -v243
	v_cmp_nlt_f32_e32 vcc, s49, v198
	v_add_f32_e32 v106, v106, v134
	v_mul_f32_e32 v106, 0xbfb8aa3b, v106
	v_cndmask_b32_e32 v199, v200, v199, vcc
	v_cmp_nlt_f32_e32 vcc, s49, v201
	v_add_f32_e32 v107, v107, v135
	v_mul_f32_e32 v107, 0xbfb8aa3b, v107
	v_cndmask_b32_e32 v202, v203, v202, vcc
	v_cmp_nlt_f32_e32 vcc, s49, v204
	v_add_f32_e32 v108, v108, v136
	v_mul_f32_e32 v108, 0xbfb8aa3b, v108
	v_cndmask_b32_e32 v205, v206, v205, vcc
	v_cmp_nlt_f32_e32 vcc, s49, v207
	v_add_f32_e32 v109, v109, v137
	v_mul_f32_e32 v109, 0xbfb8aa3b, v109
	v_cndmask_b32_e32 v208, v209, v208, vcc
	v_cmp_nlt_f32_e32 vcc, s49, v216
	v_add_f32_e32 v110, v110, v134
	v_mul_f32_e32 v110, 0xbfb8aa3b, v110
	v_cndmask_b32_e32 v217, v218, v217, vcc
	v_cmp_nlt_f32_e32 vcc, s49, v219
	v_add_f32_e32 v111, v111, v135
	v_mul_f32_e32 v111, 0xbfb8aa3b, v111
	v_cndmask_b32_e32 v238, v239, v238, vcc
	v_cmp_nlt_f32_e32 vcc, s49, v240
	v_add_f32_e32 v112, v112, v136
	v_mul_f32_e32 v112, 0xbfb8aa3b, v112
	v_cndmask_b32_e32 v241, v242, v241, vcc
	v_cmp_nlt_f32_e32 vcc, s49, v243
	v_add_f32_e32 v113, v113, v137
	v_mul_f32_e32 v113, 0xbfb8aa3b, v113
	v_cndmask_b32_e32 v244, v245, v244, vcc
	v_exp_f32_e32 v106, v106
	v_exp_f32_e32 v107, v107
	v_exp_f32_e32 v108, v108
	v_exp_f32_e32 v109, v109
	v_exp_f32_e32 v110, v110
	v_exp_f32_e32 v111, v111
	v_exp_f32_e32 v112, v112
	v_exp_f32_e32 v113, v113
	v_sqrt_f32_e32 v199, v199
	v_sqrt_f32_e32 v202, v202
	v_sqrt_f32_e32 v205, v205
	v_sqrt_f32_e32 v208, v208
	v_sqrt_f32_e32 v217, v217
	v_sqrt_f32_e32 v238, v238
	v_sqrt_f32_e32 v241, v241
	v_sqrt_f32_e32 v244, v244
	v_add_f32_e32 v106, 1.0, v106
	v_add_f32_e32 v107, 1.0, v107
	v_add_f32_e32 v108, 1.0, v108
	v_add_f32_e32 v109, 1.0, v109
	v_add_f32_e32 v110, 1.0, v110
	v_add_f32_e32 v111, 1.0, v111
	v_add_f32_e32 v112, 1.0, v112
	v_add_f32_e32 v113, 1.0, v113
	v_lshlrev_b32_e32 v200, 16, v172
	v_and_b32_e32 v203, 0xffff0000, v172
	v_lshlrev_b32_e32 v206, 16, v173
	v_and_b32_e32 v209, 0xffff0000, v173
	v_lshlrev_b32_e32 v218, 16, v174
	v_and_b32_e32 v239, 0xffff0000, v174
	v_lshlrev_b32_e32 v242, 16, v175
	v_and_b32_e32 v245, 0xffff0000, v175
	v_rcp_f32_e32 v106, v106
	v_rcp_f32_e32 v107, v107
	v_rcp_f32_e32 v108, v108
	v_rcp_f32_e32 v109, v109
	v_rcp_f32_e32 v110, v110
	v_rcp_f32_e32 v111, v111
	v_rcp_f32_e32 v112, v112
	v_rcp_f32_e32 v113, v113
	v_mul_f32_e32 v118, 0x3fb8aa3b, v118
	v_mul_f32_e32 v119, 0x3fb8aa3b, v119
	v_mul_f32_e32 v120, 0x3fb8aa3b, v120
	v_mul_f32_e32 v121, 0x3fb8aa3b, v121
	v_mul_f32_e32 v114, 0x3fb8aa3b, v114
	v_mul_f32_e32 v115, 0x3fb8aa3b, v115
	v_mul_f32_e32 v116, 0x3fb8aa3b, v116
	v_mul_f32_e32 v117, 0x3fb8aa3b, v117
	v_mul_f32_e32 v106, v106, v200
	v_mul_f32_e32 v107, v107, v203
	v_mul_f32_e32 v108, v108, v206
	v_mul_f32_e32 v109, v109, v209
	v_mul_f32_e32 v110, v110, v218
	v_mul_f32_e32 v111, v111, v239
	v_mul_f32_e32 v112, v112, v242
	v_mul_f32_e32 v113, v113, v245
	v_exp_f32_e32 v118, v118
	v_exp_f32_e32 v119, v119
	v_exp_f32_e32 v120, v120
	v_exp_f32_e32 v121, v121
	v_exp_f32_e32 v114, v114
	v_exp_f32_e32 v115, v115
	v_exp_f32_e32 v116, v116
	v_exp_f32_e32 v117, v117
	v_mul_f32_e32 v106, v106, v199
	v_mul_f32_e32 v107, v107, v202
	v_mul_f32_e32 v108, v108, v205
	v_mul_f32_e32 v109, v109, v208
	v_mul_f32_e32 v110, v110, v217
	v_mul_f32_e32 v111, v111, v238
	v_mul_f32_e32 v112, v112, v241
	v_mul_f32_e32 v113, v113, v244
	v_fmac_f32_dpp v98, v98, v126 row_shl:1 row_mask:0xf bank_mask:0xf
	v_mul_f32_dpp v126, v126, v126 row_shl:1 row_mask:0xf bank_mask:0xf
	v_fmac_f32_dpp v99, v99, v127 row_shl:1 row_mask:0xf bank_mask:0xf
	v_mul_f32_dpp v127, v127, v127 row_shl:1 row_mask:0xf bank_mask:0xf
	v_fmac_f32_dpp v100, v100, v128 row_shl:1 row_mask:0xf bank_mask:0xf
	v_mul_f32_dpp v128, v128, v128 row_shl:1 row_mask:0xf bank_mask:0xf
	v_fmac_f32_dpp v101, v101, v129 row_shl:1 row_mask:0xf bank_mask:0xf
	v_mul_f32_dpp v129, v129, v129 row_shl:1 row_mask:0xf bank_mask:0xf
	v_fmac_f32_dpp v102, v102, v122 row_shl:1 row_mask:0xf bank_mask:0xf
	v_mul_f32_dpp v122, v122, v122 row_shl:1 row_mask:0xf bank_mask:0xf
	v_fmac_f32_dpp v103, v103, v123 row_shl:1 row_mask:0xf bank_mask:0xf
; #define SCAN_STEP(D) { const float ap = dppf<(BWD ? 0x100 : 0x110) + D>(1.f, av), hp = dppf<(BWD ? 0x100 : 0x110) + D>(0.f, hv); hv = fmaf(av, hp, hv); av = av * ap; }
;     template <bool BWD>
;     __device__ __forceinline__ void epi_dir(const f32x4 (&acc)[2][2][4][2], const Unit& u, int wr, int wc, int fr, int fq) const {
;     ...
;                     for (int j = 0; j < 4; ++j) { float av = A[m][j], hv = H[m][j];
;     ...
;                         SCAN_STEP(1) SCAN_STEP(2) SCAN_STEP(4) SCAN_STEP(8)
	v_mul_f32_dpp v123, v123, v123 row_shl:1 row_mask:0xf bank_mask:0xf
	v_fmac_f32_dpp v104, v104, v124 row_shl:1 row_mask:0xf bank_mask:0xf
	v_mul_f32_dpp v124, v124, v124 row_shl:1 row_mask:0xf bank_mask:0xf
	v_fmac_f32_dpp v105, v105, v125 row_shl:1 row_mask:0xf bank_mask:0xf
	v_mul_f32_dpp v125, v125, v125 row_shl:1 row_mask:0xf bank_mask:0xf
	v_fmac_f32_dpp v106, v106, v118 row_shl:1 row_mask:0xf bank_mask:0xf
	v_mul_f32_dpp v118, v118, v118 row_shl:1 row_mask:0xf bank_mask:0xf
	v_fmac_f32_dpp v107, v107, v119 row_shl:1 row_mask:0xf bank_mask:0xf
	v_mul_f32_dpp v119, v119, v119 row_shl:1 row_mask:0xf bank_mask:0xf
	v_fmac_f32_dpp v108, v108, v120 row_shl:1 row_mask:0xf bank_mask:0xf
	v_mul_f32_dpp v120, v120, v120 row_shl:1 row_mask:0xf bank_mask:0xf
	v_fmac_f32_dpp v109, v109, v121 row_shl:1 row_mask:0xf bank_mask:0xf
	v_mul_f32_dpp v121, v121, v121 row_shl:1 row_mask:0xf bank_mask:0xf
	v_fmac_f32_dpp v110, v110, v114 row_shl:1 row_mask:0xf bank_mask:0xf
	v_mul_f32_dpp v114, v114, v114 row_shl:1 row_mask:0xf bank_mask:0xf
	v_fmac_f32_dpp v111, v111, v115 row_shl:1 row_mask:0xf bank_mask:0xf
	v_mul_f32_dpp v115, v115, v115 row_shl:1 row_mask:0xf bank_mask:0xf
	v_fmac_f32_dpp v112, v112, v116 row_shl:1 row_mask:0xf bank_mask:0xf
	v_mul_f32_dpp v116, v116, v116 row_shl:1 row_mask:0xf bank_mask:0xf
	v_fmac_f32_dpp v113, v113, v117 row_shl:1 row_mask:0xf bank_mask:0xf
	v_mul_f32_dpp v117, v117, v117 row_shl:1 row_mask:0xf bank_mask:0xf
	v_fmac_f32_dpp v98, v98, v126 row_shl:2 row_mask:0xf bank_mask:0xf
	v_mul_f32_dpp v126, v126, v126 row_shl:2 row_mask:0xf bank_mask:0xf
	v_fmac_f32_dpp v99, v99, v127 row_shl:2 row_mask:0xf bank_mask:0xf
	v_mul_f32_dpp v127, v127, v127 row_shl:2 row_mask:0xf bank_mask:0xf
	v_fmac_f32_dpp v100, v100, v128 row_shl:2 row_mask:0xf bank_mask:0xf
	v_mul_f32_dpp v128, v128, v128 row_shl:2 row_mask:0xf bank_mask:0xf
	v_fmac_f32_dpp v101, v101, v129 row_shl:2 row_mask:0xf bank_mask:0xf
	v_mul_f32_dpp v129, v129, v129 row_shl:2 row_mask:0xf bank_mask:0xf
	v_fmac_f32_dpp v102, v102, v122 row_shl:2 row_mask:0xf bank_mask:0xf
	v_mul_f32_dpp v122, v122, v122 row_shl:2 row_mask:0xf bank_mask:0xf
	v_fmac_f32_dpp v103, v103, v123 row_shl:2 row_mask:0xf bank_mask:0xf
	v_mul_f32_dpp v123, v123, v123 row_shl:2 row_mask:0xf bank_mask:0xf
	v_fmac_f32_dpp v104, v104, v124 row_shl:2 row_mask:0xf bank_mask:0xf
	v_mul_f32_dpp v124, v124, v124 row_shl:2 row_mask:0xf bank_mask:0xf
	v_fmac_f32_dpp v105, v105, v125 row_shl:2 row_mask:0xf bank_mask:0xf
	v_mul_f32_dpp v125, v125, v125 row_shl:2 row_mask:0xf bank_mask:0xf
	v_fmac_f32_dpp v106, v106, v118 row_shl:2 row_mask:0xf bank_mask:0xf
	v_mul_f32_dpp v118, v118, v118 row_shl:2 row_mask:0xf bank_mask:0xf
	v_fmac_f32_dpp v107, v107, v119 row_shl:2 row_mask:0xf bank_mask:0xf
	v_mul_f32_dpp v119, v119, v119 row_shl:2 row_mask:0xf bank_mask:0xf
	v_fmac_f32_dpp v108, v108, v120 row_shl:2 row_mask:0xf bank_mask:0xf
	v_mul_f32_dpp v120, v120, v120 row_shl:2 row_mask:0xf bank_mask:0xf
	v_fmac_f32_dpp v109, v109, v121 row_shl:2 row_mask:0xf bank_mask:0xf
	v_mul_f32_dpp v121, v121, v121 row_shl:2 row_mask:0xf bank_mask:0xf
	v_fmac_f32_dpp v110, v110, v114 row_shl:2 row_mask:0xf bank_mask:0xf
	v_mul_f32_dpp v114, v114, v114 row_shl:2 row_mask:0xf bank_mask:0xf
	v_fmac_f32_dpp v111, v111, v115 row_shl:2 row_mask:0xf bank_mask:0xf
	v_mul_f32_dpp v115, v115, v115 row_shl:2 row_mask:0xf bank_mask:0xf
	v_fmac_f32_dpp v112, v112, v116 row_shl:2 row_mask:0xf bank_mask:0xf
	v_mul_f32_dpp v116, v116, v116 row_shl:2 row_mask:0xf bank_mask:0xf
	v_fmac_f32_dpp v113, v113, v117 row_shl:2 row_mask:0xf bank_mask:0xf
	v_mul_f32_dpp v117, v117, v117 row_shl:2 row_mask:0xf bank_mask:0xf
	v_fmac_f32_dpp v98, v98, v126 row_shl:4 row_mask:0xf bank_mask:0xf
	v_mul_f32_dpp v126, v126, v126 row_shl:4 row_mask:0xf bank_mask:0xf
	v_fmac_f32_dpp v99, v99, v127 row_shl:4 row_mask:0xf bank_mask:0xf
	v_mul_f32_dpp v127, v127, v127 row_shl:4 row_mask:0xf bank_mask:0xf
	v_fmac_f32_dpp v100, v100, v128 row_shl:4 row_mask:0xf bank_mask:0xf
	v_mul_f32_dpp v128, v128, v128 row_shl:4 row_mask:0xf bank_mask:0xf
	v_fmac_f32_dpp v101, v101, v129 row_shl:4 row_mask:0xf bank_mask:0xf
	v_mul_f32_dpp v129, v129, v129 row_shl:4 row_mask:0xf bank_mask:0xf
	v_fmac_f32_dpp v102, v102, v122 row_shl:4 row_mask:0xf bank_mask:0xf
	v_mul_f32_dpp v122, v122, v122 row_shl:4 row_mask:0xf bank_mask:0xf
	v_fmac_f32_dpp v103, v103, v123 row_shl:4 row_mask:0xf bank_mask:0xf
	v_mul_f32_dpp v123, v123, v123 row_shl:4 row_mask:0xf bank_mask:0xf
	v_fmac_f32_dpp v104, v104, v124 row_shl:4 row_mask:0xf bank_mask:0xf
	v_mul_f32_dpp v124, v124, v124 row_shl:4 row_mask:0xf bank_mask:0xf
	v_fmac_f32_dpp v105, v105, v125 row_shl:4 row_mask:0xf bank_mask:0xf
	v_mul_f32_dpp v125, v125, v125 row_shl:4 row_mask:0xf bank_mask:0xf
	v_fmac_f32_dpp v106, v106, v118 row_shl:4 row_mask:0xf bank_mask:0xf
	v_mul_f32_dpp v118, v118, v118 row_shl:4 row_mask:0xf bank_mask:0xf
	v_fmac_f32_dpp v107, v107, v119 row_shl:4 row_mask:0xf bank_mask:0xf
	v_mul_f32_dpp v119, v119, v119 row_shl:4 row_mask:0xf bank_mask:0xf
	v_fmac_f32_dpp v108, v108, v120 row_shl:4 row_mask:0xf bank_mask:0xf
	v_mul_f32_dpp v120, v120, v120 row_shl:4 row_mask:0xf bank_mask:0xf
	v_fmac_f32_dpp v109, v109, v121 row_shl:4 row_mask:0xf bank_mask:0xf
	v_mul_f32_dpp v121, v121, v121 row_shl:4 row_mask:0xf bank_mask:0xf
	v_fmac_f32_dpp v110, v110, v114 row_shl:4 row_mask:0xf bank_mask:0xf
	v_mul_f32_dpp v114, v114, v114 row_shl:4 row_mask:0xf bank_mask:0xf
	v_fmac_f32_dpp v111, v111, v115 row_shl:4 row_mask:0xf bank_mask:0xf
	v_mul_f32_dpp v115, v115, v115 row_shl:4 row_mask:0xf bank_mask:0xf
; __device__ __forceinline__ unsigned pk2(float lo, float hi) { return f2bf(lo) | (f2bf(hi) << 16); }
; #define SCAN_STEP(D) { const float ap = dppf<(BWD ? 0x100 : 0x110) + D>(1.f, av), hp = dppf<(BWD ? 0x100 : 0x110) + D>(0.f, hv); hv = fmaf(av, hp, hv); av = av * ap; }
;     template <bool BWD>
;     __device__ __forceinline__ void epi_dir(const f32x4 (&acc)[2][2][4][2], const Unit& u, int wr, int wc, int fr, int fq) const {
;     ...
;                     for (int j = 0; j < 4; ++j) { float av = A[m][j], hv = H[m][j];
;     ...
;                         SCAN_STEP(1) SCAN_STEP(2) SCAN_STEP(4) SCAN_STEP(8)
;     ...
;                         A[m][j] = av; H[m][j] = hv; }
; #pragma unroll
;                 for (int j = 0; j < 4; ++j) { float Ar = 1.f, Hr = 0.f;
; #pragma unroll
;                     for (int mm = 0; mm < 4; ++mm) { const int m = BWD ? 3 - mm : mm;
;                         H[m][j] = fmaf(A[m][j], Hr, H[m][j]); A[m][j] = A[m][j] * Ar;
;                         if (mm < 3) { Ar = __shfl(A[m][j], bsel); Hr = __shfl(H[m][j], bsel); } } }
; #pragma unroll
;                 for (int m = 0; m < 4; ++m) { u32x4 w; w.x = pk2(H[m][0], H[m][1]); w.y = pk2(H[m][2], H[m][3]); w.z = pk2(A[m][0], A[m][1]); w.w = pk2(A[m][2], A[m][3]);
;                     *(u32x4*)(Hb + ((size_t)(ai * 128 + m * 16) * 1024 + n * 16) * 4 + loffh) = w; }
;                 constexpr int me = BWD ? 0 : 3;
;                 if (fr == (BWD ? 0 : 15)) { const size_t o = (size_t)chunk * 1024 + gblk * 128 + n * 16;
;                     *(f32x4*)((char*)(AGG + (size_t)(dir * 2 + 0) * NB * NCHUNK * 1024 + o) + coff) = A[me];
;                     *(f32x4*)((char*)(AGG + (size_t)(dir * 2 + 1) * NB * NCHUNK * 1024 + o) + coff) = H[me]; }
	v_fmac_f32_dpp v112, v112, v116 row_shl:4 row_mask:0xf bank_mask:0xf
	v_mul_f32_dpp v116, v116, v116 row_shl:4 row_mask:0xf bank_mask:0xf
	v_fmac_f32_dpp v113, v113, v117 row_shl:4 row_mask:0xf bank_mask:0xf
	v_mul_f32_dpp v117, v117, v117 row_shl:4 row_mask:0xf bank_mask:0xf
	v_fmac_f32_dpp v98, v98, v126 row_shl:8 row_mask:0xf bank_mask:0xf
	v_mul_f32_dpp v126, v126, v126 row_shl:8 row_mask:0xf bank_mask:0xf
	v_fmac_f32_dpp v99, v99, v127 row_shl:8 row_mask:0xf bank_mask:0xf
	v_mul_f32_dpp v127, v127, v127 row_shl:8 row_mask:0xf bank_mask:0xf
	v_fmac_f32_dpp v100, v100, v128 row_shl:8 row_mask:0xf bank_mask:0xf
	v_mul_f32_dpp v128, v128, v128 row_shl:8 row_mask:0xf bank_mask:0xf
	v_fmac_f32_dpp v101, v101, v129 row_shl:8 row_mask:0xf bank_mask:0xf
	v_mul_f32_dpp v129, v129, v129 row_shl:8 row_mask:0xf bank_mask:0xf
	v_fmac_f32_dpp v102, v102, v122 row_shl:8 row_mask:0xf bank_mask:0xf
	v_mul_f32_dpp v122, v122, v122 row_shl:8 row_mask:0xf bank_mask:0xf
	v_fmac_f32_dpp v103, v103, v123 row_shl:8 row_mask:0xf bank_mask:0xf
	v_mul_f32_dpp v123, v123, v123 row_shl:8 row_mask:0xf bank_mask:0xf
	v_fmac_f32_dpp v104, v104, v124 row_shl:8 row_mask:0xf bank_mask:0xf
	v_mul_f32_dpp v124, v124, v124 row_shl:8 row_mask:0xf bank_mask:0xf
	v_fmac_f32_dpp v105, v105, v125 row_shl:8 row_mask:0xf bank_mask:0xf
	v_mul_f32_dpp v125, v125, v125 row_shl:8 row_mask:0xf bank_mask:0xf
	v_fmac_f32_dpp v106, v106, v118 row_shl:8 row_mask:0xf bank_mask:0xf
	v_mul_f32_dpp v118, v118, v118 row_shl:8 row_mask:0xf bank_mask:0xf
	v_fmac_f32_dpp v107, v107, v119 row_shl:8 row_mask:0xf bank_mask:0xf
	v_mul_f32_dpp v119, v119, v119 row_shl:8 row_mask:0xf bank_mask:0xf
	v_fmac_f32_dpp v108, v108, v120 row_shl:8 row_mask:0xf bank_mask:0xf
	v_mul_f32_dpp v120, v120, v120 row_shl:8 row_mask:0xf bank_mask:0xf
	v_fmac_f32_dpp v109, v109, v121 row_shl:8 row_mask:0xf bank_mask:0xf
	v_mul_f32_dpp v121, v121, v121 row_shl:8 row_mask:0xf bank_mask:0xf
	v_fmac_f32_dpp v110, v110, v114 row_shl:8 row_mask:0xf bank_mask:0xf
	v_mul_f32_dpp v114, v114, v114 row_shl:8 row_mask:0xf bank_mask:0xf
	v_fmac_f32_dpp v111, v111, v115 row_shl:8 row_mask:0xf bank_mask:0xf
	v_mul_f32_dpp v115, v115, v115 row_shl:8 row_mask:0xf bank_mask:0xf
	v_fmac_f32_dpp v112, v112, v116 row_shl:8 row_mask:0xf bank_mask:0xf
	v_mul_f32_dpp v116, v116, v116 row_shl:8 row_mask:0xf bank_mask:0xf
	v_fmac_f32_dpp v113, v113, v117 row_shl:8 row_mask:0xf bank_mask:0xf
	v_mul_f32_dpp v117, v117, v117 row_shl:8 row_mask:0xf bank_mask:0xf
	v_fmac_f32_dpp v106, v110, v118 row_newbcast:0 row_mask:0xf bank_mask:0xf
	v_mul_f32_dpp v118, v114, v118 row_newbcast:0 row_mask:0xf bank_mask:0xf
	v_fmac_f32_dpp v107, v111, v119 row_newbcast:0 row_mask:0xf bank_mask:0xf
	v_mul_f32_dpp v119, v115, v119 row_newbcast:0 row_mask:0xf bank_mask:0xf
	v_fmac_f32_dpp v108, v112, v120 row_newbcast:0 row_mask:0xf bank_mask:0xf
	v_mul_f32_dpp v120, v116, v120 row_newbcast:0 row_mask:0xf bank_mask:0xf
	v_fmac_f32_dpp v109, v113, v121 row_newbcast:0 row_mask:0xf bank_mask:0xf
	v_mul_f32_dpp v121, v117, v121 row_newbcast:0 row_mask:0xf bank_mask:0xf
	v_fmac_f32_dpp v102, v106, v122 row_newbcast:0 row_mask:0xf bank_mask:0xf
	v_mul_f32_dpp v122, v118, v122 row_newbcast:0 row_mask:0xf bank_mask:0xf
	v_fmac_f32_dpp v103, v107, v123 row_newbcast:0 row_mask:0xf bank_mask:0xf
	v_mul_f32_dpp v123, v119, v123 row_newbcast:0 row_mask:0xf bank_mask:0xf
	v_fmac_f32_dpp v104, v108, v124 row_newbcast:0 row_mask:0xf bank_mask:0xf
	v_mul_f32_dpp v124, v120, v124 row_newbcast:0 row_mask:0xf bank_mask:0xf
	v_fmac_f32_dpp v105, v109, v125 row_newbcast:0 row_mask:0xf bank_mask:0xf
	v_mul_f32_dpp v125, v121, v125 row_newbcast:0 row_mask:0xf bank_mask:0xf
	v_fmac_f32_dpp v98, v102, v126 row_newbcast:0 row_mask:0xf bank_mask:0xf
	v_mul_f32_dpp v126, v122, v126 row_newbcast:0 row_mask:0xf bank_mask:0xf
	v_fmac_f32_dpp v99, v103, v127 row_newbcast:0 row_mask:0xf bank_mask:0xf
	v_mul_f32_dpp v127, v123, v127 row_newbcast:0 row_mask:0xf bank_mask:0xf
	v_fmac_f32_dpp v100, v104, v128 row_newbcast:0 row_mask:0xf bank_mask:0xf
	v_mul_f32_dpp v128, v124, v128 row_newbcast:0 row_mask:0xf bank_mask:0xf
	v_fmac_f32_dpp v101, v105, v129 row_newbcast:0 row_mask:0xf bank_mask:0xf
	v_mul_f32_dpp v129, v125, v129 row_newbcast:0 row_mask:0xf bank_mask:0xf
	s_and_saveexec_b64 s[46:47], s[40:41]
	global_store_dwordx4 v187, v[126:129], s[14:15] sc1
	global_store_dwordx4 v187, v[98:101], s[10:11] sc1
	s_mov_b64 exec, s[46:47]
	v_cvt_pk_bf16_f32 v110, v110, v111
	v_cvt_pk_bf16_f32 v111, v112, v113
	v_cvt_pk_bf16_f32 v112, v114, v115
	v_cvt_pk_bf16_f32 v113, v116, v117
	global_store_dwordx4 v197, v[110:113], s[54:55] sc1
	v_cvt_pk_bf16_f32 v106, v106, v107
	v_cvt_pk_bf16_f32 v107, v108, v109
	v_cvt_pk_bf16_f32 v108, v118, v119
	v_cvt_pk_bf16_f32 v109, v120, v121
	global_store_dwordx4 v196, v[106:109], s[54:55] sc1
	v_cvt_pk_bf16_f32 v102, v102, v103
	v_cvt_pk_bf16_f32 v103, v104, v105
	v_cvt_pk_bf16_f32 v104, v122, v123
	v_cvt_pk_bf16_f32 v105, v124, v125
	global_store_dwordx4 v195, v[102:105], s[54:55] sc1
	v_cvt_pk_bf16_f32 v98, v98, v99
	v_cvt_pk_bf16_f32 v99, v100, v101
	v_cvt_pk_bf16_f32 v100, v126, v127
	v_cvt_pk_bf16_f32 v101, v128, v129
	global_store_dwordx4 v194, v[98:101], s[54:55] sc1
	s_add_u32 s26, s83, s12
	s_addc_u32 s27, s84, 0
	global_load_dwordx4 v[156:159], v228, s[26:27] offset:64
	s_add_u32 s26, s85, s12
	s_addc_u32 s27, s86, 0
	global_load_dwordx4 v[160:163], v228, s[26:27] offset:64
	s_add_u32 s26, s92, s12
	s_addc_u32 s27, s93, 0
	global_load_dwordx4 v[164:167], v228, s[26:27] offset:64
	global_load_dwordx2 v[168:169], v190, s[50:51] offset:32
	global_load_dwordx2 v[170:171], v191, s[50:51] offset:32
	global_load_dwordx2 v[172:173], v192, s[50:51] offset:32
	global_load_dwordx2 v[174:175], v193, s[50:51] offset:32
	s_waitcnt vmcnt(13)
; __device__ __forceinline__ float sigmoid_fast(float x) { return __builtin_amdgcn_rcpf(1.f + __expf(-x)); }
; __device__ __forceinline__ float one_minus_exp(float x) { const float p = -x * (1.f + x * (0.5f + x * (0.16666667f + x * (0.041666668f + x * 0.0083333338f)))); return x > -0.1f ? p : 1.f - __expf(x); }
;     template <bool BWD>
;     __device__ __forceinline__ void epi_dir(const f32x4 (&acc)[2][2][4][2], const Unit& u, int wr, int wc, int fr, int fq) const {
;     ...
;                 const f32x4 bav = *(const f32x4*)(bap + n * 64 + coff), bxv = *(const f32x4*)(bxp + n * 64 + coff), lsl = *(const f32x4*)(lmp + n * 64 + coff);
; #pragma unroll
;                 for (int m = 0; m < 4; ++m) {
;                     const u32x2 uw = *(const u32x2*)(Ub + ((size_t)(ai * 128 + m * 16) * 1024 + n * 16) * 2 + loffu);
;                     const float uv[4] = {bflo(uw.x), bfhi(uw.x), bflo(uw.y), bfhi(uw.y)};
; #pragma unroll
;                     for (int j = 0; j < 4; ++j) { const float r = sigmoid_fast(acc[ai][0][m][n][j] + bav[j]), ig = sigmoid_fast(acc[ai][1][m][n][j] + bxv[j]);
;                         const float la = r * lsl[j]; A[m][j] = __expf(la); H[m][j] = __builtin_amdgcn_sqrtf(one_minus_exp(2.f * la)) * (ig * uv[j]); } }
	v_add_f32_e32 v62, v62, v130
	v_add_f32_e32 v63, v63, v131
	v_add_f32_e32 v64, v64, v132
	v_add_f32_e32 v65, v65, v133
	v_add_f32_e32 v58, v58, v130
	v_add_f32_e32 v59, v59, v131
	v_add_f32_e32 v60, v60, v132
	v_add_f32_e32 v61, v61, v133
	v_mul_f32_e32 v62, 0xbfb8aa3b, v62
	v_mul_f32_e32 v63, 0xbfb8aa3b, v63
	v_mul_f32_e32 v64, 0xbfb8aa3b, v64
	v_mul_f32_e32 v65, 0xbfb8aa3b, v65
	v_mul_f32_e32 v58, 0xbfb8aa3b, v58
	v_mul_f32_e32 v59, 0xbfb8aa3b, v59
	v_mul_f32_e32 v60, 0xbfb8aa3b, v60
	v_mul_f32_e32 v61, 0xbfb8aa3b, v61
	v_exp_f32_e32 v62, v62
	v_exp_f32_e32 v63, v63
	v_exp_f32_e32 v64, v64
	v_exp_f32_e32 v65, v65
	v_exp_f32_e32 v58, v58
	v_exp_f32_e32 v59, v59
	v_exp_f32_e32 v60, v60
	v_exp_f32_e32 v61, v61
	v_add_f32_e32 v62, 1.0, v62
	v_add_f32_e32 v63, 1.0, v63
	v_add_f32_e32 v64, 1.0, v64
	v_add_f32_e32 v65, 1.0, v65
	v_add_f32_e32 v58, 1.0, v58
	v_add_f32_e32 v59, 1.0, v59
	v_add_f32_e32 v60, 1.0, v60
	v_add_f32_e32 v61, 1.0, v61
	v_rcp_f32_e32 v62, v62
	v_rcp_f32_e32 v63, v63
	v_rcp_f32_e32 v64, v64
	v_rcp_f32_e32 v65, v65
	v_rcp_f32_e32 v58, v58
	v_rcp_f32_e32 v59, v59
	v_rcp_f32_e32 v60, v60
	v_rcp_f32_e32 v61, v61
	v_mul_f32_e32 v62, v138, v62
	v_mul_f32_e32 v63, v139, v63
	v_mul_f32_e32 v64, v140, v64
	v_mul_f32_e32 v65, v141, v65
	v_mul_f32_e32 v58, v138, v58
	v_mul_f32_e32 v59, v139, v59
	v_mul_f32_e32 v60, v140, v60
	v_mul_f32_e32 v61, v141, v61
	v_add_f32_e32 v198, v62, v62
	v_add_f32_e32 v201, v63, v63
	v_add_f32_e32 v204, v64, v64
	v_add_f32_e32 v207, v65, v65
	v_add_f32_e32 v216, v58, v58
	v_add_f32_e32 v219, v59, v59
	v_add_f32_e32 v240, v60, v60
	v_add_f32_e32 v243, v61, v61
	v_mul_f32_e32 v199, 0x3fb8aa3b, v198
	v_mul_f32_e32 v202, 0x3fb8aa3b, v201
	v_mul_f32_e32 v205, 0x3fb8aa3b, v204
	v_mul_f32_e32 v208, 0x3fb8aa3b, v207
	v_mul_f32_e32 v217, 0x3fb8aa3b, v216
	v_mul_f32_e32 v238, 0x3fb8aa3b, v219
	v_mul_f32_e32 v241, 0x3fb8aa3b, v240
	v_mul_f32_e32 v244, 0x3fb8aa3b, v243
	v_exp_f32_e32 v199, v199
	v_exp_f32_e32 v202, v202
	v_exp_f32_e32 v205, v205
	v_exp_f32_e32 v208, v208
	v_exp_f32_e32 v217, v217
	v_exp_f32_e32 v238, v238
	v_exp_f32_e32 v241, v241
	v_exp_f32_e32 v244, v244
	v_fmamk_f32 v200, v198, 0x3c088889, v211
	v_fmamk_f32 v203, v201, 0x3c088889, v211
	v_fmamk_f32 v206, v204, 0x3c088889, v211
	v_fmamk_f32 v209, v207, 0x3c088889, v211
	v_fmamk_f32 v218, v216, 0x3c088889, v211
	v_fmamk_f32 v239, v219, 0x3c088889, v211
	v_fmamk_f32 v242, v240, 0x3c088889, v211
	v_fmamk_f32 v245, v243, 0x3c088889, v211
	v_sub_f32_e32 v199, 1.0, v199
	v_sub_f32_e32 v202, 1.0, v202
	v_sub_f32_e32 v205, 1.0, v205
	v_sub_f32_e32 v208, 1.0, v208
	v_sub_f32_e32 v217, 1.0, v217
	v_sub_f32_e32 v238, 1.0, v238
	v_sub_f32_e32 v241, 1.0, v241
	v_sub_f32_e32 v244, 1.0, v244
	v_fmaak_f32 v200, v198, v200, 0x3e2aaaab
	v_fmaak_f32 v203, v201, v203, 0x3e2aaaab
	v_fmaak_f32 v206, v204, v206, 0x3e2aaaab
	v_fmaak_f32 v209, v207, v209, 0x3e2aaaab
	v_fmaak_f32 v218, v216, v218, 0x3e2aaaab
	v_fmaak_f32 v239, v219, v239, 0x3e2aaaab
	v_fmaak_f32 v242, v240, v242, 0x3e2aaaab
	v_fmaak_f32 v245, v243, v245, 0x3e2aaaab
	v_fma_f32 v200, v198, v200, 0.5
	v_fma_f32 v203, v201, v203, 0.5
	v_fma_f32 v206, v204, v206, 0.5
	v_fma_f32 v209, v207, v209, 0.5
	v_fma_f32 v218, v216, v218, 0.5
	v_fma_f32 v239, v219, v239, 0.5
	v_fma_f32 v242, v240, v242, 0.5
	v_fma_f32 v245, v243, v245, 0.5
	v_fma_f32 v200, v198, v200, 1.0
	v_fma_f32 v203, v201, v203, 1.0
	v_fma_f32 v206, v204, v206, 1.0
	v_fma_f32 v209, v207, v209, 1.0
	v_fma_f32 v218, v216, v218, 1.0
	v_fma_f32 v239, v219, v239, 1.0
	v_fma_f32 v242, v240, v242, 1.0
	v_fma_f32 v245, v243, v245, 1.0
	v_mul_f32_e64 v200, v200, -v198
	v_mul_f32_e64 v203, v203, -v201
	v_mul_f32_e64 v206, v206, -v204
	v_mul_f32_e64 v209, v209, -v207
	v_mul_f32_e64 v218, v218, -v216
	v_mul_f32_e64 v239, v239, -v219
	v_mul_f32_e64 v242, v242, -v240
	v_mul_f32_e64 v245, v245, -v243
	v_cmp_nlt_f32_e32 vcc, s49, v198
	v_add_f32_e32 v34, v34, v134
	v_mul_f32_e32 v34, 0xbfb8aa3b, v34
	v_cndmask_b32_e32 v199, v200, v199, vcc
	v_cmp_nlt_f32_e32 vcc, s49, v201
	v_add_f32_e32 v35, v35, v135
	v_mul_f32_e32 v35, 0xbfb8aa3b, v35
	v_cndmask_b32_e32 v202, v203, v202, vcc
	v_cmp_nlt_f32_e32 vcc, s49, v204
	v_add_f32_e32 v36, v36, v136
	v_mul_f32_e32 v36, 0xbfb8aa3b, v36
	v_cndmask_b32_e32 v205, v206, v205, vcc
	v_cmp_nlt_f32_e32 vcc, s49, v207
	v_add_f32_e32 v37, v37, v137
	v_mul_f32_e32 v37, 0xbfb8aa3b, v37
	v_cndmask_b32_e32 v208, v209, v208, vcc
	v_cmp_nlt_f32_e32 vcc, s49, v216
	v_add_f32_e32 v38, v38, v134
	v_mul_f32_e32 v38, 0xbfb8aa3b, v38
	v_cndmask_b32_e32 v217, v218, v217, vcc
	v_cmp_nlt_f32_e32 vcc, s49, v219
	v_add_f32_e32 v39, v39, v135
	v_mul_f32_e32 v39, 0xbfb8aa3b, v39
	v_cndmask_b32_e32 v238, v239, v238, vcc
	v_cmp_nlt_f32_e32 vcc, s49, v240
	v_add_f32_e32 v40, v40, v136
	v_mul_f32_e32 v40, 0xbfb8aa3b, v40
	v_cndmask_b32_e32 v241, v242, v241, vcc
	v_cmp_nlt_f32_e32 vcc, s49, v243
	v_add_f32_e32 v41, v41, v137
	v_mul_f32_e32 v41, 0xbfb8aa3b, v41
	v_cndmask_b32_e32 v244, v245, v244, vcc
	v_exp_f32_e32 v34, v34
	v_exp_f32_e32 v35, v35
	v_exp_f32_e32 v36, v36
	v_exp_f32_e32 v37, v37
	v_exp_f32_e32 v38, v38
	v_exp_f32_e32 v39, v39
	v_exp_f32_e32 v40, v40
	v_exp_f32_e32 v41, v41
	v_sqrt_f32_e32 v199, v199
	v_sqrt_f32_e32 v202, v202
	v_sqrt_f32_e32 v205, v205
	v_sqrt_f32_e32 v208, v208
	v_sqrt_f32_e32 v217, v217
	v_sqrt_f32_e32 v238, v238
	v_sqrt_f32_e32 v241, v241
	v_sqrt_f32_e32 v244, v244
	v_add_f32_e32 v34, 1.0, v34
	v_add_f32_e32 v35, 1.0, v35
	v_add_f32_e32 v36, 1.0, v36
	v_add_f32_e32 v37, 1.0, v37
	v_add_f32_e32 v38, 1.0, v38
	v_add_f32_e32 v39, 1.0, v39
	v_add_f32_e32 v40, 1.0, v40
	v_add_f32_e32 v41, 1.0, v41
	v_lshlrev_b32_e32 v200, 16, v176
; __device__ __forceinline__ float sigmoid_fast(float x) { return __builtin_amdgcn_rcpf(1.f + __expf(-x)); }
; __device__ __forceinline__ float one_minus_exp(float x) { const float p = -x * (1.f + x * (0.5f + x * (0.16666667f + x * (0.041666668f + x * 0.0083333338f)))); return x > -0.1f ? p : 1.f - __expf(x); }
;     template <bool BWD>
;     __device__ __forceinline__ void epi_dir(const f32x4 (&acc)[2][2][4][2], const Unit& u, int wr, int wc, int fr, int fq) const {
;     ...
;                 const f32x4 bav = *(const f32x4*)(bap + n * 64 + coff), bxv = *(const f32x4*)(bxp + n * 64 + coff), lsl = *(const f32x4*)(lmp + n * 64 + coff);
; #pragma unroll
;                 for (int m = 0; m < 4; ++m) {
;                     const u32x2 uw = *(const u32x2*)(Ub + ((size_t)(ai * 128 + m * 16) * 1024 + n * 16) * 2 + loffu);
;                     const float uv[4] = {bflo(uw.x), bfhi(uw.x), bflo(uw.y), bfhi(uw.y)};
; #pragma unroll
;                     for (int j = 0; j < 4; ++j) { const float r = sigmoid_fast(acc[ai][0][m][n][j] + bav[j]), ig = sigmoid_fast(acc[ai][1][m][n][j] + bxv[j]);
;                         const float la = r * lsl[j]; A[m][j] = __expf(la); H[m][j] = __builtin_amdgcn_sqrtf(one_minus_exp(2.f * la)) * (ig * uv[j]); } }
	v_and_b32_e32 v203, 0xffff0000, v176
	v_lshlrev_b32_e32 v206, 16, v177
	v_and_b32_e32 v209, 0xffff0000, v177
	v_lshlrev_b32_e32 v218, 16, v178
	v_and_b32_e32 v239, 0xffff0000, v178
	v_lshlrev_b32_e32 v242, 16, v179
	v_and_b32_e32 v245, 0xffff0000, v179
	v_rcp_f32_e32 v34, v34
	v_rcp_f32_e32 v35, v35
	v_rcp_f32_e32 v36, v36
	v_rcp_f32_e32 v37, v37
	v_rcp_f32_e32 v38, v38
	v_rcp_f32_e32 v39, v39
	v_rcp_f32_e32 v40, v40
	v_rcp_f32_e32 v41, v41
	v_mul_f32_e32 v62, 0x3fb8aa3b, v62
	v_mul_f32_e32 v63, 0x3fb8aa3b, v63
	v_mul_f32_e32 v64, 0x3fb8aa3b, v64
	v_mul_f32_e32 v65, 0x3fb8aa3b, v65
	v_mul_f32_e32 v58, 0x3fb8aa3b, v58
	v_mul_f32_e32 v59, 0x3fb8aa3b, v59
	v_mul_f32_e32 v60, 0x3fb8aa3b, v60
	v_mul_f32_e32 v61, 0x3fb8aa3b, v61
	v_mul_f32_e32 v34, v34, v200
	v_mul_f32_e32 v35, v35, v203
	v_mul_f32_e32 v36, v36, v206
	v_mul_f32_e32 v37, v37, v209
	v_mul_f32_e32 v38, v38, v218
	v_mul_f32_e32 v39, v39, v239
	v_mul_f32_e32 v40, v40, v242
	v_mul_f32_e32 v41, v41, v245
	v_exp_f32_e32 v62, v62
	v_exp_f32_e32 v63, v63
	v_exp_f32_e32 v64, v64
	v_exp_f32_e32 v65, v65
	v_exp_f32_e32 v58, v58
	v_exp_f32_e32 v59, v59
	v_exp_f32_e32 v60, v60
	v_exp_f32_e32 v61, v61
	v_mul_f32_e32 v34, v34, v199
	v_mul_f32_e32 v35, v35, v202
	v_mul_f32_e32 v36, v36, v205
	v_mul_f32_e32 v37, v37, v208
	v_mul_f32_e32 v38, v38, v217
	v_mul_f32_e32 v39, v39, v238
	v_mul_f32_e32 v40, v40, v241
	v_mul_f32_e32 v41, v41, v244
	v_add_f32_e32 v54, v54, v130
	v_add_f32_e32 v55, v55, v131
	v_add_f32_e32 v56, v56, v132
	v_add_f32_e32 v57, v57, v133
	v_add_f32_e32 v50, v50, v130
	v_add_f32_e32 v51, v51, v131
	v_add_f32_e32 v52, v52, v132
	v_add_f32_e32 v53, v53, v133
	v_mul_f32_e32 v54, 0xbfb8aa3b, v54
	v_mul_f32_e32 v55, 0xbfb8aa3b, v55
	v_mul_f32_e32 v56, 0xbfb8aa3b, v56
	v_mul_f32_e32 v57, 0xbfb8aa3b, v57
	v_mul_f32_e32 v50, 0xbfb8aa3b, v50
	v_mul_f32_e32 v51, 0xbfb8aa3b, v51
	v_mul_f32_e32 v52, 0xbfb8aa3b, v52
	v_mul_f32_e32 v53, 0xbfb8aa3b, v53
	v_exp_f32_e32 v54, v54
	v_exp_f32_e32 v55, v55
	v_exp_f32_e32 v56, v56
	v_exp_f32_e32 v57, v57
	v_exp_f32_e32 v50, v50
	v_exp_f32_e32 v51, v51
	v_exp_f32_e32 v52, v52
	v_exp_f32_e32 v53, v53
	v_add_f32_e32 v54, 1.0, v54
	v_add_f32_e32 v55, 1.0, v55
	v_add_f32_e32 v56, 1.0, v56
	v_add_f32_e32 v57, 1.0, v57
	v_add_f32_e32 v50, 1.0, v50
	v_add_f32_e32 v51, 1.0, v51
	v_add_f32_e32 v52, 1.0, v52
	v_add_f32_e32 v53, 1.0, v53
	v_rcp_f32_e32 v54, v54
	v_rcp_f32_e32 v55, v55
	v_rcp_f32_e32 v56, v56
	v_rcp_f32_e32 v57, v57
	v_rcp_f32_e32 v50, v50
	v_rcp_f32_e32 v51, v51
	v_rcp_f32_e32 v52, v52
	v_rcp_f32_e32 v53, v53
	v_mul_f32_e32 v54, v138, v54
	v_mul_f32_e32 v55, v139, v55
	v_mul_f32_e32 v56, v140, v56
	v_mul_f32_e32 v57, v141, v57
	v_mul_f32_e32 v50, v138, v50
	v_mul_f32_e32 v51, v139, v51
	v_mul_f32_e32 v52, v140, v52
	v_mul_f32_e32 v53, v141, v53
	v_add_f32_e32 v198, v54, v54
	v_add_f32_e32 v201, v55, v55
	v_add_f32_e32 v204, v56, v56
	v_add_f32_e32 v207, v57, v57
	v_add_f32_e32 v216, v50, v50
	v_add_f32_e32 v219, v51, v51
	v_add_f32_e32 v240, v52, v52
	v_add_f32_e32 v243, v53, v53
	v_mul_f32_e32 v199, 0x3fb8aa3b, v198
	v_mul_f32_e32 v202, 0x3fb8aa3b, v201
	v_mul_f32_e32 v205, 0x3fb8aa3b, v204
	v_mul_f32_e32 v208, 0x3fb8aa3b, v207
	v_mul_f32_e32 v217, 0x3fb8aa3b, v216
	v_mul_f32_e32 v238, 0x3fb8aa3b, v219
	v_mul_f32_e32 v241, 0x3fb8aa3b, v240
	v_mul_f32_e32 v244, 0x3fb8aa3b, v243
	v_exp_f32_e32 v199, v199
	v_exp_f32_e32 v202, v202
	v_exp_f32_e32 v205, v205
	v_exp_f32_e32 v208, v208
	v_exp_f32_e32 v217, v217
	v_exp_f32_e32 v238, v238
	v_exp_f32_e32 v241, v241
	v_exp_f32_e32 v244, v244
	v_fmamk_f32 v200, v198, 0x3c088889, v211
	v_fmamk_f32 v203, v201, 0x3c088889, v211
	v_fmamk_f32 v206, v204, 0x3c088889, v211
	v_fmamk_f32 v209, v207, 0x3c088889, v211
	v_fmamk_f32 v218, v216, 0x3c088889, v211
	v_fmamk_f32 v239, v219, 0x3c088889, v211
	v_fmamk_f32 v242, v240, 0x3c088889, v211
	v_fmamk_f32 v245, v243, 0x3c088889, v211
	v_sub_f32_e32 v199, 1.0, v199
	v_sub_f32_e32 v202, 1.0, v202
	v_sub_f32_e32 v205, 1.0, v205
	v_sub_f32_e32 v208, 1.0, v208
	v_sub_f32_e32 v217, 1.0, v217
	v_sub_f32_e32 v238, 1.0, v238
	v_sub_f32_e32 v241, 1.0, v241
	v_sub_f32_e32 v244, 1.0, v244
	v_fmaak_f32 v200, v198, v200, 0x3e2aaaab
	v_fmaak_f32 v203, v201, v203, 0x3e2aaaab
	v_fmaak_f32 v206, v204, v206, 0x3e2aaaab
	v_fmaak_f32 v209, v207, v209, 0x3e2aaaab
	v_fmaak_f32 v218, v216, v218, 0x3e2aaaab
	v_fmaak_f32 v239, v219, v239, 0x3e2aaaab
	v_fmaak_f32 v242, v240, v242, 0x3e2aaaab
	v_fmaak_f32 v245, v243, v245, 0x3e2aaaab
	v_fma_f32 v200, v198, v200, 0.5
	v_fma_f32 v203, v201, v203, 0.5
	v_fma_f32 v206, v204, v206, 0.5
	v_fma_f32 v209, v207, v209, 0.5
	v_fma_f32 v218, v216, v218, 0.5
	v_fma_f32 v239, v219, v239, 0.5
	v_fma_f32 v242, v240, v242, 0.5
	v_fma_f32 v245, v243, v245, 0.5
	v_fma_f32 v200, v198, v200, 1.0
	v_fma_f32 v203, v201, v203, 1.0
	v_fma_f32 v206, v204, v206, 1.0
	v_fma_f32 v209, v207, v209, 1.0
	v_fma_f32 v218, v216, v218, 1.0
	v_fma_f32 v239, v219, v239, 1.0
	v_fma_f32 v242, v240, v242, 1.0
	v_fma_f32 v245, v243, v245, 1.0
	v_mul_f32_e64 v200, v200, -v198
	v_mul_f32_e64 v203, v203, -v201
	v_mul_f32_e64 v206, v206, -v204
	v_mul_f32_e64 v209, v209, -v207
	v_mul_f32_e64 v218, v218, -v216
	v_mul_f32_e64 v239, v239, -v219
	v_mul_f32_e64 v242, v242, -v240
	v_mul_f32_e64 v245, v245, -v243
	v_cmp_nlt_f32_e32 vcc, s49, v198
	v_add_f32_e32 v42, v42, v134
	v_mul_f32_e32 v42, 0xbfb8aa3b, v42
	v_cndmask_b32_e32 v199, v200, v199, vcc
	v_cmp_nlt_f32_e32 vcc, s49, v201
	v_add_f32_e32 v43, v43, v135
	v_mul_f32_e32 v43, 0xbfb8aa3b, v43
	v_cndmask_b32_e32 v202, v203, v202, vcc
	v_cmp_nlt_f32_e32 vcc, s49, v204
	v_add_f32_e32 v44, v44, v136
	v_mul_f32_e32 v44, 0xbfb8aa3b, v44
; __device__ __forceinline__ float sigmoid_fast(float x) { return __builtin_amdgcn_rcpf(1.f + __expf(-x)); }
; __device__ __forceinline__ float one_minus_exp(float x) { const float p = -x * (1.f + x * (0.5f + x * (0.16666667f + x * (0.041666668f + x * 0.0083333338f)))); return x > -0.1f ? p : 1.f - __expf(x); }
; #define SCAN_STEP(D) { const float ap = dppf<(BWD ? 0x100 : 0x110) + D>(1.f, av), hp = dppf<(BWD ? 0x100 : 0x110) + D>(0.f, hv); hv = fmaf(av, hp, hv); av = av * ap; }
;     template <bool BWD>
;     __device__ __forceinline__ void epi_dir(const f32x4 (&acc)[2][2][4][2], const Unit& u, int wr, int wc, int fr, int fq) const {
;     ...
;                     const u32x2 uw = *(const u32x2*)(Ub + ((size_t)(ai * 128 + m * 16) * 1024 + n * 16) * 2 + loffu);
;                     const float uv[4] = {bflo(uw.x), bfhi(uw.x), bflo(uw.y), bfhi(uw.y)};
; #pragma unroll
;                     for (int j = 0; j < 4; ++j) { const float r = sigmoid_fast(acc[ai][0][m][n][j] + bav[j]), ig = sigmoid_fast(acc[ai][1][m][n][j] + bxv[j]);
;                         const float la = r * lsl[j]; A[m][j] = __expf(la); H[m][j] = __builtin_amdgcn_sqrtf(one_minus_exp(2.f * la)) * (ig * uv[j]); } }
; #pragma unroll
;                 for (int m = 0; m < 4; ++m)
; #pragma unroll
;                     for (int j = 0; j < 4; ++j) { float av = A[m][j], hv = H[m][j];
;     ...
;                         SCAN_STEP(1) SCAN_STEP(2) SCAN_STEP(4) SCAN_STEP(8)
	v_cndmask_b32_e32 v205, v206, v205, vcc
	v_cmp_nlt_f32_e32 vcc, s49, v207
	v_add_f32_e32 v45, v45, v137
	v_mul_f32_e32 v45, 0xbfb8aa3b, v45
	v_cndmask_b32_e32 v208, v209, v208, vcc
	v_cmp_nlt_f32_e32 vcc, s49, v216
	v_add_f32_e32 v46, v46, v134
	v_mul_f32_e32 v46, 0xbfb8aa3b, v46
	v_cndmask_b32_e32 v217, v218, v217, vcc
	v_cmp_nlt_f32_e32 vcc, s49, v219
	v_add_f32_e32 v47, v47, v135
	v_mul_f32_e32 v47, 0xbfb8aa3b, v47
	v_cndmask_b32_e32 v238, v239, v238, vcc
	v_cmp_nlt_f32_e32 vcc, s49, v240
	v_add_f32_e32 v48, v48, v136
	v_mul_f32_e32 v48, 0xbfb8aa3b, v48
	v_cndmask_b32_e32 v241, v242, v241, vcc
	v_cmp_nlt_f32_e32 vcc, s49, v243
	v_add_f32_e32 v49, v49, v137
	v_mul_f32_e32 v49, 0xbfb8aa3b, v49
	v_cndmask_b32_e32 v244, v245, v244, vcc
	v_exp_f32_e32 v42, v42
	v_exp_f32_e32 v43, v43
	v_exp_f32_e32 v44, v44
	v_exp_f32_e32 v45, v45
	v_exp_f32_e32 v46, v46
	v_exp_f32_e32 v47, v47
	v_exp_f32_e32 v48, v48
	v_exp_f32_e32 v49, v49
	v_sqrt_f32_e32 v199, v199
	v_sqrt_f32_e32 v202, v202
	v_sqrt_f32_e32 v205, v205
	v_sqrt_f32_e32 v208, v208
	v_sqrt_f32_e32 v217, v217
	v_sqrt_f32_e32 v238, v238
	v_sqrt_f32_e32 v241, v241
	v_sqrt_f32_e32 v244, v244
	v_add_f32_e32 v42, 1.0, v42
	v_add_f32_e32 v43, 1.0, v43
	v_add_f32_e32 v44, 1.0, v44
	v_add_f32_e32 v45, 1.0, v45
	v_add_f32_e32 v46, 1.0, v46
	v_add_f32_e32 v47, 1.0, v47
	v_add_f32_e32 v48, 1.0, v48
	v_add_f32_e32 v49, 1.0, v49
	v_lshlrev_b32_e32 v200, 16, v182
	v_and_b32_e32 v203, 0xffff0000, v182
	v_lshlrev_b32_e32 v206, 16, v183
	v_and_b32_e32 v209, 0xffff0000, v183
	v_lshlrev_b32_e32 v218, 16, v184
	v_and_b32_e32 v239, 0xffff0000, v184
	v_lshlrev_b32_e32 v242, 16, v185
	v_and_b32_e32 v245, 0xffff0000, v185
	v_rcp_f32_e32 v42, v42
	v_rcp_f32_e32 v43, v43
	v_rcp_f32_e32 v44, v44
	v_rcp_f32_e32 v45, v45
	v_rcp_f32_e32 v46, v46
	v_rcp_f32_e32 v47, v47
	v_rcp_f32_e32 v48, v48
	v_rcp_f32_e32 v49, v49
	v_mul_f32_e32 v54, 0x3fb8aa3b, v54
	v_mul_f32_e32 v55, 0x3fb8aa3b, v55
	v_mul_f32_e32 v56, 0x3fb8aa3b, v56
	v_mul_f32_e32 v57, 0x3fb8aa3b, v57
	v_mul_f32_e32 v50, 0x3fb8aa3b, v50
	v_mul_f32_e32 v51, 0x3fb8aa3b, v51
	v_mul_f32_e32 v52, 0x3fb8aa3b, v52
	v_mul_f32_e32 v53, 0x3fb8aa3b, v53
	v_mul_f32_e32 v42, v42, v200
	v_mul_f32_e32 v43, v43, v203
	v_mul_f32_e32 v44, v44, v206
	v_mul_f32_e32 v45, v45, v209
	v_mul_f32_e32 v46, v46, v218
	v_mul_f32_e32 v47, v47, v239
	v_mul_f32_e32 v48, v48, v242
	v_mul_f32_e32 v49, v49, v245
	v_exp_f32_e32 v54, v54
	v_exp_f32_e32 v55, v55
	v_exp_f32_e32 v56, v56
	v_exp_f32_e32 v57, v57
	v_exp_f32_e32 v50, v50
	v_exp_f32_e32 v51, v51
	v_exp_f32_e32 v52, v52
	v_exp_f32_e32 v53, v53
	v_mul_f32_e32 v42, v42, v199
	v_mul_f32_e32 v43, v43, v202
	v_mul_f32_e32 v44, v44, v205
	v_mul_f32_e32 v45, v45, v208
	v_mul_f32_e32 v46, v46, v217
	v_mul_f32_e32 v47, v47, v238
	v_mul_f32_e32 v48, v48, v241
	v_mul_f32_e32 v49, v49, v244
	v_fmac_f32_dpp v34, v34, v62 row_shl:1 row_mask:0xf bank_mask:0xf
	v_mul_f32_dpp v62, v62, v62 row_shl:1 row_mask:0xf bank_mask:0xf
	v_fmac_f32_dpp v35, v35, v63 row_shl:1 row_mask:0xf bank_mask:0xf
	v_mul_f32_dpp v63, v63, v63 row_shl:1 row_mask:0xf bank_mask:0xf
	v_fmac_f32_dpp v36, v36, v64 row_shl:1 row_mask:0xf bank_mask:0xf
	v_mul_f32_dpp v64, v64, v64 row_shl:1 row_mask:0xf bank_mask:0xf
	v_fmac_f32_dpp v37, v37, v65 row_shl:1 row_mask:0xf bank_mask:0xf
	v_mul_f32_dpp v65, v65, v65 row_shl:1 row_mask:0xf bank_mask:0xf
	v_fmac_f32_dpp v38, v38, v58 row_shl:1 row_mask:0xf bank_mask:0xf
	v_mul_f32_dpp v58, v58, v58 row_shl:1 row_mask:0xf bank_mask:0xf
	v_fmac_f32_dpp v39, v39, v59 row_shl:1 row_mask:0xf bank_mask:0xf
	v_mul_f32_dpp v59, v59, v59 row_shl:1 row_mask:0xf bank_mask:0xf
	v_fmac_f32_dpp v40, v40, v60 row_shl:1 row_mask:0xf bank_mask:0xf
	v_mul_f32_dpp v60, v60, v60 row_shl:1 row_mask:0xf bank_mask:0xf
	v_fmac_f32_dpp v41, v41, v61 row_shl:1 row_mask:0xf bank_mask:0xf
	v_mul_f32_dpp v61, v61, v61 row_shl:1 row_mask:0xf bank_mask:0xf
	v_fmac_f32_dpp v42, v42, v54 row_shl:1 row_mask:0xf bank_mask:0xf
	v_mul_f32_dpp v54, v54, v54 row_shl:1 row_mask:0xf bank_mask:0xf
	v_fmac_f32_dpp v43, v43, v55 row_shl:1 row_mask:0xf bank_mask:0xf
	v_mul_f32_dpp v55, v55, v55 row_shl:1 row_mask:0xf bank_mask:0xf
	v_fmac_f32_dpp v44, v44, v56 row_shl:1 row_mask:0xf bank_mask:0xf
	v_mul_f32_dpp v56, v56, v56 row_shl:1 row_mask:0xf bank_mask:0xf
	v_fmac_f32_dpp v45, v45, v57 row_shl:1 row_mask:0xf bank_mask:0xf
	v_mul_f32_dpp v57, v57, v57 row_shl:1 row_mask:0xf bank_mask:0xf
	v_fmac_f32_dpp v46, v46, v50 row_shl:1 row_mask:0xf bank_mask:0xf
	v_mul_f32_dpp v50, v50, v50 row_shl:1 row_mask:0xf bank_mask:0xf
	v_fmac_f32_dpp v47, v47, v51 row_shl:1 row_mask:0xf bank_mask:0xf
	v_mul_f32_dpp v51, v51, v51 row_shl:1 row_mask:0xf bank_mask:0xf
	v_fmac_f32_dpp v48, v48, v52 row_shl:1 row_mask:0xf bank_mask:0xf
	v_mul_f32_dpp v52, v52, v52 row_shl:1 row_mask:0xf bank_mask:0xf
	v_fmac_f32_dpp v49, v49, v53 row_shl:1 row_mask:0xf bank_mask:0xf
	v_mul_f32_dpp v53, v53, v53 row_shl:1 row_mask:0xf bank_mask:0xf
	v_fmac_f32_dpp v34, v34, v62 row_shl:2 row_mask:0xf bank_mask:0xf
	v_mul_f32_dpp v62, v62, v62 row_shl:2 row_mask:0xf bank_mask:0xf
	v_fmac_f32_dpp v35, v35, v63 row_shl:2 row_mask:0xf bank_mask:0xf
	v_mul_f32_dpp v63, v63, v63 row_shl:2 row_mask:0xf bank_mask:0xf
	v_fmac_f32_dpp v36, v36, v64 row_shl:2 row_mask:0xf bank_mask:0xf
	v_mul_f32_dpp v64, v64, v64 row_shl:2 row_mask:0xf bank_mask:0xf
	v_fmac_f32_dpp v37, v37, v65 row_shl:2 row_mask:0xf bank_mask:0xf
	v_mul_f32_dpp v65, v65, v65 row_shl:2 row_mask:0xf bank_mask:0xf
	v_fmac_f32_dpp v38, v38, v58 row_shl:2 row_mask:0xf bank_mask:0xf
	v_mul_f32_dpp v58, v58, v58 row_shl:2 row_mask:0xf bank_mask:0xf
; #define SCAN_STEP(D) { const float ap = dppf<(BWD ? 0x100 : 0x110) + D>(1.f, av), hp = dppf<(BWD ? 0x100 : 0x110) + D>(0.f, hv); hv = fmaf(av, hp, hv); av = av * ap; }
;     template <bool BWD>
;     __device__ __forceinline__ void epi_dir(const f32x4 (&acc)[2][2][4][2], const Unit& u, int wr, int wc, int fr, int fq) const {
;     ...
;                     for (int j = 0; j < 4; ++j) { float av = A[m][j], hv = H[m][j];
;     ...
;                         SCAN_STEP(1) SCAN_STEP(2) SCAN_STEP(4) SCAN_STEP(8)
	v_fmac_f32_dpp v39, v39, v59 row_shl:2 row_mask:0xf bank_mask:0xf
	v_mul_f32_dpp v59, v59, v59 row_shl:2 row_mask:0xf bank_mask:0xf
	v_fmac_f32_dpp v40, v40, v60 row_shl:2 row_mask:0xf bank_mask:0xf
	v_mul_f32_dpp v60, v60, v60 row_shl:2 row_mask:0xf bank_mask:0xf
	v_fmac_f32_dpp v41, v41, v61 row_shl:2 row_mask:0xf bank_mask:0xf
	v_mul_f32_dpp v61, v61, v61 row_shl:2 row_mask:0xf bank_mask:0xf
	v_fmac_f32_dpp v42, v42, v54 row_shl:2 row_mask:0xf bank_mask:0xf
	v_mul_f32_dpp v54, v54, v54 row_shl:2 row_mask:0xf bank_mask:0xf
	v_fmac_f32_dpp v43, v43, v55 row_shl:2 row_mask:0xf bank_mask:0xf
	v_mul_f32_dpp v55, v55, v55 row_shl:2 row_mask:0xf bank_mask:0xf
	v_fmac_f32_dpp v44, v44, v56 row_shl:2 row_mask:0xf bank_mask:0xf
	v_mul_f32_dpp v56, v56, v56 row_shl:2 row_mask:0xf bank_mask:0xf
	v_fmac_f32_dpp v45, v45, v57 row_shl:2 row_mask:0xf bank_mask:0xf
	v_mul_f32_dpp v57, v57, v57 row_shl:2 row_mask:0xf bank_mask:0xf
	v_fmac_f32_dpp v46, v46, v50 row_shl:2 row_mask:0xf bank_mask:0xf
	v_mul_f32_dpp v50, v50, v50 row_shl:2 row_mask:0xf bank_mask:0xf
	v_fmac_f32_dpp v47, v47, v51 row_shl:2 row_mask:0xf bank_mask:0xf
	v_mul_f32_dpp v51, v51, v51 row_shl:2 row_mask:0xf bank_mask:0xf
	v_fmac_f32_dpp v48, v48, v52 row_shl:2 row_mask:0xf bank_mask:0xf
	v_mul_f32_dpp v52, v52, v52 row_shl:2 row_mask:0xf bank_mask:0xf
	v_fmac_f32_dpp v49, v49, v53 row_shl:2 row_mask:0xf bank_mask:0xf
	v_mul_f32_dpp v53, v53, v53 row_shl:2 row_mask:0xf bank_mask:0xf
	v_fmac_f32_dpp v34, v34, v62 row_shl:4 row_mask:0xf bank_mask:0xf
	v_mul_f32_dpp v62, v62, v62 row_shl:4 row_mask:0xf bank_mask:0xf
	v_fmac_f32_dpp v35, v35, v63 row_shl:4 row_mask:0xf bank_mask:0xf
	v_mul_f32_dpp v63, v63, v63 row_shl:4 row_mask:0xf bank_mask:0xf
	v_fmac_f32_dpp v36, v36, v64 row_shl:4 row_mask:0xf bank_mask:0xf
	v_mul_f32_dpp v64, v64, v64 row_shl:4 row_mask:0xf bank_mask:0xf
	v_fmac_f32_dpp v37, v37, v65 row_shl:4 row_mask:0xf bank_mask:0xf
	v_mul_f32_dpp v65, v65, v65 row_shl:4 row_mask:0xf bank_mask:0xf
	v_fmac_f32_dpp v38, v38, v58 row_shl:4 row_mask:0xf bank_mask:0xf
	v_mul_f32_dpp v58, v58, v58 row_shl:4 row_mask:0xf bank_mask:0xf
	v_fmac_f32_dpp v39, v39, v59 row_shl:4 row_mask:0xf bank_mask:0xf
	v_mul_f32_dpp v59, v59, v59 row_shl:4 row_mask:0xf bank_mask:0xf
	v_fmac_f32_dpp v40, v40, v60 row_shl:4 row_mask:0xf bank_mask:0xf
	v_mul_f32_dpp v60, v60, v60 row_shl:4 row_mask:0xf bank_mask:0xf
	v_fmac_f32_dpp v41, v41, v61 row_shl:4 row_mask:0xf bank_mask:0xf
	v_mul_f32_dpp v61, v61, v61 row_shl:4 row_mask:0xf bank_mask:0xf
	v_fmac_f32_dpp v42, v42, v54 row_shl:4 row_mask:0xf bank_mask:0xf
	v_mul_f32_dpp v54, v54, v54 row_shl:4 row_mask:0xf bank_mask:0xf
	v_fmac_f32_dpp v43, v43, v55 row_shl:4 row_mask:0xf bank_mask:0xf
	v_mul_f32_dpp v55, v55, v55 row_shl:4 row_mask:0xf bank_mask:0xf
	v_fmac_f32_dpp v44, v44, v56 row_shl:4 row_mask:0xf bank_mask:0xf
	v_mul_f32_dpp v56, v56, v56 row_shl:4 row_mask:0xf bank_mask:0xf
	v_fmac_f32_dpp v45, v45, v57 row_shl:4 row_mask:0xf bank_mask:0xf
	v_mul_f32_dpp v57, v57, v57 row_shl:4 row_mask:0xf bank_mask:0xf
	v_fmac_f32_dpp v46, v46, v50 row_shl:4 row_mask:0xf bank_mask:0xf
	v_mul_f32_dpp v50, v50, v50 row_shl:4 row_mask:0xf bank_mask:0xf
	v_fmac_f32_dpp v47, v47, v51 row_shl:4 row_mask:0xf bank_mask:0xf
	v_mul_f32_dpp v51, v51, v51 row_shl:4 row_mask:0xf bank_mask:0xf
	v_fmac_f32_dpp v48, v48, v52 row_shl:4 row_mask:0xf bank_mask:0xf
	v_mul_f32_dpp v52, v52, v52 row_shl:4 row_mask:0xf bank_mask:0xf
	v_fmac_f32_dpp v49, v49, v53 row_shl:4 row_mask:0xf bank_mask:0xf
	v_mul_f32_dpp v53, v53, v53 row_shl:4 row_mask:0xf bank_mask:0xf
	v_fmac_f32_dpp v34, v34, v62 row_shl:8 row_mask:0xf bank_mask:0xf
	v_mul_f32_dpp v62, v62, v62 row_shl:8 row_mask:0xf bank_mask:0xf
	v_fmac_f32_dpp v35, v35, v63 row_shl:8 row_mask:0xf bank_mask:0xf
	v_mul_f32_dpp v63, v63, v63 row_shl:8 row_mask:0xf bank_mask:0xf
	v_fmac_f32_dpp v36, v36, v64 row_shl:8 row_mask:0xf bank_mask:0xf
	v_mul_f32_dpp v64, v64, v64 row_shl:8 row_mask:0xf bank_mask:0xf
	v_fmac_f32_dpp v37, v37, v65 row_shl:8 row_mask:0xf bank_mask:0xf
	v_mul_f32_dpp v65, v65, v65 row_shl:8 row_mask:0xf bank_mask:0xf
	v_fmac_f32_dpp v38, v38, v58 row_shl:8 row_mask:0xf bank_mask:0xf
	v_mul_f32_dpp v58, v58, v58 row_shl:8 row_mask:0xf bank_mask:0xf
	v_fmac_f32_dpp v39, v39, v59 row_shl:8 row_mask:0xf bank_mask:0xf
	v_mul_f32_dpp v59, v59, v59 row_shl:8 row_mask:0xf bank_mask:0xf
	v_fmac_f32_dpp v40, v40, v60 row_shl:8 row_mask:0xf bank_mask:0xf
	v_mul_f32_dpp v60, v60, v60 row_shl:8 row_mask:0xf bank_mask:0xf
	v_fmac_f32_dpp v41, v41, v61 row_shl:8 row_mask:0xf bank_mask:0xf
	v_mul_f32_dpp v61, v61, v61 row_shl:8 row_mask:0xf bank_mask:0xf
	v_fmac_f32_dpp v42, v42, v54 row_shl:8 row_mask:0xf bank_mask:0xf
	v_mul_f32_dpp v54, v54, v54 row_shl:8 row_mask:0xf bank_mask:0xf
	v_fmac_f32_dpp v43, v43, v55 row_shl:8 row_mask:0xf bank_mask:0xf
	v_mul_f32_dpp v55, v55, v55 row_shl:8 row_mask:0xf bank_mask:0xf
	v_fmac_f32_dpp v44, v44, v56 row_shl:8 row_mask:0xf bank_mask:0xf
	v_mul_f32_dpp v56, v56, v56 row_shl:8 row_mask:0xf bank_mask:0xf
	v_fmac_f32_dpp v45, v45, v57 row_shl:8 row_mask:0xf bank_mask:0xf
	v_mul_f32_dpp v57, v57, v57 row_shl:8 row_mask:0xf bank_mask:0xf
	v_fmac_f32_dpp v46, v46, v50 row_shl:8 row_mask:0xf bank_mask:0xf
	v_mul_f32_dpp v50, v50, v50 row_shl:8 row_mask:0xf bank_mask:0xf
	v_fmac_f32_dpp v47, v47, v51 row_shl:8 row_mask:0xf bank_mask:0xf
	v_mul_f32_dpp v51, v51, v51 row_shl:8 row_mask:0xf bank_mask:0xf
	v_fmac_f32_dpp v48, v48, v52 row_shl:8 row_mask:0xf bank_mask:0xf
	v_mul_f32_dpp v52, v52, v52 row_shl:8 row_mask:0xf bank_mask:0xf
	v_fmac_f32_dpp v49, v49, v53 row_shl:8 row_mask:0xf bank_mask:0xf
; __device__ __forceinline__ unsigned pk2(float lo, float hi) { return f2bf(lo) | (f2bf(hi) << 16); }
; #define SCAN_STEP(D) { const float ap = dppf<(BWD ? 0x100 : 0x110) + D>(1.f, av), hp = dppf<(BWD ? 0x100 : 0x110) + D>(0.f, hv); hv = fmaf(av, hp, hv); av = av * ap; }
;     template <bool BWD>
;     __device__ __forceinline__ void epi_dir(const f32x4 (&acc)[2][2][4][2], const Unit& u, int wr, int wc, int fr, int fq) const {
;     ...
;                     for (int j = 0; j < 4; ++j) { float av = A[m][j], hv = H[m][j];
;     ...
;                         SCAN_STEP(1) SCAN_STEP(2) SCAN_STEP(4) SCAN_STEP(8)
;     ...
;                         A[m][j] = av; H[m][j] = hv; }
; #pragma unroll
;                 for (int j = 0; j < 4; ++j) { float Ar = 1.f, Hr = 0.f;
; #pragma unroll
;                     for (int mm = 0; mm < 4; ++mm) { const int m = BWD ? 3 - mm : mm;
;                         H[m][j] = fmaf(A[m][j], Hr, H[m][j]); A[m][j] = A[m][j] * Ar;
;                         if (mm < 3) { Ar = __shfl(A[m][j], bsel); Hr = __shfl(H[m][j], bsel); } } }
; #pragma unroll
;                 for (int m = 0; m < 4; ++m) { u32x4 w; w.x = pk2(H[m][0], H[m][1]); w.y = pk2(H[m][2], H[m][3]); w.z = pk2(A[m][0], A[m][1]); w.w = pk2(A[m][2], A[m][3]);
;                     *(u32x4*)(Hb + ((size_t)(ai * 128 + m * 16) * 1024 + n * 16) * 4 + loffh) = w; }
;                 constexpr int me = BWD ? 0 : 3;
;                 if (fr == (BWD ? 0 : 15)) { const size_t o = (size_t)chunk * 1024 + gblk * 128 + n * 16;
;                     *(f32x4*)((char*)(AGG + (size_t)(dir * 2 + 0) * NB * NCHUNK * 1024 + o) + coff) = A[me];
;                     *(f32x4*)((char*)(AGG + (size_t)(dir * 2 + 1) * NB * NCHUNK * 1024 + o) + coff) = H[me]; }
	v_mul_f32_dpp v53, v53, v53 row_shl:8 row_mask:0xf bank_mask:0xf
	v_fmac_f32_dpp v42, v46, v54 row_newbcast:0 row_mask:0xf bank_mask:0xf
	v_mul_f32_dpp v54, v50, v54 row_newbcast:0 row_mask:0xf bank_mask:0xf
	v_fmac_f32_dpp v43, v47, v55 row_newbcast:0 row_mask:0xf bank_mask:0xf
	v_mul_f32_dpp v55, v51, v55 row_newbcast:0 row_mask:0xf bank_mask:0xf
	v_fmac_f32_dpp v44, v48, v56 row_newbcast:0 row_mask:0xf bank_mask:0xf
	v_mul_f32_dpp v56, v52, v56 row_newbcast:0 row_mask:0xf bank_mask:0xf
	v_fmac_f32_dpp v45, v49, v57 row_newbcast:0 row_mask:0xf bank_mask:0xf
	v_mul_f32_dpp v57, v53, v57 row_newbcast:0 row_mask:0xf bank_mask:0xf
	v_fmac_f32_dpp v38, v42, v58 row_newbcast:0 row_mask:0xf bank_mask:0xf
	v_mul_f32_dpp v58, v54, v58 row_newbcast:0 row_mask:0xf bank_mask:0xf
	v_fmac_f32_dpp v39, v43, v59 row_newbcast:0 row_mask:0xf bank_mask:0xf
	v_mul_f32_dpp v59, v55, v59 row_newbcast:0 row_mask:0xf bank_mask:0xf
	v_fmac_f32_dpp v40, v44, v60 row_newbcast:0 row_mask:0xf bank_mask:0xf
	v_mul_f32_dpp v60, v56, v60 row_newbcast:0 row_mask:0xf bank_mask:0xf
	v_fmac_f32_dpp v41, v45, v61 row_newbcast:0 row_mask:0xf bank_mask:0xf
	v_mul_f32_dpp v61, v57, v61 row_newbcast:0 row_mask:0xf bank_mask:0xf
	v_fmac_f32_dpp v34, v38, v62 row_newbcast:0 row_mask:0xf bank_mask:0xf
	v_mul_f32_dpp v62, v58, v62 row_newbcast:0 row_mask:0xf bank_mask:0xf
	v_fmac_f32_dpp v35, v39, v63 row_newbcast:0 row_mask:0xf bank_mask:0xf
	v_mul_f32_dpp v63, v59, v63 row_newbcast:0 row_mask:0xf bank_mask:0xf
	v_fmac_f32_dpp v36, v40, v64 row_newbcast:0 row_mask:0xf bank_mask:0xf
	v_mul_f32_dpp v64, v60, v64 row_newbcast:0 row_mask:0xf bank_mask:0xf
	v_fmac_f32_dpp v37, v41, v65 row_newbcast:0 row_mask:0xf bank_mask:0xf
	v_mul_f32_dpp v65, v61, v65 row_newbcast:0 row_mask:0xf bank_mask:0xf
	s_and_saveexec_b64 s[46:47], s[40:41]
	global_store_dwordx4 v188, v[62:65], s[14:15] sc1
	global_store_dwordx4 v188, v[34:37], s[10:11] sc1
	s_mov_b64 exec, s[46:47]
	v_cvt_pk_bf16_f32 v46, v46, v47
	v_cvt_pk_bf16_f32 v47, v48, v49
	v_cvt_pk_bf16_f32 v48, v50, v51
	v_cvt_pk_bf16_f32 v49, v52, v53
	global_store_dwordx4 v197, v[46:49], s[56:57] sc1
	v_cvt_pk_bf16_f32 v42, v42, v43
	v_cvt_pk_bf16_f32 v43, v44, v45
	v_cvt_pk_bf16_f32 v44, v54, v55
	v_cvt_pk_bf16_f32 v45, v56, v57
	global_store_dwordx4 v196, v[42:45], s[56:57] sc1
	v_cvt_pk_bf16_f32 v38, v38, v39
	v_cvt_pk_bf16_f32 v39, v40, v41
	v_cvt_pk_bf16_f32 v40, v58, v59
	v_cvt_pk_bf16_f32 v41, v60, v61
	global_store_dwordx4 v195, v[38:41], s[56:57] sc1
	v_cvt_pk_bf16_f32 v34, v34, v35
	v_cvt_pk_bf16_f32 v35, v36, v37
	v_cvt_pk_bf16_f32 v36, v62, v63
	v_cvt_pk_bf16_f32 v37, v64, v65
	global_store_dwordx4 v194, v[34:37], s[56:57] sc1
	global_load_dwordx2 v[176:177], v190, s[52:53] offset:32
	global_load_dwordx2 v[178:179], v191, s[52:53] offset:32
	global_load_dwordx2 v[182:183], v192, s[52:53] offset:32
	global_load_dwordx2 v[184:185], v193, s[52:53] offset:32
	s_waitcnt vmcnt(10)
	v_add_f32_e32 v94, v94, v156
	v_add_f32_e32 v95, v95, v157
	v_add_f32_e32 v96, v96, v158
	v_add_f32_e32 v97, v97, v159
	v_add_f32_e32 v90, v90, v156
	v_add_f32_e32 v91, v91, v157
	v_add_f32_e32 v92, v92, v158
	v_add_f32_e32 v93, v93, v159
	v_mul_f32_e32 v94, 0xbfb8aa3b, v94
	v_mul_f32_e32 v95, 0xbfb8aa3b, v95
	v_mul_f32_e32 v96, 0xbfb8aa3b, v96
	v_mul_f32_e32 v97, 0xbfb8aa3b, v97
	v_mul_f32_e32 v90, 0xbfb8aa3b, v90
	v_mul_f32_e32 v91, 0xbfb8aa3b, v91
	v_mul_f32_e32 v92, 0xbfb8aa3b, v92
	v_mul_f32_e32 v93, 0xbfb8aa3b, v93
	v_exp_f32_e32 v94, v94
	v_exp_f32_e32 v95, v95
	v_exp_f32_e32 v96, v96
	v_exp_f32_e32 v97, v97
	v_exp_f32_e32 v90, v90
	v_exp_f32_e32 v91, v91
	v_exp_f32_e32 v92, v92
	v_exp_f32_e32 v93, v93
	v_add_f32_e32 v94, 1.0, v94
	v_add_f32_e32 v95, 1.0, v95
	v_add_f32_e32 v96, 1.0, v96
	v_add_f32_e32 v97, 1.0, v97
	v_add_f32_e32 v90, 1.0, v90
	v_add_f32_e32 v91, 1.0, v91
	v_add_f32_e32 v92, 1.0, v92
	v_add_f32_e32 v93, 1.0, v93
	v_rcp_f32_e32 v94, v94
	v_rcp_f32_e32 v95, v95
	v_rcp_f32_e32 v96, v96
	v_rcp_f32_e32 v97, v97
	v_rcp_f32_e32 v90, v90
	v_rcp_f32_e32 v91, v91
	v_rcp_f32_e32 v92, v92
	v_rcp_f32_e32 v93, v93
	v_mul_f32_e32 v94, v164, v94
	v_mul_f32_e32 v95, v165, v95
	v_mul_f32_e32 v96, v166, v96
	v_mul_f32_e32 v97, v167, v97
	v_mul_f32_e32 v90, v164, v90
	v_mul_f32_e32 v91, v165, v91
	v_mul_f32_e32 v92, v166, v92
	v_mul_f32_e32 v93, v167, v93
	v_add_f32_e32 v198, v94, v94
	v_add_f32_e32 v201, v95, v95
	v_add_f32_e32 v204, v96, v96
	v_add_f32_e32 v207, v97, v97
	v_add_f32_e32 v216, v90, v90
	v_add_f32_e32 v219, v91, v91
	v_add_f32_e32 v240, v92, v92
	v_add_f32_e32 v243, v93, v93
	v_mul_f32_e32 v199, 0x3fb8aa3b, v198
	v_mul_f32_e32 v202, 0x3fb8aa3b, v201
	v_mul_f32_e32 v205, 0x3fb8aa3b, v204
	v_mul_f32_e32 v208, 0x3fb8aa3b, v207
	v_mul_f32_e32 v217, 0x3fb8aa3b, v216
	v_mul_f32_e32 v238, 0x3fb8aa3b, v219
	v_mul_f32_e32 v241, 0x3fb8aa3b, v240
	v_mul_f32_e32 v244, 0x3fb8aa3b, v243
	v_exp_f32_e32 v199, v199
	v_exp_f32_e32 v202, v202
	v_exp_f32_e32 v205, v205
	v_exp_f32_e32 v208, v208
	v_exp_f32_e32 v217, v217
	v_exp_f32_e32 v238, v238
	v_exp_f32_e32 v241, v241
	v_exp_f32_e32 v244, v244
	v_fmamk_f32 v200, v198, 0x3c088889, v211
	v_fmamk_f32 v203, v201, 0x3c088889, v211
	v_fmamk_f32 v206, v204, 0x3c088889, v211
	v_fmamk_f32 v209, v207, 0x3c088889, v211
	v_fmamk_f32 v218, v216, 0x3c088889, v211
	v_fmamk_f32 v239, v219, 0x3c088889, v211
	v_fmamk_f32 v242, v240, 0x3c088889, v211
	v_fmamk_f32 v245, v243, 0x3c088889, v211
	v_sub_f32_e32 v199, 1.0, v199
	v_sub_f32_e32 v202, 1.0, v202
	v_sub_f32_e32 v205, 1.0, v205
	v_sub_f32_e32 v208, 1.0, v208
	v_sub_f32_e32 v217, 1.0, v217
	v_sub_f32_e32 v238, 1.0, v238
	v_sub_f32_e32 v241, 1.0, v241
	v_sub_f32_e32 v244, 1.0, v244
; __device__ __forceinline__ float sigmoid_fast(float x) { return __builtin_amdgcn_rcpf(1.f + __expf(-x)); }
; __device__ __forceinline__ float one_minus_exp(float x) { const float p = -x * (1.f + x * (0.5f + x * (0.16666667f + x * (0.041666668f + x * 0.0083333338f)))); return x > -0.1f ? p : 1.f - __expf(x); }
;     template <bool BWD>
;     __device__ __forceinline__ void epi_dir(const f32x4 (&acc)[2][2][4][2], const Unit& u, int wr, int wc, int fr, int fq) const {
;     ...
;                 const f32x4 bav = *(const f32x4*)(bap + n * 64 + coff), bxv = *(const f32x4*)(bxp + n * 64 + coff), lsl = *(const f32x4*)(lmp + n * 64 + coff);
; #pragma unroll
;                 for (int m = 0; m < 4; ++m) {
;                     const u32x2 uw = *(const u32x2*)(Ub + ((size_t)(ai * 128 + m * 16) * 1024 + n * 16) * 2 + loffu);
;                     const float uv[4] = {bflo(uw.x), bfhi(uw.x), bflo(uw.y), bfhi(uw.y)};
; #pragma unroll
;                     for (int j = 0; j < 4; ++j) { const float r = sigmoid_fast(acc[ai][0][m][n][j] + bav[j]), ig = sigmoid_fast(acc[ai][1][m][n][j] + bxv[j]);
;                         const float la = r * lsl[j]; A[m][j] = __expf(la); H[m][j] = __builtin_amdgcn_sqrtf(one_minus_exp(2.f * la)) * (ig * uv[j]); } }
	v_fmaak_f32 v200, v198, v200, 0x3e2aaaab
	v_fmaak_f32 v203, v201, v203, 0x3e2aaaab
	v_fmaak_f32 v206, v204, v206, 0x3e2aaaab
	v_fmaak_f32 v209, v207, v209, 0x3e2aaaab
	v_fmaak_f32 v218, v216, v218, 0x3e2aaaab
	v_fmaak_f32 v239, v219, v239, 0x3e2aaaab
	v_fmaak_f32 v242, v240, v242, 0x3e2aaaab
	v_fmaak_f32 v245, v243, v245, 0x3e2aaaab
	v_fma_f32 v200, v198, v200, 0.5
	v_fma_f32 v203, v201, v203, 0.5
	v_fma_f32 v206, v204, v206, 0.5
	v_fma_f32 v209, v207, v209, 0.5
	v_fma_f32 v218, v216, v218, 0.5
	v_fma_f32 v239, v219, v239, 0.5
	v_fma_f32 v242, v240, v242, 0.5
	v_fma_f32 v245, v243, v245, 0.5
	v_fma_f32 v200, v198, v200, 1.0
	v_fma_f32 v203, v201, v203, 1.0
	v_fma_f32 v206, v204, v206, 1.0
	v_fma_f32 v209, v207, v209, 1.0
	v_fma_f32 v218, v216, v218, 1.0
	v_fma_f32 v239, v219, v239, 1.0
	v_fma_f32 v242, v240, v242, 1.0
	v_fma_f32 v245, v243, v245, 1.0
	v_mul_f32_e64 v200, v200, -v198
	v_mul_f32_e64 v203, v203, -v201
	v_mul_f32_e64 v206, v206, -v204
	v_mul_f32_e64 v209, v209, -v207
	v_mul_f32_e64 v218, v218, -v216
	v_mul_f32_e64 v239, v239, -v219
	v_mul_f32_e64 v242, v242, -v240
	v_mul_f32_e64 v245, v245, -v243
	v_cmp_nlt_f32_e32 vcc, s49, v198
	v_add_f32_e32 v66, v66, v160
	v_mul_f32_e32 v66, 0xbfb8aa3b, v66
	v_cndmask_b32_e32 v199, v200, v199, vcc
	v_cmp_nlt_f32_e32 vcc, s49, v201
	v_add_f32_e32 v67, v67, v161
	v_mul_f32_e32 v67, 0xbfb8aa3b, v67
	v_cndmask_b32_e32 v202, v203, v202, vcc
	v_cmp_nlt_f32_e32 vcc, s49, v204
	v_add_f32_e32 v68, v68, v162
	v_mul_f32_e32 v68, 0xbfb8aa3b, v68
	v_cndmask_b32_e32 v205, v206, v205, vcc
	v_cmp_nlt_f32_e32 vcc, s49, v207
	v_add_f32_e32 v69, v69, v163
	v_mul_f32_e32 v69, 0xbfb8aa3b, v69
	v_cndmask_b32_e32 v208, v209, v208, vcc
	v_cmp_nlt_f32_e32 vcc, s49, v216
	v_add_f32_e32 v70, v70, v160
	v_mul_f32_e32 v70, 0xbfb8aa3b, v70
	v_cndmask_b32_e32 v217, v218, v217, vcc
	v_cmp_nlt_f32_e32 vcc, s49, v219
	v_add_f32_e32 v71, v71, v161
	v_mul_f32_e32 v71, 0xbfb8aa3b, v71
	v_cndmask_b32_e32 v238, v239, v238, vcc
	v_cmp_nlt_f32_e32 vcc, s49, v240
	v_add_f32_e32 v72, v72, v162
	v_mul_f32_e32 v72, 0xbfb8aa3b, v72
	v_cndmask_b32_e32 v241, v242, v241, vcc
	v_cmp_nlt_f32_e32 vcc, s49, v243
	v_add_f32_e32 v73, v73, v163
	v_mul_f32_e32 v73, 0xbfb8aa3b, v73
	v_cndmask_b32_e32 v244, v245, v244, vcc
	v_exp_f32_e32 v66, v66
	v_exp_f32_e32 v67, v67
	v_exp_f32_e32 v68, v68
	v_exp_f32_e32 v69, v69
	v_exp_f32_e32 v70, v70
	v_exp_f32_e32 v71, v71
	v_exp_f32_e32 v72, v72
	v_exp_f32_e32 v73, v73
	v_sqrt_f32_e32 v199, v199
	v_sqrt_f32_e32 v202, v202
	v_sqrt_f32_e32 v205, v205
	v_sqrt_f32_e32 v208, v208
	v_sqrt_f32_e32 v217, v217
	v_sqrt_f32_e32 v238, v238
	v_sqrt_f32_e32 v241, v241
	v_sqrt_f32_e32 v244, v244
	v_add_f32_e32 v66, 1.0, v66
	v_add_f32_e32 v67, 1.0, v67
	v_add_f32_e32 v68, 1.0, v68
	v_add_f32_e32 v69, 1.0, v69
	v_add_f32_e32 v70, 1.0, v70
	v_add_f32_e32 v71, 1.0, v71
	v_add_f32_e32 v72, 1.0, v72
	v_add_f32_e32 v73, 1.0, v73
	v_lshlrev_b32_e32 v200, 16, v168
	v_and_b32_e32 v203, 0xffff0000, v168
	v_lshlrev_b32_e32 v206, 16, v169
	v_and_b32_e32 v209, 0xffff0000, v169
	v_lshlrev_b32_e32 v218, 16, v170
	v_and_b32_e32 v239, 0xffff0000, v170
	v_lshlrev_b32_e32 v242, 16, v171
	v_and_b32_e32 v245, 0xffff0000, v171
	v_rcp_f32_e32 v66, v66
	v_rcp_f32_e32 v67, v67
	v_rcp_f32_e32 v68, v68
	v_rcp_f32_e32 v69, v69
	v_rcp_f32_e32 v70, v70
	v_rcp_f32_e32 v71, v71
	v_rcp_f32_e32 v72, v72
	v_rcp_f32_e32 v73, v73
	v_mul_f32_e32 v94, 0x3fb8aa3b, v94
	v_mul_f32_e32 v95, 0x3fb8aa3b, v95
	v_mul_f32_e32 v96, 0x3fb8aa3b, v96
	v_mul_f32_e32 v97, 0x3fb8aa3b, v97
	v_mul_f32_e32 v90, 0x3fb8aa3b, v90
	v_mul_f32_e32 v91, 0x3fb8aa3b, v91
	v_mul_f32_e32 v92, 0x3fb8aa3b, v92
	v_mul_f32_e32 v93, 0x3fb8aa3b, v93
	v_mul_f32_e32 v66, v66, v200
	v_mul_f32_e32 v67, v67, v203
	v_mul_f32_e32 v68, v68, v206
	v_mul_f32_e32 v69, v69, v209
	v_mul_f32_e32 v70, v70, v218
	v_mul_f32_e32 v71, v71, v239
	v_mul_f32_e32 v72, v72, v242
	v_mul_f32_e32 v73, v73, v245
	v_exp_f32_e32 v94, v94
	v_exp_f32_e32 v95, v95
	v_exp_f32_e32 v96, v96
	v_exp_f32_e32 v97, v97
	v_exp_f32_e32 v90, v90
	v_exp_f32_e32 v91, v91
	v_exp_f32_e32 v92, v92
	v_exp_f32_e32 v93, v93
	v_mul_f32_e32 v66, v66, v199
	v_mul_f32_e32 v67, v67, v202
	v_mul_f32_e32 v68, v68, v205
	v_mul_f32_e32 v69, v69, v208
	v_mul_f32_e32 v70, v70, v217
	v_mul_f32_e32 v71, v71, v238
	v_mul_f32_e32 v72, v72, v241
	v_mul_f32_e32 v73, v73, v244
	v_add_f32_e32 v86, v86, v156
	v_add_f32_e32 v87, v87, v157
	v_add_f32_e32 v88, v88, v158
	v_add_f32_e32 v89, v89, v159
	v_add_f32_e32 v82, v82, v156
	v_add_f32_e32 v83, v83, v157
	v_add_f32_e32 v84, v84, v158
	v_add_f32_e32 v85, v85, v159
	v_mul_f32_e32 v86, 0xbfb8aa3b, v86
	v_mul_f32_e32 v87, 0xbfb8aa3b, v87
	v_mul_f32_e32 v88, 0xbfb8aa3b, v88
	v_mul_f32_e32 v89, 0xbfb8aa3b, v89
	v_mul_f32_e32 v82, 0xbfb8aa3b, v82
	v_mul_f32_e32 v83, 0xbfb8aa3b, v83
	v_mul_f32_e32 v84, 0xbfb8aa3b, v84
	v_mul_f32_e32 v85, 0xbfb8aa3b, v85
	v_exp_f32_e32 v86, v86
	v_exp_f32_e32 v87, v87
	v_exp_f32_e32 v88, v88
	v_exp_f32_e32 v89, v89
	v_exp_f32_e32 v82, v82
	v_exp_f32_e32 v83, v83
	v_exp_f32_e32 v84, v84
	v_exp_f32_e32 v85, v85
	v_add_f32_e32 v86, 1.0, v86
	v_add_f32_e32 v87, 1.0, v87
	v_add_f32_e32 v88, 1.0, v88
	v_add_f32_e32 v89, 1.0, v89
	v_add_f32_e32 v82, 1.0, v82
	v_add_f32_e32 v83, 1.0, v83
	v_add_f32_e32 v84, 1.0, v84
	v_add_f32_e32 v85, 1.0, v85
	v_rcp_f32_e32 v86, v86
	v_rcp_f32_e32 v87, v87
	v_rcp_f32_e32 v88, v88
	v_rcp_f32_e32 v89, v89
	v_rcp_f32_e32 v82, v82
	v_rcp_f32_e32 v83, v83
	v_rcp_f32_e32 v84, v84
	v_rcp_f32_e32 v85, v85
	v_mul_f32_e32 v86, v164, v86
	v_mul_f32_e32 v87, v165, v87
	v_mul_f32_e32 v88, v166, v88
	v_mul_f32_e32 v89, v167, v89
	v_mul_f32_e32 v82, v164, v82
; __device__ __forceinline__ float sigmoid_fast(float x) { return __builtin_amdgcn_rcpf(1.f + __expf(-x)); }
; __device__ __forceinline__ float one_minus_exp(float x) { const float p = -x * (1.f + x * (0.5f + x * (0.16666667f + x * (0.041666668f + x * 0.0083333338f)))); return x > -0.1f ? p : 1.f - __expf(x); }
;     template <bool BWD>
;     __device__ __forceinline__ void epi_dir(const f32x4 (&acc)[2][2][4][2], const Unit& u, int wr, int wc, int fr, int fq) const {
;     ...
;                 const f32x4 bav = *(const f32x4*)(bap + n * 64 + coff), bxv = *(const f32x4*)(bxp + n * 64 + coff), lsl = *(const f32x4*)(lmp + n * 64 + coff);
; #pragma unroll
;                 for (int m = 0; m < 4; ++m) {
;                     const u32x2 uw = *(const u32x2*)(Ub + ((size_t)(ai * 128 + m * 16) * 1024 + n * 16) * 2 + loffu);
;                     const float uv[4] = {bflo(uw.x), bfhi(uw.x), bflo(uw.y), bfhi(uw.y)};
; #pragma unroll
;                     for (int j = 0; j < 4; ++j) { const float r = sigmoid_fast(acc[ai][0][m][n][j] + bav[j]), ig = sigmoid_fast(acc[ai][1][m][n][j] + bxv[j]);
;                         const float la = r * lsl[j]; A[m][j] = __expf(la); H[m][j] = __builtin_amdgcn_sqrtf(one_minus_exp(2.f * la)) * (ig * uv[j]); } }
	v_mul_f32_e32 v83, v165, v83
	v_mul_f32_e32 v84, v166, v84
	v_mul_f32_e32 v85, v167, v85
	v_add_f32_e32 v198, v86, v86
	v_add_f32_e32 v201, v87, v87
	v_add_f32_e32 v204, v88, v88
	v_add_f32_e32 v207, v89, v89
	v_add_f32_e32 v216, v82, v82
	v_add_f32_e32 v219, v83, v83
	v_add_f32_e32 v240, v84, v84
	v_add_f32_e32 v243, v85, v85
	v_mul_f32_e32 v199, 0x3fb8aa3b, v198
	v_mul_f32_e32 v202, 0x3fb8aa3b, v201
	v_mul_f32_e32 v205, 0x3fb8aa3b, v204
	v_mul_f32_e32 v208, 0x3fb8aa3b, v207
	v_mul_f32_e32 v217, 0x3fb8aa3b, v216
	v_mul_f32_e32 v238, 0x3fb8aa3b, v219
	v_mul_f32_e32 v241, 0x3fb8aa3b, v240
	v_mul_f32_e32 v244, 0x3fb8aa3b, v243
	v_exp_f32_e32 v199, v199
	v_exp_f32_e32 v202, v202
	v_exp_f32_e32 v205, v205
	v_exp_f32_e32 v208, v208
	v_exp_f32_e32 v217, v217
	v_exp_f32_e32 v238, v238
	v_exp_f32_e32 v241, v241
	v_exp_f32_e32 v244, v244
	v_fmamk_f32 v200, v198, 0x3c088889, v211
	v_fmamk_f32 v203, v201, 0x3c088889, v211
	v_fmamk_f32 v206, v204, 0x3c088889, v211
	v_fmamk_f32 v209, v207, 0x3c088889, v211
	v_fmamk_f32 v218, v216, 0x3c088889, v211
	v_fmamk_f32 v239, v219, 0x3c088889, v211
	v_fmamk_f32 v242, v240, 0x3c088889, v211
	v_fmamk_f32 v245, v243, 0x3c088889, v211
	v_sub_f32_e32 v199, 1.0, v199
	v_sub_f32_e32 v202, 1.0, v202
	v_sub_f32_e32 v205, 1.0, v205
	v_sub_f32_e32 v208, 1.0, v208
	v_sub_f32_e32 v217, 1.0, v217
	v_sub_f32_e32 v238, 1.0, v238
	v_sub_f32_e32 v241, 1.0, v241
	v_sub_f32_e32 v244, 1.0, v244
	v_fmaak_f32 v200, v198, v200, 0x3e2aaaab
	v_fmaak_f32 v203, v201, v203, 0x3e2aaaab
	v_fmaak_f32 v206, v204, v206, 0x3e2aaaab
	v_fmaak_f32 v209, v207, v209, 0x3e2aaaab
	v_fmaak_f32 v218, v216, v218, 0x3e2aaaab
	v_fmaak_f32 v239, v219, v239, 0x3e2aaaab
	v_fmaak_f32 v242, v240, v242, 0x3e2aaaab
	v_fmaak_f32 v245, v243, v245, 0x3e2aaaab
	v_fma_f32 v200, v198, v200, 0.5
	v_fma_f32 v203, v201, v203, 0.5
	v_fma_f32 v206, v204, v206, 0.5
	v_fma_f32 v209, v207, v209, 0.5
	v_fma_f32 v218, v216, v218, 0.5
	v_fma_f32 v239, v219, v239, 0.5
	v_fma_f32 v242, v240, v242, 0.5
	v_fma_f32 v245, v243, v245, 0.5
	v_fma_f32 v200, v198, v200, 1.0
	v_fma_f32 v203, v201, v203, 1.0
	v_fma_f32 v206, v204, v206, 1.0
	v_fma_f32 v209, v207, v209, 1.0
	v_fma_f32 v218, v216, v218, 1.0
	v_fma_f32 v239, v219, v239, 1.0
	v_fma_f32 v242, v240, v242, 1.0
	v_fma_f32 v245, v243, v245, 1.0
	v_mul_f32_e64 v200, v200, -v198
	v_mul_f32_e64 v203, v203, -v201
	v_mul_f32_e64 v206, v206, -v204
	v_mul_f32_e64 v209, v209, -v207
	v_mul_f32_e64 v218, v218, -v216
	v_mul_f32_e64 v239, v239, -v219
	v_mul_f32_e64 v242, v242, -v240
	v_mul_f32_e64 v245, v245, -v243
	v_cmp_nlt_f32_e32 vcc, s49, v198
	v_add_f32_e32 v74, v74, v160
	v_mul_f32_e32 v74, 0xbfb8aa3b, v74
	v_cndmask_b32_e32 v199, v200, v199, vcc
	v_cmp_nlt_f32_e32 vcc, s49, v201
	v_add_f32_e32 v75, v75, v161
	v_mul_f32_e32 v75, 0xbfb8aa3b, v75
	v_cndmask_b32_e32 v202, v203, v202, vcc
	v_cmp_nlt_f32_e32 vcc, s49, v204
	v_add_f32_e32 v76, v76, v162
	v_mul_f32_e32 v76, 0xbfb8aa3b, v76
	v_cndmask_b32_e32 v205, v206, v205, vcc
	v_cmp_nlt_f32_e32 vcc, s49, v207
	v_add_f32_e32 v77, v77, v163
	v_mul_f32_e32 v77, 0xbfb8aa3b, v77
	v_cndmask_b32_e32 v208, v209, v208, vcc
	v_cmp_nlt_f32_e32 vcc, s49, v216
	v_add_f32_e32 v78, v78, v160
	v_mul_f32_e32 v78, 0xbfb8aa3b, v78
	v_cndmask_b32_e32 v217, v218, v217, vcc
	v_cmp_nlt_f32_e32 vcc, s49, v219
	v_add_f32_e32 v79, v79, v161
	v_mul_f32_e32 v79, 0xbfb8aa3b, v79
	v_cndmask_b32_e32 v238, v239, v238, vcc
	v_cmp_nlt_f32_e32 vcc, s49, v240
	v_add_f32_e32 v80, v80, v162
	v_mul_f32_e32 v80, 0xbfb8aa3b, v80
	v_cndmask_b32_e32 v241, v242, v241, vcc
	v_cmp_nlt_f32_e32 vcc, s49, v243
	v_add_f32_e32 v81, v81, v163
	v_mul_f32_e32 v81, 0xbfb8aa3b, v81
	v_cndmask_b32_e32 v244, v245, v244, vcc
	v_exp_f32_e32 v74, v74
	v_exp_f32_e32 v75, v75
	v_exp_f32_e32 v76, v76
	v_exp_f32_e32 v77, v77
	v_exp_f32_e32 v78, v78
	v_exp_f32_e32 v79, v79
	v_exp_f32_e32 v80, v80
	v_exp_f32_e32 v81, v81
	v_sqrt_f32_e32 v199, v199
	v_sqrt_f32_e32 v202, v202
	v_sqrt_f32_e32 v205, v205
	v_sqrt_f32_e32 v208, v208
	v_sqrt_f32_e32 v217, v217
	v_sqrt_f32_e32 v238, v238
	v_sqrt_f32_e32 v241, v241
	v_sqrt_f32_e32 v244, v244
	v_add_f32_e32 v74, 1.0, v74
	v_add_f32_e32 v75, 1.0, v75
	v_add_f32_e32 v76, 1.0, v76
	v_add_f32_e32 v77, 1.0, v77
	v_add_f32_e32 v78, 1.0, v78
	v_add_f32_e32 v79, 1.0, v79
	v_add_f32_e32 v80, 1.0, v80
	v_add_f32_e32 v81, 1.0, v81
	v_lshlrev_b32_e32 v200, 16, v172
	v_and_b32_e32 v203, 0xffff0000, v172
	v_lshlrev_b32_e32 v206, 16, v173
	v_and_b32_e32 v209, 0xffff0000, v173
	v_lshlrev_b32_e32 v218, 16, v174
	v_and_b32_e32 v239, 0xffff0000, v174
	v_lshlrev_b32_e32 v242, 16, v175
	v_and_b32_e32 v245, 0xffff0000, v175
	v_rcp_f32_e32 v74, v74
	v_rcp_f32_e32 v75, v75
	v_rcp_f32_e32 v76, v76
	v_rcp_f32_e32 v77, v77
	v_rcp_f32_e32 v78, v78
	v_rcp_f32_e32 v79, v79
	v_rcp_f32_e32 v80, v80
	v_rcp_f32_e32 v81, v81
	v_mul_f32_e32 v86, 0x3fb8aa3b, v86
	v_mul_f32_e32 v87, 0x3fb8aa3b, v87
	v_mul_f32_e32 v88, 0x3fb8aa3b, v88
	v_mul_f32_e32 v89, 0x3fb8aa3b, v89
	v_mul_f32_e32 v82, 0x3fb8aa3b, v82
	v_mul_f32_e32 v83, 0x3fb8aa3b, v83
	v_mul_f32_e32 v84, 0x3fb8aa3b, v84
	v_mul_f32_e32 v85, 0x3fb8aa3b, v85
	v_mul_f32_e32 v74, v74, v200
	v_mul_f32_e32 v75, v75, v203
	v_mul_f32_e32 v76, v76, v206
	v_mul_f32_e32 v77, v77, v209
	v_mul_f32_e32 v78, v78, v218
	v_mul_f32_e32 v79, v79, v239
	v_mul_f32_e32 v80, v80, v242
	v_mul_f32_e32 v81, v81, v245
	v_exp_f32_e32 v86, v86
	v_exp_f32_e32 v87, v87
	v_exp_f32_e32 v88, v88
	v_exp_f32_e32 v89, v89
	v_exp_f32_e32 v82, v82
	v_exp_f32_e32 v83, v83
	v_exp_f32_e32 v84, v84
	v_exp_f32_e32 v85, v85
	v_mul_f32_e32 v74, v74, v199
	v_mul_f32_e32 v75, v75, v202
	v_mul_f32_e32 v76, v76, v205
	v_mul_f32_e32 v77, v77, v208
; __device__ __forceinline__ float sigmoid_fast(float x) { return __builtin_amdgcn_rcpf(1.f + __expf(-x)); }
; __device__ __forceinline__ float one_minus_exp(float x) { const float p = -x * (1.f + x * (0.5f + x * (0.16666667f + x * (0.041666668f + x * 0.0083333338f)))); return x > -0.1f ? p : 1.f - __expf(x); }
; #define SCAN_STEP(D) { const float ap = dppf<(BWD ? 0x100 : 0x110) + D>(1.f, av), hp = dppf<(BWD ? 0x100 : 0x110) + D>(0.f, hv); hv = fmaf(av, hp, hv); av = av * ap; }
;     template <bool BWD>
;     __device__ __forceinline__ void epi_dir(const f32x4 (&acc)[2][2][4][2], const Unit& u, int wr, int wc, int fr, int fq) const {
;     ...
;                     for (int j = 0; j < 4; ++j) { const float r = sigmoid_fast(acc[ai][0][m][n][j] + bav[j]), ig = sigmoid_fast(acc[ai][1][m][n][j] + bxv[j]);
;                         const float la = r * lsl[j]; A[m][j] = __expf(la); H[m][j] = __builtin_amdgcn_sqrtf(one_minus_exp(2.f * la)) * (ig * uv[j]); } }
; #pragma unroll
;                 for (int m = 0; m < 4; ++m)
; #pragma unroll
;                     for (int j = 0; j < 4; ++j) { float av = A[m][j], hv = H[m][j];
;     ...
;                         SCAN_STEP(1) SCAN_STEP(2) SCAN_STEP(4) SCAN_STEP(8)
	v_mul_f32_e32 v78, v78, v217
	v_mul_f32_e32 v79, v79, v238
	v_mul_f32_e32 v80, v80, v241
	v_mul_f32_e32 v81, v81, v244
	v_fmac_f32_dpp v66, v66, v94 row_shl:1 row_mask:0xf bank_mask:0xf
	v_mul_f32_dpp v94, v94, v94 row_shl:1 row_mask:0xf bank_mask:0xf
	v_fmac_f32_dpp v67, v67, v95 row_shl:1 row_mask:0xf bank_mask:0xf
	v_mul_f32_dpp v95, v95, v95 row_shl:1 row_mask:0xf bank_mask:0xf
	v_fmac_f32_dpp v68, v68, v96 row_shl:1 row_mask:0xf bank_mask:0xf
	v_mul_f32_dpp v96, v96, v96 row_shl:1 row_mask:0xf bank_mask:0xf
	v_fmac_f32_dpp v69, v69, v97 row_shl:1 row_mask:0xf bank_mask:0xf
	v_mul_f32_dpp v97, v97, v97 row_shl:1 row_mask:0xf bank_mask:0xf
	v_fmac_f32_dpp v70, v70, v90 row_shl:1 row_mask:0xf bank_mask:0xf
	v_mul_f32_dpp v90, v90, v90 row_shl:1 row_mask:0xf bank_mask:0xf
	v_fmac_f32_dpp v71, v71, v91 row_shl:1 row_mask:0xf bank_mask:0xf
	v_mul_f32_dpp v91, v91, v91 row_shl:1 row_mask:0xf bank_mask:0xf
	v_fmac_f32_dpp v72, v72, v92 row_shl:1 row_mask:0xf bank_mask:0xf
	v_mul_f32_dpp v92, v92, v92 row_shl:1 row_mask:0xf bank_mask:0xf
	v_fmac_f32_dpp v73, v73, v93 row_shl:1 row_mask:0xf bank_mask:0xf
	v_mul_f32_dpp v93, v93, v93 row_shl:1 row_mask:0xf bank_mask:0xf
	v_fmac_f32_dpp v74, v74, v86 row_shl:1 row_mask:0xf bank_mask:0xf
	v_mul_f32_dpp v86, v86, v86 row_shl:1 row_mask:0xf bank_mask:0xf
	v_fmac_f32_dpp v75, v75, v87 row_shl:1 row_mask:0xf bank_mask:0xf
	v_mul_f32_dpp v87, v87, v87 row_shl:1 row_mask:0xf bank_mask:0xf
	v_fmac_f32_dpp v76, v76, v88 row_shl:1 row_mask:0xf bank_mask:0xf
	v_mul_f32_dpp v88, v88, v88 row_shl:1 row_mask:0xf bank_mask:0xf
	v_fmac_f32_dpp v77, v77, v89 row_shl:1 row_mask:0xf bank_mask:0xf
	v_mul_f32_dpp v89, v89, v89 row_shl:1 row_mask:0xf bank_mask:0xf
	v_fmac_f32_dpp v78, v78, v82 row_shl:1 row_mask:0xf bank_mask:0xf
	v_mul_f32_dpp v82, v82, v82 row_shl:1 row_mask:0xf bank_mask:0xf
	v_fmac_f32_dpp v79, v79, v83 row_shl:1 row_mask:0xf bank_mask:0xf
	v_mul_f32_dpp v83, v83, v83 row_shl:1 row_mask:0xf bank_mask:0xf
	v_fmac_f32_dpp v80, v80, v84 row_shl:1 row_mask:0xf bank_mask:0xf
	v_mul_f32_dpp v84, v84, v84 row_shl:1 row_mask:0xf bank_mask:0xf
	v_fmac_f32_dpp v81, v81, v85 row_shl:1 row_mask:0xf bank_mask:0xf
	v_mul_f32_dpp v85, v85, v85 row_shl:1 row_mask:0xf bank_mask:0xf
	v_fmac_f32_dpp v66, v66, v94 row_shl:2 row_mask:0xf bank_mask:0xf
	v_mul_f32_dpp v94, v94, v94 row_shl:2 row_mask:0xf bank_mask:0xf
	v_fmac_f32_dpp v67, v67, v95 row_shl:2 row_mask:0xf bank_mask:0xf
	v_mul_f32_dpp v95, v95, v95 row_shl:2 row_mask:0xf bank_mask:0xf
	v_fmac_f32_dpp v68, v68, v96 row_shl:2 row_mask:0xf bank_mask:0xf
	v_mul_f32_dpp v96, v96, v96 row_shl:2 row_mask:0xf bank_mask:0xf
	v_fmac_f32_dpp v69, v69, v97 row_shl:2 row_mask:0xf bank_mask:0xf
	v_mul_f32_dpp v97, v97, v97 row_shl:2 row_mask:0xf bank_mask:0xf
	v_fmac_f32_dpp v70, v70, v90 row_shl:2 row_mask:0xf bank_mask:0xf
	v_mul_f32_dpp v90, v90, v90 row_shl:2 row_mask:0xf bank_mask:0xf
	v_fmac_f32_dpp v71, v71, v91 row_shl:2 row_mask:0xf bank_mask:0xf
	v_mul_f32_dpp v91, v91, v91 row_shl:2 row_mask:0xf bank_mask:0xf
	v_fmac_f32_dpp v72, v72, v92 row_shl:2 row_mask:0xf bank_mask:0xf
	v_mul_f32_dpp v92, v92, v92 row_shl:2 row_mask:0xf bank_mask:0xf
	v_fmac_f32_dpp v73, v73, v93 row_shl:2 row_mask:0xf bank_mask:0xf
	v_mul_f32_dpp v93, v93, v93 row_shl:2 row_mask:0xf bank_mask:0xf
	v_fmac_f32_dpp v74, v74, v86 row_shl:2 row_mask:0xf bank_mask:0xf
	v_mul_f32_dpp v86, v86, v86 row_shl:2 row_mask:0xf bank_mask:0xf
	v_fmac_f32_dpp v75, v75, v87 row_shl:2 row_mask:0xf bank_mask:0xf
	v_mul_f32_dpp v87, v87, v87 row_shl:2 row_mask:0xf bank_mask:0xf
	v_fmac_f32_dpp v76, v76, v88 row_shl:2 row_mask:0xf bank_mask:0xf
	v_mul_f32_dpp v88, v88, v88 row_shl:2 row_mask:0xf bank_mask:0xf
	v_fmac_f32_dpp v77, v77, v89 row_shl:2 row_mask:0xf bank_mask:0xf
	v_mul_f32_dpp v89, v89, v89 row_shl:2 row_mask:0xf bank_mask:0xf
	v_fmac_f32_dpp v78, v78, v82 row_shl:2 row_mask:0xf bank_mask:0xf
	v_mul_f32_dpp v82, v82, v82 row_shl:2 row_mask:0xf bank_mask:0xf
	v_fmac_f32_dpp v79, v79, v83 row_shl:2 row_mask:0xf bank_mask:0xf
	v_mul_f32_dpp v83, v83, v83 row_shl:2 row_mask:0xf bank_mask:0xf
	v_fmac_f32_dpp v80, v80, v84 row_shl:2 row_mask:0xf bank_mask:0xf
	v_mul_f32_dpp v84, v84, v84 row_shl:2 row_mask:0xf bank_mask:0xf
	v_fmac_f32_dpp v81, v81, v85 row_shl:2 row_mask:0xf bank_mask:0xf
	v_mul_f32_dpp v85, v85, v85 row_shl:2 row_mask:0xf bank_mask:0xf
	v_fmac_f32_dpp v66, v66, v94 row_shl:4 row_mask:0xf bank_mask:0xf
	v_mul_f32_dpp v94, v94, v94 row_shl:4 row_mask:0xf bank_mask:0xf
	v_fmac_f32_dpp v67, v67, v95 row_shl:4 row_mask:0xf bank_mask:0xf
	v_mul_f32_dpp v95, v95, v95 row_shl:4 row_mask:0xf bank_mask:0xf
	v_fmac_f32_dpp v68, v68, v96 row_shl:4 row_mask:0xf bank_mask:0xf
	v_mul_f32_dpp v96, v96, v96 row_shl:4 row_mask:0xf bank_mask:0xf
	v_fmac_f32_dpp v69, v69, v97 row_shl:4 row_mask:0xf bank_mask:0xf
	v_mul_f32_dpp v97, v97, v97 row_shl:4 row_mask:0xf bank_mask:0xf
	v_fmac_f32_dpp v70, v70, v90 row_shl:4 row_mask:0xf bank_mask:0xf
	v_mul_f32_dpp v90, v90, v90 row_shl:4 row_mask:0xf bank_mask:0xf
	v_fmac_f32_dpp v71, v71, v91 row_shl:4 row_mask:0xf bank_mask:0xf
	v_mul_f32_dpp v91, v91, v91 row_shl:4 row_mask:0xf bank_mask:0xf
	v_fmac_f32_dpp v72, v72, v92 row_shl:4 row_mask:0xf bank_mask:0xf
	v_mul_f32_dpp v92, v92, v92 row_shl:4 row_mask:0xf bank_mask:0xf
	v_fmac_f32_dpp v73, v73, v93 row_shl:4 row_mask:0xf bank_mask:0xf
	v_mul_f32_dpp v93, v93, v93 row_shl:4 row_mask:0xf bank_mask:0xf
	v_fmac_f32_dpp v74, v74, v86 row_shl:4 row_mask:0xf bank_mask:0xf
	v_mul_f32_dpp v86, v86, v86 row_shl:4 row_mask:0xf bank_mask:0xf
	v_fmac_f32_dpp v75, v75, v87 row_shl:4 row_mask:0xf bank_mask:0xf
; __device__ __forceinline__ unsigned pk2(float lo, float hi) { return f2bf(lo) | (f2bf(hi) << 16); }
; #define SCAN_STEP(D) { const float ap = dppf<(BWD ? 0x100 : 0x110) + D>(1.f, av), hp = dppf<(BWD ? 0x100 : 0x110) + D>(0.f, hv); hv = fmaf(av, hp, hv); av = av * ap; }
;     template <bool BWD>
;     __device__ __forceinline__ void epi_dir(const f32x4 (&acc)[2][2][4][2], const Unit& u, int wr, int wc, int fr, int fq) const {
;     ...
;                     for (int j = 0; j < 4; ++j) { float av = A[m][j], hv = H[m][j];
;     ...
;                         SCAN_STEP(1) SCAN_STEP(2) SCAN_STEP(4) SCAN_STEP(8)
;     ...
;                         A[m][j] = av; H[m][j] = hv; }
; #pragma unroll
;                 for (int j = 0; j < 4; ++j) { float Ar = 1.f, Hr = 0.f;
; #pragma unroll
;                     for (int mm = 0; mm < 4; ++mm) { const int m = BWD ? 3 - mm : mm;
;                         H[m][j] = fmaf(A[m][j], Hr, H[m][j]); A[m][j] = A[m][j] * Ar;
;                         if (mm < 3) { Ar = __shfl(A[m][j], bsel); Hr = __shfl(H[m][j], bsel); } } }
; #pragma unroll
;                 for (int m = 0; m < 4; ++m) { u32x4 w; w.x = pk2(H[m][0], H[m][1]); w.y = pk2(H[m][2], H[m][3]); w.z = pk2(A[m][0], A[m][1]); w.w = pk2(A[m][2], A[m][3]);
;                     *(u32x4*)(Hb + ((size_t)(ai * 128 + m * 16) * 1024 + n * 16) * 4 + loffh) = w; }
;                 constexpr int me = BWD ? 0 : 3;
;                 if (fr == (BWD ? 0 : 15)) { const size_t o = (size_t)chunk * 1024 + gblk * 128 + n * 16;
;                     *(f32x4*)((char*)(AGG + (size_t)(dir * 2 + 0) * NB * NCHUNK * 1024 + o) + coff) = A[me];
;                     *(f32x4*)((char*)(AGG + (size_t)(dir * 2 + 1) * NB * NCHUNK * 1024 + o) + coff) = H[me]; }
	v_mul_f32_dpp v87, v87, v87 row_shl:4 row_mask:0xf bank_mask:0xf
	v_fmac_f32_dpp v76, v76, v88 row_shl:4 row_mask:0xf bank_mask:0xf
	v_mul_f32_dpp v88, v88, v88 row_shl:4 row_mask:0xf bank_mask:0xf
	v_fmac_f32_dpp v77, v77, v89 row_shl:4 row_mask:0xf bank_mask:0xf
	v_mul_f32_dpp v89, v89, v89 row_shl:4 row_mask:0xf bank_mask:0xf
	v_fmac_f32_dpp v78, v78, v82 row_shl:4 row_mask:0xf bank_mask:0xf
	v_mul_f32_dpp v82, v82, v82 row_shl:4 row_mask:0xf bank_mask:0xf
	v_fmac_f32_dpp v79, v79, v83 row_shl:4 row_mask:0xf bank_mask:0xf
	v_mul_f32_dpp v83, v83, v83 row_shl:4 row_mask:0xf bank_mask:0xf
	v_fmac_f32_dpp v80, v80, v84 row_shl:4 row_mask:0xf bank_mask:0xf
	v_mul_f32_dpp v84, v84, v84 row_shl:4 row_mask:0xf bank_mask:0xf
	v_fmac_f32_dpp v81, v81, v85 row_shl:4 row_mask:0xf bank_mask:0xf
	v_mul_f32_dpp v85, v85, v85 row_shl:4 row_mask:0xf bank_mask:0xf
	v_fmac_f32_dpp v66, v66, v94 row_shl:8 row_mask:0xf bank_mask:0xf
	v_mul_f32_dpp v94, v94, v94 row_shl:8 row_mask:0xf bank_mask:0xf
	v_fmac_f32_dpp v67, v67, v95 row_shl:8 row_mask:0xf bank_mask:0xf
	v_mul_f32_dpp v95, v95, v95 row_shl:8 row_mask:0xf bank_mask:0xf
	v_fmac_f32_dpp v68, v68, v96 row_shl:8 row_mask:0xf bank_mask:0xf
	v_mul_f32_dpp v96, v96, v96 row_shl:8 row_mask:0xf bank_mask:0xf
	v_fmac_f32_dpp v69, v69, v97 row_shl:8 row_mask:0xf bank_mask:0xf
	v_mul_f32_dpp v97, v97, v97 row_shl:8 row_mask:0xf bank_mask:0xf
	v_fmac_f32_dpp v70, v70, v90 row_shl:8 row_mask:0xf bank_mask:0xf
	v_mul_f32_dpp v90, v90, v90 row_shl:8 row_mask:0xf bank_mask:0xf
	v_fmac_f32_dpp v71, v71, v91 row_shl:8 row_mask:0xf bank_mask:0xf
	v_mul_f32_dpp v91, v91, v91 row_shl:8 row_mask:0xf bank_mask:0xf
	v_fmac_f32_dpp v72, v72, v92 row_shl:8 row_mask:0xf bank_mask:0xf
	v_mul_f32_dpp v92, v92, v92 row_shl:8 row_mask:0xf bank_mask:0xf
	v_fmac_f32_dpp v73, v73, v93 row_shl:8 row_mask:0xf bank_mask:0xf
	v_mul_f32_dpp v93, v93, v93 row_shl:8 row_mask:0xf bank_mask:0xf
	v_fmac_f32_dpp v74, v74, v86 row_shl:8 row_mask:0xf bank_mask:0xf
	v_mul_f32_dpp v86, v86, v86 row_shl:8 row_mask:0xf bank_mask:0xf
	v_fmac_f32_dpp v75, v75, v87 row_shl:8 row_mask:0xf bank_mask:0xf
	v_mul_f32_dpp v87, v87, v87 row_shl:8 row_mask:0xf bank_mask:0xf
	v_fmac_f32_dpp v76, v76, v88 row_shl:8 row_mask:0xf bank_mask:0xf
	v_mul_f32_dpp v88, v88, v88 row_shl:8 row_mask:0xf bank_mask:0xf
	v_fmac_f32_dpp v77, v77, v89 row_shl:8 row_mask:0xf bank_mask:0xf
	v_mul_f32_dpp v89, v89, v89 row_shl:8 row_mask:0xf bank_mask:0xf
	v_fmac_f32_dpp v78, v78, v82 row_shl:8 row_mask:0xf bank_mask:0xf
	v_mul_f32_dpp v82, v82, v82 row_shl:8 row_mask:0xf bank_mask:0xf
	v_fmac_f32_dpp v79, v79, v83 row_shl:8 row_mask:0xf bank_mask:0xf
	v_mul_f32_dpp v83, v83, v83 row_shl:8 row_mask:0xf bank_mask:0xf
	v_fmac_f32_dpp v80, v80, v84 row_shl:8 row_mask:0xf bank_mask:0xf
	v_mul_f32_dpp v84, v84, v84 row_shl:8 row_mask:0xf bank_mask:0xf
	v_fmac_f32_dpp v81, v81, v85 row_shl:8 row_mask:0xf bank_mask:0xf
	v_mul_f32_dpp v85, v85, v85 row_shl:8 row_mask:0xf bank_mask:0xf
	v_fmac_f32_dpp v74, v78, v86 row_newbcast:0 row_mask:0xf bank_mask:0xf
	v_mul_f32_dpp v86, v82, v86 row_newbcast:0 row_mask:0xf bank_mask:0xf
	v_fmac_f32_dpp v75, v79, v87 row_newbcast:0 row_mask:0xf bank_mask:0xf
	v_mul_f32_dpp v87, v83, v87 row_newbcast:0 row_mask:0xf bank_mask:0xf
	v_fmac_f32_dpp v76, v80, v88 row_newbcast:0 row_mask:0xf bank_mask:0xf
	v_mul_f32_dpp v88, v84, v88 row_newbcast:0 row_mask:0xf bank_mask:0xf
	v_fmac_f32_dpp v77, v81, v89 row_newbcast:0 row_mask:0xf bank_mask:0xf
	v_mul_f32_dpp v89, v85, v89 row_newbcast:0 row_mask:0xf bank_mask:0xf
	v_fmac_f32_dpp v70, v74, v90 row_newbcast:0 row_mask:0xf bank_mask:0xf
	v_mul_f32_dpp v90, v86, v90 row_newbcast:0 row_mask:0xf bank_mask:0xf
	v_fmac_f32_dpp v71, v75, v91 row_newbcast:0 row_mask:0xf bank_mask:0xf
	v_mul_f32_dpp v91, v87, v91 row_newbcast:0 row_mask:0xf bank_mask:0xf
	v_fmac_f32_dpp v72, v76, v92 row_newbcast:0 row_mask:0xf bank_mask:0xf
	v_mul_f32_dpp v92, v88, v92 row_newbcast:0 row_mask:0xf bank_mask:0xf
	v_fmac_f32_dpp v73, v77, v93 row_newbcast:0 row_mask:0xf bank_mask:0xf
	v_mul_f32_dpp v93, v89, v93 row_newbcast:0 row_mask:0xf bank_mask:0xf
	v_fmac_f32_dpp v66, v70, v94 row_newbcast:0 row_mask:0xf bank_mask:0xf
	v_mul_f32_dpp v94, v90, v94 row_newbcast:0 row_mask:0xf bank_mask:0xf
	v_fmac_f32_dpp v67, v71, v95 row_newbcast:0 row_mask:0xf bank_mask:0xf
	v_mul_f32_dpp v95, v91, v95 row_newbcast:0 row_mask:0xf bank_mask:0xf
	v_fmac_f32_dpp v68, v72, v96 row_newbcast:0 row_mask:0xf bank_mask:0xf
	v_mul_f32_dpp v96, v92, v96 row_newbcast:0 row_mask:0xf bank_mask:0xf
	v_fmac_f32_dpp v69, v73, v97 row_newbcast:0 row_mask:0xf bank_mask:0xf
	v_mul_f32_dpp v97, v93, v97 row_newbcast:0 row_mask:0xf bank_mask:0xf
	s_and_saveexec_b64 s[46:47], s[40:41]
	global_store_dwordx4 v187, v[94:97], s[14:15] offset:64 sc1
	global_store_dwordx4 v187, v[66:69], s[10:11] offset:64 sc1
	s_mov_b64 exec, s[46:47]
	v_cvt_pk_bf16_f32 v78, v78, v79
	v_cvt_pk_bf16_f32 v79, v80, v81
	v_cvt_pk_bf16_f32 v80, v82, v83
	v_cvt_pk_bf16_f32 v81, v84, v85
	global_store_dwordx4 v197, v[78:81], s[54:55] offset:64 sc1
	v_cvt_pk_bf16_f32 v74, v74, v75
	v_cvt_pk_bf16_f32 v75, v76, v77
	v_cvt_pk_bf16_f32 v76, v86, v87
	v_cvt_pk_bf16_f32 v77, v88, v89
	global_store_dwordx4 v196, v[74:77], s[54:55] offset:64 sc1
	v_cvt_pk_bf16_f32 v70, v70, v71
	v_cvt_pk_bf16_f32 v71, v72, v73
	v_cvt_pk_bf16_f32 v72, v90, v91
	v_cvt_pk_bf16_f32 v73, v92, v93
	global_store_dwordx4 v195, v[70:73], s[54:55] offset:64 sc1
	v_cvt_pk_bf16_f32 v66, v66, v67
	v_cvt_pk_bf16_f32 v67, v68, v69
	v_cvt_pk_bf16_f32 v68, v94, v95
	v_cvt_pk_bf16_f32 v69, v96, v97
	global_store_dwordx4 v194, v[66:69], s[54:55] offset:64 sc1
	s_waitcnt vmcnt(6)
; __device__ __forceinline__ float sigmoid_fast(float x) { return __builtin_amdgcn_rcpf(1.f + __expf(-x)); }
; __device__ __forceinline__ float one_minus_exp(float x) { const float p = -x * (1.f + x * (0.5f + x * (0.16666667f + x * (0.041666668f + x * 0.0083333338f)))); return x > -0.1f ? p : 1.f - __expf(x); }
;     template <bool BWD>
;     __device__ __forceinline__ void epi_dir(const f32x4 (&acc)[2][2][4][2], const Unit& u, int wr, int wc, int fr, int fq) const {
;     ...
;                 const f32x4 bav = *(const f32x4*)(bap + n * 64 + coff), bxv = *(const f32x4*)(bxp + n * 64 + coff), lsl = *(const f32x4*)(lmp + n * 64 + coff);
; #pragma unroll
;                 for (int m = 0; m < 4; ++m) {
;                     const u32x2 uw = *(const u32x2*)(Ub + ((size_t)(ai * 128 + m * 16) * 1024 + n * 16) * 2 + loffu);
;                     const float uv[4] = {bflo(uw.x), bfhi(uw.x), bflo(uw.y), bfhi(uw.y)};
; #pragma unroll
;                     for (int j = 0; j < 4; ++j) { const float r = sigmoid_fast(acc[ai][0][m][n][j] + bav[j]), ig = sigmoid_fast(acc[ai][1][m][n][j] + bxv[j]);
;                         const float la = r * lsl[j]; A[m][j] = __expf(la); H[m][j] = __builtin_amdgcn_sqrtf(one_minus_exp(2.f * la)) * (ig * uv[j]); } }
	v_add_f32_e32 v30, v30, v156
	v_add_f32_e32 v31, v31, v157
	v_add_f32_e32 v32, v32, v158
	v_add_f32_e32 v33, v33, v159
	v_add_f32_e32 v26, v26, v156
	v_add_f32_e32 v27, v27, v157
	v_add_f32_e32 v28, v28, v158
	v_add_f32_e32 v29, v29, v159
	v_mul_f32_e32 v30, 0xbfb8aa3b, v30
	v_mul_f32_e32 v31, 0xbfb8aa3b, v31
	v_mul_f32_e32 v32, 0xbfb8aa3b, v32
	v_mul_f32_e32 v33, 0xbfb8aa3b, v33
	v_mul_f32_e32 v26, 0xbfb8aa3b, v26
	v_mul_f32_e32 v27, 0xbfb8aa3b, v27
	v_mul_f32_e32 v28, 0xbfb8aa3b, v28
	v_mul_f32_e32 v29, 0xbfb8aa3b, v29
	v_exp_f32_e32 v30, v30
	v_exp_f32_e32 v31, v31
	v_exp_f32_e32 v32, v32
	v_exp_f32_e32 v33, v33
	v_exp_f32_e32 v26, v26
	v_exp_f32_e32 v27, v27
	v_exp_f32_e32 v28, v28
	v_exp_f32_e32 v29, v29
	v_add_f32_e32 v30, 1.0, v30
	v_add_f32_e32 v31, 1.0, v31
	v_add_f32_e32 v32, 1.0, v32
	v_add_f32_e32 v33, 1.0, v33
	v_add_f32_e32 v26, 1.0, v26
	v_add_f32_e32 v27, 1.0, v27
	v_add_f32_e32 v28, 1.0, v28
	v_add_f32_e32 v29, 1.0, v29
	v_rcp_f32_e32 v30, v30
	v_rcp_f32_e32 v31, v31
	v_rcp_f32_e32 v32, v32
	v_rcp_f32_e32 v33, v33
	v_rcp_f32_e32 v26, v26
	v_rcp_f32_e32 v27, v27
	v_rcp_f32_e32 v28, v28
	v_rcp_f32_e32 v29, v29
	v_mul_f32_e32 v30, v164, v30
	v_mul_f32_e32 v31, v165, v31
	v_mul_f32_e32 v32, v166, v32
	v_mul_f32_e32 v33, v167, v33
	v_mul_f32_e32 v26, v164, v26
	v_mul_f32_e32 v27, v165, v27
	v_mul_f32_e32 v28, v166, v28
	v_mul_f32_e32 v29, v167, v29
	v_add_f32_e32 v198, v30, v30
	v_add_f32_e32 v201, v31, v31
	v_add_f32_e32 v204, v32, v32
	v_add_f32_e32 v207, v33, v33
	v_add_f32_e32 v216, v26, v26
	v_add_f32_e32 v219, v27, v27
	v_add_f32_e32 v240, v28, v28
	v_add_f32_e32 v243, v29, v29
	v_mul_f32_e32 v199, 0x3fb8aa3b, v198
	v_mul_f32_e32 v202, 0x3fb8aa3b, v201
	v_mul_f32_e32 v205, 0x3fb8aa3b, v204
	v_mul_f32_e32 v208, 0x3fb8aa3b, v207
	v_mul_f32_e32 v217, 0x3fb8aa3b, v216
	v_mul_f32_e32 v238, 0x3fb8aa3b, v219
	v_mul_f32_e32 v241, 0x3fb8aa3b, v240
	v_mul_f32_e32 v244, 0x3fb8aa3b, v243
	v_exp_f32_e32 v199, v199
	v_exp_f32_e32 v202, v202
	v_exp_f32_e32 v205, v205
	v_exp_f32_e32 v208, v208
	v_exp_f32_e32 v217, v217
	v_exp_f32_e32 v238, v238
	v_exp_f32_e32 v241, v241
	v_exp_f32_e32 v244, v244
	v_fmamk_f32 v200, v198, 0x3c088889, v211
	v_fmamk_f32 v203, v201, 0x3c088889, v211
	v_fmamk_f32 v206, v204, 0x3c088889, v211
	v_fmamk_f32 v209, v207, 0x3c088889, v211
	v_fmamk_f32 v218, v216, 0x3c088889, v211
	v_fmamk_f32 v239, v219, 0x3c088889, v211
	v_fmamk_f32 v242, v240, 0x3c088889, v211
	v_fmamk_f32 v245, v243, 0x3c088889, v211
	v_sub_f32_e32 v199, 1.0, v199
	v_sub_f32_e32 v202, 1.0, v202
	v_sub_f32_e32 v205, 1.0, v205
	v_sub_f32_e32 v208, 1.0, v208
	v_sub_f32_e32 v217, 1.0, v217
	v_sub_f32_e32 v238, 1.0, v238
	v_sub_f32_e32 v241, 1.0, v241
	v_sub_f32_e32 v244, 1.0, v244
	v_fmaak_f32 v200, v198, v200, 0x3e2aaaab
	v_fmaak_f32 v203, v201, v203, 0x3e2aaaab
	v_fmaak_f32 v206, v204, v206, 0x3e2aaaab
	v_fmaak_f32 v209, v207, v209, 0x3e2aaaab
	v_fmaak_f32 v218, v216, v218, 0x3e2aaaab
	v_fmaak_f32 v239, v219, v239, 0x3e2aaaab
	v_fmaak_f32 v242, v240, v242, 0x3e2aaaab
	v_fmaak_f32 v245, v243, v245, 0x3e2aaaab
	v_fma_f32 v200, v198, v200, 0.5
	v_fma_f32 v203, v201, v203, 0.5
	v_fma_f32 v206, v204, v206, 0.5
	v_fma_f32 v209, v207, v209, 0.5
	v_fma_f32 v218, v216, v218, 0.5
	v_fma_f32 v239, v219, v239, 0.5
	v_fma_f32 v242, v240, v242, 0.5
	v_fma_f32 v245, v243, v245, 0.5
	v_fma_f32 v200, v198, v200, 1.0
	v_fma_f32 v203, v201, v203, 1.0
	v_fma_f32 v206, v204, v206, 1.0
	v_fma_f32 v209, v207, v209, 1.0
	v_fma_f32 v218, v216, v218, 1.0
	v_fma_f32 v239, v219, v239, 1.0
	v_fma_f32 v242, v240, v242, 1.0
	v_fma_f32 v245, v243, v245, 1.0
	v_mul_f32_e64 v200, v200, -v198
	v_mul_f32_e64 v203, v203, -v201
	v_mul_f32_e64 v206, v206, -v204
	v_mul_f32_e64 v209, v209, -v207
	v_mul_f32_e64 v218, v218, -v216
	v_mul_f32_e64 v239, v239, -v219
	v_mul_f32_e64 v242, v242, -v240
	v_mul_f32_e64 v245, v245, -v243
	v_cmp_nlt_f32_e32 vcc, s49, v198
	v_add_f32_e32 v2, v2, v160
	v_mul_f32_e32 v2, 0xbfb8aa3b, v2
	v_cndmask_b32_e32 v199, v200, v199, vcc
	v_cmp_nlt_f32_e32 vcc, s49, v201
	v_add_f32_e32 v3, v3, v161
	v_mul_f32_e32 v3, 0xbfb8aa3b, v3
	v_cndmask_b32_e32 v202, v203, v202, vcc
	v_cmp_nlt_f32_e32 vcc, s49, v204
	v_add_f32_e32 v4, v4, v162
	v_mul_f32_e32 v4, 0xbfb8aa3b, v4
	v_cndmask_b32_e32 v205, v206, v205, vcc
	v_cmp_nlt_f32_e32 vcc, s49, v207
	v_add_f32_e32 v5, v5, v163
	v_mul_f32_e32 v5, 0xbfb8aa3b, v5
	v_cndmask_b32_e32 v208, v209, v208, vcc
	v_cmp_nlt_f32_e32 vcc, s49, v216
	v_add_f32_e32 v6, v6, v160
	v_mul_f32_e32 v6, 0xbfb8aa3b, v6
	v_cndmask_b32_e32 v217, v218, v217, vcc
	v_cmp_nlt_f32_e32 vcc, s49, v219
	v_add_f32_e32 v7, v7, v161
	v_mul_f32_e32 v7, 0xbfb8aa3b, v7
	v_cndmask_b32_e32 v238, v239, v238, vcc
	v_cmp_nlt_f32_e32 vcc, s49, v240
	v_add_f32_e32 v8, v8, v162
	v_mul_f32_e32 v8, 0xbfb8aa3b, v8
	v_cndmask_b32_e32 v241, v242, v241, vcc
	v_cmp_nlt_f32_e32 vcc, s49, v243
	v_add_f32_e32 v9, v9, v163
	v_mul_f32_e32 v9, 0xbfb8aa3b, v9
	v_cndmask_b32_e32 v244, v245, v244, vcc
	v_exp_f32_e32 v2, v2
	v_exp_f32_e32 v3, v3
	v_exp_f32_e32 v4, v4
	v_exp_f32_e32 v5, v5
	v_exp_f32_e32 v6, v6
	v_exp_f32_e32 v7, v7
	v_exp_f32_e32 v8, v8
	v_exp_f32_e32 v9, v9
	v_sqrt_f32_e32 v199, v199
	v_sqrt_f32_e32 v202, v202
	v_sqrt_f32_e32 v205, v205
	v_sqrt_f32_e32 v208, v208
	v_sqrt_f32_e32 v217, v217
	v_sqrt_f32_e32 v238, v238
	v_sqrt_f32_e32 v241, v241
	v_sqrt_f32_e32 v244, v244
	v_add_f32_e32 v2, 1.0, v2
	v_add_f32_e32 v3, 1.0, v3
	v_add_f32_e32 v4, 1.0, v4
	v_add_f32_e32 v5, 1.0, v5
	v_add_f32_e32 v6, 1.0, v6
	v_add_f32_e32 v7, 1.0, v7
	v_add_f32_e32 v8, 1.0, v8
	v_add_f32_e32 v9, 1.0, v9
	v_lshlrev_b32_e32 v200, 16, v176
	v_and_b32_e32 v203, 0xffff0000, v176
; __device__ __forceinline__ float sigmoid_fast(float x) { return __builtin_amdgcn_rcpf(1.f + __expf(-x)); }
; __device__ __forceinline__ float one_minus_exp(float x) { const float p = -x * (1.f + x * (0.5f + x * (0.16666667f + x * (0.041666668f + x * 0.0083333338f)))); return x > -0.1f ? p : 1.f - __expf(x); }
;     template <bool BWD>
;     __device__ __forceinline__ void epi_dir(const f32x4 (&acc)[2][2][4][2], const Unit& u, int wr, int wc, int fr, int fq) const {
;     ...
;                 const f32x4 bav = *(const f32x4*)(bap + n * 64 + coff), bxv = *(const f32x4*)(bxp + n * 64 + coff), lsl = *(const f32x4*)(lmp + n * 64 + coff);
; #pragma unroll
;                 for (int m = 0; m < 4; ++m) {
;                     const u32x2 uw = *(const u32x2*)(Ub + ((size_t)(ai * 128 + m * 16) * 1024 + n * 16) * 2 + loffu);
;                     const float uv[4] = {bflo(uw.x), bfhi(uw.x), bflo(uw.y), bfhi(uw.y)};
; #pragma unroll
;                     for (int j = 0; j < 4; ++j) { const float r = sigmoid_fast(acc[ai][0][m][n][j] + bav[j]), ig = sigmoid_fast(acc[ai][1][m][n][j] + bxv[j]);
;                         const float la = r * lsl[j]; A[m][j] = __expf(la); H[m][j] = __builtin_amdgcn_sqrtf(one_minus_exp(2.f * la)) * (ig * uv[j]); } }
	v_lshlrev_b32_e32 v206, 16, v177
	v_and_b32_e32 v209, 0xffff0000, v177
	v_lshlrev_b32_e32 v218, 16, v178
	v_and_b32_e32 v239, 0xffff0000, v178
	v_lshlrev_b32_e32 v242, 16, v179
	v_and_b32_e32 v245, 0xffff0000, v179
	v_rcp_f32_e32 v2, v2
	v_rcp_f32_e32 v3, v3
	v_rcp_f32_e32 v4, v4
	v_rcp_f32_e32 v5, v5
	v_rcp_f32_e32 v6, v6
	v_rcp_f32_e32 v7, v7
	v_rcp_f32_e32 v8, v8
	v_rcp_f32_e32 v9, v9
	v_mul_f32_e32 v30, 0x3fb8aa3b, v30
	v_mul_f32_e32 v31, 0x3fb8aa3b, v31
	v_mul_f32_e32 v32, 0x3fb8aa3b, v32
	v_mul_f32_e32 v33, 0x3fb8aa3b, v33
	v_mul_f32_e32 v26, 0x3fb8aa3b, v26
	v_mul_f32_e32 v27, 0x3fb8aa3b, v27
	v_mul_f32_e32 v28, 0x3fb8aa3b, v28
	v_mul_f32_e32 v29, 0x3fb8aa3b, v29
	v_mul_f32_e32 v2, v2, v200
	v_mul_f32_e32 v3, v3, v203
	v_mul_f32_e32 v4, v4, v206
	v_mul_f32_e32 v5, v5, v209
	v_mul_f32_e32 v6, v6, v218
	v_mul_f32_e32 v7, v7, v239
	v_mul_f32_e32 v8, v8, v242
	v_mul_f32_e32 v9, v9, v245
	v_exp_f32_e32 v30, v30
	v_exp_f32_e32 v31, v31
	v_exp_f32_e32 v32, v32
	v_exp_f32_e32 v33, v33
	v_exp_f32_e32 v26, v26
	v_exp_f32_e32 v27, v27
	v_exp_f32_e32 v28, v28
	v_exp_f32_e32 v29, v29
	v_mul_f32_e32 v2, v2, v199
	v_mul_f32_e32 v3, v3, v202
	v_mul_f32_e32 v4, v4, v205
	v_mul_f32_e32 v5, v5, v208
	v_mul_f32_e32 v6, v6, v217
	v_mul_f32_e32 v7, v7, v238
	v_mul_f32_e32 v8, v8, v241
	v_mul_f32_e32 v9, v9, v244
	v_add_f32_e32 v22, v22, v156
	v_add_f32_e32 v23, v23, v157
	v_add_f32_e32 v24, v24, v158
	v_add_f32_e32 v25, v25, v159
	v_add_f32_e32 v18, v18, v156
	v_add_f32_e32 v19, v19, v157
	v_add_f32_e32 v20, v20, v158
	v_add_f32_e32 v21, v21, v159
	v_mul_f32_e32 v22, 0xbfb8aa3b, v22
	v_mul_f32_e32 v23, 0xbfb8aa3b, v23
	v_mul_f32_e32 v24, 0xbfb8aa3b, v24
	v_mul_f32_e32 v25, 0xbfb8aa3b, v25
	v_mul_f32_e32 v18, 0xbfb8aa3b, v18
	v_mul_f32_e32 v19, 0xbfb8aa3b, v19
	v_mul_f32_e32 v20, 0xbfb8aa3b, v20
	v_mul_f32_e32 v21, 0xbfb8aa3b, v21
	v_exp_f32_e32 v22, v22
	v_exp_f32_e32 v23, v23
	v_exp_f32_e32 v24, v24
	v_exp_f32_e32 v25, v25
	v_exp_f32_e32 v18, v18
	v_exp_f32_e32 v19, v19
	v_exp_f32_e32 v20, v20
	v_exp_f32_e32 v21, v21
	v_add_f32_e32 v22, 1.0, v22
	v_add_f32_e32 v23, 1.0, v23
	v_add_f32_e32 v24, 1.0, v24
	v_add_f32_e32 v25, 1.0, v25
	v_add_f32_e32 v18, 1.0, v18
	v_add_f32_e32 v19, 1.0, v19
	v_add_f32_e32 v20, 1.0, v20
	v_add_f32_e32 v21, 1.0, v21
	v_rcp_f32_e32 v22, v22
	v_rcp_f32_e32 v23, v23
	v_rcp_f32_e32 v24, v24
	v_rcp_f32_e32 v25, v25
	v_rcp_f32_e32 v18, v18
	v_rcp_f32_e32 v19, v19
	v_rcp_f32_e32 v20, v20
	v_rcp_f32_e32 v21, v21
	v_mul_f32_e32 v22, v164, v22
	v_mul_f32_e32 v23, v165, v23
	v_mul_f32_e32 v24, v166, v24
	v_mul_f32_e32 v25, v167, v25
	v_mul_f32_e32 v18, v164, v18
	v_mul_f32_e32 v19, v165, v19
	v_mul_f32_e32 v20, v166, v20
	v_mul_f32_e32 v21, v167, v21
	v_add_f32_e32 v198, v22, v22
	v_add_f32_e32 v201, v23, v23
	v_add_f32_e32 v204, v24, v24
	v_add_f32_e32 v207, v25, v25
	v_add_f32_e32 v216, v18, v18
	v_add_f32_e32 v219, v19, v19
	v_add_f32_e32 v240, v20, v20
	v_add_f32_e32 v243, v21, v21
	v_mul_f32_e32 v199, 0x3fb8aa3b, v198
	v_mul_f32_e32 v202, 0x3fb8aa3b, v201
	v_mul_f32_e32 v205, 0x3fb8aa3b, v204
	v_mul_f32_e32 v208, 0x3fb8aa3b, v207
	v_mul_f32_e32 v217, 0x3fb8aa3b, v216
	v_mul_f32_e32 v238, 0x3fb8aa3b, v219
	v_mul_f32_e32 v241, 0x3fb8aa3b, v240
	v_mul_f32_e32 v244, 0x3fb8aa3b, v243
	v_exp_f32_e32 v199, v199
	v_exp_f32_e32 v202, v202
	v_exp_f32_e32 v205, v205
	v_exp_f32_e32 v208, v208
	v_exp_f32_e32 v217, v217
	v_exp_f32_e32 v238, v238
	v_exp_f32_e32 v241, v241
	v_exp_f32_e32 v244, v244
	v_fmamk_f32 v200, v198, 0x3c088889, v211
	v_fmamk_f32 v203, v201, 0x3c088889, v211
	v_fmamk_f32 v206, v204, 0x3c088889, v211
	v_fmamk_f32 v209, v207, 0x3c088889, v211
	v_fmamk_f32 v218, v216, 0x3c088889, v211
	v_fmamk_f32 v239, v219, 0x3c088889, v211
	v_fmamk_f32 v242, v240, 0x3c088889, v211
	v_fmamk_f32 v245, v243, 0x3c088889, v211
	v_sub_f32_e32 v199, 1.0, v199
	v_sub_f32_e32 v202, 1.0, v202
	v_sub_f32_e32 v205, 1.0, v205
	v_sub_f32_e32 v208, 1.0, v208
	v_sub_f32_e32 v217, 1.0, v217
	v_sub_f32_e32 v238, 1.0, v238
	v_sub_f32_e32 v241, 1.0, v241
	v_sub_f32_e32 v244, 1.0, v244
	v_fmaak_f32 v200, v198, v200, 0x3e2aaaab
	v_fmaak_f32 v203, v201, v203, 0x3e2aaaab
	v_fmaak_f32 v206, v204, v206, 0x3e2aaaab
	v_fmaak_f32 v209, v207, v209, 0x3e2aaaab
	v_fmaak_f32 v218, v216, v218, 0x3e2aaaab
	v_fmaak_f32 v239, v219, v239, 0x3e2aaaab
	v_fmaak_f32 v242, v240, v242, 0x3e2aaaab
	v_fmaak_f32 v245, v243, v245, 0x3e2aaaab
	v_fma_f32 v200, v198, v200, 0.5
	v_fma_f32 v203, v201, v203, 0.5
	v_fma_f32 v206, v204, v206, 0.5
	v_fma_f32 v209, v207, v209, 0.5
	v_fma_f32 v218, v216, v218, 0.5
	v_fma_f32 v239, v219, v239, 0.5
	v_fma_f32 v242, v240, v242, 0.5
	v_fma_f32 v245, v243, v245, 0.5
	v_fma_f32 v200, v198, v200, 1.0
	v_fma_f32 v203, v201, v203, 1.0
	v_fma_f32 v206, v204, v206, 1.0
	v_fma_f32 v209, v207, v209, 1.0
	v_fma_f32 v218, v216, v218, 1.0
	v_fma_f32 v239, v219, v239, 1.0
	v_fma_f32 v242, v240, v242, 1.0
	v_fma_f32 v245, v243, v245, 1.0
	v_mul_f32_e64 v200, v200, -v198
	v_mul_f32_e64 v203, v203, -v201
	v_mul_f32_e64 v206, v206, -v204
	v_mul_f32_e64 v209, v209, -v207
	v_mul_f32_e64 v218, v218, -v216
	v_mul_f32_e64 v239, v239, -v219
	v_mul_f32_e64 v242, v242, -v240
	v_mul_f32_e64 v245, v245, -v243
	v_cmp_nlt_f32_e32 vcc, s49, v198
	v_add_f32_e32 v10, v10, v160
	v_mul_f32_e32 v10, 0xbfb8aa3b, v10
	v_cndmask_b32_e32 v199, v200, v199, vcc
	v_cmp_nlt_f32_e32 vcc, s49, v201
	v_add_f32_e32 v11, v11, v161
	v_mul_f32_e32 v11, 0xbfb8aa3b, v11
	v_cndmask_b32_e32 v202, v203, v202, vcc
	v_cmp_nlt_f32_e32 vcc, s49, v204
	v_add_f32_e32 v12, v12, v162
	v_mul_f32_e32 v12, 0xbfb8aa3b, v12
	v_cndmask_b32_e32 v205, v206, v205, vcc
	v_cmp_nlt_f32_e32 vcc, s49, v207
; __device__ __forceinline__ float sigmoid_fast(float x) { return __builtin_amdgcn_rcpf(1.f + __expf(-x)); }
; __device__ __forceinline__ float one_minus_exp(float x) { const float p = -x * (1.f + x * (0.5f + x * (0.16666667f + x * (0.041666668f + x * 0.0083333338f)))); return x > -0.1f ? p : 1.f - __expf(x); }
; #define SCAN_STEP(D) { const float ap = dppf<(BWD ? 0x100 : 0x110) + D>(1.f, av), hp = dppf<(BWD ? 0x100 : 0x110) + D>(0.f, hv); hv = fmaf(av, hp, hv); av = av * ap; }
;     template <bool BWD>
;     __device__ __forceinline__ void epi_dir(const f32x4 (&acc)[2][2][4][2], const Unit& u, int wr, int wc, int fr, int fq) const {
;     ...
;                     const u32x2 uw = *(const u32x2*)(Ub + ((size_t)(ai * 128 + m * 16) * 1024 + n * 16) * 2 + loffu);
;                     const float uv[4] = {bflo(uw.x), bfhi(uw.x), bflo(uw.y), bfhi(uw.y)};
; #pragma unroll
;                     for (int j = 0; j < 4; ++j) { const float r = sigmoid_fast(acc[ai][0][m][n][j] + bav[j]), ig = sigmoid_fast(acc[ai][1][m][n][j] + bxv[j]);
;                         const float la = r * lsl[j]; A[m][j] = __expf(la); H[m][j] = __builtin_amdgcn_sqrtf(one_minus_exp(2.f * la)) * (ig * uv[j]); } }
; #pragma unroll
;                 for (int m = 0; m < 4; ++m)
; #pragma unroll
;                     for (int j = 0; j < 4; ++j) { float av = A[m][j], hv = H[m][j];
;     ...
;                         SCAN_STEP(1) SCAN_STEP(2) SCAN_STEP(4) SCAN_STEP(8)
	v_add_f32_e32 v13, v13, v163
	v_mul_f32_e32 v13, 0xbfb8aa3b, v13
	v_cndmask_b32_e32 v208, v209, v208, vcc
	v_cmp_nlt_f32_e32 vcc, s49, v216
	v_add_f32_e32 v14, v14, v160
	v_mul_f32_e32 v14, 0xbfb8aa3b, v14
	v_cndmask_b32_e32 v217, v218, v217, vcc
	v_cmp_nlt_f32_e32 vcc, s49, v219
	v_add_f32_e32 v15, v15, v161
	v_mul_f32_e32 v15, 0xbfb8aa3b, v15
	v_cndmask_b32_e32 v238, v239, v238, vcc
	v_cmp_nlt_f32_e32 vcc, s49, v240
	v_add_f32_e32 v16, v16, v162
	v_mul_f32_e32 v16, 0xbfb8aa3b, v16
	v_cndmask_b32_e32 v241, v242, v241, vcc
	v_cmp_nlt_f32_e32 vcc, s49, v243
	v_add_f32_e32 v17, v17, v163
	v_mul_f32_e32 v17, 0xbfb8aa3b, v17
	v_cndmask_b32_e32 v244, v245, v244, vcc
	v_exp_f32_e32 v10, v10
	v_exp_f32_e32 v11, v11
	v_exp_f32_e32 v12, v12
	v_exp_f32_e32 v13, v13
	v_exp_f32_e32 v14, v14
	v_exp_f32_e32 v15, v15
	v_exp_f32_e32 v16, v16
	v_exp_f32_e32 v17, v17
	v_sqrt_f32_e32 v199, v199
	v_sqrt_f32_e32 v202, v202
	v_sqrt_f32_e32 v205, v205
	v_sqrt_f32_e32 v208, v208
	v_sqrt_f32_e32 v217, v217
	v_sqrt_f32_e32 v238, v238
	v_sqrt_f32_e32 v241, v241
	v_sqrt_f32_e32 v244, v244
	v_add_f32_e32 v10, 1.0, v10
	v_add_f32_e32 v11, 1.0, v11
	v_add_f32_e32 v12, 1.0, v12
	v_add_f32_e32 v13, 1.0, v13
	v_add_f32_e32 v14, 1.0, v14
	v_add_f32_e32 v15, 1.0, v15
	v_add_f32_e32 v16, 1.0, v16
	v_add_f32_e32 v17, 1.0, v17
	v_lshlrev_b32_e32 v200, 16, v182
	v_and_b32_e32 v203, 0xffff0000, v182
	v_lshlrev_b32_e32 v206, 16, v183
	v_and_b32_e32 v209, 0xffff0000, v183
	v_lshlrev_b32_e32 v218, 16, v184
	v_and_b32_e32 v239, 0xffff0000, v184
	v_lshlrev_b32_e32 v242, 16, v185
	v_and_b32_e32 v245, 0xffff0000, v185
	v_rcp_f32_e32 v10, v10
	v_rcp_f32_e32 v11, v11
	v_rcp_f32_e32 v12, v12
	v_rcp_f32_e32 v13, v13
	v_rcp_f32_e32 v14, v14
	v_rcp_f32_e32 v15, v15
	v_rcp_f32_e32 v16, v16
	v_rcp_f32_e32 v17, v17
	v_mul_f32_e32 v22, 0x3fb8aa3b, v22
	v_mul_f32_e32 v23, 0x3fb8aa3b, v23
	v_mul_f32_e32 v24, 0x3fb8aa3b, v24
	v_mul_f32_e32 v25, 0x3fb8aa3b, v25
	v_mul_f32_e32 v18, 0x3fb8aa3b, v18
	v_mul_f32_e32 v19, 0x3fb8aa3b, v19
	v_mul_f32_e32 v20, 0x3fb8aa3b, v20
	v_mul_f32_e32 v21, 0x3fb8aa3b, v21
	v_mul_f32_e32 v10, v10, v200
	v_mul_f32_e32 v11, v11, v203
	v_mul_f32_e32 v12, v12, v206
	v_mul_f32_e32 v13, v13, v209
	v_mul_f32_e32 v14, v14, v218
	v_mul_f32_e32 v15, v15, v239
	v_mul_f32_e32 v16, v16, v242
	v_mul_f32_e32 v17, v17, v245
	v_exp_f32_e32 v22, v22
	v_exp_f32_e32 v23, v23
	v_exp_f32_e32 v24, v24
	v_exp_f32_e32 v25, v25
	v_exp_f32_e32 v18, v18
	v_exp_f32_e32 v19, v19
	v_exp_f32_e32 v20, v20
	v_exp_f32_e32 v21, v21
	v_mul_f32_e32 v10, v10, v199
	v_mul_f32_e32 v11, v11, v202
	v_mul_f32_e32 v12, v12, v205
	v_mul_f32_e32 v13, v13, v208
	v_mul_f32_e32 v14, v14, v217
	v_mul_f32_e32 v15, v15, v238
	v_mul_f32_e32 v16, v16, v241
	v_mul_f32_e32 v17, v17, v244
	v_fmac_f32_dpp v2, v2, v30 row_shl:1 row_mask:0xf bank_mask:0xf
	v_mul_f32_dpp v30, v30, v30 row_shl:1 row_mask:0xf bank_mask:0xf
	v_fmac_f32_dpp v3, v3, v31 row_shl:1 row_mask:0xf bank_mask:0xf
	v_mul_f32_dpp v31, v31, v31 row_shl:1 row_mask:0xf bank_mask:0xf
	v_fmac_f32_dpp v4, v4, v32 row_shl:1 row_mask:0xf bank_mask:0xf
	v_mul_f32_dpp v32, v32, v32 row_shl:1 row_mask:0xf bank_mask:0xf
	v_fmac_f32_dpp v5, v5, v33 row_shl:1 row_mask:0xf bank_mask:0xf
	v_mul_f32_dpp v33, v33, v33 row_shl:1 row_mask:0xf bank_mask:0xf
	v_fmac_f32_dpp v6, v6, v26 row_shl:1 row_mask:0xf bank_mask:0xf
	v_mul_f32_dpp v26, v26, v26 row_shl:1 row_mask:0xf bank_mask:0xf
	v_fmac_f32_dpp v7, v7, v27 row_shl:1 row_mask:0xf bank_mask:0xf
	v_mul_f32_dpp v27, v27, v27 row_shl:1 row_mask:0xf bank_mask:0xf
	v_fmac_f32_dpp v8, v8, v28 row_shl:1 row_mask:0xf bank_mask:0xf
	v_mul_f32_dpp v28, v28, v28 row_shl:1 row_mask:0xf bank_mask:0xf
	v_fmac_f32_dpp v9, v9, v29 row_shl:1 row_mask:0xf bank_mask:0xf
	v_mul_f32_dpp v29, v29, v29 row_shl:1 row_mask:0xf bank_mask:0xf
	v_fmac_f32_dpp v10, v10, v22 row_shl:1 row_mask:0xf bank_mask:0xf
	v_mul_f32_dpp v22, v22, v22 row_shl:1 row_mask:0xf bank_mask:0xf
	v_fmac_f32_dpp v11, v11, v23 row_shl:1 row_mask:0xf bank_mask:0xf
	v_mul_f32_dpp v23, v23, v23 row_shl:1 row_mask:0xf bank_mask:0xf
	v_fmac_f32_dpp v12, v12, v24 row_shl:1 row_mask:0xf bank_mask:0xf
	v_mul_f32_dpp v24, v24, v24 row_shl:1 row_mask:0xf bank_mask:0xf
	v_fmac_f32_dpp v13, v13, v25 row_shl:1 row_mask:0xf bank_mask:0xf
	v_mul_f32_dpp v25, v25, v25 row_shl:1 row_mask:0xf bank_mask:0xf
	v_fmac_f32_dpp v14, v14, v18 row_shl:1 row_mask:0xf bank_mask:0xf
	v_mul_f32_dpp v18, v18, v18 row_shl:1 row_mask:0xf bank_mask:0xf
	v_fmac_f32_dpp v15, v15, v19 row_shl:1 row_mask:0xf bank_mask:0xf
	v_mul_f32_dpp v19, v19, v19 row_shl:1 row_mask:0xf bank_mask:0xf
	v_fmac_f32_dpp v16, v16, v20 row_shl:1 row_mask:0xf bank_mask:0xf
	v_mul_f32_dpp v20, v20, v20 row_shl:1 row_mask:0xf bank_mask:0xf
	v_fmac_f32_dpp v17, v17, v21 row_shl:1 row_mask:0xf bank_mask:0xf
	v_mul_f32_dpp v21, v21, v21 row_shl:1 row_mask:0xf bank_mask:0xf
	v_fmac_f32_dpp v2, v2, v30 row_shl:2 row_mask:0xf bank_mask:0xf
	v_mul_f32_dpp v30, v30, v30 row_shl:2 row_mask:0xf bank_mask:0xf
	v_fmac_f32_dpp v3, v3, v31 row_shl:2 row_mask:0xf bank_mask:0xf
	v_mul_f32_dpp v31, v31, v31 row_shl:2 row_mask:0xf bank_mask:0xf
	v_fmac_f32_dpp v4, v4, v32 row_shl:2 row_mask:0xf bank_mask:0xf
	v_mul_f32_dpp v32, v32, v32 row_shl:2 row_mask:0xf bank_mask:0xf
	v_fmac_f32_dpp v5, v5, v33 row_shl:2 row_mask:0xf bank_mask:0xf
	v_mul_f32_dpp v33, v33, v33 row_shl:2 row_mask:0xf bank_mask:0xf
	v_fmac_f32_dpp v6, v6, v26 row_shl:2 row_mask:0xf bank_mask:0xf
	v_mul_f32_dpp v26, v26, v26 row_shl:2 row_mask:0xf bank_mask:0xf
	v_fmac_f32_dpp v7, v7, v27 row_shl:2 row_mask:0xf bank_mask:0xf
	v_mul_f32_dpp v27, v27, v27 row_shl:2 row_mask:0xf bank_mask:0xf
; #define SCAN_STEP(D) { const float ap = dppf<(BWD ? 0x100 : 0x110) + D>(1.f, av), hp = dppf<(BWD ? 0x100 : 0x110) + D>(0.f, hv); hv = fmaf(av, hp, hv); av = av * ap; }
;     template <bool BWD>
;     __device__ __forceinline__ void epi_dir(const f32x4 (&acc)[2][2][4][2], const Unit& u, int wr, int wc, int fr, int fq) const {
;     ...
;                     for (int j = 0; j < 4; ++j) { float av = A[m][j], hv = H[m][j];
;     ...
;                         SCAN_STEP(1) SCAN_STEP(2) SCAN_STEP(4) SCAN_STEP(8)
;     ...
;                         A[m][j] = av; H[m][j] = hv; }
; #pragma unroll
;                 for (int j = 0; j < 4; ++j) { float Ar = 1.f, Hr = 0.f;
; #pragma unroll
;                     for (int mm = 0; mm < 4; ++mm) { const int m = BWD ? 3 - mm : mm;
;                         H[m][j] = fmaf(A[m][j], Hr, H[m][j]); A[m][j] = A[m][j] * Ar;
;                         if (mm < 3) { Ar = __shfl(A[m][j], bsel); Hr = __shfl(H[m][j], bsel); } } }
	v_fmac_f32_dpp v8, v8, v28 row_shl:2 row_mask:0xf bank_mask:0xf
	v_mul_f32_dpp v28, v28, v28 row_shl:2 row_mask:0xf bank_mask:0xf
	v_fmac_f32_dpp v9, v9, v29 row_shl:2 row_mask:0xf bank_mask:0xf
	v_mul_f32_dpp v29, v29, v29 row_shl:2 row_mask:0xf bank_mask:0xf
	v_fmac_f32_dpp v10, v10, v22 row_shl:2 row_mask:0xf bank_mask:0xf
	v_mul_f32_dpp v22, v22, v22 row_shl:2 row_mask:0xf bank_mask:0xf
	v_fmac_f32_dpp v11, v11, v23 row_shl:2 row_mask:0xf bank_mask:0xf
	v_mul_f32_dpp v23, v23, v23 row_shl:2 row_mask:0xf bank_mask:0xf
	v_fmac_f32_dpp v12, v12, v24 row_shl:2 row_mask:0xf bank_mask:0xf
	v_mul_f32_dpp v24, v24, v24 row_shl:2 row_mask:0xf bank_mask:0xf
	v_fmac_f32_dpp v13, v13, v25 row_shl:2 row_mask:0xf bank_mask:0xf
	v_mul_f32_dpp v25, v25, v25 row_shl:2 row_mask:0xf bank_mask:0xf
	v_fmac_f32_dpp v14, v14, v18 row_shl:2 row_mask:0xf bank_mask:0xf
	v_mul_f32_dpp v18, v18, v18 row_shl:2 row_mask:0xf bank_mask:0xf
	v_fmac_f32_dpp v15, v15, v19 row_shl:2 row_mask:0xf bank_mask:0xf
	v_mul_f32_dpp v19, v19, v19 row_shl:2 row_mask:0xf bank_mask:0xf
	v_fmac_f32_dpp v16, v16, v20 row_shl:2 row_mask:0xf bank_mask:0xf
	v_mul_f32_dpp v20, v20, v20 row_shl:2 row_mask:0xf bank_mask:0xf
	v_fmac_f32_dpp v17, v17, v21 row_shl:2 row_mask:0xf bank_mask:0xf
	v_mul_f32_dpp v21, v21, v21 row_shl:2 row_mask:0xf bank_mask:0xf
	v_fmac_f32_dpp v2, v2, v30 row_shl:4 row_mask:0xf bank_mask:0xf
	v_mul_f32_dpp v30, v30, v30 row_shl:4 row_mask:0xf bank_mask:0xf
	v_fmac_f32_dpp v3, v3, v31 row_shl:4 row_mask:0xf bank_mask:0xf
	v_mul_f32_dpp v31, v31, v31 row_shl:4 row_mask:0xf bank_mask:0xf
	v_fmac_f32_dpp v4, v4, v32 row_shl:4 row_mask:0xf bank_mask:0xf
	v_mul_f32_dpp v32, v32, v32 row_shl:4 row_mask:0xf bank_mask:0xf
	v_fmac_f32_dpp v5, v5, v33 row_shl:4 row_mask:0xf bank_mask:0xf
	v_mul_f32_dpp v33, v33, v33 row_shl:4 row_mask:0xf bank_mask:0xf
	v_fmac_f32_dpp v6, v6, v26 row_shl:4 row_mask:0xf bank_mask:0xf
	v_mul_f32_dpp v26, v26, v26 row_shl:4 row_mask:0xf bank_mask:0xf
	v_fmac_f32_dpp v7, v7, v27 row_shl:4 row_mask:0xf bank_mask:0xf
	v_mul_f32_dpp v27, v27, v27 row_shl:4 row_mask:0xf bank_mask:0xf
	v_fmac_f32_dpp v8, v8, v28 row_shl:4 row_mask:0xf bank_mask:0xf
	v_mul_f32_dpp v28, v28, v28 row_shl:4 row_mask:0xf bank_mask:0xf
	v_fmac_f32_dpp v9, v9, v29 row_shl:4 row_mask:0xf bank_mask:0xf
	v_mul_f32_dpp v29, v29, v29 row_shl:4 row_mask:0xf bank_mask:0xf
	v_fmac_f32_dpp v10, v10, v22 row_shl:4 row_mask:0xf bank_mask:0xf
	v_mul_f32_dpp v22, v22, v22 row_shl:4 row_mask:0xf bank_mask:0xf
	v_fmac_f32_dpp v11, v11, v23 row_shl:4 row_mask:0xf bank_mask:0xf
	v_mul_f32_dpp v23, v23, v23 row_shl:4 row_mask:0xf bank_mask:0xf
	v_fmac_f32_dpp v12, v12, v24 row_shl:4 row_mask:0xf bank_mask:0xf
	v_mul_f32_dpp v24, v24, v24 row_shl:4 row_mask:0xf bank_mask:0xf
	v_fmac_f32_dpp v13, v13, v25 row_shl:4 row_mask:0xf bank_mask:0xf
	v_mul_f32_dpp v25, v25, v25 row_shl:4 row_mask:0xf bank_mask:0xf
	v_fmac_f32_dpp v14, v14, v18 row_shl:4 row_mask:0xf bank_mask:0xf
	v_mul_f32_dpp v18, v18, v18 row_shl:4 row_mask:0xf bank_mask:0xf
	v_fmac_f32_dpp v15, v15, v19 row_shl:4 row_mask:0xf bank_mask:0xf
	v_mul_f32_dpp v19, v19, v19 row_shl:4 row_mask:0xf bank_mask:0xf
	v_fmac_f32_dpp v16, v16, v20 row_shl:4 row_mask:0xf bank_mask:0xf
	v_mul_f32_dpp v20, v20, v20 row_shl:4 row_mask:0xf bank_mask:0xf
	v_fmac_f32_dpp v17, v17, v21 row_shl:4 row_mask:0xf bank_mask:0xf
	v_mul_f32_dpp v21, v21, v21 row_shl:4 row_mask:0xf bank_mask:0xf
	v_fmac_f32_dpp v2, v2, v30 row_shl:8 row_mask:0xf bank_mask:0xf
	v_mul_f32_dpp v30, v30, v30 row_shl:8 row_mask:0xf bank_mask:0xf
	v_fmac_f32_dpp v3, v3, v31 row_shl:8 row_mask:0xf bank_mask:0xf
	v_mul_f32_dpp v31, v31, v31 row_shl:8 row_mask:0xf bank_mask:0xf
	v_fmac_f32_dpp v4, v4, v32 row_shl:8 row_mask:0xf bank_mask:0xf
	v_mul_f32_dpp v32, v32, v32 row_shl:8 row_mask:0xf bank_mask:0xf
	v_fmac_f32_dpp v5, v5, v33 row_shl:8 row_mask:0xf bank_mask:0xf
	v_mul_f32_dpp v33, v33, v33 row_shl:8 row_mask:0xf bank_mask:0xf
	v_fmac_f32_dpp v6, v6, v26 row_shl:8 row_mask:0xf bank_mask:0xf
	v_mul_f32_dpp v26, v26, v26 row_shl:8 row_mask:0xf bank_mask:0xf
	v_fmac_f32_dpp v7, v7, v27 row_shl:8 row_mask:0xf bank_mask:0xf
	v_mul_f32_dpp v27, v27, v27 row_shl:8 row_mask:0xf bank_mask:0xf
	v_fmac_f32_dpp v8, v8, v28 row_shl:8 row_mask:0xf bank_mask:0xf
	v_mul_f32_dpp v28, v28, v28 row_shl:8 row_mask:0xf bank_mask:0xf
	v_fmac_f32_dpp v9, v9, v29 row_shl:8 row_mask:0xf bank_mask:0xf
	v_mul_f32_dpp v29, v29, v29 row_shl:8 row_mask:0xf bank_mask:0xf
	v_fmac_f32_dpp v10, v10, v22 row_shl:8 row_mask:0xf bank_mask:0xf
	v_mul_f32_dpp v22, v22, v22 row_shl:8 row_mask:0xf bank_mask:0xf
	v_fmac_f32_dpp v11, v11, v23 row_shl:8 row_mask:0xf bank_mask:0xf
	v_mul_f32_dpp v23, v23, v23 row_shl:8 row_mask:0xf bank_mask:0xf
	v_fmac_f32_dpp v12, v12, v24 row_shl:8 row_mask:0xf bank_mask:0xf
	v_mul_f32_dpp v24, v24, v24 row_shl:8 row_mask:0xf bank_mask:0xf
	v_fmac_f32_dpp v13, v13, v25 row_shl:8 row_mask:0xf bank_mask:0xf
	v_mul_f32_dpp v25, v25, v25 row_shl:8 row_mask:0xf bank_mask:0xf
	v_fmac_f32_dpp v14, v14, v18 row_shl:8 row_mask:0xf bank_mask:0xf
	v_mul_f32_dpp v18, v18, v18 row_shl:8 row_mask:0xf bank_mask:0xf
	v_fmac_f32_dpp v15, v15, v19 row_shl:8 row_mask:0xf bank_mask:0xf
	v_mul_f32_dpp v19, v19, v19 row_shl:8 row_mask:0xf bank_mask:0xf
	v_fmac_f32_dpp v16, v16, v20 row_shl:8 row_mask:0xf bank_mask:0xf
	v_mul_f32_dpp v20, v20, v20 row_shl:8 row_mask:0xf bank_mask:0xf
	v_fmac_f32_dpp v17, v17, v21 row_shl:8 row_mask:0xf bank_mask:0xf
	v_mul_f32_dpp v21, v21, v21 row_shl:8 row_mask:0xf bank_mask:0xf
	v_fmac_f32_dpp v10, v14, v22 row_newbcast:0 row_mask:0xf bank_mask:0xf
; __device__ __forceinline__ unsigned pk2(float lo, float hi) { return f2bf(lo) | (f2bf(hi) << 16); }
; __device__ __forceinline__ float sigmoid_fast(float x) { return __builtin_amdgcn_rcpf(1.f + __expf(-x)); }
; __device__ __forceinline__ float one_minus_exp(float x) { const float p = -x * (1.f + x * (0.5f + x * (0.16666667f + x * (0.041666668f + x * 0.0083333338f)))); return x > -0.1f ? p : 1.f - __expf(x); }
;     template <bool BWD>
;     __device__ __forceinline__ void epi_dir(const f32x4 (&acc)[2][2][4][2], const Unit& u, int wr, int wc, int fr, int fq) const {
;     ...
;                 const f32x4 bav = *(const f32x4*)(bap + n * 64 + coff), bxv = *(const f32x4*)(bxp + n * 64 + coff), lsl = *(const f32x4*)(lmp + n * 64 + coff);
; #pragma unroll
;                 for (int m = 0; m < 4; ++m) {
;                     const u32x2 uw = *(const u32x2*)(Ub + ((size_t)(ai * 128 + m * 16) * 1024 + n * 16) * 2 + loffu);
;                     const float uv[4] = {bflo(uw.x), bfhi(uw.x), bflo(uw.y), bfhi(uw.y)};
; #pragma unroll
;                     for (int j = 0; j < 4; ++j) { const float r = sigmoid_fast(acc[ai][0][m][n][j] + bav[j]), ig = sigmoid_fast(acc[ai][1][m][n][j] + bxv[j]);
;                         const float la = r * lsl[j]; A[m][j] = __expf(la); H[m][j] = __builtin_amdgcn_sqrtf(one_minus_exp(2.f * la)) * (ig * uv[j]); } }
;     ...
;                 for (int j = 0; j < 4; ++j) { float Ar = 1.f, Hr = 0.f;
; #pragma unroll
;                     for (int mm = 0; mm < 4; ++mm) { const int m = BWD ? 3 - mm : mm;
;                         H[m][j] = fmaf(A[m][j], Hr, H[m][j]); A[m][j] = A[m][j] * Ar;
;                         if (mm < 3) { Ar = __shfl(A[m][j], bsel); Hr = __shfl(H[m][j], bsel); } } }
; #pragma unroll
;                 for (int m = 0; m < 4; ++m) { u32x4 w; w.x = pk2(H[m][0], H[m][1]); w.y = pk2(H[m][2], H[m][3]); w.z = pk2(A[m][0], A[m][1]); w.w = pk2(A[m][2], A[m][3]);
;                     *(u32x4*)(Hb + ((size_t)(ai * 128 + m * 16) * 1024 + n * 16) * 4 + loffh) = w; }
;                 constexpr int me = BWD ? 0 : 3;
;                 if (fr == (BWD ? 0 : 15)) { const size_t o = (size_t)chunk * 1024 + gblk * 128 + n * 16;
;                     *(f32x4*)((char*)(AGG + (size_t)(dir * 2 + 0) * NB * NCHUNK * 1024 + o) + coff) = A[me];
;                     *(f32x4*)((char*)(AGG + (size_t)(dir * 2 + 1) * NB * NCHUNK * 1024 + o) + coff) = H[me]; }
	v_mul_f32_dpp v22, v18, v22 row_newbcast:0 row_mask:0xf bank_mask:0xf
	v_fmac_f32_dpp v11, v15, v23 row_newbcast:0 row_mask:0xf bank_mask:0xf
	v_mul_f32_dpp v23, v19, v23 row_newbcast:0 row_mask:0xf bank_mask:0xf
	v_fmac_f32_dpp v12, v16, v24 row_newbcast:0 row_mask:0xf bank_mask:0xf
	v_mul_f32_dpp v24, v20, v24 row_newbcast:0 row_mask:0xf bank_mask:0xf
	v_fmac_f32_dpp v13, v17, v25 row_newbcast:0 row_mask:0xf bank_mask:0xf
	v_mul_f32_dpp v25, v21, v25 row_newbcast:0 row_mask:0xf bank_mask:0xf
	v_fmac_f32_dpp v6, v10, v26 row_newbcast:0 row_mask:0xf bank_mask:0xf
	v_mul_f32_dpp v26, v22, v26 row_newbcast:0 row_mask:0xf bank_mask:0xf
	v_fmac_f32_dpp v7, v11, v27 row_newbcast:0 row_mask:0xf bank_mask:0xf
	v_mul_f32_dpp v27, v23, v27 row_newbcast:0 row_mask:0xf bank_mask:0xf
	v_fmac_f32_dpp v8, v12, v28 row_newbcast:0 row_mask:0xf bank_mask:0xf
	v_mul_f32_dpp v28, v24, v28 row_newbcast:0 row_mask:0xf bank_mask:0xf
	v_fmac_f32_dpp v9, v13, v29 row_newbcast:0 row_mask:0xf bank_mask:0xf
	v_mul_f32_dpp v29, v25, v29 row_newbcast:0 row_mask:0xf bank_mask:0xf
	v_fmac_f32_dpp v2, v6, v30 row_newbcast:0 row_mask:0xf bank_mask:0xf
	v_mul_f32_dpp v30, v26, v30 row_newbcast:0 row_mask:0xf bank_mask:0xf
	v_fmac_f32_dpp v3, v7, v31 row_newbcast:0 row_mask:0xf bank_mask:0xf
	v_mul_f32_dpp v31, v27, v31 row_newbcast:0 row_mask:0xf bank_mask:0xf
	v_fmac_f32_dpp v4, v8, v32 row_newbcast:0 row_mask:0xf bank_mask:0xf
	v_mul_f32_dpp v32, v28, v32 row_newbcast:0 row_mask:0xf bank_mask:0xf
	v_fmac_f32_dpp v5, v9, v33 row_newbcast:0 row_mask:0xf bank_mask:0xf
	v_mul_f32_dpp v33, v29, v33 row_newbcast:0 row_mask:0xf bank_mask:0xf
	s_and_saveexec_b64 s[46:47], s[40:41]
	global_store_dwordx4 v188, v[30:33], s[14:15] offset:64 sc1
	global_store_dwordx4 v188, v[2:5], s[10:11] offset:64 sc1
	s_mov_b64 exec, s[46:47]
	v_cvt_pk_bf16_f32 v14, v14, v15
	v_cvt_pk_bf16_f32 v15, v16, v17
	v_cvt_pk_bf16_f32 v16, v18, v19
	v_cvt_pk_bf16_f32 v17, v20, v21
	global_store_dwordx4 v197, v[14:17], s[56:57] offset:64 sc1
	v_cvt_pk_bf16_f32 v10, v10, v11
	v_cvt_pk_bf16_f32 v11, v12, v13
	v_cvt_pk_bf16_f32 v12, v22, v23
	v_cvt_pk_bf16_f32 v13, v24, v25
	global_store_dwordx4 v196, v[10:13], s[56:57] offset:64 sc1
	v_cvt_pk_bf16_f32 v6, v6, v7
	v_cvt_pk_bf16_f32 v7, v8, v9
	v_cvt_pk_bf16_f32 v8, v26, v27
	v_cvt_pk_bf16_f32 v9, v28, v29
	global_store_dwordx4 v195, v[6:9], s[56:57] offset:64 sc1
	v_cvt_pk_bf16_f32 v2, v2, v3
	v_cvt_pk_bf16_f32 v3, v4, v5
	v_cvt_pk_bf16_f32 v4, v30, v31
	v_cvt_pk_bf16_f32 v5, v32, v33
	global_store_dwordx4 v194, v[2:5], s[56:57] offset:64 sc1
	s_branch .Lge_done
.Lge_fwd:
	s_add_u32 s56, s54, 0x80000
	s_addc_u32 s57, s55, 0
	s_add_u32 s26, s79, s12
	s_addc_u32 s27, s80, 0
	global_load_dwordx4 v[130:133], v228, s[26:27]
	s_add_u32 s26, s81, s12
	s_addc_u32 s27, s82, 0
	global_load_dwordx4 v[134:137], v228, s[26:27]
	s_add_u32 s26, s76, s12
	s_addc_u32 s27, s77, 0
	global_load_dwordx4 v[138:141], v228, s[26:27]
	global_load_dwordx2 v[168:169], v190, s[50:51]
	global_load_dwordx2 v[170:171], v191, s[50:51]
	global_load_dwordx2 v[172:173], v192, s[50:51]
	global_load_dwordx2 v[174:175], v193, s[50:51]
	global_load_dwordx2 v[176:177], v190, s[52:53]
	global_load_dwordx2 v[178:179], v191, s[52:53]
	global_load_dwordx2 v[182:183], v192, s[52:53]
	global_load_dwordx2 v[184:185], v193, s[52:53]
	s_waitcnt vmcnt(4)
	v_add_f32_e32 v126, v126, v130
	v_add_f32_e32 v127, v127, v131
	v_add_f32_e32 v128, v128, v132
	v_add_f32_e32 v129, v129, v133
	v_add_f32_e32 v122, v122, v130
	v_add_f32_e32 v123, v123, v131
	v_add_f32_e32 v124, v124, v132
	v_add_f32_e32 v125, v125, v133
	v_mul_f32_e32 v126, 0xbfb8aa3b, v126
	v_mul_f32_e32 v127, 0xbfb8aa3b, v127
	v_mul_f32_e32 v128, 0xbfb8aa3b, v128
	v_mul_f32_e32 v129, 0xbfb8aa3b, v129
	v_mul_f32_e32 v122, 0xbfb8aa3b, v122
	v_mul_f32_e32 v123, 0xbfb8aa3b, v123
	v_mul_f32_e32 v124, 0xbfb8aa3b, v124
	v_mul_f32_e32 v125, 0xbfb8aa3b, v125
	v_exp_f32_e32 v126, v126
	v_exp_f32_e32 v127, v127
	v_exp_f32_e32 v128, v128
	v_exp_f32_e32 v129, v129
	v_exp_f32_e32 v122, v122
	v_exp_f32_e32 v123, v123
	v_exp_f32_e32 v124, v124
	v_exp_f32_e32 v125, v125
	v_add_f32_e32 v126, 1.0, v126
	v_add_f32_e32 v127, 1.0, v127
	v_add_f32_e32 v128, 1.0, v128
	v_add_f32_e32 v129, 1.0, v129
	v_add_f32_e32 v122, 1.0, v122
	v_add_f32_e32 v123, 1.0, v123
	v_add_f32_e32 v124, 1.0, v124
	v_add_f32_e32 v125, 1.0, v125
	v_rcp_f32_e32 v126, v126
	v_rcp_f32_e32 v127, v127
	v_rcp_f32_e32 v128, v128
	v_rcp_f32_e32 v129, v129
	v_rcp_f32_e32 v122, v122
	v_rcp_f32_e32 v123, v123
	v_rcp_f32_e32 v124, v124
	v_rcp_f32_e32 v125, v125
	v_mul_f32_e32 v126, v138, v126
	v_mul_f32_e32 v127, v139, v127
	v_mul_f32_e32 v128, v140, v128
	v_mul_f32_e32 v129, v141, v129
	v_mul_f32_e32 v122, v138, v122
	v_mul_f32_e32 v123, v139, v123
	v_mul_f32_e32 v124, v140, v124
	v_mul_f32_e32 v125, v141, v125
	v_add_f32_e32 v198, v126, v126
	v_add_f32_e32 v201, v127, v127
	v_add_f32_e32 v204, v128, v128
	v_add_f32_e32 v207, v129, v129
	v_add_f32_e32 v216, v122, v122
	v_add_f32_e32 v219, v123, v123
	v_add_f32_e32 v240, v124, v124
	v_add_f32_e32 v243, v125, v125
	v_mul_f32_e32 v199, 0x3fb8aa3b, v198
	v_mul_f32_e32 v202, 0x3fb8aa3b, v201
	v_mul_f32_e32 v205, 0x3fb8aa3b, v204
	v_mul_f32_e32 v208, 0x3fb8aa3b, v207
	v_mul_f32_e32 v217, 0x3fb8aa3b, v216
	v_mul_f32_e32 v238, 0x3fb8aa3b, v219
	v_mul_f32_e32 v241, 0x3fb8aa3b, v240
	v_mul_f32_e32 v244, 0x3fb8aa3b, v243
	v_exp_f32_e32 v199, v199
	v_exp_f32_e32 v202, v202
	v_exp_f32_e32 v205, v205
	v_exp_f32_e32 v208, v208
	v_exp_f32_e32 v217, v217
	v_exp_f32_e32 v238, v238
	v_exp_f32_e32 v241, v241
	v_exp_f32_e32 v244, v244
	v_fmamk_f32 v200, v198, 0x3c088889, v211
; __device__ __forceinline__ float sigmoid_fast(float x) { return __builtin_amdgcn_rcpf(1.f + __expf(-x)); }
; __device__ __forceinline__ float one_minus_exp(float x) { const float p = -x * (1.f + x * (0.5f + x * (0.16666667f + x * (0.041666668f + x * 0.0083333338f)))); return x > -0.1f ? p : 1.f - __expf(x); }
;     template <bool BWD>
;     __device__ __forceinline__ void epi_dir(const f32x4 (&acc)[2][2][4][2], const Unit& u, int wr, int wc, int fr, int fq) const {
;     ...
;                     for (int j = 0; j < 4; ++j) { const float r = sigmoid_fast(acc[ai][0][m][n][j] + bav[j]), ig = sigmoid_fast(acc[ai][1][m][n][j] + bxv[j]);
;                         const float la = r * lsl[j]; A[m][j] = __expf(la); H[m][j] = __builtin_amdgcn_sqrtf(one_minus_exp(2.f * la)) * (ig * uv[j]); } }
	v_fmamk_f32 v203, v201, 0x3c088889, v211
	v_fmamk_f32 v206, v204, 0x3c088889, v211
	v_fmamk_f32 v209, v207, 0x3c088889, v211
	v_fmamk_f32 v218, v216, 0x3c088889, v211
	v_fmamk_f32 v239, v219, 0x3c088889, v211
	v_fmamk_f32 v242, v240, 0x3c088889, v211
	v_fmamk_f32 v245, v243, 0x3c088889, v211
	v_sub_f32_e32 v199, 1.0, v199
	v_sub_f32_e32 v202, 1.0, v202
	v_sub_f32_e32 v205, 1.0, v205
	v_sub_f32_e32 v208, 1.0, v208
	v_sub_f32_e32 v217, 1.0, v217
	v_sub_f32_e32 v238, 1.0, v238
	v_sub_f32_e32 v241, 1.0, v241
	v_sub_f32_e32 v244, 1.0, v244
	v_fmaak_f32 v200, v198, v200, 0x3e2aaaab
	v_fmaak_f32 v203, v201, v203, 0x3e2aaaab
	v_fmaak_f32 v206, v204, v206, 0x3e2aaaab
	v_fmaak_f32 v209, v207, v209, 0x3e2aaaab
	v_fmaak_f32 v218, v216, v218, 0x3e2aaaab
	v_fmaak_f32 v239, v219, v239, 0x3e2aaaab
	v_fmaak_f32 v242, v240, v242, 0x3e2aaaab
	v_fmaak_f32 v245, v243, v245, 0x3e2aaaab
	v_fma_f32 v200, v198, v200, 0.5
	v_fma_f32 v203, v201, v203, 0.5
	v_fma_f32 v206, v204, v206, 0.5
	v_fma_f32 v209, v207, v209, 0.5
	v_fma_f32 v218, v216, v218, 0.5
	v_fma_f32 v239, v219, v239, 0.5
	v_fma_f32 v242, v240, v242, 0.5
	v_fma_f32 v245, v243, v245, 0.5
	v_fma_f32 v200, v198, v200, 1.0
	v_fma_f32 v203, v201, v203, 1.0
	v_fma_f32 v206, v204, v206, 1.0
	v_fma_f32 v209, v207, v209, 1.0
	v_fma_f32 v218, v216, v218, 1.0
	v_fma_f32 v239, v219, v239, 1.0
	v_fma_f32 v242, v240, v242, 1.0
	v_fma_f32 v245, v243, v245, 1.0
	v_mul_f32_e64 v200, v200, -v198
	v_mul_f32_e64 v203, v203, -v201
	v_mul_f32_e64 v206, v206, -v204
	v_mul_f32_e64 v209, v209, -v207
	v_mul_f32_e64 v218, v218, -v216
	v_mul_f32_e64 v239, v239, -v219
	v_mul_f32_e64 v242, v242, -v240
	v_mul_f32_e64 v245, v245, -v243
	v_cmp_nlt_f32_e32 vcc, s49, v198
	v_add_f32_e32 v98, v98, v134
	v_mul_f32_e32 v98, 0xbfb8aa3b, v98
	v_cndmask_b32_e32 v199, v200, v199, vcc
	v_cmp_nlt_f32_e32 vcc, s49, v201
	v_add_f32_e32 v99, v99, v135
	v_mul_f32_e32 v99, 0xbfb8aa3b, v99
	v_cndmask_b32_e32 v202, v203, v202, vcc
	v_cmp_nlt_f32_e32 vcc, s49, v204
	v_add_f32_e32 v100, v100, v136
	v_mul_f32_e32 v100, 0xbfb8aa3b, v100
	v_cndmask_b32_e32 v205, v206, v205, vcc
	v_cmp_nlt_f32_e32 vcc, s49, v207
	v_add_f32_e32 v101, v101, v137
	v_mul_f32_e32 v101, 0xbfb8aa3b, v101
	v_cndmask_b32_e32 v208, v209, v208, vcc
	v_cmp_nlt_f32_e32 vcc, s49, v216
	v_add_f32_e32 v102, v102, v134
	v_mul_f32_e32 v102, 0xbfb8aa3b, v102
	v_cndmask_b32_e32 v217, v218, v217, vcc
	v_cmp_nlt_f32_e32 vcc, s49, v219
	v_add_f32_e32 v103, v103, v135
	v_mul_f32_e32 v103, 0xbfb8aa3b, v103
	v_cndmask_b32_e32 v238, v239, v238, vcc
	v_cmp_nlt_f32_e32 vcc, s49, v240
	v_add_f32_e32 v104, v104, v136
	v_mul_f32_e32 v104, 0xbfb8aa3b, v104
	v_cndmask_b32_e32 v241, v242, v241, vcc
	v_cmp_nlt_f32_e32 vcc, s49, v243
	v_add_f32_e32 v105, v105, v137
	v_mul_f32_e32 v105, 0xbfb8aa3b, v105
	v_cndmask_b32_e32 v244, v245, v244, vcc
	v_exp_f32_e32 v98, v98
	v_exp_f32_e32 v99, v99
	v_exp_f32_e32 v100, v100
	v_exp_f32_e32 v101, v101
	v_exp_f32_e32 v102, v102
	v_exp_f32_e32 v103, v103
	v_exp_f32_e32 v104, v104
	v_exp_f32_e32 v105, v105
	v_sqrt_f32_e32 v199, v199
	v_sqrt_f32_e32 v202, v202
	v_sqrt_f32_e32 v205, v205
	v_sqrt_f32_e32 v208, v208
	v_sqrt_f32_e32 v217, v217
	v_sqrt_f32_e32 v238, v238
	v_sqrt_f32_e32 v241, v241
	v_sqrt_f32_e32 v244, v244
	v_add_f32_e32 v98, 1.0, v98
	v_add_f32_e32 v99, 1.0, v99
	v_add_f32_e32 v100, 1.0, v100
	v_add_f32_e32 v101, 1.0, v101
	v_add_f32_e32 v102, 1.0, v102
	v_add_f32_e32 v103, 1.0, v103
	v_add_f32_e32 v104, 1.0, v104
	v_add_f32_e32 v105, 1.0, v105
	v_lshlrev_b32_e32 v200, 16, v168
	v_and_b32_e32 v203, 0xffff0000, v168
	v_lshlrev_b32_e32 v206, 16, v169
	v_and_b32_e32 v209, 0xffff0000, v169
	v_lshlrev_b32_e32 v218, 16, v170
	v_and_b32_e32 v239, 0xffff0000, v170
	v_lshlrev_b32_e32 v242, 16, v171
	v_and_b32_e32 v245, 0xffff0000, v171
	v_rcp_f32_e32 v98, v98
	v_rcp_f32_e32 v99, v99
	v_rcp_f32_e32 v100, v100
	v_rcp_f32_e32 v101, v101
	v_rcp_f32_e32 v102, v102
	v_rcp_f32_e32 v103, v103
	v_rcp_f32_e32 v104, v104
	v_rcp_f32_e32 v105, v105
	v_mul_f32_e32 v126, 0x3fb8aa3b, v126
	v_mul_f32_e32 v127, 0x3fb8aa3b, v127
	v_mul_f32_e32 v128, 0x3fb8aa3b, v128
	v_mul_f32_e32 v129, 0x3fb8aa3b, v129
	v_mul_f32_e32 v122, 0x3fb8aa3b, v122
	v_mul_f32_e32 v123, 0x3fb8aa3b, v123
	v_mul_f32_e32 v124, 0x3fb8aa3b, v124
	v_mul_f32_e32 v125, 0x3fb8aa3b, v125
	v_mul_f32_e32 v98, v98, v200
	v_mul_f32_e32 v99, v99, v203
	v_mul_f32_e32 v100, v100, v206
	v_mul_f32_e32 v101, v101, v209
	v_mul_f32_e32 v102, v102, v218
	v_mul_f32_e32 v103, v103, v239
	v_mul_f32_e32 v104, v104, v242
	v_mul_f32_e32 v105, v105, v245
	v_exp_f32_e32 v126, v126
	v_exp_f32_e32 v127, v127
	v_exp_f32_e32 v128, v128
	v_exp_f32_e32 v129, v129
	v_exp_f32_e32 v122, v122
	v_exp_f32_e32 v123, v123
	v_exp_f32_e32 v124, v124
	v_exp_f32_e32 v125, v125
	v_mul_f32_e32 v98, v98, v199
	v_mul_f32_e32 v99, v99, v202
	v_mul_f32_e32 v100, v100, v205
	v_mul_f32_e32 v101, v101, v208
	v_mul_f32_e32 v102, v102, v217
	v_mul_f32_e32 v103, v103, v238
	v_mul_f32_e32 v104, v104, v241
	v_mul_f32_e32 v105, v105, v244
	v_add_f32_e32 v118, v118, v130
	v_add_f32_e32 v119, v119, v131
	v_add_f32_e32 v120, v120, v132
	v_add_f32_e32 v121, v121, v133
	v_add_f32_e32 v114, v114, v130
	v_add_f32_e32 v115, v115, v131
	v_add_f32_e32 v116, v116, v132
	v_add_f32_e32 v117, v117, v133
	v_mul_f32_e32 v118, 0xbfb8aa3b, v118
	v_mul_f32_e32 v119, 0xbfb8aa3b, v119
	v_mul_f32_e32 v120, 0xbfb8aa3b, v120
	v_mul_f32_e32 v121, 0xbfb8aa3b, v121
	v_mul_f32_e32 v114, 0xbfb8aa3b, v114
	v_mul_f32_e32 v115, 0xbfb8aa3b, v115
	v_mul_f32_e32 v116, 0xbfb8aa3b, v116
	v_mul_f32_e32 v117, 0xbfb8aa3b, v117
	v_exp_f32_e32 v118, v118
	v_exp_f32_e32 v119, v119
	v_exp_f32_e32 v120, v120
; __device__ __forceinline__ float sigmoid_fast(float x) { return __builtin_amdgcn_rcpf(1.f + __expf(-x)); }
; __device__ __forceinline__ float one_minus_exp(float x) { const float p = -x * (1.f + x * (0.5f + x * (0.16666667f + x * (0.041666668f + x * 0.0083333338f)))); return x > -0.1f ? p : 1.f - __expf(x); }
;     template <bool BWD>
;     __device__ __forceinline__ void epi_dir(const f32x4 (&acc)[2][2][4][2], const Unit& u, int wr, int wc, int fr, int fq) const {
;     ...
;                     for (int j = 0; j < 4; ++j) { const float r = sigmoid_fast(acc[ai][0][m][n][j] + bav[j]), ig = sigmoid_fast(acc[ai][1][m][n][j] + bxv[j]);
;                         const float la = r * lsl[j]; A[m][j] = __expf(la); H[m][j] = __builtin_amdgcn_sqrtf(one_minus_exp(2.f * la)) * (ig * uv[j]); } }
	v_exp_f32_e32 v121, v121
	v_exp_f32_e32 v114, v114
	v_exp_f32_e32 v115, v115
	v_exp_f32_e32 v116, v116
	v_exp_f32_e32 v117, v117
	v_add_f32_e32 v118, 1.0, v118
	v_add_f32_e32 v119, 1.0, v119
	v_add_f32_e32 v120, 1.0, v120
	v_add_f32_e32 v121, 1.0, v121
	v_add_f32_e32 v114, 1.0, v114
	v_add_f32_e32 v115, 1.0, v115
	v_add_f32_e32 v116, 1.0, v116
	v_add_f32_e32 v117, 1.0, v117
	v_rcp_f32_e32 v118, v118
	v_rcp_f32_e32 v119, v119
	v_rcp_f32_e32 v120, v120
	v_rcp_f32_e32 v121, v121
	v_rcp_f32_e32 v114, v114
	v_rcp_f32_e32 v115, v115
	v_rcp_f32_e32 v116, v116
	v_rcp_f32_e32 v117, v117
	v_mul_f32_e32 v118, v138, v118
	v_mul_f32_e32 v119, v139, v119
	v_mul_f32_e32 v120, v140, v120
	v_mul_f32_e32 v121, v141, v121
	v_mul_f32_e32 v114, v138, v114
	v_mul_f32_e32 v115, v139, v115
	v_mul_f32_e32 v116, v140, v116
	v_mul_f32_e32 v117, v141, v117
	v_add_f32_e32 v198, v118, v118
	v_add_f32_e32 v201, v119, v119
	v_add_f32_e32 v204, v120, v120
	v_add_f32_e32 v207, v121, v121
	v_add_f32_e32 v216, v114, v114
	v_add_f32_e32 v219, v115, v115
	v_add_f32_e32 v240, v116, v116
	v_add_f32_e32 v243, v117, v117
	v_mul_f32_e32 v199, 0x3fb8aa3b, v198
	v_mul_f32_e32 v202, 0x3fb8aa3b, v201
	v_mul_f32_e32 v205, 0x3fb8aa3b, v204
	v_mul_f32_e32 v208, 0x3fb8aa3b, v207
	v_mul_f32_e32 v217, 0x3fb8aa3b, v216
	v_mul_f32_e32 v238, 0x3fb8aa3b, v219
	v_mul_f32_e32 v241, 0x3fb8aa3b, v240
	v_mul_f32_e32 v244, 0x3fb8aa3b, v243
	v_exp_f32_e32 v199, v199
	v_exp_f32_e32 v202, v202
	v_exp_f32_e32 v205, v205
	v_exp_f32_e32 v208, v208
	v_exp_f32_e32 v217, v217
	v_exp_f32_e32 v238, v238
	v_exp_f32_e32 v241, v241
	v_exp_f32_e32 v244, v244
	v_fmamk_f32 v200, v198, 0x3c088889, v211
	v_fmamk_f32 v203, v201, 0x3c088889, v211
	v_fmamk_f32 v206, v204, 0x3c088889, v211
	v_fmamk_f32 v209, v207, 0x3c088889, v211
	v_fmamk_f32 v218, v216, 0x3c088889, v211
	v_fmamk_f32 v239, v219, 0x3c088889, v211
	v_fmamk_f32 v242, v240, 0x3c088889, v211
	v_fmamk_f32 v245, v243, 0x3c088889, v211
	v_sub_f32_e32 v199, 1.0, v199
	v_sub_f32_e32 v202, 1.0, v202
	v_sub_f32_e32 v205, 1.0, v205
	v_sub_f32_e32 v208, 1.0, v208
	v_sub_f32_e32 v217, 1.0, v217
	v_sub_f32_e32 v238, 1.0, v238
	v_sub_f32_e32 v241, 1.0, v241
	v_sub_f32_e32 v244, 1.0, v244
	v_fmaak_f32 v200, v198, v200, 0x3e2aaaab
	v_fmaak_f32 v203, v201, v203, 0x3e2aaaab
	v_fmaak_f32 v206, v204, v206, 0x3e2aaaab
	v_fmaak_f32 v209, v207, v209, 0x3e2aaaab
	v_fmaak_f32 v218, v216, v218, 0x3e2aaaab
	v_fmaak_f32 v239, v219, v239, 0x3e2aaaab
	v_fmaak_f32 v242, v240, v242, 0x3e2aaaab
	v_fmaak_f32 v245, v243, v245, 0x3e2aaaab
	v_fma_f32 v200, v198, v200, 0.5
	v_fma_f32 v203, v201, v203, 0.5
	v_fma_f32 v206, v204, v206, 0.5
	v_fma_f32 v209, v207, v209, 0.5
	v_fma_f32 v218, v216, v218, 0.5
	v_fma_f32 v239, v219, v239, 0.5
	v_fma_f32 v242, v240, v242, 0.5
	v_fma_f32 v245, v243, v245, 0.5
	v_fma_f32 v200, v198, v200, 1.0
	v_fma_f32 v203, v201, v203, 1.0
	v_fma_f32 v206, v204, v206, 1.0
	v_fma_f32 v209, v207, v209, 1.0
	v_fma_f32 v218, v216, v218, 1.0
	v_fma_f32 v239, v219, v239, 1.0
	v_fma_f32 v242, v240, v242, 1.0
	v_fma_f32 v245, v243, v245, 1.0
	v_mul_f32_e64 v200, v200, -v198
	v_mul_f32_e64 v203, v203, -v201
	v_mul_f32_e64 v206, v206, -v204
	v_mul_f32_e64 v209, v209, -v207
	v_mul_f32_e64 v218, v218, -v216
	v_mul_f32_e64 v239, v239, -v219
	v_mul_f32_e64 v242, v242, -v240
	v_mul_f32_e64 v245, v245, -v243
	v_cmp_nlt_f32_e32 vcc, s49, v198
	v_add_f32_e32 v106, v106, v134
	v_mul_f32_e32 v106, 0xbfb8aa3b, v106
	v_cndmask_b32_e32 v199, v200, v199, vcc
	v_cmp_nlt_f32_e32 vcc, s49, v201
	v_add_f32_e32 v107, v107, v135
	v_mul_f32_e32 v107, 0xbfb8aa3b, v107
	v_cndmask_b32_e32 v202, v203, v202, vcc
	v_cmp_nlt_f32_e32 vcc, s49, v204
	v_add_f32_e32 v108, v108, v136
	v_mul_f32_e32 v108, 0xbfb8aa3b, v108
	v_cndmask_b32_e32 v205, v206, v205, vcc
	v_cmp_nlt_f32_e32 vcc, s49, v207
	v_add_f32_e32 v109, v109, v137
	v_mul_f32_e32 v109, 0xbfb8aa3b, v109
	v_cndmask_b32_e32 v208, v209, v208, vcc
	v_cmp_nlt_f32_e32 vcc, s49, v216
	v_add_f32_e32 v110, v110, v134
	v_mul_f32_e32 v110, 0xbfb8aa3b, v110
	v_cndmask_b32_e32 v217, v218, v217, vcc
	v_cmp_nlt_f32_e32 vcc, s49, v219
	v_add_f32_e32 v111, v111, v135
	v_mul_f32_e32 v111, 0xbfb8aa3b, v111
	v_cndmask_b32_e32 v238, v239, v238, vcc
	v_cmp_nlt_f32_e32 vcc, s49, v240
	v_add_f32_e32 v112, v112, v136
	v_mul_f32_e32 v112, 0xbfb8aa3b, v112
	v_cndmask_b32_e32 v241, v242, v241, vcc
	v_cmp_nlt_f32_e32 vcc, s49, v243
	v_add_f32_e32 v113, v113, v137
	v_mul_f32_e32 v113, 0xbfb8aa3b, v113
	v_cndmask_b32_e32 v244, v245, v244, vcc
	v_exp_f32_e32 v106, v106
	v_exp_f32_e32 v107, v107
	v_exp_f32_e32 v108, v108
	v_exp_f32_e32 v109, v109
	v_exp_f32_e32 v110, v110
	v_exp_f32_e32 v111, v111
	v_exp_f32_e32 v112, v112
	v_exp_f32_e32 v113, v113
	v_sqrt_f32_e32 v199, v199
	v_sqrt_f32_e32 v202, v202
	v_sqrt_f32_e32 v205, v205
	v_sqrt_f32_e32 v208, v208
	v_sqrt_f32_e32 v217, v217
	v_sqrt_f32_e32 v238, v238
	v_sqrt_f32_e32 v241, v241
	v_sqrt_f32_e32 v244, v244
	v_add_f32_e32 v106, 1.0, v106
	v_add_f32_e32 v107, 1.0, v107
	v_add_f32_e32 v108, 1.0, v108
	v_add_f32_e32 v109, 1.0, v109
	v_add_f32_e32 v110, 1.0, v110
	v_add_f32_e32 v111, 1.0, v111
	v_add_f32_e32 v112, 1.0, v112
	v_add_f32_e32 v113, 1.0, v113
	v_lshlrev_b32_e32 v200, 16, v172
	v_and_b32_e32 v203, 0xffff0000, v172
	v_lshlrev_b32_e32 v206, 16, v173
	v_and_b32_e32 v209, 0xffff0000, v173
	v_lshlrev_b32_e32 v218, 16, v174
	v_and_b32_e32 v239, 0xffff0000, v174
	v_lshlrev_b32_e32 v242, 16, v175
	v_and_b32_e32 v245, 0xffff0000, v175
	v_rcp_f32_e32 v106, v106
	v_rcp_f32_e32 v107, v107
	v_rcp_f32_e32 v108, v108
	v_rcp_f32_e32 v109, v109
	v_rcp_f32_e32 v110, v110
	v_rcp_f32_e32 v111, v111
	v_rcp_f32_e32 v112, v112
	v_rcp_f32_e32 v113, v113
; __device__ __forceinline__ float sigmoid_fast(float x) { return __builtin_amdgcn_rcpf(1.f + __expf(-x)); }
; __device__ __forceinline__ float one_minus_exp(float x) { const float p = -x * (1.f + x * (0.5f + x * (0.16666667f + x * (0.041666668f + x * 0.0083333338f)))); return x > -0.1f ? p : 1.f - __expf(x); }
; #define SCAN_STEP(D) { const float ap = dppf<(BWD ? 0x100 : 0x110) + D>(1.f, av), hp = dppf<(BWD ? 0x100 : 0x110) + D>(0.f, hv); hv = fmaf(av, hp, hv); av = av * ap; }
;     template <bool BWD>
;     __device__ __forceinline__ void epi_dir(const f32x4 (&acc)[2][2][4][2], const Unit& u, int wr, int wc, int fr, int fq) const {
;     ...
;                     for (int j = 0; j < 4; ++j) { const float r = sigmoid_fast(acc[ai][0][m][n][j] + bav[j]), ig = sigmoid_fast(acc[ai][1][m][n][j] + bxv[j]);
;                         const float la = r * lsl[j]; A[m][j] = __expf(la); H[m][j] = __builtin_amdgcn_sqrtf(one_minus_exp(2.f * la)) * (ig * uv[j]); } }
; #pragma unroll
;                 for (int m = 0; m < 4; ++m)
; #pragma unroll
;                     for (int j = 0; j < 4; ++j) { float av = A[m][j], hv = H[m][j];
;     ...
;                         SCAN_STEP(1) SCAN_STEP(2) SCAN_STEP(4) SCAN_STEP(8)
	v_mul_f32_e32 v118, 0x3fb8aa3b, v118
	v_mul_f32_e32 v119, 0x3fb8aa3b, v119
	v_mul_f32_e32 v120, 0x3fb8aa3b, v120
	v_mul_f32_e32 v121, 0x3fb8aa3b, v121
	v_mul_f32_e32 v114, 0x3fb8aa3b, v114
	v_mul_f32_e32 v115, 0x3fb8aa3b, v115
	v_mul_f32_e32 v116, 0x3fb8aa3b, v116
	v_mul_f32_e32 v117, 0x3fb8aa3b, v117
	v_mul_f32_e32 v106, v106, v200
	v_mul_f32_e32 v107, v107, v203
	v_mul_f32_e32 v108, v108, v206
	v_mul_f32_e32 v109, v109, v209
	v_mul_f32_e32 v110, v110, v218
	v_mul_f32_e32 v111, v111, v239
	v_mul_f32_e32 v112, v112, v242
	v_mul_f32_e32 v113, v113, v245
	v_exp_f32_e32 v118, v118
	v_exp_f32_e32 v119, v119
	v_exp_f32_e32 v120, v120
	v_exp_f32_e32 v121, v121
	v_exp_f32_e32 v114, v114
	v_exp_f32_e32 v115, v115
	v_exp_f32_e32 v116, v116
	v_exp_f32_e32 v117, v117
	v_mul_f32_e32 v106, v106, v199
	v_mul_f32_e32 v107, v107, v202
	v_mul_f32_e32 v108, v108, v205
	v_mul_f32_e32 v109, v109, v208
	v_mul_f32_e32 v110, v110, v217
	v_mul_f32_e32 v111, v111, v238
	v_mul_f32_e32 v112, v112, v241
	v_mul_f32_e32 v113, v113, v244
	v_fmac_f32_dpp v98, v98, v126 row_shr:1 row_mask:0xf bank_mask:0xf
	v_mul_f32_dpp v126, v126, v126 row_shr:1 row_mask:0xf bank_mask:0xf
	v_fmac_f32_dpp v99, v99, v127 row_shr:1 row_mask:0xf bank_mask:0xf
	v_mul_f32_dpp v127, v127, v127 row_shr:1 row_mask:0xf bank_mask:0xf
	v_fmac_f32_dpp v100, v100, v128 row_shr:1 row_mask:0xf bank_mask:0xf
	v_mul_f32_dpp v128, v128, v128 row_shr:1 row_mask:0xf bank_mask:0xf
	v_fmac_f32_dpp v101, v101, v129 row_shr:1 row_mask:0xf bank_mask:0xf
	v_mul_f32_dpp v129, v129, v129 row_shr:1 row_mask:0xf bank_mask:0xf
	v_fmac_f32_dpp v102, v102, v122 row_shr:1 row_mask:0xf bank_mask:0xf
	v_mul_f32_dpp v122, v122, v122 row_shr:1 row_mask:0xf bank_mask:0xf
	v_fmac_f32_dpp v103, v103, v123 row_shr:1 row_mask:0xf bank_mask:0xf
	v_mul_f32_dpp v123, v123, v123 row_shr:1 row_mask:0xf bank_mask:0xf
	v_fmac_f32_dpp v104, v104, v124 row_shr:1 row_mask:0xf bank_mask:0xf
	v_mul_f32_dpp v124, v124, v124 row_shr:1 row_mask:0xf bank_mask:0xf
	v_fmac_f32_dpp v105, v105, v125 row_shr:1 row_mask:0xf bank_mask:0xf
	v_mul_f32_dpp v125, v125, v125 row_shr:1 row_mask:0xf bank_mask:0xf
	v_fmac_f32_dpp v106, v106, v118 row_shr:1 row_mask:0xf bank_mask:0xf
	v_mul_f32_dpp v118, v118, v118 row_shr:1 row_mask:0xf bank_mask:0xf
	v_fmac_f32_dpp v107, v107, v119 row_shr:1 row_mask:0xf bank_mask:0xf
	v_mul_f32_dpp v119, v119, v119 row_shr:1 row_mask:0xf bank_mask:0xf
	v_fmac_f32_dpp v108, v108, v120 row_shr:1 row_mask:0xf bank_mask:0xf
	v_mul_f32_dpp v120, v120, v120 row_shr:1 row_mask:0xf bank_mask:0xf
	v_fmac_f32_dpp v109, v109, v121 row_shr:1 row_mask:0xf bank_mask:0xf
	v_mul_f32_dpp v121, v121, v121 row_shr:1 row_mask:0xf bank_mask:0xf
	v_fmac_f32_dpp v110, v110, v114 row_shr:1 row_mask:0xf bank_mask:0xf
	v_mul_f32_dpp v114, v114, v114 row_shr:1 row_mask:0xf bank_mask:0xf
	v_fmac_f32_dpp v111, v111, v115 row_shr:1 row_mask:0xf bank_mask:0xf
	v_mul_f32_dpp v115, v115, v115 row_shr:1 row_mask:0xf bank_mask:0xf
	v_fmac_f32_dpp v112, v112, v116 row_shr:1 row_mask:0xf bank_mask:0xf
	v_mul_f32_dpp v116, v116, v116 row_shr:1 row_mask:0xf bank_mask:0xf
	v_fmac_f32_dpp v113, v113, v117 row_shr:1 row_mask:0xf bank_mask:0xf
	v_mul_f32_dpp v117, v117, v117 row_shr:1 row_mask:0xf bank_mask:0xf
	v_fmac_f32_dpp v98, v98, v126 row_shr:2 row_mask:0xf bank_mask:0xf
	v_mul_f32_dpp v126, v126, v126 row_shr:2 row_mask:0xf bank_mask:0xf
	v_fmac_f32_dpp v99, v99, v127 row_shr:2 row_mask:0xf bank_mask:0xf
	v_mul_f32_dpp v127, v127, v127 row_shr:2 row_mask:0xf bank_mask:0xf
	v_fmac_f32_dpp v100, v100, v128 row_shr:2 row_mask:0xf bank_mask:0xf
	v_mul_f32_dpp v128, v128, v128 row_shr:2 row_mask:0xf bank_mask:0xf
	v_fmac_f32_dpp v101, v101, v129 row_shr:2 row_mask:0xf bank_mask:0xf
	v_mul_f32_dpp v129, v129, v129 row_shr:2 row_mask:0xf bank_mask:0xf
	v_fmac_f32_dpp v102, v102, v122 row_shr:2 row_mask:0xf bank_mask:0xf
	v_mul_f32_dpp v122, v122, v122 row_shr:2 row_mask:0xf bank_mask:0xf
	v_fmac_f32_dpp v103, v103, v123 row_shr:2 row_mask:0xf bank_mask:0xf
	v_mul_f32_dpp v123, v123, v123 row_shr:2 row_mask:0xf bank_mask:0xf
	v_fmac_f32_dpp v104, v104, v124 row_shr:2 row_mask:0xf bank_mask:0xf
	v_mul_f32_dpp v124, v124, v124 row_shr:2 row_mask:0xf bank_mask:0xf
	v_fmac_f32_dpp v105, v105, v125 row_shr:2 row_mask:0xf bank_mask:0xf
	v_mul_f32_dpp v125, v125, v125 row_shr:2 row_mask:0xf bank_mask:0xf
	v_fmac_f32_dpp v106, v106, v118 row_shr:2 row_mask:0xf bank_mask:0xf
	v_mul_f32_dpp v118, v118, v118 row_shr:2 row_mask:0xf bank_mask:0xf
	v_fmac_f32_dpp v107, v107, v119 row_shr:2 row_mask:0xf bank_mask:0xf
	v_mul_f32_dpp v119, v119, v119 row_shr:2 row_mask:0xf bank_mask:0xf
	v_fmac_f32_dpp v108, v108, v120 row_shr:2 row_mask:0xf bank_mask:0xf
	v_mul_f32_dpp v120, v120, v120 row_shr:2 row_mask:0xf bank_mask:0xf
	v_fmac_f32_dpp v109, v109, v121 row_shr:2 row_mask:0xf bank_mask:0xf
	v_mul_f32_dpp v121, v121, v121 row_shr:2 row_mask:0xf bank_mask:0xf
	v_fmac_f32_dpp v110, v110, v114 row_shr:2 row_mask:0xf bank_mask:0xf
	v_mul_f32_dpp v114, v114, v114 row_shr:2 row_mask:0xf bank_mask:0xf
	v_fmac_f32_dpp v111, v111, v115 row_shr:2 row_mask:0xf bank_mask:0xf
	v_mul_f32_dpp v115, v115, v115 row_shr:2 row_mask:0xf bank_mask:0xf
	v_fmac_f32_dpp v112, v112, v116 row_shr:2 row_mask:0xf bank_mask:0xf
	v_mul_f32_dpp v116, v116, v116 row_shr:2 row_mask:0xf bank_mask:0xf
	v_fmac_f32_dpp v113, v113, v117 row_shr:2 row_mask:0xf bank_mask:0xf
	v_mul_f32_dpp v117, v117, v117 row_shr:2 row_mask:0xf bank_mask:0xf
	v_fmac_f32_dpp v98, v98, v126 row_shr:4 row_mask:0xf bank_mask:0xf
	v_mul_f32_dpp v126, v126, v126 row_shr:4 row_mask:0xf bank_mask:0xf
	v_fmac_f32_dpp v99, v99, v127 row_shr:4 row_mask:0xf bank_mask:0xf
; #define SCAN_STEP(D) { const float ap = dppf<(BWD ? 0x100 : 0x110) + D>(1.f, av), hp = dppf<(BWD ? 0x100 : 0x110) + D>(0.f, hv); hv = fmaf(av, hp, hv); av = av * ap; }
;     template <bool BWD>
;     __device__ __forceinline__ void epi_dir(const f32x4 (&acc)[2][2][4][2], const Unit& u, int wr, int wc, int fr, int fq) const {
;     ...
;                 for (int m = 0; m < 4; ++m)
; #pragma unroll
;                     for (int j = 0; j < 4; ++j) { float av = A[m][j], hv = H[m][j];
;     ...
;                         SCAN_STEP(1) SCAN_STEP(2) SCAN_STEP(4) SCAN_STEP(8)
;     ...
;                         A[m][j] = av; H[m][j] = hv; }
; #pragma unroll
;                 for (int j = 0; j < 4; ++j) { float Ar = 1.f, Hr = 0.f;
; #pragma unroll
;                     for (int mm = 0; mm < 4; ++mm) { const int m = BWD ? 3 - mm : mm;
;                         H[m][j] = fmaf(A[m][j], Hr, H[m][j]); A[m][j] = A[m][j] * Ar;
;                         if (mm < 3) { Ar = __shfl(A[m][j], bsel); Hr = __shfl(H[m][j], bsel); } } }
	v_mul_f32_dpp v127, v127, v127 row_shr:4 row_mask:0xf bank_mask:0xf
	v_fmac_f32_dpp v100, v100, v128 row_shr:4 row_mask:0xf bank_mask:0xf
	v_mul_f32_dpp v128, v128, v128 row_shr:4 row_mask:0xf bank_mask:0xf
	v_fmac_f32_dpp v101, v101, v129 row_shr:4 row_mask:0xf bank_mask:0xf
	v_mul_f32_dpp v129, v129, v129 row_shr:4 row_mask:0xf bank_mask:0xf
	v_fmac_f32_dpp v102, v102, v122 row_shr:4 row_mask:0xf bank_mask:0xf
	v_mul_f32_dpp v122, v122, v122 row_shr:4 row_mask:0xf bank_mask:0xf
	v_fmac_f32_dpp v103, v103, v123 row_shr:4 row_mask:0xf bank_mask:0xf
	v_mul_f32_dpp v123, v123, v123 row_shr:4 row_mask:0xf bank_mask:0xf
	v_fmac_f32_dpp v104, v104, v124 row_shr:4 row_mask:0xf bank_mask:0xf
	v_mul_f32_dpp v124, v124, v124 row_shr:4 row_mask:0xf bank_mask:0xf
	v_fmac_f32_dpp v105, v105, v125 row_shr:4 row_mask:0xf bank_mask:0xf
	v_mul_f32_dpp v125, v125, v125 row_shr:4 row_mask:0xf bank_mask:0xf
	v_fmac_f32_dpp v106, v106, v118 row_shr:4 row_mask:0xf bank_mask:0xf
	v_mul_f32_dpp v118, v118, v118 row_shr:4 row_mask:0xf bank_mask:0xf
	v_fmac_f32_dpp v107, v107, v119 row_shr:4 row_mask:0xf bank_mask:0xf
	v_mul_f32_dpp v119, v119, v119 row_shr:4 row_mask:0xf bank_mask:0xf
	v_fmac_f32_dpp v108, v108, v120 row_shr:4 row_mask:0xf bank_mask:0xf
	v_mul_f32_dpp v120, v120, v120 row_shr:4 row_mask:0xf bank_mask:0xf
	v_fmac_f32_dpp v109, v109, v121 row_shr:4 row_mask:0xf bank_mask:0xf
	v_mul_f32_dpp v121, v121, v121 row_shr:4 row_mask:0xf bank_mask:0xf
	v_fmac_f32_dpp v110, v110, v114 row_shr:4 row_mask:0xf bank_mask:0xf
	v_mul_f32_dpp v114, v114, v114 row_shr:4 row_mask:0xf bank_mask:0xf
	v_fmac_f32_dpp v111, v111, v115 row_shr:4 row_mask:0xf bank_mask:0xf
	v_mul_f32_dpp v115, v115, v115 row_shr:4 row_mask:0xf bank_mask:0xf
	v_fmac_f32_dpp v112, v112, v116 row_shr:4 row_mask:0xf bank_mask:0xf
	v_mul_f32_dpp v116, v116, v116 row_shr:4 row_mask:0xf bank_mask:0xf
	v_fmac_f32_dpp v113, v113, v117 row_shr:4 row_mask:0xf bank_mask:0xf
	v_mul_f32_dpp v117, v117, v117 row_shr:4 row_mask:0xf bank_mask:0xf
	v_fmac_f32_dpp v98, v98, v126 row_shr:8 row_mask:0xf bank_mask:0xf
	v_mul_f32_dpp v126, v126, v126 row_shr:8 row_mask:0xf bank_mask:0xf
	v_fmac_f32_dpp v99, v99, v127 row_shr:8 row_mask:0xf bank_mask:0xf
	v_mul_f32_dpp v127, v127, v127 row_shr:8 row_mask:0xf bank_mask:0xf
	v_fmac_f32_dpp v100, v100, v128 row_shr:8 row_mask:0xf bank_mask:0xf
	v_mul_f32_dpp v128, v128, v128 row_shr:8 row_mask:0xf bank_mask:0xf
	v_fmac_f32_dpp v101, v101, v129 row_shr:8 row_mask:0xf bank_mask:0xf
	v_mul_f32_dpp v129, v129, v129 row_shr:8 row_mask:0xf bank_mask:0xf
	v_fmac_f32_dpp v102, v102, v122 row_shr:8 row_mask:0xf bank_mask:0xf
	v_mul_f32_dpp v122, v122, v122 row_shr:8 row_mask:0xf bank_mask:0xf
	v_fmac_f32_dpp v103, v103, v123 row_shr:8 row_mask:0xf bank_mask:0xf
	v_mul_f32_dpp v123, v123, v123 row_shr:8 row_mask:0xf bank_mask:0xf
	v_fmac_f32_dpp v104, v104, v124 row_shr:8 row_mask:0xf bank_mask:0xf
	v_mul_f32_dpp v124, v124, v124 row_shr:8 row_mask:0xf bank_mask:0xf
	v_fmac_f32_dpp v105, v105, v125 row_shr:8 row_mask:0xf bank_mask:0xf
	v_mul_f32_dpp v125, v125, v125 row_shr:8 row_mask:0xf bank_mask:0xf
	v_fmac_f32_dpp v106, v106, v118 row_shr:8 row_mask:0xf bank_mask:0xf
	v_mul_f32_dpp v118, v118, v118 row_shr:8 row_mask:0xf bank_mask:0xf
	v_fmac_f32_dpp v107, v107, v119 row_shr:8 row_mask:0xf bank_mask:0xf
	v_mul_f32_dpp v119, v119, v119 row_shr:8 row_mask:0xf bank_mask:0xf
	v_fmac_f32_dpp v108, v108, v120 row_shr:8 row_mask:0xf bank_mask:0xf
	v_mul_f32_dpp v120, v120, v120 row_shr:8 row_mask:0xf bank_mask:0xf
	v_fmac_f32_dpp v109, v109, v121 row_shr:8 row_mask:0xf bank_mask:0xf
	v_mul_f32_dpp v121, v121, v121 row_shr:8 row_mask:0xf bank_mask:0xf
	v_fmac_f32_dpp v110, v110, v114 row_shr:8 row_mask:0xf bank_mask:0xf
	v_mul_f32_dpp v114, v114, v114 row_shr:8 row_mask:0xf bank_mask:0xf
	v_fmac_f32_dpp v111, v111, v115 row_shr:8 row_mask:0xf bank_mask:0xf
	v_mul_f32_dpp v115, v115, v115 row_shr:8 row_mask:0xf bank_mask:0xf
	v_fmac_f32_dpp v112, v112, v116 row_shr:8 row_mask:0xf bank_mask:0xf
	v_mul_f32_dpp v116, v116, v116 row_shr:8 row_mask:0xf bank_mask:0xf
	v_fmac_f32_dpp v113, v113, v117 row_shr:8 row_mask:0xf bank_mask:0xf
	v_mul_f32_dpp v117, v117, v117 row_shr:8 row_mask:0xf bank_mask:0xf
	v_fmac_f32_dpp v102, v98, v122 row_newbcast:15 row_mask:0xf bank_mask:0xf
	v_mul_f32_dpp v122, v126, v122 row_newbcast:15 row_mask:0xf bank_mask:0xf
	v_fmac_f32_dpp v103, v99, v123 row_newbcast:15 row_mask:0xf bank_mask:0xf
	v_mul_f32_dpp v123, v127, v123 row_newbcast:15 row_mask:0xf bank_mask:0xf
	v_fmac_f32_dpp v104, v100, v124 row_newbcast:15 row_mask:0xf bank_mask:0xf
	v_mul_f32_dpp v124, v128, v124 row_newbcast:15 row_mask:0xf bank_mask:0xf
	v_fmac_f32_dpp v105, v101, v125 row_newbcast:15 row_mask:0xf bank_mask:0xf
	v_mul_f32_dpp v125, v129, v125 row_newbcast:15 row_mask:0xf bank_mask:0xf
	v_fmac_f32_dpp v106, v102, v118 row_newbcast:15 row_mask:0xf bank_mask:0xf
	v_mul_f32_dpp v118, v122, v118 row_newbcast:15 row_mask:0xf bank_mask:0xf
	v_fmac_f32_dpp v107, v103, v119 row_newbcast:15 row_mask:0xf bank_mask:0xf
	v_mul_f32_dpp v119, v123, v119 row_newbcast:15 row_mask:0xf bank_mask:0xf
	v_fmac_f32_dpp v108, v104, v120 row_newbcast:15 row_mask:0xf bank_mask:0xf
	v_mul_f32_dpp v120, v124, v120 row_newbcast:15 row_mask:0xf bank_mask:0xf
	v_fmac_f32_dpp v109, v105, v121 row_newbcast:15 row_mask:0xf bank_mask:0xf
	v_mul_f32_dpp v121, v125, v121 row_newbcast:15 row_mask:0xf bank_mask:0xf
	v_fmac_f32_dpp v110, v106, v114 row_newbcast:15 row_mask:0xf bank_mask:0xf
	v_mul_f32_dpp v114, v118, v114 row_newbcast:15 row_mask:0xf bank_mask:0xf
	v_fmac_f32_dpp v111, v107, v115 row_newbcast:15 row_mask:0xf bank_mask:0xf
; __device__ __forceinline__ unsigned pk2(float lo, float hi) { return f2bf(lo) | (f2bf(hi) << 16); }
; __device__ __forceinline__ float sigmoid_fast(float x) { return __builtin_amdgcn_rcpf(1.f + __expf(-x)); }
; __device__ __forceinline__ float one_minus_exp(float x) { const float p = -x * (1.f + x * (0.5f + x * (0.16666667f + x * (0.041666668f + x * 0.0083333338f)))); return x > -0.1f ? p : 1.f - __expf(x); }
;     template <bool BWD>
;     __device__ __forceinline__ void epi_dir(const f32x4 (&acc)[2][2][4][2], const Unit& u, int wr, int wc, int fr, int fq) const {
;     ...
;                 const f32x4 bav = *(const f32x4*)(bap + n * 64 + coff), bxv = *(const f32x4*)(bxp + n * 64 + coff), lsl = *(const f32x4*)(lmp + n * 64 + coff);
; #pragma unroll
;                 for (int m = 0; m < 4; ++m) {
;                     const u32x2 uw = *(const u32x2*)(Ub + ((size_t)(ai * 128 + m * 16) * 1024 + n * 16) * 2 + loffu);
;                     const float uv[4] = {bflo(uw.x), bfhi(uw.x), bflo(uw.y), bfhi(uw.y)};
; #pragma unroll
;                     for (int j = 0; j < 4; ++j) { const float r = sigmoid_fast(acc[ai][0][m][n][j] + bav[j]), ig = sigmoid_fast(acc[ai][1][m][n][j] + bxv[j]);
;                         const float la = r * lsl[j]; A[m][j] = __expf(la); H[m][j] = __builtin_amdgcn_sqrtf(one_minus_exp(2.f * la)) * (ig * uv[j]); } }
;     ...
;                 for (int j = 0; j < 4; ++j) { float Ar = 1.f, Hr = 0.f;
; #pragma unroll
;                     for (int mm = 0; mm < 4; ++mm) { const int m = BWD ? 3 - mm : mm;
;                         H[m][j] = fmaf(A[m][j], Hr, H[m][j]); A[m][j] = A[m][j] * Ar;
;                         if (mm < 3) { Ar = __shfl(A[m][j], bsel); Hr = __shfl(H[m][j], bsel); } } }
; #pragma unroll
;                 for (int m = 0; m < 4; ++m) { u32x4 w; w.x = pk2(H[m][0], H[m][1]); w.y = pk2(H[m][2], H[m][3]); w.z = pk2(A[m][0], A[m][1]); w.w = pk2(A[m][2], A[m][3]);
;                     *(u32x4*)(Hb + ((size_t)(ai * 128 + m * 16) * 1024 + n * 16) * 4 + loffh) = w; }
;                 constexpr int me = BWD ? 0 : 3;
;                 if (fr == (BWD ? 0 : 15)) { const size_t o = (size_t)chunk * 1024 + gblk * 128 + n * 16;
;                     *(f32x4*)((char*)(AGG + (size_t)(dir * 2 + 0) * NB * NCHUNK * 1024 + o) + coff) = A[me];
;                     *(f32x4*)((char*)(AGG + (size_t)(dir * 2 + 1) * NB * NCHUNK * 1024 + o) + coff) = H[me]; }
	v_mul_f32_dpp v115, v119, v115 row_newbcast:15 row_mask:0xf bank_mask:0xf
	v_fmac_f32_dpp v112, v108, v116 row_newbcast:15 row_mask:0xf bank_mask:0xf
	v_mul_f32_dpp v116, v120, v116 row_newbcast:15 row_mask:0xf bank_mask:0xf
	v_fmac_f32_dpp v113, v109, v117 row_newbcast:15 row_mask:0xf bank_mask:0xf
	v_mul_f32_dpp v117, v121, v117 row_newbcast:15 row_mask:0xf bank_mask:0xf
	s_and_saveexec_b64 s[46:47], s[42:43]
	global_store_dwordx4 v187, v[114:117], s[4:5] sc1
	global_store_dwordx4 v187, v[110:113], s[16:17] sc1
	s_mov_b64 exec, s[46:47]
	v_cvt_pk_bf16_f32 v98, v98, v99
	v_cvt_pk_bf16_f32 v99, v100, v101
	v_cvt_pk_bf16_f32 v100, v126, v127
	v_cvt_pk_bf16_f32 v101, v128, v129
	global_store_dwordx4 v194, v[98:101], s[54:55] sc1
	v_cvt_pk_bf16_f32 v102, v102, v103
	v_cvt_pk_bf16_f32 v103, v104, v105
	v_cvt_pk_bf16_f32 v104, v122, v123
	v_cvt_pk_bf16_f32 v105, v124, v125
	global_store_dwordx4 v195, v[102:105], s[54:55] sc1
	v_cvt_pk_bf16_f32 v106, v106, v107
	v_cvt_pk_bf16_f32 v107, v108, v109
	v_cvt_pk_bf16_f32 v108, v118, v119
	v_cvt_pk_bf16_f32 v109, v120, v121
	global_store_dwordx4 v196, v[106:109], s[54:55] sc1
	v_cvt_pk_bf16_f32 v110, v110, v111
	v_cvt_pk_bf16_f32 v111, v112, v113
	v_cvt_pk_bf16_f32 v112, v114, v115
	v_cvt_pk_bf16_f32 v113, v116, v117
	global_store_dwordx4 v197, v[110:113], s[54:55] sc1
	s_add_u32 s26, s79, s12
	s_addc_u32 s27, s80, 0
	global_load_dwordx4 v[156:159], v228, s[26:27] offset:64
	s_add_u32 s26, s81, s12
	s_addc_u32 s27, s82, 0
	global_load_dwordx4 v[160:163], v228, s[26:27] offset:64
	s_add_u32 s26, s76, s12
	s_addc_u32 s27, s77, 0
	global_load_dwordx4 v[164:167], v228, s[26:27] offset:64
	global_load_dwordx2 v[168:169], v190, s[50:51] offset:32
	global_load_dwordx2 v[170:171], v191, s[50:51] offset:32
	global_load_dwordx2 v[172:173], v192, s[50:51] offset:32
	global_load_dwordx2 v[174:175], v193, s[50:51] offset:32
	s_waitcnt vmcnt(13)
	v_add_f32_e32 v62, v62, v130
	v_add_f32_e32 v63, v63, v131
	v_add_f32_e32 v64, v64, v132
	v_add_f32_e32 v65, v65, v133
	v_add_f32_e32 v58, v58, v130
	v_add_f32_e32 v59, v59, v131
	v_add_f32_e32 v60, v60, v132
	v_add_f32_e32 v61, v61, v133
	v_mul_f32_e32 v62, 0xbfb8aa3b, v62
	v_mul_f32_e32 v63, 0xbfb8aa3b, v63
	v_mul_f32_e32 v64, 0xbfb8aa3b, v64
	v_mul_f32_e32 v65, 0xbfb8aa3b, v65
	v_mul_f32_e32 v58, 0xbfb8aa3b, v58
	v_mul_f32_e32 v59, 0xbfb8aa3b, v59
	v_mul_f32_e32 v60, 0xbfb8aa3b, v60
	v_mul_f32_e32 v61, 0xbfb8aa3b, v61
	v_exp_f32_e32 v62, v62
	v_exp_f32_e32 v63, v63
	v_exp_f32_e32 v64, v64
	v_exp_f32_e32 v65, v65
	v_exp_f32_e32 v58, v58
	v_exp_f32_e32 v59, v59
	v_exp_f32_e32 v60, v60
	v_exp_f32_e32 v61, v61
	v_add_f32_e32 v62, 1.0, v62
	v_add_f32_e32 v63, 1.0, v63
	v_add_f32_e32 v64, 1.0, v64
	v_add_f32_e32 v65, 1.0, v65
	v_add_f32_e32 v58, 1.0, v58
	v_add_f32_e32 v59, 1.0, v59
	v_add_f32_e32 v60, 1.0, v60
	v_add_f32_e32 v61, 1.0, v61
	v_rcp_f32_e32 v62, v62
	v_rcp_f32_e32 v63, v63
	v_rcp_f32_e32 v64, v64
	v_rcp_f32_e32 v65, v65
	v_rcp_f32_e32 v58, v58
	v_rcp_f32_e32 v59, v59
	v_rcp_f32_e32 v60, v60
	v_rcp_f32_e32 v61, v61
	v_mul_f32_e32 v62, v138, v62
	v_mul_f32_e32 v63, v139, v63
	v_mul_f32_e32 v64, v140, v64
	v_mul_f32_e32 v65, v141, v65
	v_mul_f32_e32 v58, v138, v58
	v_mul_f32_e32 v59, v139, v59
	v_mul_f32_e32 v60, v140, v60
	v_mul_f32_e32 v61, v141, v61
	v_add_f32_e32 v198, v62, v62
	v_add_f32_e32 v201, v63, v63
	v_add_f32_e32 v204, v64, v64
	v_add_f32_e32 v207, v65, v65
	v_add_f32_e32 v216, v58, v58
	v_add_f32_e32 v219, v59, v59
	v_add_f32_e32 v240, v60, v60
	v_add_f32_e32 v243, v61, v61
	v_mul_f32_e32 v199, 0x3fb8aa3b, v198
	v_mul_f32_e32 v202, 0x3fb8aa3b, v201
	v_mul_f32_e32 v205, 0x3fb8aa3b, v204
	v_mul_f32_e32 v208, 0x3fb8aa3b, v207
	v_mul_f32_e32 v217, 0x3fb8aa3b, v216
	v_mul_f32_e32 v238, 0x3fb8aa3b, v219
	v_mul_f32_e32 v241, 0x3fb8aa3b, v240
	v_mul_f32_e32 v244, 0x3fb8aa3b, v243
	v_exp_f32_e32 v199, v199
	v_exp_f32_e32 v202, v202
	v_exp_f32_e32 v205, v205
	v_exp_f32_e32 v208, v208
	v_exp_f32_e32 v217, v217
	v_exp_f32_e32 v238, v238
	v_exp_f32_e32 v241, v241
	v_exp_f32_e32 v244, v244
	v_fmamk_f32 v200, v198, 0x3c088889, v211
	v_fmamk_f32 v203, v201, 0x3c088889, v211
	v_fmamk_f32 v206, v204, 0x3c088889, v211
	v_fmamk_f32 v209, v207, 0x3c088889, v211
	v_fmamk_f32 v218, v216, 0x3c088889, v211
	v_fmamk_f32 v239, v219, 0x3c088889, v211
	v_fmamk_f32 v242, v240, 0x3c088889, v211
	v_fmamk_f32 v245, v243, 0x3c088889, v211
	v_sub_f32_e32 v199, 1.0, v199
	v_sub_f32_e32 v202, 1.0, v202
	v_sub_f32_e32 v205, 1.0, v205
	v_sub_f32_e32 v208, 1.0, v208
	v_sub_f32_e32 v217, 1.0, v217
	v_sub_f32_e32 v238, 1.0, v238
	v_sub_f32_e32 v241, 1.0, v241
	v_sub_f32_e32 v244, 1.0, v244
	v_fmaak_f32 v200, v198, v200, 0x3e2aaaab
	v_fmaak_f32 v203, v201, v203, 0x3e2aaaab
	v_fmaak_f32 v206, v204, v206, 0x3e2aaaab
	v_fmaak_f32 v209, v207, v209, 0x3e2aaaab
	v_fmaak_f32 v218, v216, v218, 0x3e2aaaab
	v_fmaak_f32 v239, v219, v239, 0x3e2aaaab
	v_fmaak_f32 v242, v240, v242, 0x3e2aaaab
	v_fmaak_f32 v245, v243, v245, 0x3e2aaaab
	v_fma_f32 v200, v198, v200, 0.5
	v_fma_f32 v203, v201, v203, 0.5
	v_fma_f32 v206, v204, v206, 0.5
	v_fma_f32 v209, v207, v209, 0.5
	v_fma_f32 v218, v216, v218, 0.5
	v_fma_f32 v239, v219, v239, 0.5
	v_fma_f32 v242, v240, v242, 0.5
	v_fma_f32 v245, v243, v245, 0.5
	v_fma_f32 v200, v198, v200, 1.0
	v_fma_f32 v203, v201, v203, 1.0
	v_fma_f32 v206, v204, v206, 1.0
	v_fma_f32 v209, v207, v209, 1.0
	v_fma_f32 v218, v216, v218, 1.0
	v_fma_f32 v239, v219, v239, 1.0
	v_fma_f32 v242, v240, v242, 1.0
	v_fma_f32 v245, v243, v245, 1.0
	v_mul_f32_e64 v200, v200, -v198
	v_mul_f32_e64 v203, v203, -v201
	v_mul_f32_e64 v206, v206, -v204
	v_mul_f32_e64 v209, v209, -v207
	v_mul_f32_e64 v218, v218, -v216
; __device__ __forceinline__ float sigmoid_fast(float x) { return __builtin_amdgcn_rcpf(1.f + __expf(-x)); }
; __device__ __forceinline__ float one_minus_exp(float x) { const float p = -x * (1.f + x * (0.5f + x * (0.16666667f + x * (0.041666668f + x * 0.0083333338f)))); return x > -0.1f ? p : 1.f - __expf(x); }
;     template <bool BWD>
;     __device__ __forceinline__ void epi_dir(const f32x4 (&acc)[2][2][4][2], const Unit& u, int wr, int wc, int fr, int fq) const {
;     ...
;                     for (int j = 0; j < 4; ++j) { const float r = sigmoid_fast(acc[ai][0][m][n][j] + bav[j]), ig = sigmoid_fast(acc[ai][1][m][n][j] + bxv[j]);
;                         const float la = r * lsl[j]; A[m][j] = __expf(la); H[m][j] = __builtin_amdgcn_sqrtf(one_minus_exp(2.f * la)) * (ig * uv[j]); } }
	v_mul_f32_e64 v239, v239, -v219
	v_mul_f32_e64 v242, v242, -v240
	v_mul_f32_e64 v245, v245, -v243
	v_cmp_nlt_f32_e32 vcc, s49, v198
	v_add_f32_e32 v34, v34, v134
	v_mul_f32_e32 v34, 0xbfb8aa3b, v34
	v_cndmask_b32_e32 v199, v200, v199, vcc
	v_cmp_nlt_f32_e32 vcc, s49, v201
	v_add_f32_e32 v35, v35, v135
	v_mul_f32_e32 v35, 0xbfb8aa3b, v35
	v_cndmask_b32_e32 v202, v203, v202, vcc
	v_cmp_nlt_f32_e32 vcc, s49, v204
	v_add_f32_e32 v36, v36, v136
	v_mul_f32_e32 v36, 0xbfb8aa3b, v36
	v_cndmask_b32_e32 v205, v206, v205, vcc
	v_cmp_nlt_f32_e32 vcc, s49, v207
	v_add_f32_e32 v37, v37, v137
	v_mul_f32_e32 v37, 0xbfb8aa3b, v37
	v_cndmask_b32_e32 v208, v209, v208, vcc
	v_cmp_nlt_f32_e32 vcc, s49, v216
	v_add_f32_e32 v38, v38, v134
	v_mul_f32_e32 v38, 0xbfb8aa3b, v38
	v_cndmask_b32_e32 v217, v218, v217, vcc
	v_cmp_nlt_f32_e32 vcc, s49, v219
	v_add_f32_e32 v39, v39, v135
	v_mul_f32_e32 v39, 0xbfb8aa3b, v39
	v_cndmask_b32_e32 v238, v239, v238, vcc
	v_cmp_nlt_f32_e32 vcc, s49, v240
	v_add_f32_e32 v40, v40, v136
	v_mul_f32_e32 v40, 0xbfb8aa3b, v40
	v_cndmask_b32_e32 v241, v242, v241, vcc
	v_cmp_nlt_f32_e32 vcc, s49, v243
	v_add_f32_e32 v41, v41, v137
	v_mul_f32_e32 v41, 0xbfb8aa3b, v41
	v_cndmask_b32_e32 v244, v245, v244, vcc
	v_exp_f32_e32 v34, v34
	v_exp_f32_e32 v35, v35
	v_exp_f32_e32 v36, v36
	v_exp_f32_e32 v37, v37
	v_exp_f32_e32 v38, v38
	v_exp_f32_e32 v39, v39
	v_exp_f32_e32 v40, v40
	v_exp_f32_e32 v41, v41
	v_sqrt_f32_e32 v199, v199
	v_sqrt_f32_e32 v202, v202
	v_sqrt_f32_e32 v205, v205
	v_sqrt_f32_e32 v208, v208
	v_sqrt_f32_e32 v217, v217
	v_sqrt_f32_e32 v238, v238
	v_sqrt_f32_e32 v241, v241
	v_sqrt_f32_e32 v244, v244
	v_add_f32_e32 v34, 1.0, v34
	v_add_f32_e32 v35, 1.0, v35
	v_add_f32_e32 v36, 1.0, v36
	v_add_f32_e32 v37, 1.0, v37
	v_add_f32_e32 v38, 1.0, v38
	v_add_f32_e32 v39, 1.0, v39
	v_add_f32_e32 v40, 1.0, v40
	v_add_f32_e32 v41, 1.0, v41
	v_lshlrev_b32_e32 v200, 16, v176
	v_and_b32_e32 v203, 0xffff0000, v176
	v_lshlrev_b32_e32 v206, 16, v177
	v_and_b32_e32 v209, 0xffff0000, v177
	v_lshlrev_b32_e32 v218, 16, v178
	v_and_b32_e32 v239, 0xffff0000, v178
	v_lshlrev_b32_e32 v242, 16, v179
	v_and_b32_e32 v245, 0xffff0000, v179
	v_rcp_f32_e32 v34, v34
	v_rcp_f32_e32 v35, v35
	v_rcp_f32_e32 v36, v36
	v_rcp_f32_e32 v37, v37
	v_rcp_f32_e32 v38, v38
	v_rcp_f32_e32 v39, v39
	v_rcp_f32_e32 v40, v40
	v_rcp_f32_e32 v41, v41
	v_mul_f32_e32 v62, 0x3fb8aa3b, v62
	v_mul_f32_e32 v63, 0x3fb8aa3b, v63
	v_mul_f32_e32 v64, 0x3fb8aa3b, v64
	v_mul_f32_e32 v65, 0x3fb8aa3b, v65
	v_mul_f32_e32 v58, 0x3fb8aa3b, v58
	v_mul_f32_e32 v59, 0x3fb8aa3b, v59
	v_mul_f32_e32 v60, 0x3fb8aa3b, v60
	v_mul_f32_e32 v61, 0x3fb8aa3b, v61
	v_mul_f32_e32 v34, v34, v200
	v_mul_f32_e32 v35, v35, v203
	v_mul_f32_e32 v36, v36, v206
	v_mul_f32_e32 v37, v37, v209
	v_mul_f32_e32 v38, v38, v218
	v_mul_f32_e32 v39, v39, v239
	v_mul_f32_e32 v40, v40, v242
	v_mul_f32_e32 v41, v41, v245
	v_exp_f32_e32 v62, v62
	v_exp_f32_e32 v63, v63
	v_exp_f32_e32 v64, v64
	v_exp_f32_e32 v65, v65
	v_exp_f32_e32 v58, v58
	v_exp_f32_e32 v59, v59
	v_exp_f32_e32 v60, v60
	v_exp_f32_e32 v61, v61
	v_mul_f32_e32 v34, v34, v199
	v_mul_f32_e32 v35, v35, v202
	v_mul_f32_e32 v36, v36, v205
	v_mul_f32_e32 v37, v37, v208
	v_mul_f32_e32 v38, v38, v217
	v_mul_f32_e32 v39, v39, v238
	v_mul_f32_e32 v40, v40, v241
	v_mul_f32_e32 v41, v41, v244
	v_add_f32_e32 v54, v54, v130
	v_add_f32_e32 v55, v55, v131
	v_add_f32_e32 v56, v56, v132
	v_add_f32_e32 v57, v57, v133
	v_add_f32_e32 v50, v50, v130
	v_add_f32_e32 v51, v51, v131
	v_add_f32_e32 v52, v52, v132
	v_add_f32_e32 v53, v53, v133
	v_mul_f32_e32 v54, 0xbfb8aa3b, v54
	v_mul_f32_e32 v55, 0xbfb8aa3b, v55
	v_mul_f32_e32 v56, 0xbfb8aa3b, v56
	v_mul_f32_e32 v57, 0xbfb8aa3b, v57
	v_mul_f32_e32 v50, 0xbfb8aa3b, v50
	v_mul_f32_e32 v51, 0xbfb8aa3b, v51
	v_mul_f32_e32 v52, 0xbfb8aa3b, v52
	v_mul_f32_e32 v53, 0xbfb8aa3b, v53
	v_exp_f32_e32 v54, v54
	v_exp_f32_e32 v55, v55
	v_exp_f32_e32 v56, v56
	v_exp_f32_e32 v57, v57
	v_exp_f32_e32 v50, v50
	v_exp_f32_e32 v51, v51
	v_exp_f32_e32 v52, v52
	v_exp_f32_e32 v53, v53
	v_add_f32_e32 v54, 1.0, v54
	v_add_f32_e32 v55, 1.0, v55
	v_add_f32_e32 v56, 1.0, v56
	v_add_f32_e32 v57, 1.0, v57
	v_add_f32_e32 v50, 1.0, v50
	v_add_f32_e32 v51, 1.0, v51
	v_add_f32_e32 v52, 1.0, v52
	v_add_f32_e32 v53, 1.0, v53
	v_rcp_f32_e32 v54, v54
	v_rcp_f32_e32 v55, v55
	v_rcp_f32_e32 v56, v56
	v_rcp_f32_e32 v57, v57
	v_rcp_f32_e32 v50, v50
	v_rcp_f32_e32 v51, v51
	v_rcp_f32_e32 v52, v52
	v_rcp_f32_e32 v53, v53
	v_mul_f32_e32 v54, v138, v54
	v_mul_f32_e32 v55, v139, v55
	v_mul_f32_e32 v56, v140, v56
	v_mul_f32_e32 v57, v141, v57
	v_mul_f32_e32 v50, v138, v50
	v_mul_f32_e32 v51, v139, v51
	v_mul_f32_e32 v52, v140, v52
	v_mul_f32_e32 v53, v141, v53
	v_add_f32_e32 v198, v54, v54
	v_add_f32_e32 v201, v55, v55
	v_add_f32_e32 v204, v56, v56
	v_add_f32_e32 v207, v57, v57
	v_add_f32_e32 v216, v50, v50
	v_add_f32_e32 v219, v51, v51
	v_add_f32_e32 v240, v52, v52
	v_add_f32_e32 v243, v53, v53
	v_mul_f32_e32 v199, 0x3fb8aa3b, v198
	v_mul_f32_e32 v202, 0x3fb8aa3b, v201
	v_mul_f32_e32 v205, 0x3fb8aa3b, v204
	v_mul_f32_e32 v208, 0x3fb8aa3b, v207
	v_mul_f32_e32 v217, 0x3fb8aa3b, v216
	v_mul_f32_e32 v238, 0x3fb8aa3b, v219
	v_mul_f32_e32 v241, 0x3fb8aa3b, v240
	v_mul_f32_e32 v244, 0x3fb8aa3b, v243
	v_exp_f32_e32 v199, v199
	v_exp_f32_e32 v202, v202
	v_exp_f32_e32 v205, v205
	v_exp_f32_e32 v208, v208
	v_exp_f32_e32 v217, v217
	v_exp_f32_e32 v238, v238
	v_exp_f32_e32 v241, v241
	v_exp_f32_e32 v244, v244
	v_fmamk_f32 v200, v198, 0x3c088889, v211
	v_fmamk_f32 v203, v201, 0x3c088889, v211
	v_fmamk_f32 v206, v204, 0x3c088889, v211
	v_fmamk_f32 v209, v207, 0x3c088889, v211
	v_fmamk_f32 v218, v216, 0x3c088889, v211
; __device__ __forceinline__ float sigmoid_fast(float x) { return __builtin_amdgcn_rcpf(1.f + __expf(-x)); }
; __device__ __forceinline__ float one_minus_exp(float x) { const float p = -x * (1.f + x * (0.5f + x * (0.16666667f + x * (0.041666668f + x * 0.0083333338f)))); return x > -0.1f ? p : 1.f - __expf(x); }
; #define SCAN_STEP(D) { const float ap = dppf<(BWD ? 0x100 : 0x110) + D>(1.f, av), hp = dppf<(BWD ? 0x100 : 0x110) + D>(0.f, hv); hv = fmaf(av, hp, hv); av = av * ap; }
;     template <bool BWD>
;     __device__ __forceinline__ void epi_dir(const f32x4 (&acc)[2][2][4][2], const Unit& u, int wr, int wc, int fr, int fq) const {
;     ...
;                     for (int j = 0; j < 4; ++j) { const float r = sigmoid_fast(acc[ai][0][m][n][j] + bav[j]), ig = sigmoid_fast(acc[ai][1][m][n][j] + bxv[j]);
;                         const float la = r * lsl[j]; A[m][j] = __expf(la); H[m][j] = __builtin_amdgcn_sqrtf(one_minus_exp(2.f * la)) * (ig * uv[j]); } }
; #pragma unroll
;                 for (int m = 0; m < 4; ++m)
; #pragma unroll
;                     for (int j = 0; j < 4; ++j) { float av = A[m][j], hv = H[m][j];
;     ...
;                         SCAN_STEP(1) SCAN_STEP(2) SCAN_STEP(4) SCAN_STEP(8)
	v_fmamk_f32 v239, v219, 0x3c088889, v211
	v_fmamk_f32 v242, v240, 0x3c088889, v211
	v_fmamk_f32 v245, v243, 0x3c088889, v211
	v_sub_f32_e32 v199, 1.0, v199
	v_sub_f32_e32 v202, 1.0, v202
	v_sub_f32_e32 v205, 1.0, v205
	v_sub_f32_e32 v208, 1.0, v208
	v_sub_f32_e32 v217, 1.0, v217
	v_sub_f32_e32 v238, 1.0, v238
	v_sub_f32_e32 v241, 1.0, v241
	v_sub_f32_e32 v244, 1.0, v244
	v_fmaak_f32 v200, v198, v200, 0x3e2aaaab
	v_fmaak_f32 v203, v201, v203, 0x3e2aaaab
	v_fmaak_f32 v206, v204, v206, 0x3e2aaaab
	v_fmaak_f32 v209, v207, v209, 0x3e2aaaab
	v_fmaak_f32 v218, v216, v218, 0x3e2aaaab
	v_fmaak_f32 v239, v219, v239, 0x3e2aaaab
	v_fmaak_f32 v242, v240, v242, 0x3e2aaaab
	v_fmaak_f32 v245, v243, v245, 0x3e2aaaab
	v_fma_f32 v200, v198, v200, 0.5
	v_fma_f32 v203, v201, v203, 0.5
	v_fma_f32 v206, v204, v206, 0.5
	v_fma_f32 v209, v207, v209, 0.5
	v_fma_f32 v218, v216, v218, 0.5
	v_fma_f32 v239, v219, v239, 0.5
	v_fma_f32 v242, v240, v242, 0.5
	v_fma_f32 v245, v243, v245, 0.5
	v_fma_f32 v200, v198, v200, 1.0
	v_fma_f32 v203, v201, v203, 1.0
	v_fma_f32 v206, v204, v206, 1.0
	v_fma_f32 v209, v207, v209, 1.0
	v_fma_f32 v218, v216, v218, 1.0
	v_fma_f32 v239, v219, v239, 1.0
	v_fma_f32 v242, v240, v242, 1.0
	v_fma_f32 v245, v243, v245, 1.0
	v_mul_f32_e64 v200, v200, -v198
	v_mul_f32_e64 v203, v203, -v201
	v_mul_f32_e64 v206, v206, -v204
	v_mul_f32_e64 v209, v209, -v207
	v_mul_f32_e64 v218, v218, -v216
	v_mul_f32_e64 v239, v239, -v219
	v_mul_f32_e64 v242, v242, -v240
	v_mul_f32_e64 v245, v245, -v243
	v_cmp_nlt_f32_e32 vcc, s49, v198
	v_add_f32_e32 v42, v42, v134
	v_mul_f32_e32 v42, 0xbfb8aa3b, v42
	v_cndmask_b32_e32 v199, v200, v199, vcc
	v_cmp_nlt_f32_e32 vcc, s49, v201
	v_add_f32_e32 v43, v43, v135
	v_mul_f32_e32 v43, 0xbfb8aa3b, v43
	v_cndmask_b32_e32 v202, v203, v202, vcc
	v_cmp_nlt_f32_e32 vcc, s49, v204
	v_add_f32_e32 v44, v44, v136
	v_mul_f32_e32 v44, 0xbfb8aa3b, v44
	v_cndmask_b32_e32 v205, v206, v205, vcc
	v_cmp_nlt_f32_e32 vcc, s49, v207
	v_add_f32_e32 v45, v45, v137
	v_mul_f32_e32 v45, 0xbfb8aa3b, v45
	v_cndmask_b32_e32 v208, v209, v208, vcc
	v_cmp_nlt_f32_e32 vcc, s49, v216
	v_add_f32_e32 v46, v46, v134
	v_mul_f32_e32 v46, 0xbfb8aa3b, v46
	v_cndmask_b32_e32 v217, v218, v217, vcc
	v_cmp_nlt_f32_e32 vcc, s49, v219
	v_add_f32_e32 v47, v47, v135
	v_mul_f32_e32 v47, 0xbfb8aa3b, v47
	v_cndmask_b32_e32 v238, v239, v238, vcc
	v_cmp_nlt_f32_e32 vcc, s49, v240
	v_add_f32_e32 v48, v48, v136
	v_mul_f32_e32 v48, 0xbfb8aa3b, v48
	v_cndmask_b32_e32 v241, v242, v241, vcc
	v_cmp_nlt_f32_e32 vcc, s49, v243
	v_add_f32_e32 v49, v49, v137
	v_mul_f32_e32 v49, 0xbfb8aa3b, v49
	v_cndmask_b32_e32 v244, v245, v244, vcc
	v_exp_f32_e32 v42, v42
	v_exp_f32_e32 v43, v43
	v_exp_f32_e32 v44, v44
	v_exp_f32_e32 v45, v45
	v_exp_f32_e32 v46, v46
	v_exp_f32_e32 v47, v47
	v_exp_f32_e32 v48, v48
	v_exp_f32_e32 v49, v49
	v_sqrt_f32_e32 v199, v199
	v_sqrt_f32_e32 v202, v202
	v_sqrt_f32_e32 v205, v205
	v_sqrt_f32_e32 v208, v208
	v_sqrt_f32_e32 v217, v217
	v_sqrt_f32_e32 v238, v238
	v_sqrt_f32_e32 v241, v241
	v_sqrt_f32_e32 v244, v244
	v_add_f32_e32 v42, 1.0, v42
	v_add_f32_e32 v43, 1.0, v43
	v_add_f32_e32 v44, 1.0, v44
	v_add_f32_e32 v45, 1.0, v45
	v_add_f32_e32 v46, 1.0, v46
	v_add_f32_e32 v47, 1.0, v47
	v_add_f32_e32 v48, 1.0, v48
	v_add_f32_e32 v49, 1.0, v49
	v_lshlrev_b32_e32 v200, 16, v182
	v_and_b32_e32 v203, 0xffff0000, v182
	v_lshlrev_b32_e32 v206, 16, v183
	v_and_b32_e32 v209, 0xffff0000, v183
	v_lshlrev_b32_e32 v218, 16, v184
	v_and_b32_e32 v239, 0xffff0000, v184
	v_lshlrev_b32_e32 v242, 16, v185
	v_and_b32_e32 v245, 0xffff0000, v185
	v_rcp_f32_e32 v42, v42
	v_rcp_f32_e32 v43, v43
	v_rcp_f32_e32 v44, v44
	v_rcp_f32_e32 v45, v45
	v_rcp_f32_e32 v46, v46
	v_rcp_f32_e32 v47, v47
	v_rcp_f32_e32 v48, v48
	v_rcp_f32_e32 v49, v49
	v_mul_f32_e32 v54, 0x3fb8aa3b, v54
	v_mul_f32_e32 v55, 0x3fb8aa3b, v55
	v_mul_f32_e32 v56, 0x3fb8aa3b, v56
	v_mul_f32_e32 v57, 0x3fb8aa3b, v57
	v_mul_f32_e32 v50, 0x3fb8aa3b, v50
	v_mul_f32_e32 v51, 0x3fb8aa3b, v51
	v_mul_f32_e32 v52, 0x3fb8aa3b, v52
	v_mul_f32_e32 v53, 0x3fb8aa3b, v53
	v_mul_f32_e32 v42, v42, v200
	v_mul_f32_e32 v43, v43, v203
	v_mul_f32_e32 v44, v44, v206
	v_mul_f32_e32 v45, v45, v209
	v_mul_f32_e32 v46, v46, v218
	v_mul_f32_e32 v47, v47, v239
	v_mul_f32_e32 v48, v48, v242
	v_mul_f32_e32 v49, v49, v245
	v_exp_f32_e32 v54, v54
	v_exp_f32_e32 v55, v55
	v_exp_f32_e32 v56, v56
	v_exp_f32_e32 v57, v57
	v_exp_f32_e32 v50, v50
	v_exp_f32_e32 v51, v51
	v_exp_f32_e32 v52, v52
	v_exp_f32_e32 v53, v53
	v_mul_f32_e32 v42, v42, v199
	v_mul_f32_e32 v43, v43, v202
	v_mul_f32_e32 v44, v44, v205
	v_mul_f32_e32 v45, v45, v208
	v_mul_f32_e32 v46, v46, v217
	v_mul_f32_e32 v47, v47, v238
	v_mul_f32_e32 v48, v48, v241
	v_mul_f32_e32 v49, v49, v244
	v_fmac_f32_dpp v34, v34, v62 row_shr:1 row_mask:0xf bank_mask:0xf
	v_mul_f32_dpp v62, v62, v62 row_shr:1 row_mask:0xf bank_mask:0xf
	v_fmac_f32_dpp v35, v35, v63 row_shr:1 row_mask:0xf bank_mask:0xf
	v_mul_f32_dpp v63, v63, v63 row_shr:1 row_mask:0xf bank_mask:0xf
	v_fmac_f32_dpp v36, v36, v64 row_shr:1 row_mask:0xf bank_mask:0xf
	v_mul_f32_dpp v64, v64, v64 row_shr:1 row_mask:0xf bank_mask:0xf
	v_fmac_f32_dpp v37, v37, v65 row_shr:1 row_mask:0xf bank_mask:0xf
	v_mul_f32_dpp v65, v65, v65 row_shr:1 row_mask:0xf bank_mask:0xf
	v_fmac_f32_dpp v38, v38, v58 row_shr:1 row_mask:0xf bank_mask:0xf
	v_mul_f32_dpp v58, v58, v58 row_shr:1 row_mask:0xf bank_mask:0xf
	v_fmac_f32_dpp v39, v39, v59 row_shr:1 row_mask:0xf bank_mask:0xf
	v_mul_f32_dpp v59, v59, v59 row_shr:1 row_mask:0xf bank_mask:0xf
	v_fmac_f32_dpp v40, v40, v60 row_shr:1 row_mask:0xf bank_mask:0xf
	v_mul_f32_dpp v60, v60, v60 row_shr:1 row_mask:0xf bank_mask:0xf
; #define SCAN_STEP(D) { const float ap = dppf<(BWD ? 0x100 : 0x110) + D>(1.f, av), hp = dppf<(BWD ? 0x100 : 0x110) + D>(0.f, hv); hv = fmaf(av, hp, hv); av = av * ap; }
;     template <bool BWD>
;     __device__ __forceinline__ void epi_dir(const f32x4 (&acc)[2][2][4][2], const Unit& u, int wr, int wc, int fr, int fq) const {
;     ...
;                 for (int m = 0; m < 4; ++m)
; #pragma unroll
;                     for (int j = 0; j < 4; ++j) { float av = A[m][j], hv = H[m][j];
;     ...
;                         SCAN_STEP(1) SCAN_STEP(2) SCAN_STEP(4) SCAN_STEP(8)
	v_fmac_f32_dpp v41, v41, v61 row_shr:1 row_mask:0xf bank_mask:0xf
	v_mul_f32_dpp v61, v61, v61 row_shr:1 row_mask:0xf bank_mask:0xf
	v_fmac_f32_dpp v42, v42, v54 row_shr:1 row_mask:0xf bank_mask:0xf
	v_mul_f32_dpp v54, v54, v54 row_shr:1 row_mask:0xf bank_mask:0xf
	v_fmac_f32_dpp v43, v43, v55 row_shr:1 row_mask:0xf bank_mask:0xf
	v_mul_f32_dpp v55, v55, v55 row_shr:1 row_mask:0xf bank_mask:0xf
	v_fmac_f32_dpp v44, v44, v56 row_shr:1 row_mask:0xf bank_mask:0xf
	v_mul_f32_dpp v56, v56, v56 row_shr:1 row_mask:0xf bank_mask:0xf
	v_fmac_f32_dpp v45, v45, v57 row_shr:1 row_mask:0xf bank_mask:0xf
	v_mul_f32_dpp v57, v57, v57 row_shr:1 row_mask:0xf bank_mask:0xf
	v_fmac_f32_dpp v46, v46, v50 row_shr:1 row_mask:0xf bank_mask:0xf
	v_mul_f32_dpp v50, v50, v50 row_shr:1 row_mask:0xf bank_mask:0xf
	v_fmac_f32_dpp v47, v47, v51 row_shr:1 row_mask:0xf bank_mask:0xf
	v_mul_f32_dpp v51, v51, v51 row_shr:1 row_mask:0xf bank_mask:0xf
	v_fmac_f32_dpp v48, v48, v52 row_shr:1 row_mask:0xf bank_mask:0xf
	v_mul_f32_dpp v52, v52, v52 row_shr:1 row_mask:0xf bank_mask:0xf
	v_fmac_f32_dpp v49, v49, v53 row_shr:1 row_mask:0xf bank_mask:0xf
	v_mul_f32_dpp v53, v53, v53 row_shr:1 row_mask:0xf bank_mask:0xf
	v_fmac_f32_dpp v34, v34, v62 row_shr:2 row_mask:0xf bank_mask:0xf
	v_mul_f32_dpp v62, v62, v62 row_shr:2 row_mask:0xf bank_mask:0xf
	v_fmac_f32_dpp v35, v35, v63 row_shr:2 row_mask:0xf bank_mask:0xf
	v_mul_f32_dpp v63, v63, v63 row_shr:2 row_mask:0xf bank_mask:0xf
	v_fmac_f32_dpp v36, v36, v64 row_shr:2 row_mask:0xf bank_mask:0xf
	v_mul_f32_dpp v64, v64, v64 row_shr:2 row_mask:0xf bank_mask:0xf
	v_fmac_f32_dpp v37, v37, v65 row_shr:2 row_mask:0xf bank_mask:0xf
	v_mul_f32_dpp v65, v65, v65 row_shr:2 row_mask:0xf bank_mask:0xf
	v_fmac_f32_dpp v38, v38, v58 row_shr:2 row_mask:0xf bank_mask:0xf
	v_mul_f32_dpp v58, v58, v58 row_shr:2 row_mask:0xf bank_mask:0xf
	v_fmac_f32_dpp v39, v39, v59 row_shr:2 row_mask:0xf bank_mask:0xf
	v_mul_f32_dpp v59, v59, v59 row_shr:2 row_mask:0xf bank_mask:0xf
	v_fmac_f32_dpp v40, v40, v60 row_shr:2 row_mask:0xf bank_mask:0xf
	v_mul_f32_dpp v60, v60, v60 row_shr:2 row_mask:0xf bank_mask:0xf
	v_fmac_f32_dpp v41, v41, v61 row_shr:2 row_mask:0xf bank_mask:0xf
	v_mul_f32_dpp v61, v61, v61 row_shr:2 row_mask:0xf bank_mask:0xf
	v_fmac_f32_dpp v42, v42, v54 row_shr:2 row_mask:0xf bank_mask:0xf
	v_mul_f32_dpp v54, v54, v54 row_shr:2 row_mask:0xf bank_mask:0xf
	v_fmac_f32_dpp v43, v43, v55 row_shr:2 row_mask:0xf bank_mask:0xf
	v_mul_f32_dpp v55, v55, v55 row_shr:2 row_mask:0xf bank_mask:0xf
	v_fmac_f32_dpp v44, v44, v56 row_shr:2 row_mask:0xf bank_mask:0xf
	v_mul_f32_dpp v56, v56, v56 row_shr:2 row_mask:0xf bank_mask:0xf
	v_fmac_f32_dpp v45, v45, v57 row_shr:2 row_mask:0xf bank_mask:0xf
	v_mul_f32_dpp v57, v57, v57 row_shr:2 row_mask:0xf bank_mask:0xf
	v_fmac_f32_dpp v46, v46, v50 row_shr:2 row_mask:0xf bank_mask:0xf
	v_mul_f32_dpp v50, v50, v50 row_shr:2 row_mask:0xf bank_mask:0xf
	v_fmac_f32_dpp v47, v47, v51 row_shr:2 row_mask:0xf bank_mask:0xf
	v_mul_f32_dpp v51, v51, v51 row_shr:2 row_mask:0xf bank_mask:0xf
	v_fmac_f32_dpp v48, v48, v52 row_shr:2 row_mask:0xf bank_mask:0xf
	v_mul_f32_dpp v52, v52, v52 row_shr:2 row_mask:0xf bank_mask:0xf
	v_fmac_f32_dpp v49, v49, v53 row_shr:2 row_mask:0xf bank_mask:0xf
	v_mul_f32_dpp v53, v53, v53 row_shr:2 row_mask:0xf bank_mask:0xf
	v_fmac_f32_dpp v34, v34, v62 row_shr:4 row_mask:0xf bank_mask:0xf
	v_mul_f32_dpp v62, v62, v62 row_shr:4 row_mask:0xf bank_mask:0xf
	v_fmac_f32_dpp v35, v35, v63 row_shr:4 row_mask:0xf bank_mask:0xf
	v_mul_f32_dpp v63, v63, v63 row_shr:4 row_mask:0xf bank_mask:0xf
	v_fmac_f32_dpp v36, v36, v64 row_shr:4 row_mask:0xf bank_mask:0xf
	v_mul_f32_dpp v64, v64, v64 row_shr:4 row_mask:0xf bank_mask:0xf
	v_fmac_f32_dpp v37, v37, v65 row_shr:4 row_mask:0xf bank_mask:0xf
	v_mul_f32_dpp v65, v65, v65 row_shr:4 row_mask:0xf bank_mask:0xf
	v_fmac_f32_dpp v38, v38, v58 row_shr:4 row_mask:0xf bank_mask:0xf
	v_mul_f32_dpp v58, v58, v58 row_shr:4 row_mask:0xf bank_mask:0xf
	v_fmac_f32_dpp v39, v39, v59 row_shr:4 row_mask:0xf bank_mask:0xf
	v_mul_f32_dpp v59, v59, v59 row_shr:4 row_mask:0xf bank_mask:0xf
	v_fmac_f32_dpp v40, v40, v60 row_shr:4 row_mask:0xf bank_mask:0xf
	v_mul_f32_dpp v60, v60, v60 row_shr:4 row_mask:0xf bank_mask:0xf
	v_fmac_f32_dpp v41, v41, v61 row_shr:4 row_mask:0xf bank_mask:0xf
	v_mul_f32_dpp v61, v61, v61 row_shr:4 row_mask:0xf bank_mask:0xf
	v_fmac_f32_dpp v42, v42, v54 row_shr:4 row_mask:0xf bank_mask:0xf
	v_mul_f32_dpp v54, v54, v54 row_shr:4 row_mask:0xf bank_mask:0xf
	v_fmac_f32_dpp v43, v43, v55 row_shr:4 row_mask:0xf bank_mask:0xf
	v_mul_f32_dpp v55, v55, v55 row_shr:4 row_mask:0xf bank_mask:0xf
	v_fmac_f32_dpp v44, v44, v56 row_shr:4 row_mask:0xf bank_mask:0xf
	v_mul_f32_dpp v56, v56, v56 row_shr:4 row_mask:0xf bank_mask:0xf
	v_fmac_f32_dpp v45, v45, v57 row_shr:4 row_mask:0xf bank_mask:0xf
	v_mul_f32_dpp v57, v57, v57 row_shr:4 row_mask:0xf bank_mask:0xf
	v_fmac_f32_dpp v46, v46, v50 row_shr:4 row_mask:0xf bank_mask:0xf
	v_mul_f32_dpp v50, v50, v50 row_shr:4 row_mask:0xf bank_mask:0xf
	v_fmac_f32_dpp v47, v47, v51 row_shr:4 row_mask:0xf bank_mask:0xf
	v_mul_f32_dpp v51, v51, v51 row_shr:4 row_mask:0xf bank_mask:0xf
	v_fmac_f32_dpp v48, v48, v52 row_shr:4 row_mask:0xf bank_mask:0xf
	v_mul_f32_dpp v52, v52, v52 row_shr:4 row_mask:0xf bank_mask:0xf
	v_fmac_f32_dpp v49, v49, v53 row_shr:4 row_mask:0xf bank_mask:0xf
	v_mul_f32_dpp v53, v53, v53 row_shr:4 row_mask:0xf bank_mask:0xf
	v_fmac_f32_dpp v34, v34, v62 row_shr:8 row_mask:0xf bank_mask:0xf
	v_mul_f32_dpp v62, v62, v62 row_shr:8 row_mask:0xf bank_mask:0xf
	v_fmac_f32_dpp v35, v35, v63 row_shr:8 row_mask:0xf bank_mask:0xf
; __device__ __forceinline__ unsigned pk2(float lo, float hi) { return f2bf(lo) | (f2bf(hi) << 16); }
; #define SCAN_STEP(D) { const float ap = dppf<(BWD ? 0x100 : 0x110) + D>(1.f, av), hp = dppf<(BWD ? 0x100 : 0x110) + D>(0.f, hv); hv = fmaf(av, hp, hv); av = av * ap; }
;     template <bool BWD>
;     __device__ __forceinline__ void epi_dir(const f32x4 (&acc)[2][2][4][2], const Unit& u, int wr, int wc, int fr, int fq) const {
;     ...
;                 for (int m = 0; m < 4; ++m)
; #pragma unroll
;                     for (int j = 0; j < 4; ++j) { float av = A[m][j], hv = H[m][j];
;     ...
;                         SCAN_STEP(1) SCAN_STEP(2) SCAN_STEP(4) SCAN_STEP(8)
;     ...
;                         A[m][j] = av; H[m][j] = hv; }
; #pragma unroll
;                 for (int j = 0; j < 4; ++j) { float Ar = 1.f, Hr = 0.f;
; #pragma unroll
;                     for (int mm = 0; mm < 4; ++mm) { const int m = BWD ? 3 - mm : mm;
;                         H[m][j] = fmaf(A[m][j], Hr, H[m][j]); A[m][j] = A[m][j] * Ar;
;                         if (mm < 3) { Ar = __shfl(A[m][j], bsel); Hr = __shfl(H[m][j], bsel); } } }
; #pragma unroll
;                 for (int m = 0; m < 4; ++m) { u32x4 w; w.x = pk2(H[m][0], H[m][1]); w.y = pk2(H[m][2], H[m][3]); w.z = pk2(A[m][0], A[m][1]); w.w = pk2(A[m][2], A[m][3]);
;                     *(u32x4*)(Hb + ((size_t)(ai * 128 + m * 16) * 1024 + n * 16) * 4 + loffh) = w; }
;                 constexpr int me = BWD ? 0 : 3;
;                 if (fr == (BWD ? 0 : 15)) { const size_t o = (size_t)chunk * 1024 + gblk * 128 + n * 16;
;                     *(f32x4*)((char*)(AGG + (size_t)(dir * 2 + 0) * NB * NCHUNK * 1024 + o) + coff) = A[me];
;                     *(f32x4*)((char*)(AGG + (size_t)(dir * 2 + 1) * NB * NCHUNK * 1024 + o) + coff) = H[me]; }
	v_mul_f32_dpp v63, v63, v63 row_shr:8 row_mask:0xf bank_mask:0xf
	v_fmac_f32_dpp v36, v36, v64 row_shr:8 row_mask:0xf bank_mask:0xf
	v_mul_f32_dpp v64, v64, v64 row_shr:8 row_mask:0xf bank_mask:0xf
	v_fmac_f32_dpp v37, v37, v65 row_shr:8 row_mask:0xf bank_mask:0xf
	v_mul_f32_dpp v65, v65, v65 row_shr:8 row_mask:0xf bank_mask:0xf
	v_fmac_f32_dpp v38, v38, v58 row_shr:8 row_mask:0xf bank_mask:0xf
	v_mul_f32_dpp v58, v58, v58 row_shr:8 row_mask:0xf bank_mask:0xf
	v_fmac_f32_dpp v39, v39, v59 row_shr:8 row_mask:0xf bank_mask:0xf
	v_mul_f32_dpp v59, v59, v59 row_shr:8 row_mask:0xf bank_mask:0xf
	v_fmac_f32_dpp v40, v40, v60 row_shr:8 row_mask:0xf bank_mask:0xf
	v_mul_f32_dpp v60, v60, v60 row_shr:8 row_mask:0xf bank_mask:0xf
	v_fmac_f32_dpp v41, v41, v61 row_shr:8 row_mask:0xf bank_mask:0xf
	v_mul_f32_dpp v61, v61, v61 row_shr:8 row_mask:0xf bank_mask:0xf
	v_fmac_f32_dpp v42, v42, v54 row_shr:8 row_mask:0xf bank_mask:0xf
	v_mul_f32_dpp v54, v54, v54 row_shr:8 row_mask:0xf bank_mask:0xf
	v_fmac_f32_dpp v43, v43, v55 row_shr:8 row_mask:0xf bank_mask:0xf
	v_mul_f32_dpp v55, v55, v55 row_shr:8 row_mask:0xf bank_mask:0xf
	v_fmac_f32_dpp v44, v44, v56 row_shr:8 row_mask:0xf bank_mask:0xf
	v_mul_f32_dpp v56, v56, v56 row_shr:8 row_mask:0xf bank_mask:0xf
	v_fmac_f32_dpp v45, v45, v57 row_shr:8 row_mask:0xf bank_mask:0xf
	v_mul_f32_dpp v57, v57, v57 row_shr:8 row_mask:0xf bank_mask:0xf
	v_fmac_f32_dpp v46, v46, v50 row_shr:8 row_mask:0xf bank_mask:0xf
	v_mul_f32_dpp v50, v50, v50 row_shr:8 row_mask:0xf bank_mask:0xf
	v_fmac_f32_dpp v47, v47, v51 row_shr:8 row_mask:0xf bank_mask:0xf
	v_mul_f32_dpp v51, v51, v51 row_shr:8 row_mask:0xf bank_mask:0xf
	v_fmac_f32_dpp v48, v48, v52 row_shr:8 row_mask:0xf bank_mask:0xf
	v_mul_f32_dpp v52, v52, v52 row_shr:8 row_mask:0xf bank_mask:0xf
	v_fmac_f32_dpp v49, v49, v53 row_shr:8 row_mask:0xf bank_mask:0xf
	v_mul_f32_dpp v53, v53, v53 row_shr:8 row_mask:0xf bank_mask:0xf
	v_fmac_f32_dpp v38, v34, v58 row_newbcast:15 row_mask:0xf bank_mask:0xf
	v_mul_f32_dpp v58, v62, v58 row_newbcast:15 row_mask:0xf bank_mask:0xf
	v_fmac_f32_dpp v39, v35, v59 row_newbcast:15 row_mask:0xf bank_mask:0xf
	v_mul_f32_dpp v59, v63, v59 row_newbcast:15 row_mask:0xf bank_mask:0xf
	v_fmac_f32_dpp v40, v36, v60 row_newbcast:15 row_mask:0xf bank_mask:0xf
	v_mul_f32_dpp v60, v64, v60 row_newbcast:15 row_mask:0xf bank_mask:0xf
	v_fmac_f32_dpp v41, v37, v61 row_newbcast:15 row_mask:0xf bank_mask:0xf
	v_mul_f32_dpp v61, v65, v61 row_newbcast:15 row_mask:0xf bank_mask:0xf
	v_fmac_f32_dpp v42, v38, v54 row_newbcast:15 row_mask:0xf bank_mask:0xf
	v_mul_f32_dpp v54, v58, v54 row_newbcast:15 row_mask:0xf bank_mask:0xf
	v_fmac_f32_dpp v43, v39, v55 row_newbcast:15 row_mask:0xf bank_mask:0xf
	v_mul_f32_dpp v55, v59, v55 row_newbcast:15 row_mask:0xf bank_mask:0xf
	v_fmac_f32_dpp v44, v40, v56 row_newbcast:15 row_mask:0xf bank_mask:0xf
	v_mul_f32_dpp v56, v60, v56 row_newbcast:15 row_mask:0xf bank_mask:0xf
	v_fmac_f32_dpp v45, v41, v57 row_newbcast:15 row_mask:0xf bank_mask:0xf
	v_mul_f32_dpp v57, v61, v57 row_newbcast:15 row_mask:0xf bank_mask:0xf
	v_fmac_f32_dpp v46, v42, v50 row_newbcast:15 row_mask:0xf bank_mask:0xf
	v_mul_f32_dpp v50, v54, v50 row_newbcast:15 row_mask:0xf bank_mask:0xf
	v_fmac_f32_dpp v47, v43, v51 row_newbcast:15 row_mask:0xf bank_mask:0xf
	v_mul_f32_dpp v51, v55, v51 row_newbcast:15 row_mask:0xf bank_mask:0xf
	v_fmac_f32_dpp v48, v44, v52 row_newbcast:15 row_mask:0xf bank_mask:0xf
	v_mul_f32_dpp v52, v56, v52 row_newbcast:15 row_mask:0xf bank_mask:0xf
	v_fmac_f32_dpp v49, v45, v53 row_newbcast:15 row_mask:0xf bank_mask:0xf
	v_mul_f32_dpp v53, v57, v53 row_newbcast:15 row_mask:0xf bank_mask:0xf
	s_and_saveexec_b64 s[46:47], s[42:43]
	global_store_dwordx4 v188, v[50:53], s[4:5] sc1
	global_store_dwordx4 v188, v[46:49], s[16:17] sc1
	s_mov_b64 exec, s[46:47]
	v_cvt_pk_bf16_f32 v34, v34, v35
	v_cvt_pk_bf16_f32 v35, v36, v37
	v_cvt_pk_bf16_f32 v36, v62, v63
	v_cvt_pk_bf16_f32 v37, v64, v65
	global_store_dwordx4 v194, v[34:37], s[56:57] sc1
	v_cvt_pk_bf16_f32 v38, v38, v39
	v_cvt_pk_bf16_f32 v39, v40, v41
	v_cvt_pk_bf16_f32 v40, v58, v59
	v_cvt_pk_bf16_f32 v41, v60, v61
	global_store_dwordx4 v195, v[38:41], s[56:57] sc1
	v_cvt_pk_bf16_f32 v42, v42, v43
	v_cvt_pk_bf16_f32 v43, v44, v45
	v_cvt_pk_bf16_f32 v44, v54, v55
	v_cvt_pk_bf16_f32 v45, v56, v57
	global_store_dwordx4 v196, v[42:45], s[56:57] sc1
	v_cvt_pk_bf16_f32 v46, v46, v47
	v_cvt_pk_bf16_f32 v47, v48, v49
	v_cvt_pk_bf16_f32 v48, v50, v51
	v_cvt_pk_bf16_f32 v49, v52, v53
	global_store_dwordx4 v197, v[46:49], s[56:57] sc1
	global_load_dwordx2 v[176:177], v190, s[52:53] offset:32
	global_load_dwordx2 v[178:179], v191, s[52:53] offset:32
	global_load_dwordx2 v[182:183], v192, s[52:53] offset:32
	global_load_dwordx2 v[184:185], v193, s[52:53] offset:32
	s_waitcnt vmcnt(10)
; __device__ __forceinline__ float sigmoid_fast(float x) { return __builtin_amdgcn_rcpf(1.f + __expf(-x)); }
; __device__ __forceinline__ float one_minus_exp(float x) { const float p = -x * (1.f + x * (0.5f + x * (0.16666667f + x * (0.041666668f + x * 0.0083333338f)))); return x > -0.1f ? p : 1.f - __expf(x); }
;     template <bool BWD>
;     __device__ __forceinline__ void epi_dir(const f32x4 (&acc)[2][2][4][2], const Unit& u, int wr, int wc, int fr, int fq) const {
;     ...
;                 const f32x4 bav = *(const f32x4*)(bap + n * 64 + coff), bxv = *(const f32x4*)(bxp + n * 64 + coff), lsl = *(const f32x4*)(lmp + n * 64 + coff);
; #pragma unroll
;                 for (int m = 0; m < 4; ++m) {
;                     const u32x2 uw = *(const u32x2*)(Ub + ((size_t)(ai * 128 + m * 16) * 1024 + n * 16) * 2 + loffu);
;                     const float uv[4] = {bflo(uw.x), bfhi(uw.x), bflo(uw.y), bfhi(uw.y)};
; #pragma unroll
;                     for (int j = 0; j < 4; ++j) { const float r = sigmoid_fast(acc[ai][0][m][n][j] + bav[j]), ig = sigmoid_fast(acc[ai][1][m][n][j] + bxv[j]);
;                         const float la = r * lsl[j]; A[m][j] = __expf(la); H[m][j] = __builtin_amdgcn_sqrtf(one_minus_exp(2.f * la)) * (ig * uv[j]); } }
	v_add_f32_e32 v94, v94, v156
	v_add_f32_e32 v95, v95, v157
	v_add_f32_e32 v96, v96, v158
	v_add_f32_e32 v97, v97, v159
	v_add_f32_e32 v90, v90, v156
	v_add_f32_e32 v91, v91, v157
	v_add_f32_e32 v92, v92, v158
	v_add_f32_e32 v93, v93, v159
	v_mul_f32_e32 v94, 0xbfb8aa3b, v94
	v_mul_f32_e32 v95, 0xbfb8aa3b, v95
	v_mul_f32_e32 v96, 0xbfb8aa3b, v96
	v_mul_f32_e32 v97, 0xbfb8aa3b, v97
	v_mul_f32_e32 v90, 0xbfb8aa3b, v90
	v_mul_f32_e32 v91, 0xbfb8aa3b, v91
	v_mul_f32_e32 v92, 0xbfb8aa3b, v92
	v_mul_f32_e32 v93, 0xbfb8aa3b, v93
	v_exp_f32_e32 v94, v94
	v_exp_f32_e32 v95, v95
	v_exp_f32_e32 v96, v96
	v_exp_f32_e32 v97, v97
	v_exp_f32_e32 v90, v90
	v_exp_f32_e32 v91, v91
	v_exp_f32_e32 v92, v92
	v_exp_f32_e32 v93, v93
	v_add_f32_e32 v94, 1.0, v94
	v_add_f32_e32 v95, 1.0, v95
	v_add_f32_e32 v96, 1.0, v96
	v_add_f32_e32 v97, 1.0, v97
	v_add_f32_e32 v90, 1.0, v90
	v_add_f32_e32 v91, 1.0, v91
	v_add_f32_e32 v92, 1.0, v92
	v_add_f32_e32 v93, 1.0, v93
	v_rcp_f32_e32 v94, v94
	v_rcp_f32_e32 v95, v95
	v_rcp_f32_e32 v96, v96
	v_rcp_f32_e32 v97, v97
	v_rcp_f32_e32 v90, v90
	v_rcp_f32_e32 v91, v91
	v_rcp_f32_e32 v92, v92
	v_rcp_f32_e32 v93, v93
	v_mul_f32_e32 v94, v164, v94
	v_mul_f32_e32 v95, v165, v95
	v_mul_f32_e32 v96, v166, v96
	v_mul_f32_e32 v97, v167, v97
	v_mul_f32_e32 v90, v164, v90
	v_mul_f32_e32 v91, v165, v91
	v_mul_f32_e32 v92, v166, v92
	v_mul_f32_e32 v93, v167, v93
	v_add_f32_e32 v198, v94, v94
	v_add_f32_e32 v201, v95, v95
	v_add_f32_e32 v204, v96, v96
	v_add_f32_e32 v207, v97, v97
	v_add_f32_e32 v216, v90, v90
	v_add_f32_e32 v219, v91, v91
	v_add_f32_e32 v240, v92, v92
	v_add_f32_e32 v243, v93, v93
	v_mul_f32_e32 v199, 0x3fb8aa3b, v198
	v_mul_f32_e32 v202, 0x3fb8aa3b, v201
	v_mul_f32_e32 v205, 0x3fb8aa3b, v204
	v_mul_f32_e32 v208, 0x3fb8aa3b, v207
	v_mul_f32_e32 v217, 0x3fb8aa3b, v216
	v_mul_f32_e32 v238, 0x3fb8aa3b, v219
	v_mul_f32_e32 v241, 0x3fb8aa3b, v240
	v_mul_f32_e32 v244, 0x3fb8aa3b, v243
	v_exp_f32_e32 v199, v199
	v_exp_f32_e32 v202, v202
	v_exp_f32_e32 v205, v205
	v_exp_f32_e32 v208, v208
	v_exp_f32_e32 v217, v217
	v_exp_f32_e32 v238, v238
	v_exp_f32_e32 v241, v241
	v_exp_f32_e32 v244, v244
	v_fmamk_f32 v200, v198, 0x3c088889, v211
	v_fmamk_f32 v203, v201, 0x3c088889, v211
	v_fmamk_f32 v206, v204, 0x3c088889, v211
	v_fmamk_f32 v209, v207, 0x3c088889, v211
	v_fmamk_f32 v218, v216, 0x3c088889, v211
	v_fmamk_f32 v239, v219, 0x3c088889, v211
	v_fmamk_f32 v242, v240, 0x3c088889, v211
	v_fmamk_f32 v245, v243, 0x3c088889, v211
	v_sub_f32_e32 v199, 1.0, v199
	v_sub_f32_e32 v202, 1.0, v202
	v_sub_f32_e32 v205, 1.0, v205
	v_sub_f32_e32 v208, 1.0, v208
	v_sub_f32_e32 v217, 1.0, v217
	v_sub_f32_e32 v238, 1.0, v238
	v_sub_f32_e32 v241, 1.0, v241
	v_sub_f32_e32 v244, 1.0, v244
	v_fmaak_f32 v200, v198, v200, 0x3e2aaaab
	v_fmaak_f32 v203, v201, v203, 0x3e2aaaab
	v_fmaak_f32 v206, v204, v206, 0x3e2aaaab
	v_fmaak_f32 v209, v207, v209, 0x3e2aaaab
	v_fmaak_f32 v218, v216, v218, 0x3e2aaaab
	v_fmaak_f32 v239, v219, v239, 0x3e2aaaab
	v_fmaak_f32 v242, v240, v242, 0x3e2aaaab
	v_fmaak_f32 v245, v243, v245, 0x3e2aaaab
	v_fma_f32 v200, v198, v200, 0.5
	v_fma_f32 v203, v201, v203, 0.5
	v_fma_f32 v206, v204, v206, 0.5
	v_fma_f32 v209, v207, v209, 0.5
	v_fma_f32 v218, v216, v218, 0.5
	v_fma_f32 v239, v219, v239, 0.5
	v_fma_f32 v242, v240, v242, 0.5
	v_fma_f32 v245, v243, v245, 0.5
	v_fma_f32 v200, v198, v200, 1.0
	v_fma_f32 v203, v201, v203, 1.0
	v_fma_f32 v206, v204, v206, 1.0
	v_fma_f32 v209, v207, v209, 1.0
	v_fma_f32 v218, v216, v218, 1.0
	v_fma_f32 v239, v219, v239, 1.0
	v_fma_f32 v242, v240, v242, 1.0
	v_fma_f32 v245, v243, v245, 1.0
	v_mul_f32_e64 v200, v200, -v198
	v_mul_f32_e64 v203, v203, -v201
	v_mul_f32_e64 v206, v206, -v204
	v_mul_f32_e64 v209, v209, -v207
	v_mul_f32_e64 v218, v218, -v216
	v_mul_f32_e64 v239, v239, -v219
	v_mul_f32_e64 v242, v242, -v240
	v_mul_f32_e64 v245, v245, -v243
	v_cmp_nlt_f32_e32 vcc, s49, v198
	v_add_f32_e32 v66, v66, v160
	v_mul_f32_e32 v66, 0xbfb8aa3b, v66
	v_cndmask_b32_e32 v199, v200, v199, vcc
	v_cmp_nlt_f32_e32 vcc, s49, v201
	v_add_f32_e32 v67, v67, v161
	v_mul_f32_e32 v67, 0xbfb8aa3b, v67
	v_cndmask_b32_e32 v202, v203, v202, vcc
	v_cmp_nlt_f32_e32 vcc, s49, v204
	v_add_f32_e32 v68, v68, v162
	v_mul_f32_e32 v68, 0xbfb8aa3b, v68
	v_cndmask_b32_e32 v205, v206, v205, vcc
	v_cmp_nlt_f32_e32 vcc, s49, v207
	v_add_f32_e32 v69, v69, v163
	v_mul_f32_e32 v69, 0xbfb8aa3b, v69
	v_cndmask_b32_e32 v208, v209, v208, vcc
	v_cmp_nlt_f32_e32 vcc, s49, v216
	v_add_f32_e32 v70, v70, v160
	v_mul_f32_e32 v70, 0xbfb8aa3b, v70
	v_cndmask_b32_e32 v217, v218, v217, vcc
	v_cmp_nlt_f32_e32 vcc, s49, v219
	v_add_f32_e32 v71, v71, v161
	v_mul_f32_e32 v71, 0xbfb8aa3b, v71
	v_cndmask_b32_e32 v238, v239, v238, vcc
	v_cmp_nlt_f32_e32 vcc, s49, v240
	v_add_f32_e32 v72, v72, v162
	v_mul_f32_e32 v72, 0xbfb8aa3b, v72
	v_cndmask_b32_e32 v241, v242, v241, vcc
	v_cmp_nlt_f32_e32 vcc, s49, v243
	v_add_f32_e32 v73, v73, v163
	v_mul_f32_e32 v73, 0xbfb8aa3b, v73
	v_cndmask_b32_e32 v244, v245, v244, vcc
	v_exp_f32_e32 v66, v66
	v_exp_f32_e32 v67, v67
	v_exp_f32_e32 v68, v68
	v_exp_f32_e32 v69, v69
	v_exp_f32_e32 v70, v70
	v_exp_f32_e32 v71, v71
	v_exp_f32_e32 v72, v72
	v_exp_f32_e32 v73, v73
	v_sqrt_f32_e32 v199, v199
	v_sqrt_f32_e32 v202, v202
	v_sqrt_f32_e32 v205, v205
	v_sqrt_f32_e32 v208, v208
	v_sqrt_f32_e32 v217, v217
	v_sqrt_f32_e32 v238, v238
	v_sqrt_f32_e32 v241, v241
	v_sqrt_f32_e32 v244, v244
	v_add_f32_e32 v66, 1.0, v66
	v_add_f32_e32 v67, 1.0, v67
	v_add_f32_e32 v68, 1.0, v68
	v_add_f32_e32 v69, 1.0, v69
	v_add_f32_e32 v70, 1.0, v70
	v_add_f32_e32 v71, 1.0, v71
	v_add_f32_e32 v72, 1.0, v72
	v_add_f32_e32 v73, 1.0, v73
	v_lshlrev_b32_e32 v200, 16, v168
; __device__ __forceinline__ float sigmoid_fast(float x) { return __builtin_amdgcn_rcpf(1.f + __expf(-x)); }
; __device__ __forceinline__ float one_minus_exp(float x) { const float p = -x * (1.f + x * (0.5f + x * (0.16666667f + x * (0.041666668f + x * 0.0083333338f)))); return x > -0.1f ? p : 1.f - __expf(x); }
;     template <bool BWD>
;     __device__ __forceinline__ void epi_dir(const f32x4 (&acc)[2][2][4][2], const Unit& u, int wr, int wc, int fr, int fq) const {
;     ...
;                     for (int j = 0; j < 4; ++j) { const float r = sigmoid_fast(acc[ai][0][m][n][j] + bav[j]), ig = sigmoid_fast(acc[ai][1][m][n][j] + bxv[j]);
;                         const float la = r * lsl[j]; A[m][j] = __expf(la); H[m][j] = __builtin_amdgcn_sqrtf(one_minus_exp(2.f * la)) * (ig * uv[j]); } }
	v_and_b32_e32 v203, 0xffff0000, v168
	v_lshlrev_b32_e32 v206, 16, v169
	v_and_b32_e32 v209, 0xffff0000, v169
	v_lshlrev_b32_e32 v218, 16, v170
	v_and_b32_e32 v239, 0xffff0000, v170
	v_lshlrev_b32_e32 v242, 16, v171
	v_and_b32_e32 v245, 0xffff0000, v171
	v_rcp_f32_e32 v66, v66
	v_rcp_f32_e32 v67, v67
	v_rcp_f32_e32 v68, v68
	v_rcp_f32_e32 v69, v69
	v_rcp_f32_e32 v70, v70
	v_rcp_f32_e32 v71, v71
	v_rcp_f32_e32 v72, v72
	v_rcp_f32_e32 v73, v73
	v_mul_f32_e32 v94, 0x3fb8aa3b, v94
	v_mul_f32_e32 v95, 0x3fb8aa3b, v95
	v_mul_f32_e32 v96, 0x3fb8aa3b, v96
	v_mul_f32_e32 v97, 0x3fb8aa3b, v97
	v_mul_f32_e32 v90, 0x3fb8aa3b, v90
	v_mul_f32_e32 v91, 0x3fb8aa3b, v91
	v_mul_f32_e32 v92, 0x3fb8aa3b, v92
	v_mul_f32_e32 v93, 0x3fb8aa3b, v93
	v_mul_f32_e32 v66, v66, v200
	v_mul_f32_e32 v67, v67, v203
	v_mul_f32_e32 v68, v68, v206
	v_mul_f32_e32 v69, v69, v209
	v_mul_f32_e32 v70, v70, v218
	v_mul_f32_e32 v71, v71, v239
	v_mul_f32_e32 v72, v72, v242
	v_mul_f32_e32 v73, v73, v245
	v_exp_f32_e32 v94, v94
	v_exp_f32_e32 v95, v95
	v_exp_f32_e32 v96, v96
	v_exp_f32_e32 v97, v97
	v_exp_f32_e32 v90, v90
	v_exp_f32_e32 v91, v91
	v_exp_f32_e32 v92, v92
	v_exp_f32_e32 v93, v93
	v_mul_f32_e32 v66, v66, v199
	v_mul_f32_e32 v67, v67, v202
	v_mul_f32_e32 v68, v68, v205
	v_mul_f32_e32 v69, v69, v208
	v_mul_f32_e32 v70, v70, v217
	v_mul_f32_e32 v71, v71, v238
	v_mul_f32_e32 v72, v72, v241
	v_mul_f32_e32 v73, v73, v244
	v_add_f32_e32 v86, v86, v156
	v_add_f32_e32 v87, v87, v157
	v_add_f32_e32 v88, v88, v158
	v_add_f32_e32 v89, v89, v159
	v_add_f32_e32 v82, v82, v156
	v_add_f32_e32 v83, v83, v157
	v_add_f32_e32 v84, v84, v158
	v_add_f32_e32 v85, v85, v159
	v_mul_f32_e32 v86, 0xbfb8aa3b, v86
	v_mul_f32_e32 v87, 0xbfb8aa3b, v87
	v_mul_f32_e32 v88, 0xbfb8aa3b, v88
	v_mul_f32_e32 v89, 0xbfb8aa3b, v89
	v_mul_f32_e32 v82, 0xbfb8aa3b, v82
	v_mul_f32_e32 v83, 0xbfb8aa3b, v83
	v_mul_f32_e32 v84, 0xbfb8aa3b, v84
	v_mul_f32_e32 v85, 0xbfb8aa3b, v85
	v_exp_f32_e32 v86, v86
	v_exp_f32_e32 v87, v87
	v_exp_f32_e32 v88, v88
	v_exp_f32_e32 v89, v89
	v_exp_f32_e32 v82, v82
	v_exp_f32_e32 v83, v83
	v_exp_f32_e32 v84, v84
	v_exp_f32_e32 v85, v85
	v_add_f32_e32 v86, 1.0, v86
	v_add_f32_e32 v87, 1.0, v87
	v_add_f32_e32 v88, 1.0, v88
	v_add_f32_e32 v89, 1.0, v89
	v_add_f32_e32 v82, 1.0, v82
	v_add_f32_e32 v83, 1.0, v83
	v_add_f32_e32 v84, 1.0, v84
	v_add_f32_e32 v85, 1.0, v85
	v_rcp_f32_e32 v86, v86
	v_rcp_f32_e32 v87, v87
	v_rcp_f32_e32 v88, v88
	v_rcp_f32_e32 v89, v89
	v_rcp_f32_e32 v82, v82
	v_rcp_f32_e32 v83, v83
	v_rcp_f32_e32 v84, v84
	v_rcp_f32_e32 v85, v85
	v_mul_f32_e32 v86, v164, v86
	v_mul_f32_e32 v87, v165, v87
	v_mul_f32_e32 v88, v166, v88
	v_mul_f32_e32 v89, v167, v89
	v_mul_f32_e32 v82, v164, v82
	v_mul_f32_e32 v83, v165, v83
	v_mul_f32_e32 v84, v166, v84
	v_mul_f32_e32 v85, v167, v85
	v_add_f32_e32 v198, v86, v86
	v_add_f32_e32 v201, v87, v87
	v_add_f32_e32 v204, v88, v88
	v_add_f32_e32 v207, v89, v89
	v_add_f32_e32 v216, v82, v82
	v_add_f32_e32 v219, v83, v83
	v_add_f32_e32 v240, v84, v84
	v_add_f32_e32 v243, v85, v85
	v_mul_f32_e32 v199, 0x3fb8aa3b, v198
	v_mul_f32_e32 v202, 0x3fb8aa3b, v201
	v_mul_f32_e32 v205, 0x3fb8aa3b, v204
	v_mul_f32_e32 v208, 0x3fb8aa3b, v207
	v_mul_f32_e32 v217, 0x3fb8aa3b, v216
	v_mul_f32_e32 v238, 0x3fb8aa3b, v219
	v_mul_f32_e32 v241, 0x3fb8aa3b, v240
	v_mul_f32_e32 v244, 0x3fb8aa3b, v243
	v_exp_f32_e32 v199, v199
	v_exp_f32_e32 v202, v202
	v_exp_f32_e32 v205, v205
	v_exp_f32_e32 v208, v208
	v_exp_f32_e32 v217, v217
	v_exp_f32_e32 v238, v238
	v_exp_f32_e32 v241, v241
	v_exp_f32_e32 v244, v244
	v_fmamk_f32 v200, v198, 0x3c088889, v211
	v_fmamk_f32 v203, v201, 0x3c088889, v211
	v_fmamk_f32 v206, v204, 0x3c088889, v211
	v_fmamk_f32 v209, v207, 0x3c088889, v211
	v_fmamk_f32 v218, v216, 0x3c088889, v211
	v_fmamk_f32 v239, v219, 0x3c088889, v211
	v_fmamk_f32 v242, v240, 0x3c088889, v211
	v_fmamk_f32 v245, v243, 0x3c088889, v211
	v_sub_f32_e32 v199, 1.0, v199
	v_sub_f32_e32 v202, 1.0, v202
	v_sub_f32_e32 v205, 1.0, v205
	v_sub_f32_e32 v208, 1.0, v208
	v_sub_f32_e32 v217, 1.0, v217
	v_sub_f32_e32 v238, 1.0, v238
	v_sub_f32_e32 v241, 1.0, v241
	v_sub_f32_e32 v244, 1.0, v244
	v_fmaak_f32 v200, v198, v200, 0x3e2aaaab
	v_fmaak_f32 v203, v201, v203, 0x3e2aaaab
	v_fmaak_f32 v206, v204, v206, 0x3e2aaaab
	v_fmaak_f32 v209, v207, v209, 0x3e2aaaab
	v_fmaak_f32 v218, v216, v218, 0x3e2aaaab
	v_fmaak_f32 v239, v219, v239, 0x3e2aaaab
	v_fmaak_f32 v242, v240, v242, 0x3e2aaaab
	v_fmaak_f32 v245, v243, v245, 0x3e2aaaab
	v_fma_f32 v200, v198, v200, 0.5
	v_fma_f32 v203, v201, v203, 0.5
	v_fma_f32 v206, v204, v206, 0.5
	v_fma_f32 v209, v207, v209, 0.5
	v_fma_f32 v218, v216, v218, 0.5
	v_fma_f32 v239, v219, v239, 0.5
	v_fma_f32 v242, v240, v242, 0.5
	v_fma_f32 v245, v243, v245, 0.5
	v_fma_f32 v200, v198, v200, 1.0
	v_fma_f32 v203, v201, v203, 1.0
	v_fma_f32 v206, v204, v206, 1.0
	v_fma_f32 v209, v207, v209, 1.0
	v_fma_f32 v218, v216, v218, 1.0
	v_fma_f32 v239, v219, v239, 1.0
	v_fma_f32 v242, v240, v242, 1.0
	v_fma_f32 v245, v243, v245, 1.0
	v_mul_f32_e64 v200, v200, -v198
	v_mul_f32_e64 v203, v203, -v201
	v_mul_f32_e64 v206, v206, -v204
	v_mul_f32_e64 v209, v209, -v207
	v_mul_f32_e64 v218, v218, -v216
	v_mul_f32_e64 v239, v239, -v219
	v_mul_f32_e64 v242, v242, -v240
	v_mul_f32_e64 v245, v245, -v243
	v_cmp_nlt_f32_e32 vcc, s49, v198
	v_add_f32_e32 v74, v74, v160
	v_mul_f32_e32 v74, 0xbfb8aa3b, v74
	v_cndmask_b32_e32 v199, v200, v199, vcc
	v_cmp_nlt_f32_e32 vcc, s49, v201
	v_add_f32_e32 v75, v75, v161
	v_mul_f32_e32 v75, 0xbfb8aa3b, v75
	v_cndmask_b32_e32 v202, v203, v202, vcc
	v_cmp_nlt_f32_e32 vcc, s49, v204
	v_add_f32_e32 v76, v76, v162
	v_mul_f32_e32 v76, 0xbfb8aa3b, v76
; __device__ __forceinline__ float sigmoid_fast(float x) { return __builtin_amdgcn_rcpf(1.f + __expf(-x)); }
; __device__ __forceinline__ float one_minus_exp(float x) { const float p = -x * (1.f + x * (0.5f + x * (0.16666667f + x * (0.041666668f + x * 0.0083333338f)))); return x > -0.1f ? p : 1.f - __expf(x); }
; #define SCAN_STEP(D) { const float ap = dppf<(BWD ? 0x100 : 0x110) + D>(1.f, av), hp = dppf<(BWD ? 0x100 : 0x110) + D>(0.f, hv); hv = fmaf(av, hp, hv); av = av * ap; }
;     template <bool BWD>
;     __device__ __forceinline__ void epi_dir(const f32x4 (&acc)[2][2][4][2], const Unit& u, int wr, int wc, int fr, int fq) const {
;     ...
;                     for (int j = 0; j < 4; ++j) { const float r = sigmoid_fast(acc[ai][0][m][n][j] + bav[j]), ig = sigmoid_fast(acc[ai][1][m][n][j] + bxv[j]);
;                         const float la = r * lsl[j]; A[m][j] = __expf(la); H[m][j] = __builtin_amdgcn_sqrtf(one_minus_exp(2.f * la)) * (ig * uv[j]); } }
; #pragma unroll
;                 for (int m = 0; m < 4; ++m)
; #pragma unroll
;                     for (int j = 0; j < 4; ++j) { float av = A[m][j], hv = H[m][j];
;     ...
;                         SCAN_STEP(1) SCAN_STEP(2) SCAN_STEP(4) SCAN_STEP(8)
	v_cndmask_b32_e32 v205, v206, v205, vcc
	v_cmp_nlt_f32_e32 vcc, s49, v207
	v_add_f32_e32 v77, v77, v163
	v_mul_f32_e32 v77, 0xbfb8aa3b, v77
	v_cndmask_b32_e32 v208, v209, v208, vcc
	v_cmp_nlt_f32_e32 vcc, s49, v216
	v_add_f32_e32 v78, v78, v160
	v_mul_f32_e32 v78, 0xbfb8aa3b, v78
	v_cndmask_b32_e32 v217, v218, v217, vcc
	v_cmp_nlt_f32_e32 vcc, s49, v219
	v_add_f32_e32 v79, v79, v161
	v_mul_f32_e32 v79, 0xbfb8aa3b, v79
	v_cndmask_b32_e32 v238, v239, v238, vcc
	v_cmp_nlt_f32_e32 vcc, s49, v240
	v_add_f32_e32 v80, v80, v162
	v_mul_f32_e32 v80, 0xbfb8aa3b, v80
	v_cndmask_b32_e32 v241, v242, v241, vcc
	v_cmp_nlt_f32_e32 vcc, s49, v243
	v_add_f32_e32 v81, v81, v163
	v_mul_f32_e32 v81, 0xbfb8aa3b, v81
	v_cndmask_b32_e32 v244, v245, v244, vcc
	v_exp_f32_e32 v74, v74
	v_exp_f32_e32 v75, v75
	v_exp_f32_e32 v76, v76
	v_exp_f32_e32 v77, v77
	v_exp_f32_e32 v78, v78
	v_exp_f32_e32 v79, v79
	v_exp_f32_e32 v80, v80
	v_exp_f32_e32 v81, v81
	v_sqrt_f32_e32 v199, v199
	v_sqrt_f32_e32 v202, v202
	v_sqrt_f32_e32 v205, v205
	v_sqrt_f32_e32 v208, v208
	v_sqrt_f32_e32 v217, v217
	v_sqrt_f32_e32 v238, v238
	v_sqrt_f32_e32 v241, v241
	v_sqrt_f32_e32 v244, v244
	v_add_f32_e32 v74, 1.0, v74
	v_add_f32_e32 v75, 1.0, v75
	v_add_f32_e32 v76, 1.0, v76
	v_add_f32_e32 v77, 1.0, v77
	v_add_f32_e32 v78, 1.0, v78
	v_add_f32_e32 v79, 1.0, v79
	v_add_f32_e32 v80, 1.0, v80
	v_add_f32_e32 v81, 1.0, v81
	v_lshlrev_b32_e32 v200, 16, v172
	v_and_b32_e32 v203, 0xffff0000, v172
	v_lshlrev_b32_e32 v206, 16, v173
	v_and_b32_e32 v209, 0xffff0000, v173
	v_lshlrev_b32_e32 v218, 16, v174
	v_and_b32_e32 v239, 0xffff0000, v174
	v_lshlrev_b32_e32 v242, 16, v175
	v_and_b32_e32 v245, 0xffff0000, v175
	v_rcp_f32_e32 v74, v74
	v_rcp_f32_e32 v75, v75
	v_rcp_f32_e32 v76, v76
	v_rcp_f32_e32 v77, v77
	v_rcp_f32_e32 v78, v78
	v_rcp_f32_e32 v79, v79
	v_rcp_f32_e32 v80, v80
	v_rcp_f32_e32 v81, v81
	v_mul_f32_e32 v86, 0x3fb8aa3b, v86
	v_mul_f32_e32 v87, 0x3fb8aa3b, v87
	v_mul_f32_e32 v88, 0x3fb8aa3b, v88
	v_mul_f32_e32 v89, 0x3fb8aa3b, v89
	v_mul_f32_e32 v82, 0x3fb8aa3b, v82
	v_mul_f32_e32 v83, 0x3fb8aa3b, v83
	v_mul_f32_e32 v84, 0x3fb8aa3b, v84
	v_mul_f32_e32 v85, 0x3fb8aa3b, v85
	v_mul_f32_e32 v74, v74, v200
	v_mul_f32_e32 v75, v75, v203
	v_mul_f32_e32 v76, v76, v206
	v_mul_f32_e32 v77, v77, v209
	v_mul_f32_e32 v78, v78, v218
	v_mul_f32_e32 v79, v79, v239
	v_mul_f32_e32 v80, v80, v242
	v_mul_f32_e32 v81, v81, v245
	v_exp_f32_e32 v86, v86
	v_exp_f32_e32 v87, v87
	v_exp_f32_e32 v88, v88
	v_exp_f32_e32 v89, v89
	v_exp_f32_e32 v82, v82
	v_exp_f32_e32 v83, v83
	v_exp_f32_e32 v84, v84
	v_exp_f32_e32 v85, v85
	v_mul_f32_e32 v74, v74, v199
	v_mul_f32_e32 v75, v75, v202
	v_mul_f32_e32 v76, v76, v205
	v_mul_f32_e32 v77, v77, v208
	v_mul_f32_e32 v78, v78, v217
	v_mul_f32_e32 v79, v79, v238
	v_mul_f32_e32 v80, v80, v241
	v_mul_f32_e32 v81, v81, v244
	v_fmac_f32_dpp v66, v66, v94 row_shr:1 row_mask:0xf bank_mask:0xf
	v_mul_f32_dpp v94, v94, v94 row_shr:1 row_mask:0xf bank_mask:0xf
	v_fmac_f32_dpp v67, v67, v95 row_shr:1 row_mask:0xf bank_mask:0xf
	v_mul_f32_dpp v95, v95, v95 row_shr:1 row_mask:0xf bank_mask:0xf
	v_fmac_f32_dpp v68, v68, v96 row_shr:1 row_mask:0xf bank_mask:0xf
	v_mul_f32_dpp v96, v96, v96 row_shr:1 row_mask:0xf bank_mask:0xf
	v_fmac_f32_dpp v69, v69, v97 row_shr:1 row_mask:0xf bank_mask:0xf
	v_mul_f32_dpp v97, v97, v97 row_shr:1 row_mask:0xf bank_mask:0xf
	v_fmac_f32_dpp v70, v70, v90 row_shr:1 row_mask:0xf bank_mask:0xf
	v_mul_f32_dpp v90, v90, v90 row_shr:1 row_mask:0xf bank_mask:0xf
	v_fmac_f32_dpp v71, v71, v91 row_shr:1 row_mask:0xf bank_mask:0xf
	v_mul_f32_dpp v91, v91, v91 row_shr:1 row_mask:0xf bank_mask:0xf
	v_fmac_f32_dpp v72, v72, v92 row_shr:1 row_mask:0xf bank_mask:0xf
	v_mul_f32_dpp v92, v92, v92 row_shr:1 row_mask:0xf bank_mask:0xf
	v_fmac_f32_dpp v73, v73, v93 row_shr:1 row_mask:0xf bank_mask:0xf
	v_mul_f32_dpp v93, v93, v93 row_shr:1 row_mask:0xf bank_mask:0xf
	v_fmac_f32_dpp v74, v74, v86 row_shr:1 row_mask:0xf bank_mask:0xf
	v_mul_f32_dpp v86, v86, v86 row_shr:1 row_mask:0xf bank_mask:0xf
	v_fmac_f32_dpp v75, v75, v87 row_shr:1 row_mask:0xf bank_mask:0xf
	v_mul_f32_dpp v87, v87, v87 row_shr:1 row_mask:0xf bank_mask:0xf
	v_fmac_f32_dpp v76, v76, v88 row_shr:1 row_mask:0xf bank_mask:0xf
	v_mul_f32_dpp v88, v88, v88 row_shr:1 row_mask:0xf bank_mask:0xf
	v_fmac_f32_dpp v77, v77, v89 row_shr:1 row_mask:0xf bank_mask:0xf
	v_mul_f32_dpp v89, v89, v89 row_shr:1 row_mask:0xf bank_mask:0xf
	v_fmac_f32_dpp v78, v78, v82 row_shr:1 row_mask:0xf bank_mask:0xf
	v_mul_f32_dpp v82, v82, v82 row_shr:1 row_mask:0xf bank_mask:0xf
	v_fmac_f32_dpp v79, v79, v83 row_shr:1 row_mask:0xf bank_mask:0xf
	v_mul_f32_dpp v83, v83, v83 row_shr:1 row_mask:0xf bank_mask:0xf
	v_fmac_f32_dpp v80, v80, v84 row_shr:1 row_mask:0xf bank_mask:0xf
	v_mul_f32_dpp v84, v84, v84 row_shr:1 row_mask:0xf bank_mask:0xf
	v_fmac_f32_dpp v81, v81, v85 row_shr:1 row_mask:0xf bank_mask:0xf
	v_mul_f32_dpp v85, v85, v85 row_shr:1 row_mask:0xf bank_mask:0xf
	v_fmac_f32_dpp v66, v66, v94 row_shr:2 row_mask:0xf bank_mask:0xf
	v_mul_f32_dpp v94, v94, v94 row_shr:2 row_mask:0xf bank_mask:0xf
	v_fmac_f32_dpp v67, v67, v95 row_shr:2 row_mask:0xf bank_mask:0xf
	v_mul_f32_dpp v95, v95, v95 row_shr:2 row_mask:0xf bank_mask:0xf
	v_fmac_f32_dpp v68, v68, v96 row_shr:2 row_mask:0xf bank_mask:0xf
	v_mul_f32_dpp v96, v96, v96 row_shr:2 row_mask:0xf bank_mask:0xf
	v_fmac_f32_dpp v69, v69, v97 row_shr:2 row_mask:0xf bank_mask:0xf
	v_mul_f32_dpp v97, v97, v97 row_shr:2 row_mask:0xf bank_mask:0xf
	v_fmac_f32_dpp v70, v70, v90 row_shr:2 row_mask:0xf bank_mask:0xf
	v_mul_f32_dpp v90, v90, v90 row_shr:2 row_mask:0xf bank_mask:0xf
; #define SCAN_STEP(D) { const float ap = dppf<(BWD ? 0x100 : 0x110) + D>(1.f, av), hp = dppf<(BWD ? 0x100 : 0x110) + D>(0.f, hv); hv = fmaf(av, hp, hv); av = av * ap; }
;     template <bool BWD>
;     __device__ __forceinline__ void epi_dir(const f32x4 (&acc)[2][2][4][2], const Unit& u, int wr, int wc, int fr, int fq) const {
;     ...
;                 for (int m = 0; m < 4; ++m)
; #pragma unroll
;                     for (int j = 0; j < 4; ++j) { float av = A[m][j], hv = H[m][j];
;     ...
;                         SCAN_STEP(1) SCAN_STEP(2) SCAN_STEP(4) SCAN_STEP(8)
	v_fmac_f32_dpp v71, v71, v91 row_shr:2 row_mask:0xf bank_mask:0xf
	v_mul_f32_dpp v91, v91, v91 row_shr:2 row_mask:0xf bank_mask:0xf
	v_fmac_f32_dpp v72, v72, v92 row_shr:2 row_mask:0xf bank_mask:0xf
	v_mul_f32_dpp v92, v92, v92 row_shr:2 row_mask:0xf bank_mask:0xf
	v_fmac_f32_dpp v73, v73, v93 row_shr:2 row_mask:0xf bank_mask:0xf
	v_mul_f32_dpp v93, v93, v93 row_shr:2 row_mask:0xf bank_mask:0xf
	v_fmac_f32_dpp v74, v74, v86 row_shr:2 row_mask:0xf bank_mask:0xf
	v_mul_f32_dpp v86, v86, v86 row_shr:2 row_mask:0xf bank_mask:0xf
	v_fmac_f32_dpp v75, v75, v87 row_shr:2 row_mask:0xf bank_mask:0xf
	v_mul_f32_dpp v87, v87, v87 row_shr:2 row_mask:0xf bank_mask:0xf
	v_fmac_f32_dpp v76, v76, v88 row_shr:2 row_mask:0xf bank_mask:0xf
	v_mul_f32_dpp v88, v88, v88 row_shr:2 row_mask:0xf bank_mask:0xf
	v_fmac_f32_dpp v77, v77, v89 row_shr:2 row_mask:0xf bank_mask:0xf
	v_mul_f32_dpp v89, v89, v89 row_shr:2 row_mask:0xf bank_mask:0xf
	v_fmac_f32_dpp v78, v78, v82 row_shr:2 row_mask:0xf bank_mask:0xf
	v_mul_f32_dpp v82, v82, v82 row_shr:2 row_mask:0xf bank_mask:0xf
	v_fmac_f32_dpp v79, v79, v83 row_shr:2 row_mask:0xf bank_mask:0xf
	v_mul_f32_dpp v83, v83, v83 row_shr:2 row_mask:0xf bank_mask:0xf
	v_fmac_f32_dpp v80, v80, v84 row_shr:2 row_mask:0xf bank_mask:0xf
	v_mul_f32_dpp v84, v84, v84 row_shr:2 row_mask:0xf bank_mask:0xf
	v_fmac_f32_dpp v81, v81, v85 row_shr:2 row_mask:0xf bank_mask:0xf
	v_mul_f32_dpp v85, v85, v85 row_shr:2 row_mask:0xf bank_mask:0xf
	v_fmac_f32_dpp v66, v66, v94 row_shr:4 row_mask:0xf bank_mask:0xf
	v_mul_f32_dpp v94, v94, v94 row_shr:4 row_mask:0xf bank_mask:0xf
	v_fmac_f32_dpp v67, v67, v95 row_shr:4 row_mask:0xf bank_mask:0xf
	v_mul_f32_dpp v95, v95, v95 row_shr:4 row_mask:0xf bank_mask:0xf
	v_fmac_f32_dpp v68, v68, v96 row_shr:4 row_mask:0xf bank_mask:0xf
	v_mul_f32_dpp v96, v96, v96 row_shr:4 row_mask:0xf bank_mask:0xf
	v_fmac_f32_dpp v69, v69, v97 row_shr:4 row_mask:0xf bank_mask:0xf
	v_mul_f32_dpp v97, v97, v97 row_shr:4 row_mask:0xf bank_mask:0xf
	v_fmac_f32_dpp v70, v70, v90 row_shr:4 row_mask:0xf bank_mask:0xf
	v_mul_f32_dpp v90, v90, v90 row_shr:4 row_mask:0xf bank_mask:0xf
	v_fmac_f32_dpp v71, v71, v91 row_shr:4 row_mask:0xf bank_mask:0xf
	v_mul_f32_dpp v91, v91, v91 row_shr:4 row_mask:0xf bank_mask:0xf
	v_fmac_f32_dpp v72, v72, v92 row_shr:4 row_mask:0xf bank_mask:0xf
	v_mul_f32_dpp v92, v92, v92 row_shr:4 row_mask:0xf bank_mask:0xf
	v_fmac_f32_dpp v73, v73, v93 row_shr:4 row_mask:0xf bank_mask:0xf
	v_mul_f32_dpp v93, v93, v93 row_shr:4 row_mask:0xf bank_mask:0xf
	v_fmac_f32_dpp v74, v74, v86 row_shr:4 row_mask:0xf bank_mask:0xf
	v_mul_f32_dpp v86, v86, v86 row_shr:4 row_mask:0xf bank_mask:0xf
	v_fmac_f32_dpp v75, v75, v87 row_shr:4 row_mask:0xf bank_mask:0xf
	v_mul_f32_dpp v87, v87, v87 row_shr:4 row_mask:0xf bank_mask:0xf
	v_fmac_f32_dpp v76, v76, v88 row_shr:4 row_mask:0xf bank_mask:0xf
	v_mul_f32_dpp v88, v88, v88 row_shr:4 row_mask:0xf bank_mask:0xf
	v_fmac_f32_dpp v77, v77, v89 row_shr:4 row_mask:0xf bank_mask:0xf
	v_mul_f32_dpp v89, v89, v89 row_shr:4 row_mask:0xf bank_mask:0xf
	v_fmac_f32_dpp v78, v78, v82 row_shr:4 row_mask:0xf bank_mask:0xf
	v_mul_f32_dpp v82, v82, v82 row_shr:4 row_mask:0xf bank_mask:0xf
	v_fmac_f32_dpp v79, v79, v83 row_shr:4 row_mask:0xf bank_mask:0xf
	v_mul_f32_dpp v83, v83, v83 row_shr:4 row_mask:0xf bank_mask:0xf
	v_fmac_f32_dpp v80, v80, v84 row_shr:4 row_mask:0xf bank_mask:0xf
	v_mul_f32_dpp v84, v84, v84 row_shr:4 row_mask:0xf bank_mask:0xf
	v_fmac_f32_dpp v81, v81, v85 row_shr:4 row_mask:0xf bank_mask:0xf
	v_mul_f32_dpp v85, v85, v85 row_shr:4 row_mask:0xf bank_mask:0xf
	v_fmac_f32_dpp v66, v66, v94 row_shr:8 row_mask:0xf bank_mask:0xf
	v_mul_f32_dpp v94, v94, v94 row_shr:8 row_mask:0xf bank_mask:0xf
	v_fmac_f32_dpp v67, v67, v95 row_shr:8 row_mask:0xf bank_mask:0xf
	v_mul_f32_dpp v95, v95, v95 row_shr:8 row_mask:0xf bank_mask:0xf
	v_fmac_f32_dpp v68, v68, v96 row_shr:8 row_mask:0xf bank_mask:0xf
	v_mul_f32_dpp v96, v96, v96 row_shr:8 row_mask:0xf bank_mask:0xf
	v_fmac_f32_dpp v69, v69, v97 row_shr:8 row_mask:0xf bank_mask:0xf
	v_mul_f32_dpp v97, v97, v97 row_shr:8 row_mask:0xf bank_mask:0xf
	v_fmac_f32_dpp v70, v70, v90 row_shr:8 row_mask:0xf bank_mask:0xf
	v_mul_f32_dpp v90, v90, v90 row_shr:8 row_mask:0xf bank_mask:0xf
	v_fmac_f32_dpp v71, v71, v91 row_shr:8 row_mask:0xf bank_mask:0xf
	v_mul_f32_dpp v91, v91, v91 row_shr:8 row_mask:0xf bank_mask:0xf
	v_fmac_f32_dpp v72, v72, v92 row_shr:8 row_mask:0xf bank_mask:0xf
	v_mul_f32_dpp v92, v92, v92 row_shr:8 row_mask:0xf bank_mask:0xf
	v_fmac_f32_dpp v73, v73, v93 row_shr:8 row_mask:0xf bank_mask:0xf
	v_mul_f32_dpp v93, v93, v93 row_shr:8 row_mask:0xf bank_mask:0xf
	v_fmac_f32_dpp v74, v74, v86 row_shr:8 row_mask:0xf bank_mask:0xf
	v_mul_f32_dpp v86, v86, v86 row_shr:8 row_mask:0xf bank_mask:0xf
	v_fmac_f32_dpp v75, v75, v87 row_shr:8 row_mask:0xf bank_mask:0xf
	v_mul_f32_dpp v87, v87, v87 row_shr:8 row_mask:0xf bank_mask:0xf
	v_fmac_f32_dpp v76, v76, v88 row_shr:8 row_mask:0xf bank_mask:0xf
	v_mul_f32_dpp v88, v88, v88 row_shr:8 row_mask:0xf bank_mask:0xf
	v_fmac_f32_dpp v77, v77, v89 row_shr:8 row_mask:0xf bank_mask:0xf
	v_mul_f32_dpp v89, v89, v89 row_shr:8 row_mask:0xf bank_mask:0xf
	v_fmac_f32_dpp v78, v78, v82 row_shr:8 row_mask:0xf bank_mask:0xf
	v_mul_f32_dpp v82, v82, v82 row_shr:8 row_mask:0xf bank_mask:0xf
	v_fmac_f32_dpp v79, v79, v83 row_shr:8 row_mask:0xf bank_mask:0xf
	v_mul_f32_dpp v83, v83, v83 row_shr:8 row_mask:0xf bank_mask:0xf
	v_fmac_f32_dpp v80, v80, v84 row_shr:8 row_mask:0xf bank_mask:0xf
	v_mul_f32_dpp v84, v84, v84 row_shr:8 row_mask:0xf bank_mask:0xf
	v_fmac_f32_dpp v81, v81, v85 row_shr:8 row_mask:0xf bank_mask:0xf
; __device__ __forceinline__ unsigned pk2(float lo, float hi) { return f2bf(lo) | (f2bf(hi) << 16); }
; __device__ __forceinline__ float sigmoid_fast(float x) { return __builtin_amdgcn_rcpf(1.f + __expf(-x)); }
; __device__ __forceinline__ float one_minus_exp(float x) { const float p = -x * (1.f + x * (0.5f + x * (0.16666667f + x * (0.041666668f + x * 0.0083333338f)))); return x > -0.1f ? p : 1.f - __expf(x); }
;     template <bool BWD>
;     __device__ __forceinline__ void epi_dir(const f32x4 (&acc)[2][2][4][2], const Unit& u, int wr, int wc, int fr, int fq) const {
;     ...
;                 for (int m = 0; m < 4; ++m) {
;                     const u32x2 uw = *(const u32x2*)(Ub + ((size_t)(ai * 128 + m * 16) * 1024 + n * 16) * 2 + loffu);
;                     const float uv[4] = {bflo(uw.x), bfhi(uw.x), bflo(uw.y), bfhi(uw.y)};
; #pragma unroll
;                     for (int j = 0; j < 4; ++j) { const float r = sigmoid_fast(acc[ai][0][m][n][j] + bav[j]), ig = sigmoid_fast(acc[ai][1][m][n][j] + bxv[j]);
;                         const float la = r * lsl[j]; A[m][j] = __expf(la); H[m][j] = __builtin_amdgcn_sqrtf(one_minus_exp(2.f * la)) * (ig * uv[j]); } }
;     ...
;                 for (int j = 0; j < 4; ++j) { float Ar = 1.f, Hr = 0.f;
; #pragma unroll
;                     for (int mm = 0; mm < 4; ++mm) { const int m = BWD ? 3 - mm : mm;
;                         H[m][j] = fmaf(A[m][j], Hr, H[m][j]); A[m][j] = A[m][j] * Ar;
;                         if (mm < 3) { Ar = __shfl(A[m][j], bsel); Hr = __shfl(H[m][j], bsel); } } }
; #pragma unroll
;                 for (int m = 0; m < 4; ++m) { u32x4 w; w.x = pk2(H[m][0], H[m][1]); w.y = pk2(H[m][2], H[m][3]); w.z = pk2(A[m][0], A[m][1]); w.w = pk2(A[m][2], A[m][3]);
;                     *(u32x4*)(Hb + ((size_t)(ai * 128 + m * 16) * 1024 + n * 16) * 4 + loffh) = w; }
;                 constexpr int me = BWD ? 0 : 3;
;                 if (fr == (BWD ? 0 : 15)) { const size_t o = (size_t)chunk * 1024 + gblk * 128 + n * 16;
;                     *(f32x4*)((char*)(AGG + (size_t)(dir * 2 + 0) * NB * NCHUNK * 1024 + o) + coff) = A[me];
;                     *(f32x4*)((char*)(AGG + (size_t)(dir * 2 + 1) * NB * NCHUNK * 1024 + o) + coff) = H[me]; }
	v_mul_f32_dpp v85, v85, v85 row_shr:8 row_mask:0xf bank_mask:0xf
	v_fmac_f32_dpp v70, v66, v90 row_newbcast:15 row_mask:0xf bank_mask:0xf
	v_mul_f32_dpp v90, v94, v90 row_newbcast:15 row_mask:0xf bank_mask:0xf
	v_fmac_f32_dpp v71, v67, v91 row_newbcast:15 row_mask:0xf bank_mask:0xf
	v_mul_f32_dpp v91, v95, v91 row_newbcast:15 row_mask:0xf bank_mask:0xf
	v_fmac_f32_dpp v72, v68, v92 row_newbcast:15 row_mask:0xf bank_mask:0xf
	v_mul_f32_dpp v92, v96, v92 row_newbcast:15 row_mask:0xf bank_mask:0xf
	v_fmac_f32_dpp v73, v69, v93 row_newbcast:15 row_mask:0xf bank_mask:0xf
	v_mul_f32_dpp v93, v97, v93 row_newbcast:15 row_mask:0xf bank_mask:0xf
	v_fmac_f32_dpp v74, v70, v86 row_newbcast:15 row_mask:0xf bank_mask:0xf
	v_mul_f32_dpp v86, v90, v86 row_newbcast:15 row_mask:0xf bank_mask:0xf
	v_fmac_f32_dpp v75, v71, v87 row_newbcast:15 row_mask:0xf bank_mask:0xf
	v_mul_f32_dpp v87, v91, v87 row_newbcast:15 row_mask:0xf bank_mask:0xf
	v_fmac_f32_dpp v76, v72, v88 row_newbcast:15 row_mask:0xf bank_mask:0xf
	v_mul_f32_dpp v88, v92, v88 row_newbcast:15 row_mask:0xf bank_mask:0xf
	v_fmac_f32_dpp v77, v73, v89 row_newbcast:15 row_mask:0xf bank_mask:0xf
	v_mul_f32_dpp v89, v93, v89 row_newbcast:15 row_mask:0xf bank_mask:0xf
	v_fmac_f32_dpp v78, v74, v82 row_newbcast:15 row_mask:0xf bank_mask:0xf
	v_mul_f32_dpp v82, v86, v82 row_newbcast:15 row_mask:0xf bank_mask:0xf
	v_fmac_f32_dpp v79, v75, v83 row_newbcast:15 row_mask:0xf bank_mask:0xf
	v_mul_f32_dpp v83, v87, v83 row_newbcast:15 row_mask:0xf bank_mask:0xf
	v_fmac_f32_dpp v80, v76, v84 row_newbcast:15 row_mask:0xf bank_mask:0xf
	v_mul_f32_dpp v84, v88, v84 row_newbcast:15 row_mask:0xf bank_mask:0xf
	v_fmac_f32_dpp v81, v77, v85 row_newbcast:15 row_mask:0xf bank_mask:0xf
	v_mul_f32_dpp v85, v89, v85 row_newbcast:15 row_mask:0xf bank_mask:0xf
	s_and_saveexec_b64 s[46:47], s[42:43]
	global_store_dwordx4 v187, v[82:85], s[4:5] offset:64 sc1
	global_store_dwordx4 v187, v[78:81], s[16:17] offset:64 sc1
	s_mov_b64 exec, s[46:47]
	v_cvt_pk_bf16_f32 v66, v66, v67
	v_cvt_pk_bf16_f32 v67, v68, v69
	v_cvt_pk_bf16_f32 v68, v94, v95
	v_cvt_pk_bf16_f32 v69, v96, v97
	global_store_dwordx4 v194, v[66:69], s[54:55] offset:64 sc1
	v_cvt_pk_bf16_f32 v70, v70, v71
	v_cvt_pk_bf16_f32 v71, v72, v73
	v_cvt_pk_bf16_f32 v72, v90, v91
	v_cvt_pk_bf16_f32 v73, v92, v93
	global_store_dwordx4 v195, v[70:73], s[54:55] offset:64 sc1
	v_cvt_pk_bf16_f32 v74, v74, v75
	v_cvt_pk_bf16_f32 v75, v76, v77
	v_cvt_pk_bf16_f32 v76, v86, v87
	v_cvt_pk_bf16_f32 v77, v88, v89
	global_store_dwordx4 v196, v[74:77], s[54:55] offset:64 sc1
	v_cvt_pk_bf16_f32 v78, v78, v79
	v_cvt_pk_bf16_f32 v79, v80, v81
	v_cvt_pk_bf16_f32 v80, v82, v83
	v_cvt_pk_bf16_f32 v81, v84, v85
	global_store_dwordx4 v197, v[78:81], s[54:55] offset:64 sc1
	s_waitcnt vmcnt(6)
	v_add_f32_e32 v30, v30, v156
	v_add_f32_e32 v31, v31, v157
	v_add_f32_e32 v32, v32, v158
	v_add_f32_e32 v33, v33, v159
	v_add_f32_e32 v26, v26, v156
	v_add_f32_e32 v27, v27, v157
	v_add_f32_e32 v28, v28, v158
	v_add_f32_e32 v29, v29, v159
	v_mul_f32_e32 v30, 0xbfb8aa3b, v30
	v_mul_f32_e32 v31, 0xbfb8aa3b, v31
	v_mul_f32_e32 v32, 0xbfb8aa3b, v32
	v_mul_f32_e32 v33, 0xbfb8aa3b, v33
	v_mul_f32_e32 v26, 0xbfb8aa3b, v26
	v_mul_f32_e32 v27, 0xbfb8aa3b, v27
	v_mul_f32_e32 v28, 0xbfb8aa3b, v28
	v_mul_f32_e32 v29, 0xbfb8aa3b, v29
	v_exp_f32_e32 v30, v30
	v_exp_f32_e32 v31, v31
	v_exp_f32_e32 v32, v32
	v_exp_f32_e32 v33, v33
	v_exp_f32_e32 v26, v26
	v_exp_f32_e32 v27, v27
	v_exp_f32_e32 v28, v28
	v_exp_f32_e32 v29, v29
	v_add_f32_e32 v30, 1.0, v30
	v_add_f32_e32 v31, 1.0, v31
	v_add_f32_e32 v32, 1.0, v32
	v_add_f32_e32 v33, 1.0, v33
	v_add_f32_e32 v26, 1.0, v26
	v_add_f32_e32 v27, 1.0, v27
	v_add_f32_e32 v28, 1.0, v28
	v_add_f32_e32 v29, 1.0, v29
	v_rcp_f32_e32 v30, v30
	v_rcp_f32_e32 v31, v31
	v_rcp_f32_e32 v32, v32
	v_rcp_f32_e32 v33, v33
	v_rcp_f32_e32 v26, v26
	v_rcp_f32_e32 v27, v27
	v_rcp_f32_e32 v28, v28
	v_rcp_f32_e32 v29, v29
	v_mul_f32_e32 v30, v164, v30
	v_mul_f32_e32 v31, v165, v31
	v_mul_f32_e32 v32, v166, v32
	v_mul_f32_e32 v33, v167, v33
	v_mul_f32_e32 v26, v164, v26
	v_mul_f32_e32 v27, v165, v27
	v_mul_f32_e32 v28, v166, v28
	v_mul_f32_e32 v29, v167, v29
	v_add_f32_e32 v198, v30, v30
	v_add_f32_e32 v201, v31, v31
	v_add_f32_e32 v204, v32, v32
	v_add_f32_e32 v207, v33, v33
	v_add_f32_e32 v216, v26, v26
	v_add_f32_e32 v219, v27, v27
	v_add_f32_e32 v240, v28, v28
	v_add_f32_e32 v243, v29, v29
	v_mul_f32_e32 v199, 0x3fb8aa3b, v198
	v_mul_f32_e32 v202, 0x3fb8aa3b, v201
	v_mul_f32_e32 v205, 0x3fb8aa3b, v204
	v_mul_f32_e32 v208, 0x3fb8aa3b, v207
	v_mul_f32_e32 v217, 0x3fb8aa3b, v216
	v_mul_f32_e32 v238, 0x3fb8aa3b, v219
	v_mul_f32_e32 v241, 0x3fb8aa3b, v240
	v_mul_f32_e32 v244, 0x3fb8aa3b, v243
	v_exp_f32_e32 v199, v199
	v_exp_f32_e32 v202, v202
	v_exp_f32_e32 v205, v205
	v_exp_f32_e32 v208, v208
	v_exp_f32_e32 v217, v217
	v_exp_f32_e32 v238, v238
	v_exp_f32_e32 v241, v241
	v_exp_f32_e32 v244, v244
	v_fmamk_f32 v200, v198, 0x3c088889, v211
	v_fmamk_f32 v203, v201, 0x3c088889, v211
	v_fmamk_f32 v206, v204, 0x3c088889, v211
	v_fmamk_f32 v209, v207, 0x3c088889, v211
	v_fmamk_f32 v218, v216, 0x3c088889, v211
	v_fmamk_f32 v239, v219, 0x3c088889, v211
	v_fmamk_f32 v242, v240, 0x3c088889, v211
	v_fmamk_f32 v245, v243, 0x3c088889, v211
	v_sub_f32_e32 v199, 1.0, v199
	v_sub_f32_e32 v202, 1.0, v202
	v_sub_f32_e32 v205, 1.0, v205
	v_sub_f32_e32 v208, 1.0, v208
	v_sub_f32_e32 v217, 1.0, v217
	v_sub_f32_e32 v238, 1.0, v238
	v_sub_f32_e32 v241, 1.0, v241
	v_sub_f32_e32 v244, 1.0, v244
	v_fmaak_f32 v200, v198, v200, 0x3e2aaaab
	v_fmaak_f32 v203, v201, v203, 0x3e2aaaab
	v_fmaak_f32 v206, v204, v206, 0x3e2aaaab
; __device__ __forceinline__ float sigmoid_fast(float x) { return __builtin_amdgcn_rcpf(1.f + __expf(-x)); }
; __device__ __forceinline__ float one_minus_exp(float x) { const float p = -x * (1.f + x * (0.5f + x * (0.16666667f + x * (0.041666668f + x * 0.0083333338f)))); return x > -0.1f ? p : 1.f - __expf(x); }
;     template <bool BWD>
;     __device__ __forceinline__ void epi_dir(const f32x4 (&acc)[2][2][4][2], const Unit& u, int wr, int wc, int fr, int fq) const {
;     ...
;                     for (int j = 0; j < 4; ++j) { const float r = sigmoid_fast(acc[ai][0][m][n][j] + bav[j]), ig = sigmoid_fast(acc[ai][1][m][n][j] + bxv[j]);
;                         const float la = r * lsl[j]; A[m][j] = __expf(la); H[m][j] = __builtin_amdgcn_sqrtf(one_minus_exp(2.f * la)) * (ig * uv[j]); } }
	v_fmaak_f32 v209, v207, v209, 0x3e2aaaab
	v_fmaak_f32 v218, v216, v218, 0x3e2aaaab
	v_fmaak_f32 v239, v219, v239, 0x3e2aaaab
	v_fmaak_f32 v242, v240, v242, 0x3e2aaaab
	v_fmaak_f32 v245, v243, v245, 0x3e2aaaab
	v_fma_f32 v200, v198, v200, 0.5
	v_fma_f32 v203, v201, v203, 0.5
	v_fma_f32 v206, v204, v206, 0.5
	v_fma_f32 v209, v207, v209, 0.5
	v_fma_f32 v218, v216, v218, 0.5
	v_fma_f32 v239, v219, v239, 0.5
	v_fma_f32 v242, v240, v242, 0.5
	v_fma_f32 v245, v243, v245, 0.5
	v_fma_f32 v200, v198, v200, 1.0
	v_fma_f32 v203, v201, v203, 1.0
	v_fma_f32 v206, v204, v206, 1.0
	v_fma_f32 v209, v207, v209, 1.0
	v_fma_f32 v218, v216, v218, 1.0
	v_fma_f32 v239, v219, v239, 1.0
	v_fma_f32 v242, v240, v242, 1.0
	v_fma_f32 v245, v243, v245, 1.0
	v_mul_f32_e64 v200, v200, -v198
	v_mul_f32_e64 v203, v203, -v201
	v_mul_f32_e64 v206, v206, -v204
	v_mul_f32_e64 v209, v209, -v207
	v_mul_f32_e64 v218, v218, -v216
	v_mul_f32_e64 v239, v239, -v219
	v_mul_f32_e64 v242, v242, -v240
	v_mul_f32_e64 v245, v245, -v243
	v_cmp_nlt_f32_e32 vcc, s49, v198
	v_add_f32_e32 v2, v2, v160
	v_mul_f32_e32 v2, 0xbfb8aa3b, v2
	v_cndmask_b32_e32 v199, v200, v199, vcc
	v_cmp_nlt_f32_e32 vcc, s49, v201
	v_add_f32_e32 v3, v3, v161
	v_mul_f32_e32 v3, 0xbfb8aa3b, v3
	v_cndmask_b32_e32 v202, v203, v202, vcc
	v_cmp_nlt_f32_e32 vcc, s49, v204
	v_add_f32_e32 v4, v4, v162
	v_mul_f32_e32 v4, 0xbfb8aa3b, v4
	v_cndmask_b32_e32 v205, v206, v205, vcc
	v_cmp_nlt_f32_e32 vcc, s49, v207
	v_add_f32_e32 v5, v5, v163
	v_mul_f32_e32 v5, 0xbfb8aa3b, v5
	v_cndmask_b32_e32 v208, v209, v208, vcc
	v_cmp_nlt_f32_e32 vcc, s49, v216
	v_add_f32_e32 v6, v6, v160
	v_mul_f32_e32 v6, 0xbfb8aa3b, v6
	v_cndmask_b32_e32 v217, v218, v217, vcc
	v_cmp_nlt_f32_e32 vcc, s49, v219
	v_add_f32_e32 v7, v7, v161
	v_mul_f32_e32 v7, 0xbfb8aa3b, v7
	v_cndmask_b32_e32 v238, v239, v238, vcc
	v_cmp_nlt_f32_e32 vcc, s49, v240
	v_add_f32_e32 v8, v8, v162
	v_mul_f32_e32 v8, 0xbfb8aa3b, v8
	v_cndmask_b32_e32 v241, v242, v241, vcc
	v_cmp_nlt_f32_e32 vcc, s49, v243
	v_add_f32_e32 v9, v9, v163
	v_mul_f32_e32 v9, 0xbfb8aa3b, v9
	v_cndmask_b32_e32 v244, v245, v244, vcc
	v_exp_f32_e32 v2, v2
	v_exp_f32_e32 v3, v3
	v_exp_f32_e32 v4, v4
	v_exp_f32_e32 v5, v5
	v_exp_f32_e32 v6, v6
	v_exp_f32_e32 v7, v7
	v_exp_f32_e32 v8, v8
	v_exp_f32_e32 v9, v9
	v_sqrt_f32_e32 v199, v199
	v_sqrt_f32_e32 v202, v202
	v_sqrt_f32_e32 v205, v205
	v_sqrt_f32_e32 v208, v208
	v_sqrt_f32_e32 v217, v217
	v_sqrt_f32_e32 v238, v238
	v_sqrt_f32_e32 v241, v241
	v_sqrt_f32_e32 v244, v244
	v_add_f32_e32 v2, 1.0, v2
	v_add_f32_e32 v3, 1.0, v3
	v_add_f32_e32 v4, 1.0, v4
	v_add_f32_e32 v5, 1.0, v5
	v_add_f32_e32 v6, 1.0, v6
	v_add_f32_e32 v7, 1.0, v7
	v_add_f32_e32 v8, 1.0, v8
	v_add_f32_e32 v9, 1.0, v9
	v_lshlrev_b32_e32 v200, 16, v176
	v_and_b32_e32 v203, 0xffff0000, v176
	v_lshlrev_b32_e32 v206, 16, v177
	v_and_b32_e32 v209, 0xffff0000, v177
	v_lshlrev_b32_e32 v218, 16, v178
	v_and_b32_e32 v239, 0xffff0000, v178
	v_lshlrev_b32_e32 v242, 16, v179
	v_and_b32_e32 v245, 0xffff0000, v179
	v_rcp_f32_e32 v2, v2
	v_rcp_f32_e32 v3, v3
	v_rcp_f32_e32 v4, v4
	v_rcp_f32_e32 v5, v5
	v_rcp_f32_e32 v6, v6
	v_rcp_f32_e32 v7, v7
	v_rcp_f32_e32 v8, v8
	v_rcp_f32_e32 v9, v9
	v_mul_f32_e32 v30, 0x3fb8aa3b, v30
	v_mul_f32_e32 v31, 0x3fb8aa3b, v31
	v_mul_f32_e32 v32, 0x3fb8aa3b, v32
	v_mul_f32_e32 v33, 0x3fb8aa3b, v33
	v_mul_f32_e32 v26, 0x3fb8aa3b, v26
	v_mul_f32_e32 v27, 0x3fb8aa3b, v27
	v_mul_f32_e32 v28, 0x3fb8aa3b, v28
	v_mul_f32_e32 v29, 0x3fb8aa3b, v29
	v_mul_f32_e32 v2, v2, v200
	v_mul_f32_e32 v3, v3, v203
	v_mul_f32_e32 v4, v4, v206
	v_mul_f32_e32 v5, v5, v209
	v_mul_f32_e32 v6, v6, v218
	v_mul_f32_e32 v7, v7, v239
	v_mul_f32_e32 v8, v8, v242
	v_mul_f32_e32 v9, v9, v245
	v_exp_f32_e32 v30, v30
	v_exp_f32_e32 v31, v31
	v_exp_f32_e32 v32, v32
	v_exp_f32_e32 v33, v33
	v_exp_f32_e32 v26, v26
	v_exp_f32_e32 v27, v27
	v_exp_f32_e32 v28, v28
	v_exp_f32_e32 v29, v29
	v_mul_f32_e32 v2, v2, v199
	v_mul_f32_e32 v3, v3, v202
	v_mul_f32_e32 v4, v4, v205
	v_mul_f32_e32 v5, v5, v208
	v_mul_f32_e32 v6, v6, v217
	v_mul_f32_e32 v7, v7, v238
	v_mul_f32_e32 v8, v8, v241
	v_mul_f32_e32 v9, v9, v244
	v_add_f32_e32 v22, v22, v156
	v_add_f32_e32 v23, v23, v157
	v_add_f32_e32 v24, v24, v158
	v_add_f32_e32 v25, v25, v159
	v_add_f32_e32 v18, v18, v156
	v_add_f32_e32 v19, v19, v157
	v_add_f32_e32 v20, v20, v158
	v_add_f32_e32 v21, v21, v159
	v_mul_f32_e32 v22, 0xbfb8aa3b, v22
	v_mul_f32_e32 v23, 0xbfb8aa3b, v23
	v_mul_f32_e32 v24, 0xbfb8aa3b, v24
	v_mul_f32_e32 v25, 0xbfb8aa3b, v25
	v_mul_f32_e32 v18, 0xbfb8aa3b, v18
	v_mul_f32_e32 v19, 0xbfb8aa3b, v19
	v_mul_f32_e32 v20, 0xbfb8aa3b, v20
	v_mul_f32_e32 v21, 0xbfb8aa3b, v21
	v_exp_f32_e32 v22, v22
	v_exp_f32_e32 v23, v23
	v_exp_f32_e32 v24, v24
	v_exp_f32_e32 v25, v25
	v_exp_f32_e32 v18, v18
	v_exp_f32_e32 v19, v19
	v_exp_f32_e32 v20, v20
	v_exp_f32_e32 v21, v21
	v_add_f32_e32 v22, 1.0, v22
	v_add_f32_e32 v23, 1.0, v23
	v_add_f32_e32 v24, 1.0, v24
	v_add_f32_e32 v25, 1.0, v25
	v_add_f32_e32 v18, 1.0, v18
	v_add_f32_e32 v19, 1.0, v19
	v_add_f32_e32 v20, 1.0, v20
	v_add_f32_e32 v21, 1.0, v21
	v_rcp_f32_e32 v22, v22
	v_rcp_f32_e32 v23, v23
	v_rcp_f32_e32 v24, v24
	v_rcp_f32_e32 v25, v25
	v_rcp_f32_e32 v18, v18
	v_rcp_f32_e32 v19, v19
	v_rcp_f32_e32 v20, v20
	v_rcp_f32_e32 v21, v21
	v_mul_f32_e32 v22, v164, v22
	v_mul_f32_e32 v23, v165, v23
	v_mul_f32_e32 v24, v166, v24
	v_mul_f32_e32 v25, v167, v25
	v_mul_f32_e32 v18, v164, v18
	v_mul_f32_e32 v19, v165, v19
	v_mul_f32_e32 v20, v166, v20
	v_mul_f32_e32 v21, v167, v21
	v_add_f32_e32 v198, v22, v22
	v_add_f32_e32 v201, v23, v23
	v_add_f32_e32 v204, v24, v24
	v_add_f32_e32 v207, v25, v25
	v_add_f32_e32 v216, v18, v18
; __device__ __forceinline__ float sigmoid_fast(float x) { return __builtin_amdgcn_rcpf(1.f + __expf(-x)); }
; __device__ __forceinline__ float one_minus_exp(float x) { const float p = -x * (1.f + x * (0.5f + x * (0.16666667f + x * (0.041666668f + x * 0.0083333338f)))); return x > -0.1f ? p : 1.f - __expf(x); }
; #define SCAN_STEP(D) { const float ap = dppf<(BWD ? 0x100 : 0x110) + D>(1.f, av), hp = dppf<(BWD ? 0x100 : 0x110) + D>(0.f, hv); hv = fmaf(av, hp, hv); av = av * ap; }
;     template <bool BWD>
;     __device__ __forceinline__ void epi_dir(const f32x4 (&acc)[2][2][4][2], const Unit& u, int wr, int wc, int fr, int fq) const {
;     ...
;                     for (int j = 0; j < 4; ++j) { const float r = sigmoid_fast(acc[ai][0][m][n][j] + bav[j]), ig = sigmoid_fast(acc[ai][1][m][n][j] + bxv[j]);
;                         const float la = r * lsl[j]; A[m][j] = __expf(la); H[m][j] = __builtin_amdgcn_sqrtf(one_minus_exp(2.f * la)) * (ig * uv[j]); } }
; #pragma unroll
;                 for (int m = 0; m < 4; ++m)
; #pragma unroll
;                     for (int j = 0; j < 4; ++j) { float av = A[m][j], hv = H[m][j];
;     ...
;                         SCAN_STEP(1) SCAN_STEP(2) SCAN_STEP(4) SCAN_STEP(8)
	v_add_f32_e32 v219, v19, v19
	v_add_f32_e32 v240, v20, v20
	v_add_f32_e32 v243, v21, v21
	v_mul_f32_e32 v199, 0x3fb8aa3b, v198
	v_mul_f32_e32 v202, 0x3fb8aa3b, v201
	v_mul_f32_e32 v205, 0x3fb8aa3b, v204
	v_mul_f32_e32 v208, 0x3fb8aa3b, v207
	v_mul_f32_e32 v217, 0x3fb8aa3b, v216
	v_mul_f32_e32 v238, 0x3fb8aa3b, v219
	v_mul_f32_e32 v241, 0x3fb8aa3b, v240
	v_mul_f32_e32 v244, 0x3fb8aa3b, v243
	v_exp_f32_e32 v199, v199
	v_exp_f32_e32 v202, v202
	v_exp_f32_e32 v205, v205
	v_exp_f32_e32 v208, v208
	v_exp_f32_e32 v217, v217
	v_exp_f32_e32 v238, v238
	v_exp_f32_e32 v241, v241
	v_exp_f32_e32 v244, v244
	v_fmamk_f32 v200, v198, 0x3c088889, v211
	v_fmamk_f32 v203, v201, 0x3c088889, v211
	v_fmamk_f32 v206, v204, 0x3c088889, v211
	v_fmamk_f32 v209, v207, 0x3c088889, v211
	v_fmamk_f32 v218, v216, 0x3c088889, v211
	v_fmamk_f32 v239, v219, 0x3c088889, v211
	v_fmamk_f32 v242, v240, 0x3c088889, v211
	v_fmamk_f32 v245, v243, 0x3c088889, v211
	v_sub_f32_e32 v199, 1.0, v199
	v_sub_f32_e32 v202, 1.0, v202
	v_sub_f32_e32 v205, 1.0, v205
	v_sub_f32_e32 v208, 1.0, v208
	v_sub_f32_e32 v217, 1.0, v217
	v_sub_f32_e32 v238, 1.0, v238
	v_sub_f32_e32 v241, 1.0, v241
	v_sub_f32_e32 v244, 1.0, v244
	v_fmaak_f32 v200, v198, v200, 0x3e2aaaab
	v_fmaak_f32 v203, v201, v203, 0x3e2aaaab
	v_fmaak_f32 v206, v204, v206, 0x3e2aaaab
	v_fmaak_f32 v209, v207, v209, 0x3e2aaaab
	v_fmaak_f32 v218, v216, v218, 0x3e2aaaab
	v_fmaak_f32 v239, v219, v239, 0x3e2aaaab
	v_fmaak_f32 v242, v240, v242, 0x3e2aaaab
	v_fmaak_f32 v245, v243, v245, 0x3e2aaaab
	v_fma_f32 v200, v198, v200, 0.5
	v_fma_f32 v203, v201, v203, 0.5
	v_fma_f32 v206, v204, v206, 0.5
	v_fma_f32 v209, v207, v209, 0.5
	v_fma_f32 v218, v216, v218, 0.5
	v_fma_f32 v239, v219, v239, 0.5
	v_fma_f32 v242, v240, v242, 0.5
	v_fma_f32 v245, v243, v245, 0.5
	v_fma_f32 v200, v198, v200, 1.0
	v_fma_f32 v203, v201, v203, 1.0
	v_fma_f32 v206, v204, v206, 1.0
	v_fma_f32 v209, v207, v209, 1.0
	v_fma_f32 v218, v216, v218, 1.0
	v_fma_f32 v239, v219, v239, 1.0
	v_fma_f32 v242, v240, v242, 1.0
	v_fma_f32 v245, v243, v245, 1.0
	v_mul_f32_e64 v200, v200, -v198
	v_mul_f32_e64 v203, v203, -v201
	v_mul_f32_e64 v206, v206, -v204
	v_mul_f32_e64 v209, v209, -v207
	v_mul_f32_e64 v218, v218, -v216
	v_mul_f32_e64 v239, v239, -v219
	v_mul_f32_e64 v242, v242, -v240
	v_mul_f32_e64 v245, v245, -v243
	v_cmp_nlt_f32_e32 vcc, s49, v198
	v_add_f32_e32 v10, v10, v160
	v_mul_f32_e32 v10, 0xbfb8aa3b, v10
	v_cndmask_b32_e32 v199, v200, v199, vcc
	v_cmp_nlt_f32_e32 vcc, s49, v201
	v_add_f32_e32 v11, v11, v161
	v_mul_f32_e32 v11, 0xbfb8aa3b, v11
	v_cndmask_b32_e32 v202, v203, v202, vcc
	v_cmp_nlt_f32_e32 vcc, s49, v204
	v_add_f32_e32 v12, v12, v162
	v_mul_f32_e32 v12, 0xbfb8aa3b, v12
	v_cndmask_b32_e32 v205, v206, v205, vcc
	v_cmp_nlt_f32_e32 vcc, s49, v207
	v_add_f32_e32 v13, v13, v163
	v_mul_f32_e32 v13, 0xbfb8aa3b, v13
	v_cndmask_b32_e32 v208, v209, v208, vcc
	v_cmp_nlt_f32_e32 vcc, s49, v216
	v_add_f32_e32 v14, v14, v160
	v_mul_f32_e32 v14, 0xbfb8aa3b, v14
	v_cndmask_b32_e32 v217, v218, v217, vcc
	v_cmp_nlt_f32_e32 vcc, s49, v219
	v_add_f32_e32 v15, v15, v161
	v_mul_f32_e32 v15, 0xbfb8aa3b, v15
	v_cndmask_b32_e32 v238, v239, v238, vcc
	v_cmp_nlt_f32_e32 vcc, s49, v240
	v_add_f32_e32 v16, v16, v162
	v_mul_f32_e32 v16, 0xbfb8aa3b, v16
	v_cndmask_b32_e32 v241, v242, v241, vcc
	v_cmp_nlt_f32_e32 vcc, s49, v243
	v_add_f32_e32 v17, v17, v163
	v_mul_f32_e32 v17, 0xbfb8aa3b, v17
	v_cndmask_b32_e32 v244, v245, v244, vcc
	v_exp_f32_e32 v10, v10
	v_exp_f32_e32 v11, v11
	v_exp_f32_e32 v12, v12
	v_exp_f32_e32 v13, v13
	v_exp_f32_e32 v14, v14
	v_exp_f32_e32 v15, v15
	v_exp_f32_e32 v16, v16
	v_exp_f32_e32 v17, v17
	v_sqrt_f32_e32 v199, v199
	v_sqrt_f32_e32 v202, v202
	v_sqrt_f32_e32 v205, v205
	v_sqrt_f32_e32 v208, v208
	v_sqrt_f32_e32 v217, v217
	v_sqrt_f32_e32 v238, v238
	v_sqrt_f32_e32 v241, v241
	v_sqrt_f32_e32 v244, v244
	v_add_f32_e32 v10, 1.0, v10
	v_add_f32_e32 v11, 1.0, v11
	v_add_f32_e32 v12, 1.0, v12
	v_add_f32_e32 v13, 1.0, v13
	v_add_f32_e32 v14, 1.0, v14
	v_add_f32_e32 v15, 1.0, v15
	v_add_f32_e32 v16, 1.0, v16
	v_add_f32_e32 v17, 1.0, v17
	v_lshlrev_b32_e32 v200, 16, v182
	v_and_b32_e32 v203, 0xffff0000, v182
	v_lshlrev_b32_e32 v206, 16, v183
	v_and_b32_e32 v209, 0xffff0000, v183
	v_lshlrev_b32_e32 v218, 16, v184
	v_and_b32_e32 v239, 0xffff0000, v184
	v_lshlrev_b32_e32 v242, 16, v185
	v_and_b32_e32 v245, 0xffff0000, v185
	v_rcp_f32_e32 v10, v10
	v_rcp_f32_e32 v11, v11
	v_rcp_f32_e32 v12, v12
	v_rcp_f32_e32 v13, v13
	v_rcp_f32_e32 v14, v14
	v_rcp_f32_e32 v15, v15
	v_rcp_f32_e32 v16, v16
	v_rcp_f32_e32 v17, v17
	v_mul_f32_e32 v22, 0x3fb8aa3b, v22
	v_mul_f32_e32 v23, 0x3fb8aa3b, v23
	v_mul_f32_e32 v24, 0x3fb8aa3b, v24
	v_mul_f32_e32 v25, 0x3fb8aa3b, v25
	v_mul_f32_e32 v18, 0x3fb8aa3b, v18
	v_mul_f32_e32 v19, 0x3fb8aa3b, v19
	v_mul_f32_e32 v20, 0x3fb8aa3b, v20
	v_mul_f32_e32 v21, 0x3fb8aa3b, v21
	v_mul_f32_e32 v10, v10, v200
	v_mul_f32_e32 v11, v11, v203
	v_mul_f32_e32 v12, v12, v206
	v_mul_f32_e32 v13, v13, v209
	v_mul_f32_e32 v14, v14, v218
	v_mul_f32_e32 v15, v15, v239
	v_mul_f32_e32 v16, v16, v242
	v_mul_f32_e32 v17, v17, v245
	v_exp_f32_e32 v22, v22
	v_exp_f32_e32 v23, v23
	v_exp_f32_e32 v24, v24
	v_exp_f32_e32 v25, v25
	v_exp_f32_e32 v18, v18
	v_exp_f32_e32 v19, v19
	v_exp_f32_e32 v20, v20
	v_exp_f32_e32 v21, v21
	v_mul_f32_e32 v10, v10, v199
	v_mul_f32_e32 v11, v11, v202
	v_mul_f32_e32 v12, v12, v205
	v_mul_f32_e32 v13, v13, v208
	v_mul_f32_e32 v14, v14, v217
	v_mul_f32_e32 v15, v15, v238
	v_mul_f32_e32 v16, v16, v241
	v_mul_f32_e32 v17, v17, v244
	v_fmac_f32_dpp v2, v2, v30 row_shr:1 row_mask:0xf bank_mask:0xf
	v_mul_f32_dpp v30, v30, v30 row_shr:1 row_mask:0xf bank_mask:0xf
; #define SCAN_STEP(D) { const float ap = dppf<(BWD ? 0x100 : 0x110) + D>(1.f, av), hp = dppf<(BWD ? 0x100 : 0x110) + D>(0.f, hv); hv = fmaf(av, hp, hv); av = av * ap; }
;     template <bool BWD>
;     __device__ __forceinline__ void epi_dir(const f32x4 (&acc)[2][2][4][2], const Unit& u, int wr, int wc, int fr, int fq) const {
;     ...
;                 for (int m = 0; m < 4; ++m)
; #pragma unroll
;                     for (int j = 0; j < 4; ++j) { float av = A[m][j], hv = H[m][j];
;     ...
;                         SCAN_STEP(1) SCAN_STEP(2) SCAN_STEP(4) SCAN_STEP(8)
	v_fmac_f32_dpp v3, v3, v31 row_shr:1 row_mask:0xf bank_mask:0xf
	v_mul_f32_dpp v31, v31, v31 row_shr:1 row_mask:0xf bank_mask:0xf
	v_fmac_f32_dpp v4, v4, v32 row_shr:1 row_mask:0xf bank_mask:0xf
	v_mul_f32_dpp v32, v32, v32 row_shr:1 row_mask:0xf bank_mask:0xf
	v_fmac_f32_dpp v5, v5, v33 row_shr:1 row_mask:0xf bank_mask:0xf
	v_mul_f32_dpp v33, v33, v33 row_shr:1 row_mask:0xf bank_mask:0xf
	v_fmac_f32_dpp v6, v6, v26 row_shr:1 row_mask:0xf bank_mask:0xf
	v_mul_f32_dpp v26, v26, v26 row_shr:1 row_mask:0xf bank_mask:0xf
	v_fmac_f32_dpp v7, v7, v27 row_shr:1 row_mask:0xf bank_mask:0xf
	v_mul_f32_dpp v27, v27, v27 row_shr:1 row_mask:0xf bank_mask:0xf
	v_fmac_f32_dpp v8, v8, v28 row_shr:1 row_mask:0xf bank_mask:0xf
	v_mul_f32_dpp v28, v28, v28 row_shr:1 row_mask:0xf bank_mask:0xf
	v_fmac_f32_dpp v9, v9, v29 row_shr:1 row_mask:0xf bank_mask:0xf
	v_mul_f32_dpp v29, v29, v29 row_shr:1 row_mask:0xf bank_mask:0xf
	v_fmac_f32_dpp v10, v10, v22 row_shr:1 row_mask:0xf bank_mask:0xf
	v_mul_f32_dpp v22, v22, v22 row_shr:1 row_mask:0xf bank_mask:0xf
	v_fmac_f32_dpp v11, v11, v23 row_shr:1 row_mask:0xf bank_mask:0xf
	v_mul_f32_dpp v23, v23, v23 row_shr:1 row_mask:0xf bank_mask:0xf
	v_fmac_f32_dpp v12, v12, v24 row_shr:1 row_mask:0xf bank_mask:0xf
	v_mul_f32_dpp v24, v24, v24 row_shr:1 row_mask:0xf bank_mask:0xf
	v_fmac_f32_dpp v13, v13, v25 row_shr:1 row_mask:0xf bank_mask:0xf
	v_mul_f32_dpp v25, v25, v25 row_shr:1 row_mask:0xf bank_mask:0xf
	v_fmac_f32_dpp v14, v14, v18 row_shr:1 row_mask:0xf bank_mask:0xf
	v_mul_f32_dpp v18, v18, v18 row_shr:1 row_mask:0xf bank_mask:0xf
	v_fmac_f32_dpp v15, v15, v19 row_shr:1 row_mask:0xf bank_mask:0xf
	v_mul_f32_dpp v19, v19, v19 row_shr:1 row_mask:0xf bank_mask:0xf
	v_fmac_f32_dpp v16, v16, v20 row_shr:1 row_mask:0xf bank_mask:0xf
	v_mul_f32_dpp v20, v20, v20 row_shr:1 row_mask:0xf bank_mask:0xf
	v_fmac_f32_dpp v17, v17, v21 row_shr:1 row_mask:0xf bank_mask:0xf
	v_mul_f32_dpp v21, v21, v21 row_shr:1 row_mask:0xf bank_mask:0xf
	v_fmac_f32_dpp v2, v2, v30 row_shr:2 row_mask:0xf bank_mask:0xf
	v_mul_f32_dpp v30, v30, v30 row_shr:2 row_mask:0xf bank_mask:0xf
	v_fmac_f32_dpp v3, v3, v31 row_shr:2 row_mask:0xf bank_mask:0xf
	v_mul_f32_dpp v31, v31, v31 row_shr:2 row_mask:0xf bank_mask:0xf
	v_fmac_f32_dpp v4, v4, v32 row_shr:2 row_mask:0xf bank_mask:0xf
	v_mul_f32_dpp v32, v32, v32 row_shr:2 row_mask:0xf bank_mask:0xf
	v_fmac_f32_dpp v5, v5, v33 row_shr:2 row_mask:0xf bank_mask:0xf
	v_mul_f32_dpp v33, v33, v33 row_shr:2 row_mask:0xf bank_mask:0xf
	v_fmac_f32_dpp v6, v6, v26 row_shr:2 row_mask:0xf bank_mask:0xf
	v_mul_f32_dpp v26, v26, v26 row_shr:2 row_mask:0xf bank_mask:0xf
	v_fmac_f32_dpp v7, v7, v27 row_shr:2 row_mask:0xf bank_mask:0xf
	v_mul_f32_dpp v27, v27, v27 row_shr:2 row_mask:0xf bank_mask:0xf
	v_fmac_f32_dpp v8, v8, v28 row_shr:2 row_mask:0xf bank_mask:0xf
	v_mul_f32_dpp v28, v28, v28 row_shr:2 row_mask:0xf bank_mask:0xf
	v_fmac_f32_dpp v9, v9, v29 row_shr:2 row_mask:0xf bank_mask:0xf
	v_mul_f32_dpp v29, v29, v29 row_shr:2 row_mask:0xf bank_mask:0xf
	v_fmac_f32_dpp v10, v10, v22 row_shr:2 row_mask:0xf bank_mask:0xf
	v_mul_f32_dpp v22, v22, v22 row_shr:2 row_mask:0xf bank_mask:0xf
	v_fmac_f32_dpp v11, v11, v23 row_shr:2 row_mask:0xf bank_mask:0xf
	v_mul_f32_dpp v23, v23, v23 row_shr:2 row_mask:0xf bank_mask:0xf
	v_fmac_f32_dpp v12, v12, v24 row_shr:2 row_mask:0xf bank_mask:0xf
	v_mul_f32_dpp v24, v24, v24 row_shr:2 row_mask:0xf bank_mask:0xf
	v_fmac_f32_dpp v13, v13, v25 row_shr:2 row_mask:0xf bank_mask:0xf
	v_mul_f32_dpp v25, v25, v25 row_shr:2 row_mask:0xf bank_mask:0xf
	v_fmac_f32_dpp v14, v14, v18 row_shr:2 row_mask:0xf bank_mask:0xf
	v_mul_f32_dpp v18, v18, v18 row_shr:2 row_mask:0xf bank_mask:0xf
	v_fmac_f32_dpp v15, v15, v19 row_shr:2 row_mask:0xf bank_mask:0xf
	v_mul_f32_dpp v19, v19, v19 row_shr:2 row_mask:0xf bank_mask:0xf
	v_fmac_f32_dpp v16, v16, v20 row_shr:2 row_mask:0xf bank_mask:0xf
	v_mul_f32_dpp v20, v20, v20 row_shr:2 row_mask:0xf bank_mask:0xf
	v_fmac_f32_dpp v17, v17, v21 row_shr:2 row_mask:0xf bank_mask:0xf
	v_mul_f32_dpp v21, v21, v21 row_shr:2 row_mask:0xf bank_mask:0xf
	v_fmac_f32_dpp v2, v2, v30 row_shr:4 row_mask:0xf bank_mask:0xf
	v_mul_f32_dpp v30, v30, v30 row_shr:4 row_mask:0xf bank_mask:0xf
	v_fmac_f32_dpp v3, v3, v31 row_shr:4 row_mask:0xf bank_mask:0xf
	v_mul_f32_dpp v31, v31, v31 row_shr:4 row_mask:0xf bank_mask:0xf
	v_fmac_f32_dpp v4, v4, v32 row_shr:4 row_mask:0xf bank_mask:0xf
	v_mul_f32_dpp v32, v32, v32 row_shr:4 row_mask:0xf bank_mask:0xf
	v_fmac_f32_dpp v5, v5, v33 row_shr:4 row_mask:0xf bank_mask:0xf
	v_mul_f32_dpp v33, v33, v33 row_shr:4 row_mask:0xf bank_mask:0xf
	v_fmac_f32_dpp v6, v6, v26 row_shr:4 row_mask:0xf bank_mask:0xf
	v_mul_f32_dpp v26, v26, v26 row_shr:4 row_mask:0xf bank_mask:0xf
	v_fmac_f32_dpp v7, v7, v27 row_shr:4 row_mask:0xf bank_mask:0xf
	v_mul_f32_dpp v27, v27, v27 row_shr:4 row_mask:0xf bank_mask:0xf
	v_fmac_f32_dpp v8, v8, v28 row_shr:4 row_mask:0xf bank_mask:0xf
	v_mul_f32_dpp v28, v28, v28 row_shr:4 row_mask:0xf bank_mask:0xf
	v_fmac_f32_dpp v9, v9, v29 row_shr:4 row_mask:0xf bank_mask:0xf
	v_mul_f32_dpp v29, v29, v29 row_shr:4 row_mask:0xf bank_mask:0xf
	v_fmac_f32_dpp v10, v10, v22 row_shr:4 row_mask:0xf bank_mask:0xf
	v_mul_f32_dpp v22, v22, v22 row_shr:4 row_mask:0xf bank_mask:0xf
	v_fmac_f32_dpp v11, v11, v23 row_shr:4 row_mask:0xf bank_mask:0xf
	v_mul_f32_dpp v23, v23, v23 row_shr:4 row_mask:0xf bank_mask:0xf
	v_fmac_f32_dpp v12, v12, v24 row_shr:4 row_mask:0xf bank_mask:0xf
; __device__ __forceinline__ unsigned pk2(float lo, float hi) { return f2bf(lo) | (f2bf(hi) << 16); }
; #define SCAN_STEP(D) { const float ap = dppf<(BWD ? 0x100 : 0x110) + D>(1.f, av), hp = dppf<(BWD ? 0x100 : 0x110) + D>(0.f, hv); hv = fmaf(av, hp, hv); av = av * ap; }
;     template <bool BWD>
;     __device__ __forceinline__ void epi_dir(const f32x4 (&acc)[2][2][4][2], const Unit& u, int wr, int wc, int fr, int fq) const {
;     ...
;                 for (int m = 0; m < 4; ++m)
; #pragma unroll
;                     for (int j = 0; j < 4; ++j) { float av = A[m][j], hv = H[m][j];
;     ...
;                         SCAN_STEP(1) SCAN_STEP(2) SCAN_STEP(4) SCAN_STEP(8)
;     ...
;                         A[m][j] = av; H[m][j] = hv; }
; #pragma unroll
;                 for (int j = 0; j < 4; ++j) { float Ar = 1.f, Hr = 0.f;
; #pragma unroll
;                     for (int mm = 0; mm < 4; ++mm) { const int m = BWD ? 3 - mm : mm;
;                         H[m][j] = fmaf(A[m][j], Hr, H[m][j]); A[m][j] = A[m][j] * Ar;
;                         if (mm < 3) { Ar = __shfl(A[m][j], bsel); Hr = __shfl(H[m][j], bsel); } } }
; #pragma unroll
;                 for (int m = 0; m < 4; ++m) { u32x4 w; w.x = pk2(H[m][0], H[m][1]); w.y = pk2(H[m][2], H[m][3]); w.z = pk2(A[m][0], A[m][1]); w.w = pk2(A[m][2], A[m][3]);
;                     *(u32x4*)(Hb + ((size_t)(ai * 128 + m * 16) * 1024 + n * 16) * 4 + loffh) = w; }
;                 constexpr int me = BWD ? 0 : 3;
;                 if (fr == (BWD ? 0 : 15)) { const size_t o = (size_t)chunk * 1024 + gblk * 128 + n * 16;
;                     *(f32x4*)((char*)(AGG + (size_t)(dir * 2 + 0) * NB * NCHUNK * 1024 + o) + coff) = A[me];
;                     *(f32x4*)((char*)(AGG + (size_t)(dir * 2 + 1) * NB * NCHUNK * 1024 + o) + coff) = H[me]; }
	v_mul_f32_dpp v24, v24, v24 row_shr:4 row_mask:0xf bank_mask:0xf
	v_fmac_f32_dpp v13, v13, v25 row_shr:4 row_mask:0xf bank_mask:0xf
	v_mul_f32_dpp v25, v25, v25 row_shr:4 row_mask:0xf bank_mask:0xf
	v_fmac_f32_dpp v14, v14, v18 row_shr:4 row_mask:0xf bank_mask:0xf
	v_mul_f32_dpp v18, v18, v18 row_shr:4 row_mask:0xf bank_mask:0xf
	v_fmac_f32_dpp v15, v15, v19 row_shr:4 row_mask:0xf bank_mask:0xf
	v_mul_f32_dpp v19, v19, v19 row_shr:4 row_mask:0xf bank_mask:0xf
	v_fmac_f32_dpp v16, v16, v20 row_shr:4 row_mask:0xf bank_mask:0xf
	v_mul_f32_dpp v20, v20, v20 row_shr:4 row_mask:0xf bank_mask:0xf
	v_fmac_f32_dpp v17, v17, v21 row_shr:4 row_mask:0xf bank_mask:0xf
	v_mul_f32_dpp v21, v21, v21 row_shr:4 row_mask:0xf bank_mask:0xf
	v_fmac_f32_dpp v2, v2, v30 row_shr:8 row_mask:0xf bank_mask:0xf
	v_mul_f32_dpp v30, v30, v30 row_shr:8 row_mask:0xf bank_mask:0xf
	v_fmac_f32_dpp v3, v3, v31 row_shr:8 row_mask:0xf bank_mask:0xf
	v_mul_f32_dpp v31, v31, v31 row_shr:8 row_mask:0xf bank_mask:0xf
	v_fmac_f32_dpp v4, v4, v32 row_shr:8 row_mask:0xf bank_mask:0xf
	v_mul_f32_dpp v32, v32, v32 row_shr:8 row_mask:0xf bank_mask:0xf
	v_fmac_f32_dpp v5, v5, v33 row_shr:8 row_mask:0xf bank_mask:0xf
	v_mul_f32_dpp v33, v33, v33 row_shr:8 row_mask:0xf bank_mask:0xf
	v_fmac_f32_dpp v6, v6, v26 row_shr:8 row_mask:0xf bank_mask:0xf
	v_mul_f32_dpp v26, v26, v26 row_shr:8 row_mask:0xf bank_mask:0xf
	v_fmac_f32_dpp v7, v7, v27 row_shr:8 row_mask:0xf bank_mask:0xf
	v_mul_f32_dpp v27, v27, v27 row_shr:8 row_mask:0xf bank_mask:0xf
	v_fmac_f32_dpp v8, v8, v28 row_shr:8 row_mask:0xf bank_mask:0xf
	v_mul_f32_dpp v28, v28, v28 row_shr:8 row_mask:0xf bank_mask:0xf
	v_fmac_f32_dpp v9, v9, v29 row_shr:8 row_mask:0xf bank_mask:0xf
	v_mul_f32_dpp v29, v29, v29 row_shr:8 row_mask:0xf bank_mask:0xf
	v_fmac_f32_dpp v10, v10, v22 row_shr:8 row_mask:0xf bank_mask:0xf
	v_mul_f32_dpp v22, v22, v22 row_shr:8 row_mask:0xf bank_mask:0xf
	v_fmac_f32_dpp v11, v11, v23 row_shr:8 row_mask:0xf bank_mask:0xf
	v_mul_f32_dpp v23, v23, v23 row_shr:8 row_mask:0xf bank_mask:0xf
	v_fmac_f32_dpp v12, v12, v24 row_shr:8 row_mask:0xf bank_mask:0xf
	v_mul_f32_dpp v24, v24, v24 row_shr:8 row_mask:0xf bank_mask:0xf
	v_fmac_f32_dpp v13, v13, v25 row_shr:8 row_mask:0xf bank_mask:0xf
	v_mul_f32_dpp v25, v25, v25 row_shr:8 row_mask:0xf bank_mask:0xf
	v_fmac_f32_dpp v14, v14, v18 row_shr:8 row_mask:0xf bank_mask:0xf
	v_mul_f32_dpp v18, v18, v18 row_shr:8 row_mask:0xf bank_mask:0xf
	v_fmac_f32_dpp v15, v15, v19 row_shr:8 row_mask:0xf bank_mask:0xf
	v_mul_f32_dpp v19, v19, v19 row_shr:8 row_mask:0xf bank_mask:0xf
	v_fmac_f32_dpp v16, v16, v20 row_shr:8 row_mask:0xf bank_mask:0xf
	v_mul_f32_dpp v20, v20, v20 row_shr:8 row_mask:0xf bank_mask:0xf
	v_fmac_f32_dpp v17, v17, v21 row_shr:8 row_mask:0xf bank_mask:0xf
	v_mul_f32_dpp v21, v21, v21 row_shr:8 row_mask:0xf bank_mask:0xf
	v_fmac_f32_dpp v6, v2, v26 row_newbcast:15 row_mask:0xf bank_mask:0xf
	v_mul_f32_dpp v26, v30, v26 row_newbcast:15 row_mask:0xf bank_mask:0xf
	v_fmac_f32_dpp v7, v3, v27 row_newbcast:15 row_mask:0xf bank_mask:0xf
	v_mul_f32_dpp v27, v31, v27 row_newbcast:15 row_mask:0xf bank_mask:0xf
	v_fmac_f32_dpp v8, v4, v28 row_newbcast:15 row_mask:0xf bank_mask:0xf
	v_mul_f32_dpp v28, v32, v28 row_newbcast:15 row_mask:0xf bank_mask:0xf
	v_fmac_f32_dpp v9, v5, v29 row_newbcast:15 row_mask:0xf bank_mask:0xf
	v_mul_f32_dpp v29, v33, v29 row_newbcast:15 row_mask:0xf bank_mask:0xf
	v_fmac_f32_dpp v10, v6, v22 row_newbcast:15 row_mask:0xf bank_mask:0xf
	v_mul_f32_dpp v22, v26, v22 row_newbcast:15 row_mask:0xf bank_mask:0xf
	v_fmac_f32_dpp v11, v7, v23 row_newbcast:15 row_mask:0xf bank_mask:0xf
	v_mul_f32_dpp v23, v27, v23 row_newbcast:15 row_mask:0xf bank_mask:0xf
	v_fmac_f32_dpp v12, v8, v24 row_newbcast:15 row_mask:0xf bank_mask:0xf
	v_mul_f32_dpp v24, v28, v24 row_newbcast:15 row_mask:0xf bank_mask:0xf
	v_fmac_f32_dpp v13, v9, v25 row_newbcast:15 row_mask:0xf bank_mask:0xf
	v_mul_f32_dpp v25, v29, v25 row_newbcast:15 row_mask:0xf bank_mask:0xf
	v_fmac_f32_dpp v14, v10, v18 row_newbcast:15 row_mask:0xf bank_mask:0xf
	v_mul_f32_dpp v18, v22, v18 row_newbcast:15 row_mask:0xf bank_mask:0xf
	v_fmac_f32_dpp v15, v11, v19 row_newbcast:15 row_mask:0xf bank_mask:0xf
	v_mul_f32_dpp v19, v23, v19 row_newbcast:15 row_mask:0xf bank_mask:0xf
	v_fmac_f32_dpp v16, v12, v20 row_newbcast:15 row_mask:0xf bank_mask:0xf
	v_mul_f32_dpp v20, v24, v20 row_newbcast:15 row_mask:0xf bank_mask:0xf
	v_fmac_f32_dpp v17, v13, v21 row_newbcast:15 row_mask:0xf bank_mask:0xf
	v_mul_f32_dpp v21, v25, v21 row_newbcast:15 row_mask:0xf bank_mask:0xf
	s_and_saveexec_b64 s[46:47], s[42:43]
	global_store_dwordx4 v188, v[18:21], s[4:5] offset:64 sc1
	global_store_dwordx4 v188, v[14:17], s[16:17] offset:64 sc1
	s_mov_b64 exec, s[46:47]
	v_cvt_pk_bf16_f32 v2, v2, v3
	v_cvt_pk_bf16_f32 v3, v4, v5
	v_cvt_pk_bf16_f32 v4, v30, v31
	v_cvt_pk_bf16_f32 v5, v32, v33
	global_store_dwordx4 v194, v[2:5], s[56:57] offset:64 sc1
	v_cvt_pk_bf16_f32 v6, v6, v7
	v_cvt_pk_bf16_f32 v7, v8, v9
	v_cvt_pk_bf16_f32 v8, v26, v27
	v_cvt_pk_bf16_f32 v9, v28, v29
	global_store_dwordx4 v195, v[6:9], s[56:57] offset:64 sc1
	v_cvt_pk_bf16_f32 v10, v10, v11
	v_cvt_pk_bf16_f32 v11, v12, v13
	v_cvt_pk_bf16_f32 v12, v22, v23
	v_cvt_pk_bf16_f32 v13, v24, v25
	global_store_dwordx4 v196, v[10:13], s[56:57] offset:64 sc1
	v_cvt_pk_bf16_f32 v14, v14, v15
	v_cvt_pk_bf16_f32 v15, v16, v17
	v_cvt_pk_bf16_f32 v16, v18, v19
	v_cvt_pk_bf16_f32 v17, v20, v21
	global_store_dwordx4 v197, v[14:17], s[56:57] offset:64 sc1

; __device__ __forceinline__ unsigned pk2(float lo, float hi) { return f2bf(lo) | (f2bf(hi) << 16); }
;     __device__ __forceinline__ void epi(const f32x4 (&acc)[2][2][4][2], const Unit& u, int wr, int wc, int fr, int fq) const {
;     ...
;                 for (int bj = 0; bj < 2; ++bj) { const int cofs = bj * 128;
;                     const f32x4 g0 = *(const f32x4*)(g1 + cofs * 4 + lcol * 4), g1v = *(const f32x4*)(g1 + cofs * 4 + lcol * 4 + 16);
;                     f32x4 x0, x1v;
;                     if (f32in) { x0 = *(const f32x4*)(xin + (ro + cofs) * 4 + loff4); x1v = *(const f32x4*)(xin + (ro + cofs) * 4 + loff4 + 16); }
;                     else { const u32x4 w = *(const u32x4*)(xin + (ro + cofs) * 2 + loff2); x0 = (f32x4){bflo(w.x), bfhi(w.x), bflo(w.y), bfhi(w.y)}; x1v = (f32x4){bflo(w.z), bfhi(w.z), bflo(w.w), bfhi(w.w)}; }
;                     const f32x4 o0 = x0 + g0 * acc[ai][bj][m][0], o1 = x1v + g1v * acc[ai][bj][m][1];
;                     u32x4 ow; ow.x = pk2(o0[0], o0[1]); ow.y = pk2(o0[2], o0[3]); ow.z = pk2(o1[0], o1[1]); ow.w = pk2(o1[2], o1[3]);
;                     *(u32x4*)(xo + (ro + cofs) * 2 + loff2) = ow; }
.LBB0_1779:
	s_waitcnt vmcnt(0)
	v_pk_fma_f32 v[126:127], v[126:127], v[134:135], v[142:143]
	v_pk_fma_f32 v[132:133], v[124:125], v[132:133], v[140:141]
	v_pk_fma_f32 v[124:125], v[122:123], v[130:131], v[138:139]
	v_pk_fma_f32 v[128:129], v[128:129], v[136:137], v[144:145]
	v_cvt_pk_bf16_f32 v122, v126, v127
	v_cvt_pk_bf16_f32 v123, v128, v129
	v_bfe_u32 v1, v124, 16, 1
	v_add3_u32 v1, v124, v1, s37
	v_bfe_u32 v124, v125, 16, 1
	s_add_u32 s12, s69, s42
	v_lshrrev_b32_e32 v1, 16, v1
	v_add3_u32 v124, v125, v124, s37
	s_addc_u32 s17, s70, s43
	v_and_or_b32 v124, v124, s33, v1
	s_add_u32 s24, s12, s44
	s_addc_u32 s25, s17, s45
	v_lshl_add_u64 v[160:161], s[24:25], 0, v[146:147]
	v_cvt_pk_bf16_f32 v125, v132, v133
	global_store_dwordx4 v[160:161], v[122:125], off sc1
	global_load_dwordx4 v[122:125], v[164:165], off offset:528
	s_nop 0
	global_load_dwordx4 v[126:129], v[164:165], off offset:512
	s_and_b64 vcc, exec, s[40:41]
	s_cbranch_vccnz .LBB0_1830
	global_load_dwordx4 v[130:133], v[162:163], off offset:528
	global_load_dwordx4 v[134:137], v[162:163], off offset:512
	s_cbranch_execnz .LBB0_1782

; __device__ __forceinline__ unsigned pk2(float lo, float hi) { return f2bf(lo) | (f2bf(hi) << 16); }
;     __device__ __forceinline__ void epi(const f32x4 (&acc)[2][2][4][2], const Unit& u, int wr, int wc, int fr, int fq) const {
;     ...
;                 for (int bj = 0; bj < 2; ++bj) { const int cofs = bj * 128;
;                     const f32x4 g0 = *(const f32x4*)(g1 + cofs * 4 + lcol * 4), g1v = *(const f32x4*)(g1 + cofs * 4 + lcol * 4 + 16);
;                     f32x4 x0, x1v;
;                     if (f32in) { x0 = *(const f32x4*)(xin + (ro + cofs) * 4 + loff4); x1v = *(const f32x4*)(xin + (ro + cofs) * 4 + loff4 + 16); }
;                     else { const u32x4 w = *(const u32x4*)(xin + (ro + cofs) * 2 + loff2); x0 = (f32x4){bflo(w.x), bfhi(w.x), bflo(w.y), bfhi(w.y)}; x1v = (f32x4){bflo(w.z), bfhi(w.z), bflo(w.w), bfhi(w.w)}; }
;                     const f32x4 o0 = x0 + g0 * acc[ai][bj][m][0], o1 = x1v + g1v * acc[ai][bj][m][1];
;                     u32x4 ow; ow.x = pk2(o0[0], o0[1]); ow.y = pk2(o0[2], o0[3]); ow.z = pk2(o1[0], o1[1]); ow.w = pk2(o1[2], o1[3]);
;                     *(u32x4*)(xo + (ro + cofs) * 2 + loff2) = ow; }
.LBB0_1782:
	s_waitcnt vmcnt(0)
	v_pk_fma_f32 v[118:119], v[118:119], v[126:127], v[134:135]
	v_pk_fma_f32 v[124:125], v[116:117], v[124:125], v[132:133]
	v_pk_fma_f32 v[116:117], v[114:115], v[122:123], v[130:131]
	v_pk_fma_f32 v[120:121], v[120:121], v[128:129], v[136:137]
	v_cvt_pk_bf16_f32 v114, v118, v119
	v_cvt_pk_bf16_f32 v115, v120, v121
	v_bfe_u32 v1, v116, 16, 1
	v_add3_u32 v1, v116, v1, s37
	v_bfe_u32 v116, v117, 16, 1
	v_lshrrev_b32_e32 v1, 16, v1
	v_add3_u32 v116, v117, v116, s37
	v_and_or_b32 v116, v116, s33, v1
	v_cvt_pk_bf16_f32 v117, v124, v125
	global_store_dwordx4 v[160:161], v[114:117], off offset:256 sc1
	global_load_dwordx4 v[114:117], v[164:165], off offset:16
	global_load_dwordx4 v[118:121], v[164:165], off
	s_and_b64 vcc, exec, s[40:41]
	s_cbranch_vccnz .LBB0_1831
	s_mov_b64 s[24:25], 0x20000
	v_add_co_u32_e32 v124, vcc, 0x20000, v162
	v_lshl_add_u64 v[122:123], v[162:163], 0, s[24:25]
	s_nop 0
	v_addc_co_u32_e32 v125, vcc, 0, v163, vcc
	global_load_dwordx4 v[126:129], v[124:125], off
	s_nop 0
	global_load_dwordx4 v[122:125], v[122:123], off offset:16
	s_cbranch_execnz .LBB0_1785

; __device__ __forceinline__ unsigned pk2(float lo, float hi) { return f2bf(lo) | (f2bf(hi) << 16); }
;     __device__ __forceinline__ void epi(const f32x4 (&acc)[2][2][4][2], const Unit& u, int wr, int wc, int fr, int fq) const {
;     ...
;                 for (int bj = 0; bj < 2; ++bj) { const int cofs = bj * 128;
;                     const f32x4 g0 = *(const f32x4*)(g1 + cofs * 4 + lcol * 4), g1v = *(const f32x4*)(g1 + cofs * 4 + lcol * 4 + 16);
;                     f32x4 x0, x1v;
;                     if (f32in) { x0 = *(const f32x4*)(xin + (ro + cofs) * 4 + loff4); x1v = *(const f32x4*)(xin + (ro + cofs) * 4 + loff4 + 16); }
;                     else { const u32x4 w = *(const u32x4*)(xin + (ro + cofs) * 2 + loff2); x0 = (f32x4){bflo(w.x), bfhi(w.x), bflo(w.y), bfhi(w.y)}; x1v = (f32x4){bflo(w.z), bfhi(w.z), bflo(w.w), bfhi(w.w)}; }
;                     const f32x4 o0 = x0 + g0 * acc[ai][bj][m][0], o1 = x1v + g1v * acc[ai][bj][m][1];
;                     u32x4 ow; ow.x = pk2(o0[0], o0[1]); ow.y = pk2(o0[2], o0[3]); ow.z = pk2(o1[0], o1[1]); ow.w = pk2(o1[2], o1[3]);
;                     *(u32x4*)(xo + (ro + cofs) * 2 + loff2) = ow; }
.LBB0_1785:
	s_waitcnt vmcnt(0)
	v_pk_fma_f32 v[110:111], v[110:111], v[118:119], v[126:127]
	v_pk_fma_f32 v[116:117], v[108:109], v[116:117], v[124:125]
	v_pk_fma_f32 v[108:109], v[106:107], v[114:115], v[122:123]
	v_pk_fma_f32 v[112:113], v[112:113], v[120:121], v[128:129]
	v_cvt_pk_bf16_f32 v106, v110, v111
	v_cvt_pk_bf16_f32 v107, v112, v113
	v_bfe_u32 v1, v108, 16, 1
	v_add3_u32 v1, v108, v1, s37
	v_bfe_u32 v108, v109, 16, 1
	v_lshrrev_b32_e32 v1, 16, v1
	v_add3_u32 v108, v109, v108, s37
	v_and_or_b32 v108, v108, s33, v1
	v_add_co_u32_e32 v110, vcc, 0x10000, v160
	v_cvt_pk_bf16_f32 v109, v116, v117
	s_nop 0
	v_addc_co_u32_e32 v111, vcc, 0, v161, vcc
	global_store_dwordx4 v[110:111], v[106:109], off sc1
	global_load_dwordx4 v[106:109], v[164:165], off offset:528
	s_nop 0
	global_load_dwordx4 v[110:113], v[164:165], off offset:512
	s_and_b64 vcc, exec, s[40:41]
	s_cbranch_vccnz .LBB0_1832
	s_mov_b64 s[24:25], 0x20200
	v_add_co_u32_e32 v116, vcc, 0x20000, v162
	v_lshl_add_u64 v[114:115], v[162:163], 0, s[24:25]
	s_nop 0
	v_addc_co_u32_e32 v117, vcc, 0, v163, vcc
	global_load_dwordx4 v[118:121], v[116:117], off offset:512
	s_nop 0
	global_load_dwordx4 v[114:117], v[114:115], off offset:16
	s_cbranch_execnz .LBB0_1788

; __device__ __forceinline__ unsigned pk2(float lo, float hi) { return f2bf(lo) | (f2bf(hi) << 16); }
;     __device__ __forceinline__ void epi(const f32x4 (&acc)[2][2][4][2], const Unit& u, int wr, int wc, int fr, int fq) const {
;     ...
;                 for (int bj = 0; bj < 2; ++bj) { const int cofs = bj * 128;
;                     const f32x4 g0 = *(const f32x4*)(g1 + cofs * 4 + lcol * 4), g1v = *(const f32x4*)(g1 + cofs * 4 + lcol * 4 + 16);
;                     f32x4 x0, x1v;
;                     if (f32in) { x0 = *(const f32x4*)(xin + (ro + cofs) * 4 + loff4); x1v = *(const f32x4*)(xin + (ro + cofs) * 4 + loff4 + 16); }
;                     else { const u32x4 w = *(const u32x4*)(xin + (ro + cofs) * 2 + loff2); x0 = (f32x4){bflo(w.x), bfhi(w.x), bflo(w.y), bfhi(w.y)}; x1v = (f32x4){bflo(w.z), bfhi(w.z), bflo(w.w), bfhi(w.w)}; }
;                     const f32x4 o0 = x0 + g0 * acc[ai][bj][m][0], o1 = x1v + g1v * acc[ai][bj][m][1];
;                     u32x4 ow; ow.x = pk2(o0[0], o0[1]); ow.y = pk2(o0[2], o0[3]); ow.z = pk2(o1[0], o1[1]); ow.w = pk2(o1[2], o1[3]);
;                     *(u32x4*)(xo + (ro + cofs) * 2 + loff2) = ow; }
.LBB0_1788:
	s_waitcnt vmcnt(0)
	v_pk_fma_f32 v[102:103], v[102:103], v[110:111], v[118:119]
	v_pk_fma_f32 v[108:109], v[100:101], v[108:109], v[116:117]
	v_pk_fma_f32 v[100:101], v[98:99], v[106:107], v[114:115]
	v_pk_fma_f32 v[104:105], v[104:105], v[112:113], v[120:121]
	v_cvt_pk_bf16_f32 v98, v102, v103
	v_cvt_pk_bf16_f32 v99, v104, v105
	v_bfe_u32 v1, v100, 16, 1
	v_add3_u32 v1, v100, v1, s37
	v_bfe_u32 v100, v101, 16, 1
	v_lshrrev_b32_e32 v1, 16, v1
	v_add3_u32 v100, v101, v100, s37
	v_and_or_b32 v100, v100, s33, v1
	v_add_co_u32_e32 v102, vcc, 0x10000, v160
	v_cvt_pk_bf16_f32 v101, v108, v109
	s_nop 0
	v_addc_co_u32_e32 v103, vcc, 0, v161, vcc
	global_store_dwordx4 v[102:103], v[98:101], off offset:256 sc1
	global_load_dwordx4 v[98:101], v[164:165], off offset:16
	global_load_dwordx4 v[102:105], v[164:165], off
	s_and_b64 vcc, exec, s[40:41]
	s_cbranch_vccnz .LBB0_1833
	s_mov_b64 s[24:25], 0x40000
	v_add_co_u32_e32 v108, vcc, 0x40000, v162
	v_lshl_add_u64 v[106:107], v[162:163], 0, s[24:25]
	s_nop 0
	v_addc_co_u32_e32 v109, vcc, 0, v163, vcc
	global_load_dwordx4 v[110:113], v[108:109], off
	s_nop 0
	global_load_dwordx4 v[106:109], v[106:107], off offset:16
	s_cbranch_execnz .LBB0_1791

; __device__ __forceinline__ unsigned pk2(float lo, float hi) { return f2bf(lo) | (f2bf(hi) << 16); }
;     __device__ __forceinline__ void epi(const f32x4 (&acc)[2][2][4][2], const Unit& u, int wr, int wc, int fr, int fq) const {
;     ...
;                 for (int bj = 0; bj < 2; ++bj) { const int cofs = bj * 128;
;                     const f32x4 g0 = *(const f32x4*)(g1 + cofs * 4 + lcol * 4), g1v = *(const f32x4*)(g1 + cofs * 4 + lcol * 4 + 16);
;                     f32x4 x0, x1v;
;                     if (f32in) { x0 = *(const f32x4*)(xin + (ro + cofs) * 4 + loff4); x1v = *(const f32x4*)(xin + (ro + cofs) * 4 + loff4 + 16); }
;                     else { const u32x4 w = *(const u32x4*)(xin + (ro + cofs) * 2 + loff2); x0 = (f32x4){bflo(w.x), bfhi(w.x), bflo(w.y), bfhi(w.y)}; x1v = (f32x4){bflo(w.z), bfhi(w.z), bflo(w.w), bfhi(w.w)}; }
;                     const f32x4 o0 = x0 + g0 * acc[ai][bj][m][0], o1 = x1v + g1v * acc[ai][bj][m][1];
;                     u32x4 ow; ow.x = pk2(o0[0], o0[1]); ow.y = pk2(o0[2], o0[3]); ow.z = pk2(o1[0], o1[1]); ow.w = pk2(o1[2], o1[3]);
;                     *(u32x4*)(xo + (ro + cofs) * 2 + loff2) = ow; }
.LBB0_1791:
	s_waitcnt vmcnt(0)
	v_pk_fma_f32 v[94:95], v[94:95], v[102:103], v[110:111]
	v_pk_fma_f32 v[100:101], v[92:93], v[100:101], v[108:109]
	v_pk_fma_f32 v[92:93], v[90:91], v[98:99], v[106:107]
	v_pk_fma_f32 v[96:97], v[96:97], v[104:105], v[112:113]
	v_cvt_pk_bf16_f32 v90, v94, v95
	v_cvt_pk_bf16_f32 v91, v96, v97
	v_bfe_u32 v1, v92, 16, 1
	v_add3_u32 v1, v92, v1, s37
	v_bfe_u32 v92, v93, 16, 1
	v_lshrrev_b32_e32 v1, 16, v1
	v_add3_u32 v92, v93, v92, s37
	v_and_or_b32 v92, v92, s33, v1
	v_add_co_u32_e32 v94, vcc, 0x20000, v160
	v_cvt_pk_bf16_f32 v93, v100, v101
	s_nop 0
	v_addc_co_u32_e32 v95, vcc, 0, v161, vcc
	global_store_dwordx4 v[94:95], v[90:93], off sc1
	global_load_dwordx4 v[90:93], v[164:165], off offset:528
	s_nop 0
	global_load_dwordx4 v[94:97], v[164:165], off offset:512
	s_and_b64 vcc, exec, s[40:41]
	s_cbranch_vccnz .LBB0_1834
	s_mov_b64 s[24:25], 0x40200
	v_add_co_u32_e32 v100, vcc, 0x40000, v162
	v_lshl_add_u64 v[98:99], v[162:163], 0, s[24:25]
	s_nop 0
	v_addc_co_u32_e32 v101, vcc, 0, v163, vcc
	global_load_dwordx4 v[102:105], v[100:101], off offset:512
	s_nop 0
	global_load_dwordx4 v[98:101], v[98:99], off offset:16
	s_cbranch_execnz .LBB0_1794

; __device__ __forceinline__ unsigned pk2(float lo, float hi) { return f2bf(lo) | (f2bf(hi) << 16); }
;     __device__ __forceinline__ void epi(const f32x4 (&acc)[2][2][4][2], const Unit& u, int wr, int wc, int fr, int fq) const {
;     ...
;                 for (int bj = 0; bj < 2; ++bj) { const int cofs = bj * 128;
;                     const f32x4 g0 = *(const f32x4*)(g1 + cofs * 4 + lcol * 4), g1v = *(const f32x4*)(g1 + cofs * 4 + lcol * 4 + 16);
;                     f32x4 x0, x1v;
;                     if (f32in) { x0 = *(const f32x4*)(xin + (ro + cofs) * 4 + loff4); x1v = *(const f32x4*)(xin + (ro + cofs) * 4 + loff4 + 16); }
;                     else { const u32x4 w = *(const u32x4*)(xin + (ro + cofs) * 2 + loff2); x0 = (f32x4){bflo(w.x), bfhi(w.x), bflo(w.y), bfhi(w.y)}; x1v = (f32x4){bflo(w.z), bfhi(w.z), bflo(w.w), bfhi(w.w)}; }
;                     const f32x4 o0 = x0 + g0 * acc[ai][bj][m][0], o1 = x1v + g1v * acc[ai][bj][m][1];
;                     u32x4 ow; ow.x = pk2(o0[0], o0[1]); ow.y = pk2(o0[2], o0[3]); ow.z = pk2(o1[0], o1[1]); ow.w = pk2(o1[2], o1[3]);
;                     *(u32x4*)(xo + (ro + cofs) * 2 + loff2) = ow; }
.LBB0_1794:
	s_waitcnt vmcnt(0)
	v_pk_fma_f32 v[86:87], v[86:87], v[94:95], v[102:103]
	v_pk_fma_f32 v[92:93], v[84:85], v[92:93], v[100:101]
	v_pk_fma_f32 v[84:85], v[82:83], v[90:91], v[98:99]
	v_pk_fma_f32 v[88:89], v[88:89], v[96:97], v[104:105]
	v_cvt_pk_bf16_f32 v82, v86, v87
	v_cvt_pk_bf16_f32 v83, v88, v89
	v_bfe_u32 v1, v84, 16, 1
	v_add3_u32 v1, v84, v1, s37
	v_bfe_u32 v84, v85, 16, 1
	v_lshrrev_b32_e32 v1, 16, v1
	v_add3_u32 v84, v85, v84, s37
	v_and_or_b32 v84, v84, s33, v1
	v_add_co_u32_e32 v86, vcc, 0x20000, v160
	v_cvt_pk_bf16_f32 v85, v92, v93
	s_nop 0
	v_addc_co_u32_e32 v87, vcc, 0, v161, vcc
	global_store_dwordx4 v[86:87], v[82:85], off offset:256 sc1
	global_load_dwordx4 v[82:85], v[164:165], off offset:16
	global_load_dwordx4 v[86:89], v[164:165], off
	s_and_b64 vcc, exec, s[40:41]
	s_cbranch_vccnz .LBB0_1835
	s_mov_b64 s[24:25], 0x60000
	v_add_co_u32_e32 v92, vcc, 0x60000, v162
	v_lshl_add_u64 v[90:91], v[162:163], 0, s[24:25]
	s_nop 0
	v_addc_co_u32_e32 v93, vcc, 0, v163, vcc
	global_load_dwordx4 v[94:97], v[92:93], off
	s_nop 0
	global_load_dwordx4 v[90:93], v[90:91], off offset:16
	s_cbranch_execnz .LBB0_1797

; __device__ __forceinline__ unsigned pk2(float lo, float hi) { return f2bf(lo) | (f2bf(hi) << 16); }
;     __device__ __forceinline__ void epi(const f32x4 (&acc)[2][2][4][2], const Unit& u, int wr, int wc, int fr, int fq) const {
;     ...
;                 for (int bj = 0; bj < 2; ++bj) { const int cofs = bj * 128;
;                     const f32x4 g0 = *(const f32x4*)(g1 + cofs * 4 + lcol * 4), g1v = *(const f32x4*)(g1 + cofs * 4 + lcol * 4 + 16);
;                     f32x4 x0, x1v;
;                     if (f32in) { x0 = *(const f32x4*)(xin + (ro + cofs) * 4 + loff4); x1v = *(const f32x4*)(xin + (ro + cofs) * 4 + loff4 + 16); }
;                     else { const u32x4 w = *(const u32x4*)(xin + (ro + cofs) * 2 + loff2); x0 = (f32x4){bflo(w.x), bfhi(w.x), bflo(w.y), bfhi(w.y)}; x1v = (f32x4){bflo(w.z), bfhi(w.z), bflo(w.w), bfhi(w.w)}; }
;                     const f32x4 o0 = x0 + g0 * acc[ai][bj][m][0], o1 = x1v + g1v * acc[ai][bj][m][1];
;                     u32x4 ow; ow.x = pk2(o0[0], o0[1]); ow.y = pk2(o0[2], o0[3]); ow.z = pk2(o1[0], o1[1]); ow.w = pk2(o1[2], o1[3]);
;                     *(u32x4*)(xo + (ro + cofs) * 2 + loff2) = ow; }
.LBB0_1797:
	s_waitcnt vmcnt(0)
	v_pk_fma_f32 v[78:79], v[78:79], v[86:87], v[94:95]
	v_pk_fma_f32 v[84:85], v[76:77], v[84:85], v[92:93]
	v_pk_fma_f32 v[76:77], v[74:75], v[82:83], v[90:91]
	v_pk_fma_f32 v[80:81], v[80:81], v[88:89], v[96:97]
	v_cvt_pk_bf16_f32 v74, v78, v79
	v_cvt_pk_bf16_f32 v75, v80, v81
	v_bfe_u32 v1, v76, 16, 1
	v_add3_u32 v1, v76, v1, s37
	v_bfe_u32 v76, v77, 16, 1
	v_lshrrev_b32_e32 v1, 16, v1
	v_add3_u32 v76, v77, v76, s37
	v_and_or_b32 v76, v76, s33, v1
	v_add_co_u32_e32 v78, vcc, 0x30000, v160
	v_cvt_pk_bf16_f32 v77, v84, v85
	s_nop 0
	v_addc_co_u32_e32 v79, vcc, 0, v161, vcc
	global_store_dwordx4 v[78:79], v[74:77], off sc1
	global_load_dwordx4 v[74:77], v[164:165], off offset:528
	s_nop 0
	global_load_dwordx4 v[78:81], v[164:165], off offset:512
	s_and_b64 vcc, exec, s[40:41]
	s_cbranch_vccnz .LBB0_1836
	s_mov_b64 s[24:25], 0x60200
	v_add_co_u32_e32 v84, vcc, 0x60000, v162
	v_lshl_add_u64 v[82:83], v[162:163], 0, s[24:25]
	s_nop 0
	v_addc_co_u32_e32 v85, vcc, 0, v163, vcc
	global_load_dwordx4 v[86:89], v[84:85], off offset:512
	s_nop 0
	global_load_dwordx4 v[82:85], v[82:83], off offset:16
	s_cbranch_execnz .LBB0_1800

; __device__ __forceinline__ unsigned pk2(float lo, float hi) { return f2bf(lo) | (f2bf(hi) << 16); }
;     __device__ __forceinline__ void epi(const f32x4 (&acc)[2][2][4][2], const Unit& u, int wr, int wc, int fr, int fq) const {
;     ...
;                 for (int bj = 0; bj < 2; ++bj) { const int cofs = bj * 128;
;                     const f32x4 g0 = *(const f32x4*)(g1 + cofs * 4 + lcol * 4), g1v = *(const f32x4*)(g1 + cofs * 4 + lcol * 4 + 16);
;                     f32x4 x0, x1v;
;                     if (f32in) { x0 = *(const f32x4*)(xin + (ro + cofs) * 4 + loff4); x1v = *(const f32x4*)(xin + (ro + cofs) * 4 + loff4 + 16); }
;                     else { const u32x4 w = *(const u32x4*)(xin + (ro + cofs) * 2 + loff2); x0 = (f32x4){bflo(w.x), bfhi(w.x), bflo(w.y), bfhi(w.y)}; x1v = (f32x4){bflo(w.z), bfhi(w.z), bflo(w.w), bfhi(w.w)}; }
;                     const f32x4 o0 = x0 + g0 * acc[ai][bj][m][0], o1 = x1v + g1v * acc[ai][bj][m][1];
;                     u32x4 ow; ow.x = pk2(o0[0], o0[1]); ow.y = pk2(o0[2], o0[3]); ow.z = pk2(o1[0], o1[1]); ow.w = pk2(o1[2], o1[3]);
;                     *(u32x4*)(xo + (ro + cofs) * 2 + loff2) = ow; }
.LBB0_1800:
	s_waitcnt vmcnt(0)
	v_pk_fma_f32 v[70:71], v[70:71], v[78:79], v[86:87]
	v_pk_fma_f32 v[76:77], v[68:69], v[76:77], v[84:85]
	v_pk_fma_f32 v[68:69], v[66:67], v[74:75], v[82:83]
	v_pk_fma_f32 v[72:73], v[72:73], v[80:81], v[88:89]
	v_cvt_pk_bf16_f32 v66, v70, v71
	v_cvt_pk_bf16_f32 v67, v72, v73
	v_bfe_u32 v1, v68, 16, 1
	v_add3_u32 v1, v68, v1, s37
	v_bfe_u32 v68, v69, 16, 1
	v_lshrrev_b32_e32 v1, 16, v1
	v_add3_u32 v68, v69, v68, s37
	v_and_or_b32 v68, v68, s33, v1
	v_add_co_u32_e32 v70, vcc, 0x30000, v160
	v_cvt_pk_bf16_f32 v69, v76, v77
	s_nop 0
	v_addc_co_u32_e32 v71, vcc, 0, v161, vcc
	global_store_dwordx4 v[70:71], v[66:69], off offset:256 sc1
	global_load_dwordx4 v[66:69], v[164:165], off offset:16
	global_load_dwordx4 v[70:73], v[164:165], off
	s_and_b64 vcc, exec, s[40:41]
	s_cbranch_vccnz .LBB0_1837
	s_mov_b64 s[24:25], 0x100000
	v_add_co_u32_e32 v76, vcc, 0x100000, v162
	v_lshl_add_u64 v[74:75], v[162:163], 0, s[24:25]
	s_nop 0
	v_addc_co_u32_e32 v77, vcc, 0, v163, vcc
	global_load_dwordx4 v[78:81], v[76:77], off
	s_nop 0
	global_load_dwordx4 v[74:77], v[74:75], off offset:16
	s_cbranch_execnz .LBB0_1803

; __device__ __forceinline__ unsigned pk2(float lo, float hi) { return f2bf(lo) | (f2bf(hi) << 16); }
;     __device__ __forceinline__ void epi(const f32x4 (&acc)[2][2][4][2], const Unit& u, int wr, int wc, int fr, int fq) const {
;     ...
;                 for (int bj = 0; bj < 2; ++bj) { const int cofs = bj * 128;
;                     const f32x4 g0 = *(const f32x4*)(g1 + cofs * 4 + lcol * 4), g1v = *(const f32x4*)(g1 + cofs * 4 + lcol * 4 + 16);
;                     f32x4 x0, x1v;
;                     if (f32in) { x0 = *(const f32x4*)(xin + (ro + cofs) * 4 + loff4); x1v = *(const f32x4*)(xin + (ro + cofs) * 4 + loff4 + 16); }
;                     else { const u32x4 w = *(const u32x4*)(xin + (ro + cofs) * 2 + loff2); x0 = (f32x4){bflo(w.x), bfhi(w.x), bflo(w.y), bfhi(w.y)}; x1v = (f32x4){bflo(w.z), bfhi(w.z), bflo(w.w), bfhi(w.w)}; }
;                     const f32x4 o0 = x0 + g0 * acc[ai][bj][m][0], o1 = x1v + g1v * acc[ai][bj][m][1];
;                     u32x4 ow; ow.x = pk2(o0[0], o0[1]); ow.y = pk2(o0[2], o0[3]); ow.z = pk2(o1[0], o1[1]); ow.w = pk2(o1[2], o1[3]);
;                     *(u32x4*)(xo + (ro + cofs) * 2 + loff2) = ow; }
.LBB0_1803:
	s_waitcnt vmcnt(0)
	v_pk_fma_f32 v[62:63], v[62:63], v[70:71], v[78:79]
	v_pk_fma_f32 v[68:69], v[60:61], v[68:69], v[76:77]
	v_pk_fma_f32 v[60:61], v[58:59], v[66:67], v[74:75]
	v_pk_fma_f32 v[64:65], v[64:65], v[72:73], v[80:81]
	v_cvt_pk_bf16_f32 v58, v62, v63
	v_cvt_pk_bf16_f32 v59, v64, v65
	v_bfe_u32 v1, v60, 16, 1
	v_add3_u32 v1, v60, v1, s37
	v_bfe_u32 v60, v61, 16, 1
	v_lshrrev_b32_e32 v1, 16, v1
	v_add3_u32 v60, v61, v60, s37
	v_and_or_b32 v60, v60, s33, v1
	v_add_co_u32_e32 v62, vcc, 0x80000, v160
	v_cvt_pk_bf16_f32 v61, v68, v69
	s_nop 0
	v_addc_co_u32_e32 v63, vcc, 0, v161, vcc
	global_store_dwordx4 v[62:63], v[58:61], off sc1
	global_load_dwordx4 v[58:61], v[164:165], off offset:528
	s_nop 0
	global_load_dwordx4 v[62:65], v[164:165], off offset:512
	s_and_b64 vcc, exec, s[40:41]
	s_cbranch_vccnz .LBB0_1838
	s_mov_b64 s[24:25], 0x100200
	v_add_co_u32_e32 v68, vcc, 0x100000, v162
	v_lshl_add_u64 v[66:67], v[162:163], 0, s[24:25]
	s_nop 0
	v_addc_co_u32_e32 v69, vcc, 0, v163, vcc
	global_load_dwordx4 v[70:73], v[68:69], off offset:512
	s_nop 0
	global_load_dwordx4 v[66:69], v[66:67], off offset:16
	s_cbranch_execnz .LBB0_1806

; __device__ __forceinline__ unsigned pk2(float lo, float hi) { return f2bf(lo) | (f2bf(hi) << 16); }
;     __device__ __forceinline__ void epi(const f32x4 (&acc)[2][2][4][2], const Unit& u, int wr, int wc, int fr, int fq) const {
;     ...
;                 for (int bj = 0; bj < 2; ++bj) { const int cofs = bj * 128;
;                     const f32x4 g0 = *(const f32x4*)(g1 + cofs * 4 + lcol * 4), g1v = *(const f32x4*)(g1 + cofs * 4 + lcol * 4 + 16);
;                     f32x4 x0, x1v;
;                     if (f32in) { x0 = *(const f32x4*)(xin + (ro + cofs) * 4 + loff4); x1v = *(const f32x4*)(xin + (ro + cofs) * 4 + loff4 + 16); }
;                     else { const u32x4 w = *(const u32x4*)(xin + (ro + cofs) * 2 + loff2); x0 = (f32x4){bflo(w.x), bfhi(w.x), bflo(w.y), bfhi(w.y)}; x1v = (f32x4){bflo(w.z), bfhi(w.z), bflo(w.w), bfhi(w.w)}; }
;                     const f32x4 o0 = x0 + g0 * acc[ai][bj][m][0], o1 = x1v + g1v * acc[ai][bj][m][1];
;                     u32x4 ow; ow.x = pk2(o0[0], o0[1]); ow.y = pk2(o0[2], o0[3]); ow.z = pk2(o1[0], o1[1]); ow.w = pk2(o1[2], o1[3]);
;                     *(u32x4*)(xo + (ro + cofs) * 2 + loff2) = ow; }
.LBB0_1806:
	s_waitcnt vmcnt(0)
	v_pk_fma_f32 v[54:55], v[54:55], v[62:63], v[70:71]
	v_pk_fma_f32 v[60:61], v[52:53], v[60:61], v[68:69]
	v_pk_fma_f32 v[52:53], v[50:51], v[58:59], v[66:67]
	v_pk_fma_f32 v[56:57], v[56:57], v[64:65], v[72:73]
	v_cvt_pk_bf16_f32 v50, v54, v55
	v_cvt_pk_bf16_f32 v51, v56, v57
	v_bfe_u32 v1, v52, 16, 1
	v_add3_u32 v1, v52, v1, s37
	v_bfe_u32 v52, v53, 16, 1
	v_lshrrev_b32_e32 v1, 16, v1
	v_add3_u32 v52, v53, v52, s37
	v_and_or_b32 v52, v52, s33, v1
	v_add_co_u32_e32 v54, vcc, 0x80000, v160
	v_cvt_pk_bf16_f32 v53, v60, v61
	s_nop 0
	v_addc_co_u32_e32 v55, vcc, 0, v161, vcc
	global_store_dwordx4 v[54:55], v[50:53], off offset:256 sc1
	global_load_dwordx4 v[50:53], v[164:165], off offset:16
	global_load_dwordx4 v[54:57], v[164:165], off
	s_and_b64 vcc, exec, s[40:41]
	s_cbranch_vccnz .LBB0_1839
	s_mov_b64 s[24:25], 0x120000
	v_add_co_u32_e32 v60, vcc, 0x120000, v162
	v_lshl_add_u64 v[58:59], v[162:163], 0, s[24:25]
	s_nop 0
	v_addc_co_u32_e32 v61, vcc, 0, v163, vcc
	global_load_dwordx4 v[62:65], v[60:61], off
	s_nop 0
	global_load_dwordx4 v[58:61], v[58:59], off offset:16
	s_cbranch_execnz .LBB0_1809

; __device__ __forceinline__ unsigned pk2(float lo, float hi) { return f2bf(lo) | (f2bf(hi) << 16); }
;     __device__ __forceinline__ void epi(const f32x4 (&acc)[2][2][4][2], const Unit& u, int wr, int wc, int fr, int fq) const {
;     ...
;                 for (int bj = 0; bj < 2; ++bj) { const int cofs = bj * 128;
;                     const f32x4 g0 = *(const f32x4*)(g1 + cofs * 4 + lcol * 4), g1v = *(const f32x4*)(g1 + cofs * 4 + lcol * 4 + 16);
;                     f32x4 x0, x1v;
;                     if (f32in) { x0 = *(const f32x4*)(xin + (ro + cofs) * 4 + loff4); x1v = *(const f32x4*)(xin + (ro + cofs) * 4 + loff4 + 16); }
;                     else { const u32x4 w = *(const u32x4*)(xin + (ro + cofs) * 2 + loff2); x0 = (f32x4){bflo(w.x), bfhi(w.x), bflo(w.y), bfhi(w.y)}; x1v = (f32x4){bflo(w.z), bfhi(w.z), bflo(w.w), bfhi(w.w)}; }
;                     const f32x4 o0 = x0 + g0 * acc[ai][bj][m][0], o1 = x1v + g1v * acc[ai][bj][m][1];
;                     u32x4 ow; ow.x = pk2(o0[0], o0[1]); ow.y = pk2(o0[2], o0[3]); ow.z = pk2(o1[0], o1[1]); ow.w = pk2(o1[2], o1[3]);
;                     *(u32x4*)(xo + (ro + cofs) * 2 + loff2) = ow; }
.LBB0_1809:
	s_waitcnt vmcnt(0)
	v_pk_fma_f32 v[46:47], v[46:47], v[54:55], v[62:63]
	v_pk_fma_f32 v[52:53], v[44:45], v[52:53], v[60:61]
	v_pk_fma_f32 v[44:45], v[42:43], v[50:51], v[58:59]
	v_pk_fma_f32 v[48:49], v[48:49], v[56:57], v[64:65]
	v_cvt_pk_bf16_f32 v42, v46, v47
	v_cvt_pk_bf16_f32 v43, v48, v49
	v_bfe_u32 v1, v44, 16, 1
	v_add3_u32 v1, v44, v1, s37
	v_bfe_u32 v44, v45, 16, 1
	v_lshrrev_b32_e32 v1, 16, v1
	v_add3_u32 v44, v45, v44, s37
	v_and_or_b32 v44, v44, s33, v1
	v_add_co_u32_e32 v46, vcc, 0x90000, v160
	v_cvt_pk_bf16_f32 v45, v52, v53
	s_nop 0
	v_addc_co_u32_e32 v47, vcc, 0, v161, vcc
	global_store_dwordx4 v[46:47], v[42:45], off sc1
	global_load_dwordx4 v[42:45], v[164:165], off offset:528
	s_nop 0
	global_load_dwordx4 v[46:49], v[164:165], off offset:512
	s_and_b64 vcc, exec, s[40:41]
	s_cbranch_vccnz .LBB0_1840
	s_mov_b64 s[24:25], 0x120200
	v_add_co_u32_e32 v52, vcc, 0x120000, v162
	v_lshl_add_u64 v[50:51], v[162:163], 0, s[24:25]
	s_nop 0
	v_addc_co_u32_e32 v53, vcc, 0, v163, vcc
	global_load_dwordx4 v[54:57], v[52:53], off offset:512
	s_nop 0
	global_load_dwordx4 v[50:53], v[50:51], off offset:16
	s_cbranch_execnz .LBB0_1812

; __device__ __forceinline__ unsigned pk2(float lo, float hi) { return f2bf(lo) | (f2bf(hi) << 16); }
;     __device__ __forceinline__ void epi(const f32x4 (&acc)[2][2][4][2], const Unit& u, int wr, int wc, int fr, int fq) const {
;     ...
;                 for (int bj = 0; bj < 2; ++bj) { const int cofs = bj * 128;
;                     const f32x4 g0 = *(const f32x4*)(g1 + cofs * 4 + lcol * 4), g1v = *(const f32x4*)(g1 + cofs * 4 + lcol * 4 + 16);
;                     f32x4 x0, x1v;
;                     if (f32in) { x0 = *(const f32x4*)(xin + (ro + cofs) * 4 + loff4); x1v = *(const f32x4*)(xin + (ro + cofs) * 4 + loff4 + 16); }
;                     else { const u32x4 w = *(const u32x4*)(xin + (ro + cofs) * 2 + loff2); x0 = (f32x4){bflo(w.x), bfhi(w.x), bflo(w.y), bfhi(w.y)}; x1v = (f32x4){bflo(w.z), bfhi(w.z), bflo(w.w), bfhi(w.w)}; }
;                     const f32x4 o0 = x0 + g0 * acc[ai][bj][m][0], o1 = x1v + g1v * acc[ai][bj][m][1];
;                     u32x4 ow; ow.x = pk2(o0[0], o0[1]); ow.y = pk2(o0[2], o0[3]); ow.z = pk2(o1[0], o1[1]); ow.w = pk2(o1[2], o1[3]);
;                     *(u32x4*)(xo + (ro + cofs) * 2 + loff2) = ow; }
.LBB0_1812:
	s_waitcnt vmcnt(0)
	v_pk_fma_f32 v[38:39], v[38:39], v[46:47], v[54:55]
	v_pk_fma_f32 v[44:45], v[36:37], v[44:45], v[52:53]
	v_pk_fma_f32 v[36:37], v[34:35], v[42:43], v[50:51]
	v_pk_fma_f32 v[40:41], v[40:41], v[48:49], v[56:57]
	v_cvt_pk_bf16_f32 v34, v38, v39
	v_cvt_pk_bf16_f32 v35, v40, v41
	v_bfe_u32 v1, v36, 16, 1
	v_add3_u32 v1, v36, v1, s37
	v_bfe_u32 v36, v37, 16, 1
	v_lshrrev_b32_e32 v1, 16, v1
	v_add3_u32 v36, v37, v36, s37
	v_and_or_b32 v36, v36, s33, v1
	v_add_co_u32_e32 v38, vcc, 0x90000, v160
	v_cvt_pk_bf16_f32 v37, v44, v45
	s_nop 0
	v_addc_co_u32_e32 v39, vcc, 0, v161, vcc
	global_store_dwordx4 v[38:39], v[34:37], off offset:256 sc1
	global_load_dwordx4 v[34:37], v[164:165], off offset:16
	global_load_dwordx4 v[38:41], v[164:165], off
	s_and_b64 vcc, exec, s[40:41]
	s_cbranch_vccnz .LBB0_1841
	s_mov_b64 s[24:25], 0x140000
	v_add_co_u32_e32 v44, vcc, 0x140000, v162
	v_lshl_add_u64 v[42:43], v[162:163], 0, s[24:25]
	s_nop 0
	v_addc_co_u32_e32 v45, vcc, 0, v163, vcc
	global_load_dwordx4 v[46:49], v[44:45], off
	s_nop 0
	global_load_dwordx4 v[42:45], v[42:43], off offset:16
	s_cbranch_execnz .LBB0_1815

; __device__ __forceinline__ unsigned pk2(float lo, float hi) { return f2bf(lo) | (f2bf(hi) << 16); }
;     __device__ __forceinline__ void epi(const f32x4 (&acc)[2][2][4][2], const Unit& u, int wr, int wc, int fr, int fq) const {
;     ...
;                 for (int bj = 0; bj < 2; ++bj) { const int cofs = bj * 128;
;                     const f32x4 g0 = *(const f32x4*)(g1 + cofs * 4 + lcol * 4), g1v = *(const f32x4*)(g1 + cofs * 4 + lcol * 4 + 16);
;                     f32x4 x0, x1v;
;                     if (f32in) { x0 = *(const f32x4*)(xin + (ro + cofs) * 4 + loff4); x1v = *(const f32x4*)(xin + (ro + cofs) * 4 + loff4 + 16); }
;                     else { const u32x4 w = *(const u32x4*)(xin + (ro + cofs) * 2 + loff2); x0 = (f32x4){bflo(w.x), bfhi(w.x), bflo(w.y), bfhi(w.y)}; x1v = (f32x4){bflo(w.z), bfhi(w.z), bflo(w.w), bfhi(w.w)}; }
;                     const f32x4 o0 = x0 + g0 * acc[ai][bj][m][0], o1 = x1v + g1v * acc[ai][bj][m][1];
;                     u32x4 ow; ow.x = pk2(o0[0], o0[1]); ow.y = pk2(o0[2], o0[3]); ow.z = pk2(o1[0], o1[1]); ow.w = pk2(o1[2], o1[3]);
;                     *(u32x4*)(xo + (ro + cofs) * 2 + loff2) = ow; }
.LBB0_1815:
	s_waitcnt vmcnt(0)
	v_pk_fma_f32 v[30:31], v[30:31], v[38:39], v[46:47]
	v_pk_fma_f32 v[36:37], v[28:29], v[36:37], v[44:45]
	v_pk_fma_f32 v[28:29], v[26:27], v[34:35], v[42:43]
	v_pk_fma_f32 v[32:33], v[32:33], v[40:41], v[48:49]
	v_cvt_pk_bf16_f32 v26, v30, v31
	v_cvt_pk_bf16_f32 v27, v32, v33
	v_bfe_u32 v1, v28, 16, 1
	v_add3_u32 v1, v28, v1, s37
	v_bfe_u32 v28, v29, 16, 1
	v_lshrrev_b32_e32 v1, 16, v1
	v_add3_u32 v28, v29, v28, s37
	v_and_or_b32 v28, v28, s33, v1
	v_add_co_u32_e32 v30, vcc, 0xa0000, v160
	v_cvt_pk_bf16_f32 v29, v36, v37
	s_nop 0
	v_addc_co_u32_e32 v31, vcc, 0, v161, vcc
	global_store_dwordx4 v[30:31], v[26:29], off sc1
	global_load_dwordx4 v[26:29], v[164:165], off offset:528
	s_nop 0
	global_load_dwordx4 v[30:33], v[164:165], off offset:512
	s_and_b64 vcc, exec, s[40:41]
	s_cbranch_vccnz .LBB0_1842
	s_mov_b64 s[24:25], 0x140200
	v_add_co_u32_e32 v36, vcc, 0x140000, v162
	v_lshl_add_u64 v[34:35], v[162:163], 0, s[24:25]
	s_nop 0
	v_addc_co_u32_e32 v37, vcc, 0, v163, vcc
	global_load_dwordx4 v[38:41], v[36:37], off offset:512
	s_nop 0
	global_load_dwordx4 v[34:37], v[34:35], off offset:16
	s_cbranch_execnz .LBB0_1818

; __device__ __forceinline__ unsigned pk2(float lo, float hi) { return f2bf(lo) | (f2bf(hi) << 16); }
;     __device__ __forceinline__ void epi(const f32x4 (&acc)[2][2][4][2], const Unit& u, int wr, int wc, int fr, int fq) const {
;     ...
;                 for (int bj = 0; bj < 2; ++bj) { const int cofs = bj * 128;
;                     const f32x4 g0 = *(const f32x4*)(g1 + cofs * 4 + lcol * 4), g1v = *(const f32x4*)(g1 + cofs * 4 + lcol * 4 + 16);
;                     f32x4 x0, x1v;
;                     if (f32in) { x0 = *(const f32x4*)(xin + (ro + cofs) * 4 + loff4); x1v = *(const f32x4*)(xin + (ro + cofs) * 4 + loff4 + 16); }
;                     else { const u32x4 w = *(const u32x4*)(xin + (ro + cofs) * 2 + loff2); x0 = (f32x4){bflo(w.x), bfhi(w.x), bflo(w.y), bfhi(w.y)}; x1v = (f32x4){bflo(w.z), bfhi(w.z), bflo(w.w), bfhi(w.w)}; }
;                     const f32x4 o0 = x0 + g0 * acc[ai][bj][m][0], o1 = x1v + g1v * acc[ai][bj][m][1];
;                     u32x4 ow; ow.x = pk2(o0[0], o0[1]); ow.y = pk2(o0[2], o0[3]); ow.z = pk2(o1[0], o1[1]); ow.w = pk2(o1[2], o1[3]);
;                     *(u32x4*)(xo + (ro + cofs) * 2 + loff2) = ow; }
;                 asm volatile("" ::: "memory"); }
.LBB0_1818:
	s_waitcnt vmcnt(0)
	v_pk_fma_f32 v[22:23], v[22:23], v[30:31], v[38:39]
	v_pk_fma_f32 v[28:29], v[20:21], v[28:29], v[36:37]
	v_pk_fma_f32 v[20:21], v[18:19], v[26:27], v[34:35]
	v_pk_fma_f32 v[24:25], v[24:25], v[32:33], v[40:41]
	v_cvt_pk_bf16_f32 v18, v22, v23
	v_cvt_pk_bf16_f32 v19, v24, v25
	v_bfe_u32 v1, v20, 16, 1
	v_add3_u32 v1, v20, v1, s37
	v_bfe_u32 v20, v21, 16, 1
	v_lshrrev_b32_e32 v1, 16, v1
	v_add3_u32 v20, v21, v20, s37
	v_and_or_b32 v20, v20, s33, v1
	v_add_co_u32_e32 v22, vcc, 0xa0000, v160
	v_cvt_pk_bf16_f32 v21, v28, v29
	s_nop 0
	v_addc_co_u32_e32 v23, vcc, 0, v161, vcc
	global_store_dwordx4 v[22:23], v[18:21], off offset:256 sc1
	global_load_dwordx4 v[18:21], v[164:165], off offset:16
	global_load_dwordx4 v[22:25], v[164:165], off
	s_and_b64 vcc, exec, s[40:41]
	s_cbranch_vccnz .LBB0_1843
	s_mov_b64 s[24:25], 0x160000
	v_add_co_u32_e32 v28, vcc, 0x160000, v162
	v_lshl_add_u64 v[26:27], v[162:163], 0, s[24:25]
	s_nop 0
	v_addc_co_u32_e32 v29, vcc, 0, v163, vcc
	global_load_dwordx4 v[30:33], v[28:29], off
	s_nop 0
	global_load_dwordx4 v[26:29], v[26:27], off offset:16
	s_cbranch_execnz .LBB0_1821

; __device__ __forceinline__ unsigned pk2(float lo, float hi) { return f2bf(lo) | (f2bf(hi) << 16); }
;     __device__ __forceinline__ void epi(const f32x4 (&acc)[2][2][4][2], const Unit& u, int wr, int wc, int fr, int fq) const {
;     ...
;                 for (int bj = 0; bj < 2; ++bj) { const int cofs = bj * 128;
;                     const f32x4 g0 = *(const f32x4*)(g1 + cofs * 4 + lcol * 4), g1v = *(const f32x4*)(g1 + cofs * 4 + lcol * 4 + 16);
;                     f32x4 x0, x1v;
;                     if (f32in) { x0 = *(const f32x4*)(xin + (ro + cofs) * 4 + loff4); x1v = *(const f32x4*)(xin + (ro + cofs) * 4 + loff4 + 16); }
;                     else { const u32x4 w = *(const u32x4*)(xin + (ro + cofs) * 2 + loff2); x0 = (f32x4){bflo(w.x), bfhi(w.x), bflo(w.y), bfhi(w.y)}; x1v = (f32x4){bflo(w.z), bfhi(w.z), bflo(w.w), bfhi(w.w)}; }
;                     const f32x4 o0 = x0 + g0 * acc[ai][bj][m][0], o1 = x1v + g1v * acc[ai][bj][m][1];
;                     u32x4 ow; ow.x = pk2(o0[0], o0[1]); ow.y = pk2(o0[2], o0[3]); ow.z = pk2(o1[0], o1[1]); ow.w = pk2(o1[2], o1[3]);
;                     *(u32x4*)(xo + (ro + cofs) * 2 + loff2) = ow; }
;                 asm volatile("" ::: "memory"); }
.LBB0_1821:
	s_waitcnt vmcnt(0)
	v_pk_fma_f32 v[14:15], v[14:15], v[22:23], v[30:31]
	v_pk_fma_f32 v[20:21], v[12:13], v[20:21], v[28:29]
	v_pk_fma_f32 v[12:13], v[10:11], v[18:19], v[26:27]
	v_pk_fma_f32 v[16:17], v[16:17], v[24:25], v[32:33]
	v_cvt_pk_bf16_f32 v10, v14, v15
	v_cvt_pk_bf16_f32 v11, v16, v17
	v_bfe_u32 v1, v12, 16, 1
	v_add3_u32 v1, v12, v1, s37
	v_bfe_u32 v12, v13, 16, 1
	v_lshrrev_b32_e32 v1, 16, v1
	v_add3_u32 v12, v13, v12, s37
	v_and_or_b32 v12, v12, s33, v1
	v_add_co_u32_e32 v14, vcc, 0xb0000, v160
	v_cvt_pk_bf16_f32 v13, v20, v21
	s_nop 0
	v_addc_co_u32_e32 v15, vcc, 0, v161, vcc
	global_store_dwordx4 v[14:15], v[10:13], off sc1
	global_load_dwordx4 v[10:13], v[164:165], off offset:528
	s_nop 0
	global_load_dwordx4 v[14:17], v[164:165], off offset:512
	s_and_b64 vcc, exec, s[40:41]
	s_cbranch_vccnz .LBB0_1844
	s_mov_b64 s[24:25], 0x160200
	v_add_co_u32_e32 v20, vcc, 0x160000, v162
	v_lshl_add_u64 v[18:19], v[162:163], 0, s[24:25]
	s_nop 0
	v_addc_co_u32_e32 v21, vcc, 0, v163, vcc
	global_load_dwordx4 v[22:25], v[20:21], off offset:512
	s_nop 0
	global_load_dwordx4 v[18:21], v[18:19], off offset:16
	s_cbranch_execnz .LBB0_1824

; __device__ __forceinline__ unsigned pk2(float lo, float hi) { return f2bf(lo) | (f2bf(hi) << 16); }
;     __device__ __forceinline__ void epi(const f32x4 (&acc)[2][2][4][2], const Unit& u, int wr, int wc, int fr, int fq) const {
;     ...
;                 for (int bj = 0; bj < 2; ++bj) { const int cofs = bj * 128;
;                     const f32x4 g0 = *(const f32x4*)(g1 + cofs * 4 + lcol * 4), g1v = *(const f32x4*)(g1 + cofs * 4 + lcol * 4 + 16);
;                     f32x4 x0, x1v;
;                     if (f32in) { x0 = *(const f32x4*)(xin + (ro + cofs) * 4 + loff4); x1v = *(const f32x4*)(xin + (ro + cofs) * 4 + loff4 + 16); }
;                     else { const u32x4 w = *(const u32x4*)(xin + (ro + cofs) * 2 + loff2); x0 = (f32x4){bflo(w.x), bfhi(w.x), bflo(w.y), bfhi(w.y)}; x1v = (f32x4){bflo(w.z), bfhi(w.z), bflo(w.w), bfhi(w.w)}; }
;                     const f32x4 o0 = x0 + g0 * acc[ai][bj][m][0], o1 = x1v + g1v * acc[ai][bj][m][1];
;                     u32x4 ow; ow.x = pk2(o0[0], o0[1]); ow.y = pk2(o0[2], o0[3]); ow.z = pk2(o1[0], o1[1]); ow.w = pk2(o1[2], o1[3]);
;                     *(u32x4*)(xo + (ro + cofs) * 2 + loff2) = ow; }
;                 asm volatile("" ::: "memory"); }
.LBB0_1824:
	s_waitcnt vmcnt(0)
	v_pk_fma_f32 v[6:7], v[6:7], v[14:15], v[22:23]
	v_pk_fma_f32 v[12:13], v[4:5], v[12:13], v[20:21]
	v_pk_fma_f32 v[4:5], v[2:3], v[10:11], v[18:19]
	v_pk_fma_f32 v[8:9], v[8:9], v[16:17], v[24:25]
	v_cvt_pk_bf16_f32 v2, v6, v7
	v_cvt_pk_bf16_f32 v3, v8, v9
	v_bfe_u32 v1, v4, 16, 1
	v_add3_u32 v1, v4, v1, s37
	v_bfe_u32 v4, v5, 16, 1
	v_lshrrev_b32_e32 v1, 16, v1
	v_add3_u32 v4, v5, v4, s37
	v_and_or_b32 v4, v4, s33, v1
	v_add_co_u32_e32 v6, vcc, 0xb0000, v160
	v_cvt_pk_bf16_f32 v5, v12, v13
	s_nop 0
	v_addc_co_u32_e32 v7, vcc, 0, v161, vcc
	global_store_dwordx4 v[6:7], v[2:5], off offset:256 sc1
	s_andn2_b64 vcc, exec, s[38:39]
	s_mov_b64 s[24:25], -1
	s_cbranch_vccnz .LBB0_1761
	s_andn2_b64 vcc, exec, s[4:5]
	s_cbranch_vccnz .LBB0_1760
	s_barrier
	s_branch .LBB0_1760

; __device__ __forceinline__ unsigned pk2(float lo, float hi) { return f2bf(lo) | (f2bf(hi) << 16); }
;     __device__ __forceinline__ void epi(const f32x4 (&acc)[2][2][4][2], const Unit& u, int wr, int wc, int fr, int fq) const {
;     ...
;                 for (int bj = 0; bj < 2; ++bj) { const int cofs = bj * 128;
;                     const f32x4 g0 = *(const f32x4*)(g1 + cofs * 4 + lcol * 4), g1v = *(const f32x4*)(g1 + cofs * 4 + lcol * 4 + 16);
;                     f32x4 x0, x1v;
;                     if (f32in) { x0 = *(const f32x4*)(xin + (ro + cofs) * 4 + loff4); x1v = *(const f32x4*)(xin + (ro + cofs) * 4 + loff4 + 16); }
;                     else { const u32x4 w = *(const u32x4*)(xin + (ro + cofs) * 2 + loff2); x0 = (f32x4){bflo(w.x), bfhi(w.x), bflo(w.y), bfhi(w.y)}; x1v = (f32x4){bflo(w.z), bfhi(w.z), bflo(w.w), bfhi(w.w)}; }
;                     const f32x4 o0 = x0 + g0 * acc[ai][bj][m][0], o1 = x1v + g1v * acc[ai][bj][m][1];
;                     u32x4 ow; ow.x = pk2(o0[0], o0[1]); ow.y = pk2(o0[2], o0[3]); ow.z = pk2(o1[0], o1[1]); ow.w = pk2(o1[2], o1[3]);
;                     *(u32x4*)(xo + (ro + cofs) * 2 + loff2) = ow; }
;                 asm volatile("" ::: "memory"); }
.LBB0_1960:
	s_waitcnt vmcnt(0)
	v_pk_fma_f32 v[126:127], v[126:127], v[134:135], v[142:143]
	v_pk_fma_f32 v[132:133], v[124:125], v[132:133], v[140:141]
	v_pk_fma_f32 v[124:125], v[122:123], v[130:131], v[138:139]
	v_pk_fma_f32 v[128:129], v[128:129], v[136:137], v[144:145]
	v_cvt_pk_bf16_f32 v122, v126, v127
	v_cvt_pk_bf16_f32 v123, v128, v129
	v_bfe_u32 v1, v124, 16, 1
	v_add3_u32 v1, v124, v1, s37
	v_bfe_u32 v124, v125, 16, 1
	s_add_u32 s19, s64, s40
	v_lshrrev_b32_e32 v1, 16, v1
	v_add3_u32 v124, v125, v124, s37
	s_addc_u32 s21, s65, s41
	v_and_or_b32 v124, v124, s33, v1
	s_add_u32 s26, s19, s42
	s_addc_u32 s27, s21, s43
	v_lshl_add_u64 v[160:161], s[26:27], 0, v[146:147]
	v_cvt_pk_bf16_f32 v125, v132, v133
	global_store_dwordx4 v[160:161], v[122:125], off sc1
	global_load_dwordx4 v[122:125], v[164:165], off offset:528
	s_nop 0
	global_load_dwordx4 v[126:129], v[164:165], off offset:512
	s_and_b64 vcc, exec, s[38:39]
	s_cbranch_vccnz .LBB0_2011
	global_load_dwordx4 v[130:133], v[162:163], off offset:528
	global_load_dwordx4 v[134:137], v[162:163], off offset:512
	s_cbranch_execnz .LBB0_1963

; __device__ __forceinline__ unsigned pk2(float lo, float hi) { return f2bf(lo) | (f2bf(hi) << 16); }
;     __device__ __forceinline__ void epi(const f32x4 (&acc)[2][2][4][2], const Unit& u, int wr, int wc, int fr, int fq) const {
;     ...
;                 for (int bj = 0; bj < 2; ++bj) { const int cofs = bj * 128;
;                     const f32x4 g0 = *(const f32x4*)(g1 + cofs * 4 + lcol * 4), g1v = *(const f32x4*)(g1 + cofs * 4 + lcol * 4 + 16);
;                     f32x4 x0, x1v;
;                     if (f32in) { x0 = *(const f32x4*)(xin + (ro + cofs) * 4 + loff4); x1v = *(const f32x4*)(xin + (ro + cofs) * 4 + loff4 + 16); }
;                     else { const u32x4 w = *(const u32x4*)(xin + (ro + cofs) * 2 + loff2); x0 = (f32x4){bflo(w.x), bfhi(w.x), bflo(w.y), bfhi(w.y)}; x1v = (f32x4){bflo(w.z), bfhi(w.z), bflo(w.w), bfhi(w.w)}; }
;                     const f32x4 o0 = x0 + g0 * acc[ai][bj][m][0], o1 = x1v + g1v * acc[ai][bj][m][1];
;                     u32x4 ow; ow.x = pk2(o0[0], o0[1]); ow.y = pk2(o0[2], o0[3]); ow.z = pk2(o1[0], o1[1]); ow.w = pk2(o1[2], o1[3]);
;                     *(u32x4*)(xo + (ro + cofs) * 2 + loff2) = ow; }
;                 asm volatile("" ::: "memory"); }
.LBB0_1963:
	s_waitcnt vmcnt(0)
	v_pk_fma_f32 v[118:119], v[118:119], v[126:127], v[134:135]
	v_pk_fma_f32 v[124:125], v[116:117], v[124:125], v[132:133]
	v_pk_fma_f32 v[116:117], v[114:115], v[122:123], v[130:131]
	v_pk_fma_f32 v[120:121], v[120:121], v[128:129], v[136:137]
	v_cvt_pk_bf16_f32 v114, v118, v119
	v_cvt_pk_bf16_f32 v115, v120, v121
	v_bfe_u32 v1, v116, 16, 1
	v_add3_u32 v1, v116, v1, s37
	v_bfe_u32 v116, v117, 16, 1
	v_lshrrev_b32_e32 v1, 16, v1
	v_add3_u32 v116, v117, v116, s37
	v_and_or_b32 v116, v116, s33, v1
	v_cvt_pk_bf16_f32 v117, v124, v125
	global_store_dwordx4 v[160:161], v[114:117], off offset:256 sc1
	global_load_dwordx4 v[114:117], v[164:165], off offset:16
	global_load_dwordx4 v[118:121], v[164:165], off
	s_and_b64 vcc, exec, s[38:39]
	s_cbranch_vccnz .LBB0_2012
	s_mov_b64 s[26:27], 0x20000
	v_add_co_u32_e32 v124, vcc, 0x20000, v162
	v_lshl_add_u64 v[122:123], v[162:163], 0, s[26:27]
	s_nop 0
	v_addc_co_u32_e32 v125, vcc, 0, v163, vcc
	global_load_dwordx4 v[126:129], v[124:125], off
	s_nop 0
	global_load_dwordx4 v[122:125], v[122:123], off offset:16
	s_cbranch_execnz .LBB0_1966

; __device__ __forceinline__ unsigned pk2(float lo, float hi) { return f2bf(lo) | (f2bf(hi) << 16); }
;     __device__ __forceinline__ void epi(const f32x4 (&acc)[2][2][4][2], const Unit& u, int wr, int wc, int fr, int fq) const {
;     ...
;                 for (int bj = 0; bj < 2; ++bj) { const int cofs = bj * 128;
;                     const f32x4 g0 = *(const f32x4*)(g1 + cofs * 4 + lcol * 4), g1v = *(const f32x4*)(g1 + cofs * 4 + lcol * 4 + 16);
;                     f32x4 x0, x1v;
;                     if (f32in) { x0 = *(const f32x4*)(xin + (ro + cofs) * 4 + loff4); x1v = *(const f32x4*)(xin + (ro + cofs) * 4 + loff4 + 16); }
;                     else { const u32x4 w = *(const u32x4*)(xin + (ro + cofs) * 2 + loff2); x0 = (f32x4){bflo(w.x), bfhi(w.x), bflo(w.y), bfhi(w.y)}; x1v = (f32x4){bflo(w.z), bfhi(w.z), bflo(w.w), bfhi(w.w)}; }
;                     const f32x4 o0 = x0 + g0 * acc[ai][bj][m][0], o1 = x1v + g1v * acc[ai][bj][m][1];
;                     u32x4 ow; ow.x = pk2(o0[0], o0[1]); ow.y = pk2(o0[2], o0[3]); ow.z = pk2(o1[0], o1[1]); ow.w = pk2(o1[2], o1[3]);
;                     *(u32x4*)(xo + (ro + cofs) * 2 + loff2) = ow; }
;                 asm volatile("" ::: "memory"); }
.LBB0_1966:
	s_waitcnt vmcnt(0)
	v_pk_fma_f32 v[110:111], v[110:111], v[118:119], v[126:127]
	v_pk_fma_f32 v[116:117], v[108:109], v[116:117], v[124:125]
	v_pk_fma_f32 v[108:109], v[106:107], v[114:115], v[122:123]
	v_pk_fma_f32 v[112:113], v[112:113], v[120:121], v[128:129]
	v_cvt_pk_bf16_f32 v106, v110, v111
	v_cvt_pk_bf16_f32 v107, v112, v113
	v_bfe_u32 v1, v108, 16, 1
	v_add3_u32 v1, v108, v1, s37
	v_bfe_u32 v108, v109, 16, 1
	v_lshrrev_b32_e32 v1, 16, v1
	v_add3_u32 v108, v109, v108, s37
	v_and_or_b32 v108, v108, s33, v1
	v_add_co_u32_e32 v110, vcc, 0x10000, v160
	v_cvt_pk_bf16_f32 v109, v116, v117
	s_nop 0
	v_addc_co_u32_e32 v111, vcc, 0, v161, vcc
	global_store_dwordx4 v[110:111], v[106:109], off sc1
	global_load_dwordx4 v[106:109], v[164:165], off offset:528
	s_nop 0
	global_load_dwordx4 v[110:113], v[164:165], off offset:512
	s_and_b64 vcc, exec, s[38:39]
	s_cbranch_vccnz .LBB0_2013
	s_mov_b64 s[26:27], 0x20200
	v_add_co_u32_e32 v116, vcc, 0x20000, v162
	v_lshl_add_u64 v[114:115], v[162:163], 0, s[26:27]
	s_nop 0
	v_addc_co_u32_e32 v117, vcc, 0, v163, vcc
	global_load_dwordx4 v[118:121], v[116:117], off offset:512
	s_nop 0
	global_load_dwordx4 v[114:117], v[114:115], off offset:16
	s_cbranch_execnz .LBB0_1969

; __device__ __forceinline__ unsigned pk2(float lo, float hi) { return f2bf(lo) | (f2bf(hi) << 16); }
;     __device__ __forceinline__ void epi(const f32x4 (&acc)[2][2][4][2], const Unit& u, int wr, int wc, int fr, int fq) const {
;     ...
;                 for (int bj = 0; bj < 2; ++bj) { const int cofs = bj * 128;
;                     const f32x4 g0 = *(const f32x4*)(g1 + cofs * 4 + lcol * 4), g1v = *(const f32x4*)(g1 + cofs * 4 + lcol * 4 + 16);
;                     f32x4 x0, x1v;
;                     if (f32in) { x0 = *(const f32x4*)(xin + (ro + cofs) * 4 + loff4); x1v = *(const f32x4*)(xin + (ro + cofs) * 4 + loff4 + 16); }
;                     else { const u32x4 w = *(const u32x4*)(xin + (ro + cofs) * 2 + loff2); x0 = (f32x4){bflo(w.x), bfhi(w.x), bflo(w.y), bfhi(w.y)}; x1v = (f32x4){bflo(w.z), bfhi(w.z), bflo(w.w), bfhi(w.w)}; }
;                     const f32x4 o0 = x0 + g0 * acc[ai][bj][m][0], o1 = x1v + g1v * acc[ai][bj][m][1];
;                     u32x4 ow; ow.x = pk2(o0[0], o0[1]); ow.y = pk2(o0[2], o0[3]); ow.z = pk2(o1[0], o1[1]); ow.w = pk2(o1[2], o1[3]);
;                     *(u32x4*)(xo + (ro + cofs) * 2 + loff2) = ow; }
;                 asm volatile("" ::: "memory"); }
.LBB0_1969:
	s_waitcnt vmcnt(0)
	v_pk_fma_f32 v[102:103], v[102:103], v[110:111], v[118:119]
	v_pk_fma_f32 v[108:109], v[100:101], v[108:109], v[116:117]
	v_pk_fma_f32 v[100:101], v[98:99], v[106:107], v[114:115]
	v_pk_fma_f32 v[104:105], v[104:105], v[112:113], v[120:121]
	v_cvt_pk_bf16_f32 v98, v102, v103
	v_cvt_pk_bf16_f32 v99, v104, v105
	v_bfe_u32 v1, v100, 16, 1
	v_add3_u32 v1, v100, v1, s37
	v_bfe_u32 v100, v101, 16, 1
	v_lshrrev_b32_e32 v1, 16, v1
	v_add3_u32 v100, v101, v100, s37
	v_and_or_b32 v100, v100, s33, v1
	v_add_co_u32_e32 v102, vcc, 0x10000, v160
	v_cvt_pk_bf16_f32 v101, v108, v109
	s_nop 0
	v_addc_co_u32_e32 v103, vcc, 0, v161, vcc
	global_store_dwordx4 v[102:103], v[98:101], off offset:256 sc1
	global_load_dwordx4 v[98:101], v[164:165], off offset:16
	global_load_dwordx4 v[102:105], v[164:165], off
	s_and_b64 vcc, exec, s[38:39]
	s_cbranch_vccnz .LBB0_2014
	s_mov_b64 s[26:27], 0x40000
	v_add_co_u32_e32 v108, vcc, 0x40000, v162
	v_lshl_add_u64 v[106:107], v[162:163], 0, s[26:27]
	s_nop 0
	v_addc_co_u32_e32 v109, vcc, 0, v163, vcc
	global_load_dwordx4 v[110:113], v[108:109], off
	s_nop 0
	global_load_dwordx4 v[106:109], v[106:107], off offset:16
	s_cbranch_execnz .LBB0_1972

; __device__ __forceinline__ unsigned pk2(float lo, float hi) { return f2bf(lo) | (f2bf(hi) << 16); }
;     __device__ __forceinline__ void epi(const f32x4 (&acc)[2][2][4][2], const Unit& u, int wr, int wc, int fr, int fq) const {
;     ...
;                 for (int bj = 0; bj < 2; ++bj) { const int cofs = bj * 128;
;                     const f32x4 g0 = *(const f32x4*)(g1 + cofs * 4 + lcol * 4), g1v = *(const f32x4*)(g1 + cofs * 4 + lcol * 4 + 16);
;                     f32x4 x0, x1v;
;                     if (f32in) { x0 = *(const f32x4*)(xin + (ro + cofs) * 4 + loff4); x1v = *(const f32x4*)(xin + (ro + cofs) * 4 + loff4 + 16); }
;                     else { const u32x4 w = *(const u32x4*)(xin + (ro + cofs) * 2 + loff2); x0 = (f32x4){bflo(w.x), bfhi(w.x), bflo(w.y), bfhi(w.y)}; x1v = (f32x4){bflo(w.z), bfhi(w.z), bflo(w.w), bfhi(w.w)}; }
;                     const f32x4 o0 = x0 + g0 * acc[ai][bj][m][0], o1 = x1v + g1v * acc[ai][bj][m][1];
;                     u32x4 ow; ow.x = pk2(o0[0], o0[1]); ow.y = pk2(o0[2], o0[3]); ow.z = pk2(o1[0], o1[1]); ow.w = pk2(o1[2], o1[3]);
;                     *(u32x4*)(xo + (ro + cofs) * 2 + loff2) = ow; }
;                 asm volatile("" ::: "memory"); }
.LBB0_1972:
	s_waitcnt vmcnt(0)
	v_pk_fma_f32 v[94:95], v[94:95], v[102:103], v[110:111]
	v_pk_fma_f32 v[100:101], v[92:93], v[100:101], v[108:109]
	v_pk_fma_f32 v[92:93], v[90:91], v[98:99], v[106:107]
	v_pk_fma_f32 v[96:97], v[96:97], v[104:105], v[112:113]
	v_cvt_pk_bf16_f32 v90, v94, v95
	v_cvt_pk_bf16_f32 v91, v96, v97
	v_bfe_u32 v1, v92, 16, 1
	v_add3_u32 v1, v92, v1, s37
	v_bfe_u32 v92, v93, 16, 1
	v_lshrrev_b32_e32 v1, 16, v1
	v_add3_u32 v92, v93, v92, s37
	v_and_or_b32 v92, v92, s33, v1
	v_add_co_u32_e32 v94, vcc, 0x20000, v160
	v_cvt_pk_bf16_f32 v93, v100, v101
	s_nop 0
	v_addc_co_u32_e32 v95, vcc, 0, v161, vcc
	global_store_dwordx4 v[94:95], v[90:93], off sc1
	global_load_dwordx4 v[90:93], v[164:165], off offset:528
	s_nop 0
	global_load_dwordx4 v[94:97], v[164:165], off offset:512
	s_and_b64 vcc, exec, s[38:39]
	s_cbranch_vccnz .LBB0_2015
	s_mov_b64 s[26:27], 0x40200
	v_add_co_u32_e32 v100, vcc, 0x40000, v162
	v_lshl_add_u64 v[98:99], v[162:163], 0, s[26:27]
	s_nop 0
	v_addc_co_u32_e32 v101, vcc, 0, v163, vcc
	global_load_dwordx4 v[102:105], v[100:101], off offset:512
	s_nop 0
	global_load_dwordx4 v[98:101], v[98:99], off offset:16
	s_cbranch_execnz .LBB0_1975

; __device__ __forceinline__ unsigned pk2(float lo, float hi) { return f2bf(lo) | (f2bf(hi) << 16); }
;     __device__ __forceinline__ void epi(const f32x4 (&acc)[2][2][4][2], const Unit& u, int wr, int wc, int fr, int fq) const {
;     ...
;                 for (int bj = 0; bj < 2; ++bj) { const int cofs = bj * 128;
;                     const f32x4 g0 = *(const f32x4*)(g1 + cofs * 4 + lcol * 4), g1v = *(const f32x4*)(g1 + cofs * 4 + lcol * 4 + 16);
;                     f32x4 x0, x1v;
;                     if (f32in) { x0 = *(const f32x4*)(xin + (ro + cofs) * 4 + loff4); x1v = *(const f32x4*)(xin + (ro + cofs) * 4 + loff4 + 16); }
;                     else { const u32x4 w = *(const u32x4*)(xin + (ro + cofs) * 2 + loff2); x0 = (f32x4){bflo(w.x), bfhi(w.x), bflo(w.y), bfhi(w.y)}; x1v = (f32x4){bflo(w.z), bfhi(w.z), bflo(w.w), bfhi(w.w)}; }
;                     const f32x4 o0 = x0 + g0 * acc[ai][bj][m][0], o1 = x1v + g1v * acc[ai][bj][m][1];
;                     u32x4 ow; ow.x = pk2(o0[0], o0[1]); ow.y = pk2(o0[2], o0[3]); ow.z = pk2(o1[0], o1[1]); ow.w = pk2(o1[2], o1[3]);
;                     *(u32x4*)(xo + (ro + cofs) * 2 + loff2) = ow; }
;                 asm volatile("" ::: "memory"); }
.LBB0_1975:
	s_waitcnt vmcnt(0)
	v_pk_fma_f32 v[86:87], v[86:87], v[94:95], v[102:103]
	v_pk_fma_f32 v[92:93], v[84:85], v[92:93], v[100:101]
	v_pk_fma_f32 v[84:85], v[82:83], v[90:91], v[98:99]
	v_pk_fma_f32 v[88:89], v[88:89], v[96:97], v[104:105]
	v_cvt_pk_bf16_f32 v82, v86, v87
	v_cvt_pk_bf16_f32 v83, v88, v89
	v_bfe_u32 v1, v84, 16, 1
	v_add3_u32 v1, v84, v1, s37
	v_bfe_u32 v84, v85, 16, 1
	v_lshrrev_b32_e32 v1, 16, v1
	v_add3_u32 v84, v85, v84, s37
	v_and_or_b32 v84, v84, s33, v1
	v_add_co_u32_e32 v86, vcc, 0x20000, v160
	v_cvt_pk_bf16_f32 v85, v92, v93
	s_nop 0
	v_addc_co_u32_e32 v87, vcc, 0, v161, vcc
	global_store_dwordx4 v[86:87], v[82:85], off offset:256 sc1
	global_load_dwordx4 v[82:85], v[164:165], off offset:16
	global_load_dwordx4 v[86:89], v[164:165], off
	s_and_b64 vcc, exec, s[38:39]
	s_cbranch_vccnz .LBB0_2016
	s_mov_b64 s[26:27], 0x60000
	v_add_co_u32_e32 v92, vcc, 0x60000, v162
	v_lshl_add_u64 v[90:91], v[162:163], 0, s[26:27]
	s_nop 0
	v_addc_co_u32_e32 v93, vcc, 0, v163, vcc
	global_load_dwordx4 v[94:97], v[92:93], off
	s_nop 0
	global_load_dwordx4 v[90:93], v[90:91], off offset:16
	s_cbranch_execnz .LBB0_1978

; __device__ __forceinline__ unsigned pk2(float lo, float hi) { return f2bf(lo) | (f2bf(hi) << 16); }
;     __device__ __forceinline__ void epi(const f32x4 (&acc)[2][2][4][2], const Unit& u, int wr, int wc, int fr, int fq) const {
;     ...
;                 for (int bj = 0; bj < 2; ++bj) { const int cofs = bj * 128;
;                     const f32x4 g0 = *(const f32x4*)(g1 + cofs * 4 + lcol * 4), g1v = *(const f32x4*)(g1 + cofs * 4 + lcol * 4 + 16);
;                     f32x4 x0, x1v;
;                     if (f32in) { x0 = *(const f32x4*)(xin + (ro + cofs) * 4 + loff4); x1v = *(const f32x4*)(xin + (ro + cofs) * 4 + loff4 + 16); }
;                     else { const u32x4 w = *(const u32x4*)(xin + (ro + cofs) * 2 + loff2); x0 = (f32x4){bflo(w.x), bfhi(w.x), bflo(w.y), bfhi(w.y)}; x1v = (f32x4){bflo(w.z), bfhi(w.z), bflo(w.w), bfhi(w.w)}; }
;                     const f32x4 o0 = x0 + g0 * acc[ai][bj][m][0], o1 = x1v + g1v * acc[ai][bj][m][1];
;                     u32x4 ow; ow.x = pk2(o0[0], o0[1]); ow.y = pk2(o0[2], o0[3]); ow.z = pk2(o1[0], o1[1]); ow.w = pk2(o1[2], o1[3]);
;                     *(u32x4*)(xo + (ro + cofs) * 2 + loff2) = ow; }
;                 asm volatile("" ::: "memory"); }
.LBB0_1978:
	s_waitcnt vmcnt(0)
	v_pk_fma_f32 v[78:79], v[78:79], v[86:87], v[94:95]
	v_pk_fma_f32 v[84:85], v[76:77], v[84:85], v[92:93]
	v_pk_fma_f32 v[76:77], v[74:75], v[82:83], v[90:91]
	v_pk_fma_f32 v[80:81], v[80:81], v[88:89], v[96:97]
	v_cvt_pk_bf16_f32 v74, v78, v79
	v_cvt_pk_bf16_f32 v75, v80, v81
	v_bfe_u32 v1, v76, 16, 1
	v_add3_u32 v1, v76, v1, s37
	v_bfe_u32 v76, v77, 16, 1
	v_lshrrev_b32_e32 v1, 16, v1
	v_add3_u32 v76, v77, v76, s37
	v_and_or_b32 v76, v76, s33, v1
	v_add_co_u32_e32 v78, vcc, 0x30000, v160
	v_cvt_pk_bf16_f32 v77, v84, v85
	s_nop 0
	v_addc_co_u32_e32 v79, vcc, 0, v161, vcc
	global_store_dwordx4 v[78:79], v[74:77], off sc1
	global_load_dwordx4 v[74:77], v[164:165], off offset:528
	s_nop 0
	global_load_dwordx4 v[78:81], v[164:165], off offset:512
	s_and_b64 vcc, exec, s[38:39]
	s_cbranch_vccnz .LBB0_2017
	s_mov_b64 s[26:27], 0x60200
	v_add_co_u32_e32 v84, vcc, 0x60000, v162
	v_lshl_add_u64 v[82:83], v[162:163], 0, s[26:27]
	s_nop 0
	v_addc_co_u32_e32 v85, vcc, 0, v163, vcc
	global_load_dwordx4 v[86:89], v[84:85], off offset:512
	s_nop 0
	global_load_dwordx4 v[82:85], v[82:83], off offset:16
	s_cbranch_execnz .LBB0_1981

; __device__ __forceinline__ unsigned pk2(float lo, float hi) { return f2bf(lo) | (f2bf(hi) << 16); }
;     __device__ __forceinline__ void epi(const f32x4 (&acc)[2][2][4][2], const Unit& u, int wr, int wc, int fr, int fq) const {
;     ...
;                 for (int bj = 0; bj < 2; ++bj) { const int cofs = bj * 128;
;                     const f32x4 g0 = *(const f32x4*)(g1 + cofs * 4 + lcol * 4), g1v = *(const f32x4*)(g1 + cofs * 4 + lcol * 4 + 16);
;                     f32x4 x0, x1v;
;                     if (f32in) { x0 = *(const f32x4*)(xin + (ro + cofs) * 4 + loff4); x1v = *(const f32x4*)(xin + (ro + cofs) * 4 + loff4 + 16); }
;                     else { const u32x4 w = *(const u32x4*)(xin + (ro + cofs) * 2 + loff2); x0 = (f32x4){bflo(w.x), bfhi(w.x), bflo(w.y), bfhi(w.y)}; x1v = (f32x4){bflo(w.z), bfhi(w.z), bflo(w.w), bfhi(w.w)}; }
;                     const f32x4 o0 = x0 + g0 * acc[ai][bj][m][0], o1 = x1v + g1v * acc[ai][bj][m][1];
;                     u32x4 ow; ow.x = pk2(o0[0], o0[1]); ow.y = pk2(o0[2], o0[3]); ow.z = pk2(o1[0], o1[1]); ow.w = pk2(o1[2], o1[3]);
;                     *(u32x4*)(xo + (ro + cofs) * 2 + loff2) = ow; }
;                 asm volatile("" ::: "memory"); }
.LBB0_1981:
	s_waitcnt vmcnt(0)
	v_pk_fma_f32 v[70:71], v[70:71], v[78:79], v[86:87]
	v_pk_fma_f32 v[76:77], v[68:69], v[76:77], v[84:85]
	v_pk_fma_f32 v[68:69], v[66:67], v[74:75], v[82:83]
	v_pk_fma_f32 v[72:73], v[72:73], v[80:81], v[88:89]
	v_cvt_pk_bf16_f32 v66, v70, v71
	v_cvt_pk_bf16_f32 v67, v72, v73
	v_bfe_u32 v1, v68, 16, 1
	v_add3_u32 v1, v68, v1, s37
	v_bfe_u32 v68, v69, 16, 1
	v_lshrrev_b32_e32 v1, 16, v1
	v_add3_u32 v68, v69, v68, s37
	v_and_or_b32 v68, v68, s33, v1
	v_add_co_u32_e32 v70, vcc, 0x30000, v160
	v_cvt_pk_bf16_f32 v69, v76, v77
	s_nop 0
	v_addc_co_u32_e32 v71, vcc, 0, v161, vcc
	global_store_dwordx4 v[70:71], v[66:69], off offset:256 sc1
	global_load_dwordx4 v[66:69], v[164:165], off offset:16
	global_load_dwordx4 v[70:73], v[164:165], off
	s_and_b64 vcc, exec, s[38:39]
	s_cbranch_vccnz .LBB0_2018
	s_mov_b64 s[26:27], 0x100000
	v_add_co_u32_e32 v76, vcc, 0x100000, v162
	v_lshl_add_u64 v[74:75], v[162:163], 0, s[26:27]
	s_nop 0
	v_addc_co_u32_e32 v77, vcc, 0, v163, vcc
	global_load_dwordx4 v[78:81], v[76:77], off
	s_nop 0
	global_load_dwordx4 v[74:77], v[74:75], off offset:16
	s_cbranch_execnz .LBB0_1984

; __device__ __forceinline__ unsigned pk2(float lo, float hi) { return f2bf(lo) | (f2bf(hi) << 16); }
;     __device__ __forceinline__ void epi(const f32x4 (&acc)[2][2][4][2], const Unit& u, int wr, int wc, int fr, int fq) const {
;     ...
;                 for (int bj = 0; bj < 2; ++bj) { const int cofs = bj * 128;
;                     const f32x4 g0 = *(const f32x4*)(g1 + cofs * 4 + lcol * 4), g1v = *(const f32x4*)(g1 + cofs * 4 + lcol * 4 + 16);
;                     f32x4 x0, x1v;
;                     if (f32in) { x0 = *(const f32x4*)(xin + (ro + cofs) * 4 + loff4); x1v = *(const f32x4*)(xin + (ro + cofs) * 4 + loff4 + 16); }
;                     else { const u32x4 w = *(const u32x4*)(xin + (ro + cofs) * 2 + loff2); x0 = (f32x4){bflo(w.x), bfhi(w.x), bflo(w.y), bfhi(w.y)}; x1v = (f32x4){bflo(w.z), bfhi(w.z), bflo(w.w), bfhi(w.w)}; }
;                     const f32x4 o0 = x0 + g0 * acc[ai][bj][m][0], o1 = x1v + g1v * acc[ai][bj][m][1];
;                     u32x4 ow; ow.x = pk2(o0[0], o0[1]); ow.y = pk2(o0[2], o0[3]); ow.z = pk2(o1[0], o1[1]); ow.w = pk2(o1[2], o1[3]);
;                     *(u32x4*)(xo + (ro + cofs) * 2 + loff2) = ow; }
;                 asm volatile("" ::: "memory"); }
.LBB0_1984:
	s_waitcnt vmcnt(0)
	v_pk_fma_f32 v[62:63], v[62:63], v[70:71], v[78:79]
	v_pk_fma_f32 v[68:69], v[60:61], v[68:69], v[76:77]
	v_pk_fma_f32 v[60:61], v[58:59], v[66:67], v[74:75]
	v_pk_fma_f32 v[64:65], v[64:65], v[72:73], v[80:81]
	v_cvt_pk_bf16_f32 v58, v62, v63
	v_cvt_pk_bf16_f32 v59, v64, v65
	v_bfe_u32 v1, v60, 16, 1
	v_add3_u32 v1, v60, v1, s37
	v_bfe_u32 v60, v61, 16, 1
	v_lshrrev_b32_e32 v1, 16, v1
	v_add3_u32 v60, v61, v60, s37
	v_and_or_b32 v60, v60, s33, v1
	v_add_co_u32_e32 v62, vcc, 0x80000, v160
	v_cvt_pk_bf16_f32 v61, v68, v69
	s_nop 0
	v_addc_co_u32_e32 v63, vcc, 0, v161, vcc
	global_store_dwordx4 v[62:63], v[58:61], off sc1
	global_load_dwordx4 v[58:61], v[164:165], off offset:528
	s_nop 0
	global_load_dwordx4 v[62:65], v[164:165], off offset:512
	s_and_b64 vcc, exec, s[38:39]
	s_cbranch_vccnz .LBB0_2019
	s_mov_b64 s[26:27], 0x100200
	v_add_co_u32_e32 v68, vcc, 0x100000, v162
	v_lshl_add_u64 v[66:67], v[162:163], 0, s[26:27]
	s_nop 0
	v_addc_co_u32_e32 v69, vcc, 0, v163, vcc
	global_load_dwordx4 v[70:73], v[68:69], off offset:512
	s_nop 0
	global_load_dwordx4 v[66:69], v[66:67], off offset:16
	s_cbranch_execnz .LBB0_1987

; __device__ __forceinline__ unsigned pk2(float lo, float hi) { return f2bf(lo) | (f2bf(hi) << 16); }
;     __device__ __forceinline__ void epi(const f32x4 (&acc)[2][2][4][2], const Unit& u, int wr, int wc, int fr, int fq) const {
;     ...
;                 for (int bj = 0; bj < 2; ++bj) { const int cofs = bj * 128;
;                     const f32x4 g0 = *(const f32x4*)(g1 + cofs * 4 + lcol * 4), g1v = *(const f32x4*)(g1 + cofs * 4 + lcol * 4 + 16);
;                     f32x4 x0, x1v;
;                     if (f32in) { x0 = *(const f32x4*)(xin + (ro + cofs) * 4 + loff4); x1v = *(const f32x4*)(xin + (ro + cofs) * 4 + loff4 + 16); }
;                     else { const u32x4 w = *(const u32x4*)(xin + (ro + cofs) * 2 + loff2); x0 = (f32x4){bflo(w.x), bfhi(w.x), bflo(w.y), bfhi(w.y)}; x1v = (f32x4){bflo(w.z), bfhi(w.z), bflo(w.w), bfhi(w.w)}; }
;                     const f32x4 o0 = x0 + g0 * acc[ai][bj][m][0], o1 = x1v + g1v * acc[ai][bj][m][1];
;                     u32x4 ow; ow.x = pk2(o0[0], o0[1]); ow.y = pk2(o0[2], o0[3]); ow.z = pk2(o1[0], o1[1]); ow.w = pk2(o1[2], o1[3]);
;                     *(u32x4*)(xo + (ro + cofs) * 2 + loff2) = ow; }
;                 asm volatile("" ::: "memory"); }
.LBB0_1987:
	s_waitcnt vmcnt(0)
	v_pk_fma_f32 v[54:55], v[54:55], v[62:63], v[70:71]
	v_pk_fma_f32 v[60:61], v[52:53], v[60:61], v[68:69]
	v_pk_fma_f32 v[52:53], v[50:51], v[58:59], v[66:67]
	v_pk_fma_f32 v[56:57], v[56:57], v[64:65], v[72:73]
	v_cvt_pk_bf16_f32 v50, v54, v55
	v_cvt_pk_bf16_f32 v51, v56, v57
	v_bfe_u32 v1, v52, 16, 1
	v_add3_u32 v1, v52, v1, s37
	v_bfe_u32 v52, v53, 16, 1
	v_lshrrev_b32_e32 v1, 16, v1
	v_add3_u32 v52, v53, v52, s37
	v_and_or_b32 v52, v52, s33, v1
	v_add_co_u32_e32 v54, vcc, 0x80000, v160
	v_cvt_pk_bf16_f32 v53, v60, v61
	s_nop 0
	v_addc_co_u32_e32 v55, vcc, 0, v161, vcc
	global_store_dwordx4 v[54:55], v[50:53], off offset:256 sc1
	global_load_dwordx4 v[50:53], v[164:165], off offset:16
	global_load_dwordx4 v[54:57], v[164:165], off
	s_and_b64 vcc, exec, s[38:39]
	s_cbranch_vccnz .LBB0_2020
	s_mov_b64 s[26:27], 0x120000
	v_add_co_u32_e32 v60, vcc, 0x120000, v162
	v_lshl_add_u64 v[58:59], v[162:163], 0, s[26:27]
	s_nop 0
	v_addc_co_u32_e32 v61, vcc, 0, v163, vcc
	global_load_dwordx4 v[62:65], v[60:61], off
	s_nop 0
	global_load_dwordx4 v[58:61], v[58:59], off offset:16
	s_cbranch_execnz .LBB0_1990

; __device__ __forceinline__ unsigned pk2(float lo, float hi) { return f2bf(lo) | (f2bf(hi) << 16); }
;     __device__ __forceinline__ void epi(const f32x4 (&acc)[2][2][4][2], const Unit& u, int wr, int wc, int fr, int fq) const {
;     ...
;                 for (int bj = 0; bj < 2; ++bj) { const int cofs = bj * 128;
;                     const f32x4 g0 = *(const f32x4*)(g1 + cofs * 4 + lcol * 4), g1v = *(const f32x4*)(g1 + cofs * 4 + lcol * 4 + 16);
;                     f32x4 x0, x1v;
;                     if (f32in) { x0 = *(const f32x4*)(xin + (ro + cofs) * 4 + loff4); x1v = *(const f32x4*)(xin + (ro + cofs) * 4 + loff4 + 16); }
;                     else { const u32x4 w = *(const u32x4*)(xin + (ro + cofs) * 2 + loff2); x0 = (f32x4){bflo(w.x), bfhi(w.x), bflo(w.y), bfhi(w.y)}; x1v = (f32x4){bflo(w.z), bfhi(w.z), bflo(w.w), bfhi(w.w)}; }
;                     const f32x4 o0 = x0 + g0 * acc[ai][bj][m][0], o1 = x1v + g1v * acc[ai][bj][m][1];
;                     u32x4 ow; ow.x = pk2(o0[0], o0[1]); ow.y = pk2(o0[2], o0[3]); ow.z = pk2(o1[0], o1[1]); ow.w = pk2(o1[2], o1[3]);
;                     *(u32x4*)(xo + (ro + cofs) * 2 + loff2) = ow; }
;                 asm volatile("" ::: "memory"); }
.LBB0_1990:
	s_waitcnt vmcnt(0)
	v_pk_fma_f32 v[46:47], v[46:47], v[54:55], v[62:63]
	v_pk_fma_f32 v[52:53], v[44:45], v[52:53], v[60:61]
	v_pk_fma_f32 v[44:45], v[42:43], v[50:51], v[58:59]
	v_pk_fma_f32 v[48:49], v[48:49], v[56:57], v[64:65]
	v_cvt_pk_bf16_f32 v42, v46, v47
	v_cvt_pk_bf16_f32 v43, v48, v49
	v_bfe_u32 v1, v44, 16, 1
	v_add3_u32 v1, v44, v1, s37
	v_bfe_u32 v44, v45, 16, 1
	v_lshrrev_b32_e32 v1, 16, v1
	v_add3_u32 v44, v45, v44, s37
	v_and_or_b32 v44, v44, s33, v1
	v_add_co_u32_e32 v46, vcc, 0x90000, v160
	v_cvt_pk_bf16_f32 v45, v52, v53
	s_nop 0
	v_addc_co_u32_e32 v47, vcc, 0, v161, vcc
	global_store_dwordx4 v[46:47], v[42:45], off sc1
	global_load_dwordx4 v[42:45], v[164:165], off offset:528
	s_nop 0
	global_load_dwordx4 v[46:49], v[164:165], off offset:512
	s_and_b64 vcc, exec, s[38:39]
	s_cbranch_vccnz .LBB0_2021
	s_mov_b64 s[26:27], 0x120200
	v_add_co_u32_e32 v52, vcc, 0x120000, v162
	v_lshl_add_u64 v[50:51], v[162:163], 0, s[26:27]
	s_nop 0
	v_addc_co_u32_e32 v53, vcc, 0, v163, vcc
	global_load_dwordx4 v[54:57], v[52:53], off offset:512
	s_nop 0
	global_load_dwordx4 v[50:53], v[50:51], off offset:16
	s_cbranch_execnz .LBB0_1993

; __device__ __forceinline__ unsigned pk2(float lo, float hi) { return f2bf(lo) | (f2bf(hi) << 16); }
;     __device__ __forceinline__ void epi(const f32x4 (&acc)[2][2][4][2], const Unit& u, int wr, int wc, int fr, int fq) const {
;     ...
;                 for (int bj = 0; bj < 2; ++bj) { const int cofs = bj * 128;
;                     const f32x4 g0 = *(const f32x4*)(g1 + cofs * 4 + lcol * 4), g1v = *(const f32x4*)(g1 + cofs * 4 + lcol * 4 + 16);
;                     f32x4 x0, x1v;
;                     if (f32in) { x0 = *(const f32x4*)(xin + (ro + cofs) * 4 + loff4); x1v = *(const f32x4*)(xin + (ro + cofs) * 4 + loff4 + 16); }
;                     else { const u32x4 w = *(const u32x4*)(xin + (ro + cofs) * 2 + loff2); x0 = (f32x4){bflo(w.x), bfhi(w.x), bflo(w.y), bfhi(w.y)}; x1v = (f32x4){bflo(w.z), bfhi(w.z), bflo(w.w), bfhi(w.w)}; }
;                     const f32x4 o0 = x0 + g0 * acc[ai][bj][m][0], o1 = x1v + g1v * acc[ai][bj][m][1];
;                     u32x4 ow; ow.x = pk2(o0[0], o0[1]); ow.y = pk2(o0[2], o0[3]); ow.z = pk2(o1[0], o1[1]); ow.w = pk2(o1[2], o1[3]);
;                     *(u32x4*)(xo + (ro + cofs) * 2 + loff2) = ow; }
;                 asm volatile("" ::: "memory"); }
.LBB0_1993:
	s_waitcnt vmcnt(0)
	v_pk_fma_f32 v[38:39], v[38:39], v[46:47], v[54:55]
	v_pk_fma_f32 v[44:45], v[36:37], v[44:45], v[52:53]
	v_pk_fma_f32 v[36:37], v[34:35], v[42:43], v[50:51]
	v_pk_fma_f32 v[40:41], v[40:41], v[48:49], v[56:57]
	v_cvt_pk_bf16_f32 v34, v38, v39
	v_cvt_pk_bf16_f32 v35, v40, v41
	v_bfe_u32 v1, v36, 16, 1
	v_add3_u32 v1, v36, v1, s37
	v_bfe_u32 v36, v37, 16, 1
	v_lshrrev_b32_e32 v1, 16, v1
	v_add3_u32 v36, v37, v36, s37
	v_and_or_b32 v36, v36, s33, v1
	v_add_co_u32_e32 v38, vcc, 0x90000, v160
	v_cvt_pk_bf16_f32 v37, v44, v45
	s_nop 0
	v_addc_co_u32_e32 v39, vcc, 0, v161, vcc
	global_store_dwordx4 v[38:39], v[34:37], off offset:256 sc1
	global_load_dwordx4 v[34:37], v[164:165], off offset:16
	global_load_dwordx4 v[38:41], v[164:165], off
	s_and_b64 vcc, exec, s[38:39]
	s_cbranch_vccnz .LBB0_2022
	s_mov_b64 s[26:27], 0x140000
	v_add_co_u32_e32 v44, vcc, 0x140000, v162
	v_lshl_add_u64 v[42:43], v[162:163], 0, s[26:27]
	s_nop 0
	v_addc_co_u32_e32 v45, vcc, 0, v163, vcc
	global_load_dwordx4 v[46:49], v[44:45], off
	s_nop 0
	global_load_dwordx4 v[42:45], v[42:43], off offset:16
	s_cbranch_execnz .LBB0_1996

; __device__ __forceinline__ unsigned pk2(float lo, float hi) { return f2bf(lo) | (f2bf(hi) << 16); }
;     __device__ __forceinline__ void epi(const f32x4 (&acc)[2][2][4][2], const Unit& u, int wr, int wc, int fr, int fq) const {
;     ...
;                 for (int bj = 0; bj < 2; ++bj) { const int cofs = bj * 128;
;                     const f32x4 g0 = *(const f32x4*)(g1 + cofs * 4 + lcol * 4), g1v = *(const f32x4*)(g1 + cofs * 4 + lcol * 4 + 16);
;                     f32x4 x0, x1v;
;                     if (f32in) { x0 = *(const f32x4*)(xin + (ro + cofs) * 4 + loff4); x1v = *(const f32x4*)(xin + (ro + cofs) * 4 + loff4 + 16); }
;                     else { const u32x4 w = *(const u32x4*)(xin + (ro + cofs) * 2 + loff2); x0 = (f32x4){bflo(w.x), bfhi(w.x), bflo(w.y), bfhi(w.y)}; x1v = (f32x4){bflo(w.z), bfhi(w.z), bflo(w.w), bfhi(w.w)}; }
;                     const f32x4 o0 = x0 + g0 * acc[ai][bj][m][0], o1 = x1v + g1v * acc[ai][bj][m][1];
;                     u32x4 ow; ow.x = pk2(o0[0], o0[1]); ow.y = pk2(o0[2], o0[3]); ow.z = pk2(o1[0], o1[1]); ow.w = pk2(o1[2], o1[3]);
;                     *(u32x4*)(xo + (ro + cofs) * 2 + loff2) = ow; }
;                 asm volatile("" ::: "memory"); }
.LBB0_1996:
	s_waitcnt vmcnt(0)
	v_pk_fma_f32 v[30:31], v[30:31], v[38:39], v[46:47]
	v_pk_fma_f32 v[36:37], v[28:29], v[36:37], v[44:45]
	v_pk_fma_f32 v[28:29], v[26:27], v[34:35], v[42:43]
	v_pk_fma_f32 v[32:33], v[32:33], v[40:41], v[48:49]
	v_cvt_pk_bf16_f32 v26, v30, v31
	v_cvt_pk_bf16_f32 v27, v32, v33
	v_bfe_u32 v1, v28, 16, 1
	v_add3_u32 v1, v28, v1, s37
	v_bfe_u32 v28, v29, 16, 1
	v_lshrrev_b32_e32 v1, 16, v1
	v_add3_u32 v28, v29, v28, s37
	v_and_or_b32 v28, v28, s33, v1
	v_add_co_u32_e32 v30, vcc, 0xa0000, v160
	v_cvt_pk_bf16_f32 v29, v36, v37
	s_nop 0
	v_addc_co_u32_e32 v31, vcc, 0, v161, vcc
	global_store_dwordx4 v[30:31], v[26:29], off sc1
	global_load_dwordx4 v[26:29], v[164:165], off offset:528
	s_nop 0
	global_load_dwordx4 v[30:33], v[164:165], off offset:512
	s_and_b64 vcc, exec, s[38:39]
	s_cbranch_vccnz .LBB0_2023
	s_mov_b64 s[26:27], 0x140200
	v_add_co_u32_e32 v36, vcc, 0x140000, v162
	v_lshl_add_u64 v[34:35], v[162:163], 0, s[26:27]
	s_nop 0
	v_addc_co_u32_e32 v37, vcc, 0, v163, vcc
	global_load_dwordx4 v[38:41], v[36:37], off offset:512
	s_nop 0
	global_load_dwordx4 v[34:37], v[34:35], off offset:16
	s_cbranch_execnz .LBB0_1999

; __device__ __forceinline__ unsigned pk2(float lo, float hi) { return f2bf(lo) | (f2bf(hi) << 16); }
;     __device__ __forceinline__ void epi(const f32x4 (&acc)[2][2][4][2], const Unit& u, int wr, int wc, int fr, int fq) const {
;     ...
;                 for (int bj = 0; bj < 2; ++bj) { const int cofs = bj * 128;
;                     const f32x4 g0 = *(const f32x4*)(g1 + cofs * 4 + lcol * 4), g1v = *(const f32x4*)(g1 + cofs * 4 + lcol * 4 + 16);
;                     f32x4 x0, x1v;
;                     if (f32in) { x0 = *(const f32x4*)(xin + (ro + cofs) * 4 + loff4); x1v = *(const f32x4*)(xin + (ro + cofs) * 4 + loff4 + 16); }
;                     else { const u32x4 w = *(const u32x4*)(xin + (ro + cofs) * 2 + loff2); x0 = (f32x4){bflo(w.x), bfhi(w.x), bflo(w.y), bfhi(w.y)}; x1v = (f32x4){bflo(w.z), bfhi(w.z), bflo(w.w), bfhi(w.w)}; }
;                     const f32x4 o0 = x0 + g0 * acc[ai][bj][m][0], o1 = x1v + g1v * acc[ai][bj][m][1];
;                     u32x4 ow; ow.x = pk2(o0[0], o0[1]); ow.y = pk2(o0[2], o0[3]); ow.z = pk2(o1[0], o1[1]); ow.w = pk2(o1[2], o1[3]);
;                     *(u32x4*)(xo + (ro + cofs) * 2 + loff2) = ow; }
;                 asm volatile("" ::: "memory"); }
.LBB0_1999:
	s_waitcnt vmcnt(0)
	v_pk_fma_f32 v[22:23], v[22:23], v[30:31], v[38:39]
	v_pk_fma_f32 v[28:29], v[20:21], v[28:29], v[36:37]
	v_pk_fma_f32 v[20:21], v[18:19], v[26:27], v[34:35]
	v_pk_fma_f32 v[24:25], v[24:25], v[32:33], v[40:41]
	v_cvt_pk_bf16_f32 v18, v22, v23
	v_cvt_pk_bf16_f32 v19, v24, v25
	v_bfe_u32 v1, v20, 16, 1
	v_add3_u32 v1, v20, v1, s37
	v_bfe_u32 v20, v21, 16, 1
	v_lshrrev_b32_e32 v1, 16, v1
	v_add3_u32 v20, v21, v20, s37
	v_and_or_b32 v20, v20, s33, v1
	v_add_co_u32_e32 v22, vcc, 0xa0000, v160
	v_cvt_pk_bf16_f32 v21, v28, v29
	s_nop 0
	v_addc_co_u32_e32 v23, vcc, 0, v161, vcc
	global_store_dwordx4 v[22:23], v[18:21], off offset:256 sc1
	global_load_dwordx4 v[18:21], v[164:165], off offset:16
	global_load_dwordx4 v[22:25], v[164:165], off
	s_and_b64 vcc, exec, s[38:39]
	s_cbranch_vccnz .LBB0_2024
	s_mov_b64 s[26:27], 0x160000
	v_add_co_u32_e32 v28, vcc, 0x160000, v162
	v_lshl_add_u64 v[26:27], v[162:163], 0, s[26:27]
	s_nop 0
	v_addc_co_u32_e32 v29, vcc, 0, v163, vcc
	global_load_dwordx4 v[30:33], v[28:29], off
	s_nop 0
	global_load_dwordx4 v[26:29], v[26:27], off offset:16
	s_cbranch_execnz .LBB0_2002

; __device__ __forceinline__ unsigned pk2(float lo, float hi) { return f2bf(lo) | (f2bf(hi) << 16); }
;     __device__ __forceinline__ void epi(const f32x4 (&acc)[2][2][4][2], const Unit& u, int wr, int wc, int fr, int fq) const {
;     ...
;                 for (int bj = 0; bj < 2; ++bj) { const int cofs = bj * 128;
;                     const f32x4 g0 = *(const f32x4*)(g1 + cofs * 4 + lcol * 4), g1v = *(const f32x4*)(g1 + cofs * 4 + lcol * 4 + 16);
;                     f32x4 x0, x1v;
;                     if (f32in) { x0 = *(const f32x4*)(xin + (ro + cofs) * 4 + loff4); x1v = *(const f32x4*)(xin + (ro + cofs) * 4 + loff4 + 16); }
;                     else { const u32x4 w = *(const u32x4*)(xin + (ro + cofs) * 2 + loff2); x0 = (f32x4){bflo(w.x), bfhi(w.x), bflo(w.y), bfhi(w.y)}; x1v = (f32x4){bflo(w.z), bfhi(w.z), bflo(w.w), bfhi(w.w)}; }
;                     const f32x4 o0 = x0 + g0 * acc[ai][bj][m][0], o1 = x1v + g1v * acc[ai][bj][m][1];
;                     u32x4 ow; ow.x = pk2(o0[0], o0[1]); ow.y = pk2(o0[2], o0[3]); ow.z = pk2(o1[0], o1[1]); ow.w = pk2(o1[2], o1[3]);
;                     *(u32x4*)(xo + (ro + cofs) * 2 + loff2) = ow; }
;                 asm volatile("" ::: "memory"); }
.LBB0_2002:
	s_waitcnt vmcnt(0)
	v_pk_fma_f32 v[14:15], v[14:15], v[22:23], v[30:31]
	v_pk_fma_f32 v[20:21], v[12:13], v[20:21], v[28:29]
	v_pk_fma_f32 v[12:13], v[10:11], v[18:19], v[26:27]
	v_pk_fma_f32 v[16:17], v[16:17], v[24:25], v[32:33]
	v_cvt_pk_bf16_f32 v10, v14, v15
	v_cvt_pk_bf16_f32 v11, v16, v17
	v_bfe_u32 v1, v12, 16, 1
	v_add3_u32 v1, v12, v1, s37
	v_bfe_u32 v12, v13, 16, 1
	v_lshrrev_b32_e32 v1, 16, v1
	v_add3_u32 v12, v13, v12, s37
	v_and_or_b32 v12, v12, s33, v1
	v_add_co_u32_e32 v14, vcc, 0xb0000, v160
	v_cvt_pk_bf16_f32 v13, v20, v21
	s_nop 0
	v_addc_co_u32_e32 v15, vcc, 0, v161, vcc
	global_store_dwordx4 v[14:15], v[10:13], off sc1
	global_load_dwordx4 v[10:13], v[164:165], off offset:528
	s_nop 0
	global_load_dwordx4 v[14:17], v[164:165], off offset:512
	s_and_b64 vcc, exec, s[38:39]
	s_cbranch_vccnz .LBB0_2025
	s_mov_b64 s[26:27], 0x160200
	v_add_co_u32_e32 v20, vcc, 0x160000, v162
	v_lshl_add_u64 v[18:19], v[162:163], 0, s[26:27]
	s_nop 0
	v_addc_co_u32_e32 v21, vcc, 0, v163, vcc
	global_load_dwordx4 v[22:25], v[20:21], off offset:512
	s_nop 0
	global_load_dwordx4 v[18:21], v[18:19], off offset:16
	s_cbranch_execnz .LBB0_2005

; __device__ __forceinline__ unsigned pk2(float lo, float hi) { return f2bf(lo) | (f2bf(hi) << 16); }
;     __device__ __forceinline__ void epi(const f32x4 (&acc)[2][2][4][2], const Unit& u, int wr, int wc, int fr, int fq) const {
;     ...
;                 for (int bj = 0; bj < 2; ++bj) { const int cofs = bj * 128;
;                     const f32x4 g0 = *(const f32x4*)(g1 + cofs * 4 + lcol * 4), g1v = *(const f32x4*)(g1 + cofs * 4 + lcol * 4 + 16);
;                     f32x4 x0, x1v;
;                     if (f32in) { x0 = *(const f32x4*)(xin + (ro + cofs) * 4 + loff4); x1v = *(const f32x4*)(xin + (ro + cofs) * 4 + loff4 + 16); }
;                     else { const u32x4 w = *(const u32x4*)(xin + (ro + cofs) * 2 + loff2); x0 = (f32x4){bflo(w.x), bfhi(w.x), bflo(w.y), bfhi(w.y)}; x1v = (f32x4){bflo(w.z), bfhi(w.z), bflo(w.w), bfhi(w.w)}; }
;                     const f32x4 o0 = x0 + g0 * acc[ai][bj][m][0], o1 = x1v + g1v * acc[ai][bj][m][1];
;                     u32x4 ow; ow.x = pk2(o0[0], o0[1]); ow.y = pk2(o0[2], o0[3]); ow.z = pk2(o1[0], o1[1]); ow.w = pk2(o1[2], o1[3]);
;                     *(u32x4*)(xo + (ro + cofs) * 2 + loff2) = ow; }
;                 asm volatile("" ::: "memory"); }
.LBB0_2005:
	s_waitcnt vmcnt(0)
	v_pk_fma_f32 v[6:7], v[6:7], v[14:15], v[22:23]
	v_pk_fma_f32 v[12:13], v[4:5], v[12:13], v[20:21]
	v_pk_fma_f32 v[4:5], v[2:3], v[10:11], v[18:19]
	v_pk_fma_f32 v[8:9], v[8:9], v[16:17], v[24:25]
	v_cvt_pk_bf16_f32 v2, v6, v7
	v_cvt_pk_bf16_f32 v3, v8, v9
	v_bfe_u32 v1, v4, 16, 1
	v_add3_u32 v1, v4, v1, s37
	v_bfe_u32 v4, v5, 16, 1
	v_lshrrev_b32_e32 v1, 16, v1
	v_add3_u32 v4, v5, v4, s37
	v_and_or_b32 v4, v4, s33, v1
	v_add_co_u32_e32 v6, vcc, 0xb0000, v160
	v_cvt_pk_bf16_f32 v5, v12, v13
	s_nop 0
	v_addc_co_u32_e32 v7, vcc, 0, v161, vcc
	global_store_dwordx4 v[6:7], v[2:5], off offset:256 sc1
	s_andn2_b64 vcc, exec, s[16:17]
	s_mov_b64 s[16:17], -1
	s_cbranch_vccnz .LBB0_1938
	s_andn2_b64 vcc, exec, s[4:5]
	s_cbranch_vccnz .LBB0_1937
	s_barrier
	s_branch .LBB0_1937

; __device__ __forceinline__ void phase_topk(const Args& a, const Ctx& c0, int l, bool last) {
;     ...
;         for (int s0 = wave * 8; s0 < capq; s0 += 64) {
;             u32x4 t[8][2];
; #pragma unroll
;             for (int q = 0; q < 8; ++q) { const u32x4* src = (const u32x4*)(H + (size_t)selrow[s0 + q] * DM);
; #pragma unroll
;                 for (int j = 0; j < 2; ++j) t[q][j] = src[lane + 64 * j]; }
; #pragma unroll
;             for (int q = 0; q < 8; ++q) { u32x4* dst = (u32x4*)(XG + ((size_t)e * EROWS + slot0 + slo + s0 + q) * DM);
; #pragma unroll
;                 for (int j = 0; j < 2; ++j) dst[lane + 64 * j] = t[q][j]; } }
.LBB0_2320:
	s_nop 0
	v_mov_b32_e32 v1, s4
	ds_read_b128 v[8:11], v1
	ds_read_b128 v[76:79], v1 offset:16
	v_lshl_add_u64 v[100:101], v[58:59], 0, s[2:3]
	s_mov_b32 s6, 0x5db00000
	v_add_co_u32_e32 v100, vcc, s6, v100
	s_waitcnt lgkmcnt(1)
	v_ashrrev_i32_e32 v3, 31, v8
	v_mov_b32_e32 v2, v8
	v_ashrrev_i32_e32 v5, 31, v9
	v_mov_b32_e32 v4, v9
	v_lshlrev_b64 v[2:3], 11, v[2:3]
	v_lshlrev_b64 v[4:5], 11, v[4:5]
	v_lshl_add_u64 v[2:3], v[60:61], 0, v[2:3]
	v_ashrrev_i32_e32 v13, 31, v10
	v_mov_b32_e32 v12, v10
	global_load_dwordx4 v[18:21], v[2:3], off
	global_load_dwordx4 v[22:25], v[2:3], off offset:1024
	v_lshl_add_u64 v[6:7], v[60:61], 0, v[4:5]
	v_ashrrev_i32_e32 v15, 31, v11
	v_mov_b32_e32 v14, v11
	v_lshlrev_b64 v[12:13], 11, v[12:13]
	global_load_dwordx4 v[2:5], v[6:7], off
	s_nop 0
	global_load_dwordx4 v[6:9], v[6:7], off offset:1024
	v_lshlrev_b64 v[10:11], 11, v[14:15]
	v_lshl_add_u64 v[12:13], v[60:61], 0, v[12:13]
	s_waitcnt lgkmcnt(0)
	v_ashrrev_i32_e32 v27, 31, v76
	v_mov_b32_e32 v26, v76
	global_load_dwordx4 v[34:37], v[12:13], off
	global_load_dwordx4 v[38:41], v[12:13], off offset:1024
	v_lshl_add_u64 v[14:15], v[60:61], 0, v[10:11]
	v_ashrrev_i32_e32 v29, 31, v77
	v_mov_b32_e32 v28, v77
	v_lshlrev_b64 v[26:27], 11, v[26:27]
	global_load_dwordx4 v[10:13], v[14:15], off
	s_nop 0
	global_load_dwordx4 v[14:17], v[14:15], off offset:1024
	v_lshlrev_b64 v[28:29], 11, v[28:29]
	v_lshl_add_u64 v[26:27], v[60:61], 0, v[26:27]
	global_load_dwordx4 v[80:83], v[26:27], off
	global_load_dwordx4 v[84:87], v[26:27], off offset:1024
	v_lshl_add_u64 v[30:31], v[60:61], 0, v[28:29]
	global_load_dwordx4 v[26:29], v[30:31], off
	s_nop 0
	global_load_dwordx4 v[30:33], v[30:31], off offset:1024
	v_ashrrev_i32_e32 v77, 31, v78
	v_mov_b32_e32 v76, v78
	v_ashrrev_i32_e32 v89, 31, v79
	v_mov_b32_e32 v88, v79
	v_lshlrev_b64 v[76:77], 11, v[76:77]
	v_lshlrev_b64 v[92:93], 11, v[88:89]
	v_lshl_add_u64 v[88:89], v[60:61], 0, v[76:77]
	global_load_dwordx4 v[76:79], v[88:89], off
	s_nop 0
	global_load_dwordx4 v[88:91], v[88:89], off offset:1024
	v_lshl_add_u64 v[96:97], v[60:61], 0, v[92:93]
	global_load_dwordx4 v[92:95], v[96:97], off
	s_nop 0
	global_load_dwordx4 v[96:99], v[96:97], off offset:1024
	v_addc_co_u32_e32 v101, vcc, 0, v101, vcc
	s_or_b32 s6, s2, 0x800
	s_mov_b32 s7, s3
	s_add_i32 s5, s5, 64
	s_addk_i32 s4, 0x100
	s_waitcnt vmcnt(15)
	global_store_dwordx4 v[100:101], v[18:21], off sc1
	s_waitcnt vmcnt(15)
	global_store_dwordx4 v[100:101], v[22:25], off offset:1024 sc1
	v_lshl_add_u64 v[18:19], v[62:63], 0, s[6:7]
	s_or_b32 s6, s2, 0x1000
	s_waitcnt vmcnt(15)
	global_store_dwordx4 v[18:19], v[2:5], off sc1
	s_waitcnt vmcnt(15)
	global_store_dwordx4 v[18:19], v[6:9], off offset:1024 sc1
	v_lshl_add_u64 v[2:3], v[62:63], 0, s[6:7]
	s_or_b32 s6, s2, 0x1800
	s_waitcnt vmcnt(15)
	global_store_dwordx4 v[2:3], v[34:37], off sc1
	s_waitcnt vmcnt(15)
	global_store_dwordx4 v[2:3], v[38:41], off offset:1024 sc1
	v_lshl_add_u64 v[2:3], v[62:63], 0, s[6:7]
	s_or_b32 s6, s2, 0x2000
	s_waitcnt vmcnt(15)
	global_store_dwordx4 v[2:3], v[10:13], off sc1
	s_waitcnt vmcnt(15)
	global_store_dwordx4 v[2:3], v[14:17], off offset:1024 sc1
	v_lshl_add_u64 v[2:3], v[62:63], 0, s[6:7]
	s_or_b32 s6, s2, 0x2800
	s_waitcnt vmcnt(15)
	global_store_dwordx4 v[2:3], v[80:83], off sc1
	s_waitcnt vmcnt(15)
	global_store_dwordx4 v[2:3], v[84:87], off offset:1024 sc1
	v_lshl_add_u64 v[2:3], v[62:63], 0, s[6:7]
	s_or_b32 s6, s2, 0x3000
	s_waitcnt vmcnt(15)
	global_store_dwordx4 v[2:3], v[26:29], off sc1
	s_waitcnt vmcnt(15)
	global_store_dwordx4 v[2:3], v[30:33], off offset:1024 sc1
	v_lshl_add_u64 v[2:3], v[62:63], 0, s[6:7]
	s_or_b32 s6, s2, 0x3800
	s_add_u32 s2, s2, 0x20000
	s_addc_u32 s3, s3, 0
	s_waitcnt vmcnt(15)
	global_store_dwordx4 v[2:3], v[76:79], off sc1
	s_waitcnt vmcnt(15)
	global_store_dwordx4 v[2:3], v[88:91], off offset:1024 sc1
	v_lshl_add_u64 v[2:3], v[62:63], 0, s[6:7]
	s_cmp_ge_i32 s5, s47
	s_waitcnt vmcnt(15)
	global_store_dwordx4 v[2:3], v[92:95], off sc1
	s_waitcnt vmcnt(15)
	global_store_dwordx4 v[2:3], v[96:99], off offset:1024 sc1
	s_cbranch_scc0 .LBB0_2320

; __device__ __forceinline__ void phase_topk(const Args& a, const Ctx& c0, int l, bool last) {
;     ...
;         if (seg == 1 && b == 0) {
;             u32x4* dst = (u32x4*)(XG + ((size_t)e * EROWS + 2176) * DM);
;             for (int i = tid; i < 128 * DM / 16; i += 512) dst[i] = (u32x4){0u, 0u, 0u, 0u};
;             if (tid < 128) GATEV[e * EROWS + 2176 + tid] = 0.f; }
.LBB0_2324:
	v_add_u32_e32 v4, 0x200, v4
	s_movk_i32 s6, 0x3dff
	v_cmp_lt_i32_e32 vcc, s6, v4
	global_store_dwordx4 v[2:3], v[234:237], off sc1
	s_or_b64 s[4:5], vcc, s[4:5]
	v_lshl_add_u64 v[2:3], v[2:3], 0, s[8:9]
	s_andn2_b64 exec, exec, s[4:5]
	s_cbranch_execnz .LBB0_2324

; __device__ __forceinline__ unsigned pk2(float lo, float hi) { return f2bf(lo) | (f2bf(hi) << 16); }
;     __device__ __forceinline__ void epi(const f32x4 (&acc)[2][2][4][2], const Unit& u, int wr, int wc, int fr, int fq) const {
;         const int e = u.pm / tpe, t = u.pm - e * tpe; const size_t rowt = (size_t)e * EROWS + (size_t)t * 256;
;         char* base = (char*)(YE + rowt * 2048 + (size_t)u.pn * 256); const char* gp = (const char*)(gatev + rowt);
;         unsigned loff = (unsigned)((wr * 64 + fr) * 2048 + wc * 32 + 8 * fq) * 2u, goff = (unsigned)(wr * 64 + fr) * 4u; asm volatile("" : "+v"(loff), "+v"(goff));
; #pragma unroll
;         for (int ai = 0; ai < 2; ++ai)
; #pragma unroll
;             for (int m = 0; m < 4; ++m) { const float g = *(const float*)(gp + (ai * 128 + m * 16) * 4 + goff) * (1.f / W8_SCALE);
; #pragma unroll
;                 for (int bj = 0; bj < 2; ++bj) { const f32x4 v0 = acc[ai][bj][m][0] * g, v1 = acc[ai][bj][m][1] * g;
;                     u32x4 w; w.x = pk2(v0[0], v0[1]); w.y = pk2(v0[2], v0[3]); w.z = pk2(v1[0], v1[1]); w.w = pk2(v1[2], v1[3]);
;                     *(u32x4*)(base + ((size_t)(ai * 128 + m * 16) * 2048 + bj * 128) * 2 + loff) = w; } }
;     }
.LBB0_2666:
	s_abs_i32 s18, s17
	s_mul_hi_u32 s19, s18, s45
	s_mul_i32 s20, s19, s24
	s_sub_i32 s18, s18, s20
	s_ashr_i32 s11, s17, 31
	s_add_i32 s20, s19, 1
	s_sub_i32 s21, s18, s24
	s_cmp_ge_u32 s18, s24
	s_cselect_b32 s19, s20, s19
	s_cselect_b32 s18, s21, s18
	s_add_i32 s20, s19, 1
	s_cmp_ge_u32 s18, s24
	s_cselect_b32 s18, s20, s19
	s_xor_b32 s18, s18, s11
	s_sub_i32 s11, s18, s11
	s_mul_i32 s18, s11, s24
	s_sub_i32 s18, s17, s18
	s_ashr_i32 s19, s18, 31
	s_mul_hi_i32 s17, s11, 0x900
	s_mulk_i32 s11, 0x900
	s_lshl_b64 s[18:19], s[18:19], 8
	s_add_u32 s20, s18, s11
	s_addc_u32 s21, s19, s17
	s_lshl_b64 s[18:19], s[20:21], 12
	s_add_u32 s11, s50, s18
	s_addc_u32 s19, s51, s19
	s_ashr_i32 s17, s16, 31
	s_lshl_b64 s[16:17], s[16:17], 9
	s_add_u32 s18, s11, s16
	s_addc_u32 s19, s19, s17
	s_lshl_b64 s[16:17], s[20:21], 2
	s_add_u32 s16, s52, s16
	s_addc_u32 s17, s53, s17
	v_mov_b32_e32 v4, v186
	v_mov_b32_e32 v146, v188
	global_load_dword v1, v4, s[16:17]
	s_mov_b32 s11, 0x20000
	s_waitcnt vmcnt(0)
	v_mul_f32_e32 v2, 0x3c800000, v1
	v_pk_mul_f32 v[6:7], v[162:163], v[2:3] op_sel_hi:[1,0]
	v_pk_mul_f32 v[8:9], v[160:161], v[2:3] op_sel_hi:[1,0]
	v_pk_mul_f32 v[10:11], v[158:159], v[2:3] op_sel_hi:[1,0]
	v_pk_mul_f32 v[12:13], v[156:157], v[2:3] op_sel_hi:[1,0]
	v_pk_mul_f32 v[14:15], v[154:155], v[2:3] op_sel_hi:[1,0]
	v_pk_mul_f32 v[16:17], v[152:153], v[2:3] op_sel_hi:[1,0]
	v_pk_mul_f32 v[18:19], v[150:151], v[2:3] op_sel_hi:[1,0]
	v_pk_mul_f32 v[2:3], v[148:149], v[2:3] op_sel_hi:[1,0]
	v_bfe_u32 v1, v8, 16, 1
	v_bfe_u32 v20, v6, 16, 1
	v_bfe_u32 v22, v12, 16, 1
	v_bfe_u32 v24, v10, 16, 1
	v_bfe_u32 v5, v9, 16, 1
	v_bfe_u32 v21, v7, 16, 1
	v_bfe_u32 v23, v13, 16, 1
	v_bfe_u32 v25, v11, 16, 1
	v_bfe_u32 v26, v16, 16, 1
	v_bfe_u32 v28, v14, 16, 1
	v_bfe_u32 v30, v2, 16, 1
	v_bfe_u32 v32, v18, 16, 1
	v_add3_u32 v1, v8, v1, s37
	v_add3_u32 v6, v6, v20, s37
	v_add3_u32 v8, v12, v22, s37
	v_add3_u32 v10, v10, v24, s37
	v_bfe_u32 v27, v17, 16, 1
	v_bfe_u32 v29, v15, 16, 1
	v_bfe_u32 v31, v3, 16, 1
	v_bfe_u32 v33, v19, 16, 1
	v_add3_u32 v5, v9, v5, s37
	v_add3_u32 v7, v7, v21, s37
	v_add3_u32 v9, v13, v23, s37
	v_add3_u32 v11, v11, v25, s37
	v_add3_u32 v12, v16, v26, s37
	v_add3_u32 v14, v14, v28, s37
	v_add3_u32 v2, v2, v30, s37
	v_add3_u32 v16, v18, v32, s37
	v_lshrrev_b32_e32 v1, 16, v1
	v_lshrrev_b32_e32 v18, 16, v6
	v_lshrrev_b32_e32 v8, 16, v8
	v_lshrrev_b32_e32 v10, 16, v10
	v_add3_u32 v13, v17, v27, s37
	v_add3_u32 v15, v15, v29, s37
	v_add3_u32 v3, v3, v31, s37
	v_add3_u32 v17, v19, v33, s37
	v_lshrrev_b32_e32 v12, 16, v12
	v_lshrrev_b32_e32 v14, 16, v14
	v_lshrrev_b32_e32 v2, 16, v2
	v_lshrrev_b32_e32 v16, 16, v16
	v_and_or_b32 v6, v5, s33, v1
	v_and_or_b32 v7, v7, s33, v18
	v_and_or_b32 v8, v9, s33, v8
	v_and_or_b32 v9, v11, s33, v10
	v_and_or_b32 v10, v13, s33, v12
	v_and_or_b32 v11, v15, s33, v14
	v_and_or_b32 v12, v3, s33, v2
	v_and_or_b32 v13, v17, s33, v16
	global_store_dwordx4 v146, v[6:9], s[18:19] sc1
	global_store_dwordx4 v146, v[10:13], s[18:19] offset:256 sc1
	global_load_dword v1, v4, s[16:17] offset:64
	v_lshl_add_u64 v[2:3], s[18:19], 0, v[146:147]
	v_add_co_u32_e32 v14, vcc, s81, v2
	s_waitcnt vmcnt(0)
	v_mul_f32_e32 v6, 0x3c800000, v1
	v_pk_mul_f32 v[8:9], v[144:145], v[6:7] op_sel_hi:[1,0]
	v_pk_mul_f32 v[10:11], v[142:143], v[6:7] op_sel_hi:[1,0]
	v_pk_mul_f32 v[12:13], v[140:141], v[6:7] op_sel_hi:[1,0]
	v_pk_mul_f32 v[16:17], v[138:139], v[6:7] op_sel_hi:[1,0]
	v_pk_mul_f32 v[18:19], v[136:137], v[6:7] op_sel_hi:[1,0]
	v_pk_mul_f32 v[20:21], v[134:135], v[6:7] op_sel_hi:[1,0]
	v_pk_mul_f32 v[22:23], v[132:133], v[6:7] op_sel_hi:[1,0]
	v_pk_mul_f32 v[6:7], v[130:131], v[6:7] op_sel_hi:[1,0]
	v_bfe_u32 v1, v10, 16, 1
	v_bfe_u32 v24, v8, 16, 1
	v_bfe_u32 v26, v16, 16, 1
	v_bfe_u32 v28, v12, 16, 1
	v_bfe_u32 v5, v11, 16, 1
	v_bfe_u32 v25, v9, 16, 1
	v_bfe_u32 v27, v17, 16, 1
	v_bfe_u32 v29, v13, 16, 1
	v_bfe_u32 v30, v20, 16, 1
	v_bfe_u32 v32, v18, 16, 1
	v_bfe_u32 v130, v6, 16, 1
	v_bfe_u32 v131, v7, 16, 1
	v_bfe_u32 v132, v22, 16, 1
	v_add3_u32 v1, v10, v1, s37
	v_add3_u32 v8, v8, v24, s37
	v_add3_u32 v10, v16, v26, s37
	v_add3_u32 v12, v12, v28, s37
	v_bfe_u32 v31, v21, 16, 1
	v_bfe_u32 v33, v19, 16, 1
	v_bfe_u32 v133, v23, 16, 1
	v_add3_u32 v5, v11, v5, s37
	v_add3_u32 v9, v9, v25, s37
	v_add3_u32 v11, v17, v27, s37
	v_add3_u32 v13, v13, v29, s37
	v_add3_u32 v16, v20, v30, s37
	v_add3_u32 v18, v18, v32, s37
	v_add3_u32 v6, v6, v130, s37
	v_add3_u32 v20, v7, v131, s37
	v_add3_u32 v7, v22, v132, s37
	v_lshrrev_b32_e32 v1, 16, v1
	v_lshrrev_b32_e32 v8, 16, v8
	v_lshrrev_b32_e32 v10, 16, v10
	v_lshrrev_b32_e32 v12, 16, v12
	v_addc_co_u32_e32 v15, vcc, 0, v3, vcc
	v_add3_u32 v17, v21, v31, s37
	v_add3_u32 v19, v19, v33, s37
	v_add3_u32 v21, v23, v133, s37
	v_lshrrev_b32_e32 v16, 16, v16
	v_lshrrev_b32_e32 v18, 16, v18
	v_lshrrev_b32_e32 v22, 16, v6
	v_lshrrev_b32_e32 v23, 16, v7
	v_and_or_b32 v6, v5, s33, v1
	v_and_or_b32 v7, v9, s33, v8
	v_and_or_b32 v8, v11, s33, v10
	v_and_or_b32 v9, v13, s33, v12
	v_and_or_b32 v10, v17, s33, v16
	v_and_or_b32 v11, v19, s33, v18
	v_and_or_b32 v12, v20, s33, v22
	v_and_or_b32 v13, v21, s33, v23
	global_store_dwordx4 v[14:15], v[6:9], off sc1
	global_store_dwordx4 v[14:15], v[10:13], off offset:256 sc1
	global_load_dword v1, v4, s[16:17] offset:128
	v_add_co_u32_e32 v14, vcc, s11, v2
	s_mov_b32 s11, 0x30000
	s_nop 0
	v_addc_co_u32_e32 v15, vcc, 0, v3, vcc
	s_waitcnt vmcnt(0)
; __device__ __forceinline__ unsigned pk2(float lo, float hi) { return f2bf(lo) | (f2bf(hi) << 16); }
;     __device__ __forceinline__ void epi(const f32x4 (&acc)[2][2][4][2], const Unit& u, int wr, int wc, int fr, int fq) const {
;         const int e = u.pm / tpe, t = u.pm - e * tpe; const size_t rowt = (size_t)e * EROWS + (size_t)t * 256;
;         char* base = (char*)(YE + rowt * 2048 + (size_t)u.pn * 256); const char* gp = (const char*)(gatev + rowt);
;         unsigned loff = (unsigned)((wr * 64 + fr) * 2048 + wc * 32 + 8 * fq) * 2u, goff = (unsigned)(wr * 64 + fr) * 4u; asm volatile("" : "+v"(loff), "+v"(goff));
; #pragma unroll
;         for (int ai = 0; ai < 2; ++ai)
; #pragma unroll
;             for (int m = 0; m < 4; ++m) { const float g = *(const float*)(gp + (ai * 128 + m * 16) * 4 + goff) * (1.f / W8_SCALE);
; #pragma unroll
;                 for (int bj = 0; bj < 2; ++bj) { const f32x4 v0 = acc[ai][bj][m][0] * g, v1 = acc[ai][bj][m][1] * g;
;                     u32x4 w; w.x = pk2(v0[0], v0[1]); w.y = pk2(v0[2], v0[3]); w.z = pk2(v1[0], v1[1]); w.w = pk2(v1[2], v1[3]);
;                     *(u32x4*)(base + ((size_t)(ai * 128 + m * 16) * 2048 + bj * 128) * 2 + loff) = w; } }
;     }
	v_mul_f32_e32 v6, 0x3c800000, v1
	v_pk_mul_f32 v[8:9], v[128:129], v[6:7] op_sel_hi:[1,0]
	v_pk_mul_f32 v[10:11], v[126:127], v[6:7] op_sel_hi:[1,0]
	v_pk_mul_f32 v[12:13], v[124:125], v[6:7] op_sel_hi:[1,0]
	v_pk_mul_f32 v[16:17], v[122:123], v[6:7] op_sel_hi:[1,0]
	v_pk_mul_f32 v[18:19], v[120:121], v[6:7] op_sel_hi:[1,0]
	v_pk_mul_f32 v[20:21], v[118:119], v[6:7] op_sel_hi:[1,0]
	v_pk_mul_f32 v[22:23], v[116:117], v[6:7] op_sel_hi:[1,0]
	v_pk_mul_f32 v[6:7], v[114:115], v[6:7] op_sel_hi:[1,0]
	v_bfe_u32 v1, v10, 16, 1
	v_bfe_u32 v24, v8, 16, 1
	v_bfe_u32 v26, v16, 16, 1
	v_bfe_u32 v28, v12, 16, 1
	v_bfe_u32 v5, v11, 16, 1
	v_bfe_u32 v25, v9, 16, 1
	v_bfe_u32 v27, v17, 16, 1
	v_bfe_u32 v29, v13, 16, 1
	v_bfe_u32 v30, v20, 16, 1
	v_bfe_u32 v32, v18, 16, 1
	v_bfe_u32 v114, v6, 16, 1
	v_bfe_u32 v115, v7, 16, 1
	v_bfe_u32 v116, v22, 16, 1
	v_add3_u32 v1, v10, v1, s37
	v_add3_u32 v8, v8, v24, s37
	v_add3_u32 v10, v16, v26, s37
	v_add3_u32 v12, v12, v28, s37
	v_bfe_u32 v31, v21, 16, 1
	v_bfe_u32 v33, v19, 16, 1
	v_bfe_u32 v117, v23, 16, 1
	v_add3_u32 v5, v11, v5, s37
	v_add3_u32 v9, v9, v25, s37
	v_add3_u32 v11, v17, v27, s37
	v_add3_u32 v13, v13, v29, s37
	v_add3_u32 v16, v20, v30, s37
	v_add3_u32 v18, v18, v32, s37
	v_add3_u32 v6, v6, v114, s37
	v_add3_u32 v20, v7, v115, s37
	v_add3_u32 v7, v22, v116, s37
	v_lshrrev_b32_e32 v1, 16, v1
	v_lshrrev_b32_e32 v8, 16, v8
	v_lshrrev_b32_e32 v10, 16, v10
	v_lshrrev_b32_e32 v12, 16, v12
	v_add3_u32 v17, v21, v31, s37
	v_add3_u32 v19, v19, v33, s37
	v_add3_u32 v21, v23, v117, s37
	v_lshrrev_b32_e32 v16, 16, v16
	v_lshrrev_b32_e32 v18, 16, v18
	v_lshrrev_b32_e32 v22, 16, v6
	v_lshrrev_b32_e32 v23, 16, v7
	v_and_or_b32 v6, v5, s33, v1
	v_and_or_b32 v7, v9, s33, v8
	v_and_or_b32 v8, v11, s33, v10
	v_and_or_b32 v9, v13, s33, v12
	v_and_or_b32 v10, v17, s33, v16
	v_and_or_b32 v11, v19, s33, v18
	v_and_or_b32 v12, v20, s33, v22
	v_and_or_b32 v13, v21, s33, v23
	global_store_dwordx4 v[14:15], v[6:9], off sc1
	global_store_dwordx4 v[14:15], v[10:13], off offset:256 sc1
	global_load_dword v1, v4, s[16:17] offset:192
	v_add_co_u32_e32 v14, vcc, s11, v2
	s_mov_b32 s11, 0x80000
	s_nop 0
	v_addc_co_u32_e32 v15, vcc, 0, v3, vcc
	s_waitcnt vmcnt(0)
	v_mul_f32_e32 v6, 0x3c800000, v1
	v_pk_mul_f32 v[8:9], v[112:113], v[6:7] op_sel_hi:[1,0]
	v_pk_mul_f32 v[10:11], v[110:111], v[6:7] op_sel_hi:[1,0]
	v_pk_mul_f32 v[12:13], v[108:109], v[6:7] op_sel_hi:[1,0]
	v_pk_mul_f32 v[16:17], v[106:107], v[6:7] op_sel_hi:[1,0]
	v_pk_mul_f32 v[18:19], v[104:105], v[6:7] op_sel_hi:[1,0]
	v_pk_mul_f32 v[20:21], v[102:103], v[6:7] op_sel_hi:[1,0]
	v_pk_mul_f32 v[22:23], v[100:101], v[6:7] op_sel_hi:[1,0]
	v_pk_mul_f32 v[6:7], v[98:99], v[6:7] op_sel_hi:[1,0]
	v_bfe_u32 v1, v10, 16, 1
	v_bfe_u32 v24, v8, 16, 1
	v_bfe_u32 v26, v16, 16, 1
	v_bfe_u32 v28, v12, 16, 1
	v_bfe_u32 v5, v11, 16, 1
	v_bfe_u32 v25, v9, 16, 1
	v_bfe_u32 v27, v17, 16, 1
	v_bfe_u32 v29, v13, 16, 1
	v_bfe_u32 v30, v20, 16, 1
	v_bfe_u32 v32, v18, 16, 1
	v_bfe_u32 v98, v6, 16, 1
	v_bfe_u32 v99, v7, 16, 1
	v_bfe_u32 v100, v22, 16, 1
	v_add3_u32 v1, v10, v1, s37
	v_add3_u32 v8, v8, v24, s37
	v_add3_u32 v10, v16, v26, s37
	v_add3_u32 v12, v12, v28, s37
	v_bfe_u32 v31, v21, 16, 1
	v_bfe_u32 v33, v19, 16, 1
	v_bfe_u32 v101, v23, 16, 1
	v_add3_u32 v5, v11, v5, s37
	v_add3_u32 v9, v9, v25, s37
	v_add3_u32 v11, v17, v27, s37
	v_add3_u32 v13, v13, v29, s37
	v_add3_u32 v16, v20, v30, s37
	v_add3_u32 v18, v18, v32, s37
	v_add3_u32 v6, v6, v98, s37
	v_add3_u32 v20, v7, v99, s37
	v_add3_u32 v7, v22, v100, s37
	v_lshrrev_b32_e32 v1, 16, v1
	v_lshrrev_b32_e32 v8, 16, v8
	v_lshrrev_b32_e32 v10, 16, v10
	v_lshrrev_b32_e32 v12, 16, v12
	v_add3_u32 v17, v21, v31, s37
	v_add3_u32 v19, v19, v33, s37
	v_add3_u32 v21, v23, v101, s37
	v_lshrrev_b32_e32 v16, 16, v16
	v_lshrrev_b32_e32 v18, 16, v18
	v_lshrrev_b32_e32 v22, 16, v6
	v_lshrrev_b32_e32 v23, 16, v7
	v_and_or_b32 v6, v5, s33, v1
	v_and_or_b32 v7, v9, s33, v8
	v_and_or_b32 v8, v11, s33, v10
	v_and_or_b32 v9, v13, s33, v12
	v_and_or_b32 v10, v17, s33, v16
	v_and_or_b32 v11, v19, s33, v18
	v_and_or_b32 v12, v20, s33, v22
	v_and_or_b32 v13, v21, s33, v23
	global_store_dwordx4 v[14:15], v[6:9], off sc1
	global_store_dwordx4 v[14:15], v[10:13], off offset:256 sc1
	global_load_dword v1, v4, s[16:17] offset:512
	v_add_co_u32_e32 v14, vcc, s11, v2
	s_mov_b32 s11, 0x90000
	s_nop 0
	v_addc_co_u32_e32 v15, vcc, 0, v3, vcc
	s_waitcnt vmcnt(0)
	v_mul_f32_e32 v6, 0x3c800000, v1
	v_pk_mul_f32 v[8:9], v[96:97], v[6:7] op_sel_hi:[1,0]
	v_pk_mul_f32 v[10:11], v[94:95], v[6:7] op_sel_hi:[1,0]
	v_pk_mul_f32 v[12:13], v[92:93], v[6:7] op_sel_hi:[1,0]
	v_pk_mul_f32 v[16:17], v[90:91], v[6:7] op_sel_hi:[1,0]
	v_pk_mul_f32 v[18:19], v[88:89], v[6:7] op_sel_hi:[1,0]
	v_pk_mul_f32 v[20:21], v[86:87], v[6:7] op_sel_hi:[1,0]
	v_pk_mul_f32 v[22:23], v[84:85], v[6:7] op_sel_hi:[1,0]
	v_pk_mul_f32 v[6:7], v[82:83], v[6:7] op_sel_hi:[1,0]
	v_bfe_u32 v1, v10, 16, 1
	v_bfe_u32 v24, v8, 16, 1
	v_bfe_u32 v26, v16, 16, 1
	v_bfe_u32 v28, v12, 16, 1
	v_bfe_u32 v5, v11, 16, 1
	v_bfe_u32 v25, v9, 16, 1
	v_bfe_u32 v27, v17, 16, 1
	v_bfe_u32 v29, v13, 16, 1
	v_bfe_u32 v30, v20, 16, 1
	v_bfe_u32 v32, v18, 16, 1
	v_bfe_u32 v82, v6, 16, 1
	v_bfe_u32 v83, v7, 16, 1
	v_bfe_u32 v84, v22, 16, 1
	v_add3_u32 v1, v10, v1, s37
	v_add3_u32 v8, v8, v24, s37
	v_add3_u32 v10, v16, v26, s37
	v_add3_u32 v12, v12, v28, s37
	v_bfe_u32 v31, v21, 16, 1
	v_bfe_u32 v33, v19, 16, 1
	v_bfe_u32 v85, v23, 16, 1
	v_add3_u32 v5, v11, v5, s37
	v_add3_u32 v9, v9, v25, s37
	v_add3_u32 v11, v17, v27, s37
	v_add3_u32 v13, v13, v29, s37
	v_add3_u32 v16, v20, v30, s37
	v_add3_u32 v18, v18, v32, s37
	v_add3_u32 v6, v6, v82, s37
	v_add3_u32 v20, v7, v83, s37
	v_add3_u32 v7, v22, v84, s37
	v_lshrrev_b32_e32 v1, 16, v1
	v_lshrrev_b32_e32 v8, 16, v8
	v_lshrrev_b32_e32 v10, 16, v10
	v_lshrrev_b32_e32 v12, 16, v12
	v_add3_u32 v17, v21, v31, s37
	v_add3_u32 v19, v19, v33, s37
	v_add3_u32 v21, v23, v85, s37
	v_lshrrev_b32_e32 v16, 16, v16
	v_lshrrev_b32_e32 v18, 16, v18
	v_lshrrev_b32_e32 v22, 16, v6
	v_lshrrev_b32_e32 v23, 16, v7
	v_and_or_b32 v6, v5, s33, v1
	v_and_or_b32 v7, v9, s33, v8
	v_and_or_b32 v8, v11, s33, v10
	v_and_or_b32 v9, v13, s33, v12
	v_and_or_b32 v10, v17, s33, v16
	v_and_or_b32 v11, v19, s33, v18
	v_and_or_b32 v12, v20, s33, v22
	v_and_or_b32 v13, v21, s33, v23
	global_store_dwordx4 v[14:15], v[6:9], off sc1
	global_store_dwordx4 v[14:15], v[10:13], off offset:256 sc1
	global_load_dword v1, v4, s[16:17] offset:576
	v_add_co_u32_e32 v14, vcc, s11, v2
	s_mov_b32 s11, 0xa0000
	s_nop 0
	v_addc_co_u32_e32 v15, vcc, 0, v3, vcc
	s_waitcnt vmcnt(0)
; __device__ __forceinline__ unsigned pk2(float lo, float hi) { return f2bf(lo) | (f2bf(hi) << 16); }
;     __device__ __forceinline__ void epi(const f32x4 (&acc)[2][2][4][2], const Unit& u, int wr, int wc, int fr, int fq) const {
;         const int e = u.pm / tpe, t = u.pm - e * tpe; const size_t rowt = (size_t)e * EROWS + (size_t)t * 256;
;         char* base = (char*)(YE + rowt * 2048 + (size_t)u.pn * 256); const char* gp = (const char*)(gatev + rowt);
;         unsigned loff = (unsigned)((wr * 64 + fr) * 2048 + wc * 32 + 8 * fq) * 2u, goff = (unsigned)(wr * 64 + fr) * 4u; asm volatile("" : "+v"(loff), "+v"(goff));
; #pragma unroll
;         for (int ai = 0; ai < 2; ++ai)
; #pragma unroll
;             for (int m = 0; m < 4; ++m) { const float g = *(const float*)(gp + (ai * 128 + m * 16) * 4 + goff) * (1.f / W8_SCALE);
; #pragma unroll
;                 for (int bj = 0; bj < 2; ++bj) { const f32x4 v0 = acc[ai][bj][m][0] * g, v1 = acc[ai][bj][m][1] * g;
;                     u32x4 w; w.x = pk2(v0[0], v0[1]); w.y = pk2(v0[2], v0[3]); w.z = pk2(v1[0], v1[1]); w.w = pk2(v1[2], v1[3]);
;                     *(u32x4*)(base + ((size_t)(ai * 128 + m * 16) * 2048 + bj * 128) * 2 + loff) = w; } }
;     }
	v_mul_f32_e32 v6, 0x3c800000, v1
	v_pk_mul_f32 v[8:9], v[80:81], v[6:7] op_sel_hi:[1,0]
	v_pk_mul_f32 v[10:11], v[78:79], v[6:7] op_sel_hi:[1,0]
	v_pk_mul_f32 v[12:13], v[76:77], v[6:7] op_sel_hi:[1,0]
	v_pk_mul_f32 v[16:17], v[74:75], v[6:7] op_sel_hi:[1,0]
	v_pk_mul_f32 v[18:19], v[72:73], v[6:7] op_sel_hi:[1,0]
	v_pk_mul_f32 v[20:21], v[70:71], v[6:7] op_sel_hi:[1,0]
	v_pk_mul_f32 v[22:23], v[68:69], v[6:7] op_sel_hi:[1,0]
	v_pk_mul_f32 v[6:7], v[66:67], v[6:7] op_sel_hi:[1,0]
	v_bfe_u32 v1, v10, 16, 1
	v_bfe_u32 v24, v8, 16, 1
	v_bfe_u32 v26, v16, 16, 1
	v_bfe_u32 v28, v12, 16, 1
	v_bfe_u32 v5, v11, 16, 1
	v_bfe_u32 v25, v9, 16, 1
	v_bfe_u32 v27, v17, 16, 1
	v_bfe_u32 v29, v13, 16, 1
	v_bfe_u32 v30, v20, 16, 1
	v_bfe_u32 v32, v18, 16, 1
	v_bfe_u32 v66, v6, 16, 1
	v_bfe_u32 v67, v7, 16, 1
	v_bfe_u32 v68, v22, 16, 1
	v_add3_u32 v1, v10, v1, s37
	v_add3_u32 v8, v8, v24, s37
	v_add3_u32 v10, v16, v26, s37
	v_add3_u32 v12, v12, v28, s37
	v_bfe_u32 v31, v21, 16, 1
	v_bfe_u32 v33, v19, 16, 1
	v_bfe_u32 v69, v23, 16, 1
	v_add3_u32 v5, v11, v5, s37
	v_add3_u32 v9, v9, v25, s37
	v_add3_u32 v11, v17, v27, s37
	v_add3_u32 v13, v13, v29, s37
	v_add3_u32 v16, v20, v30, s37
	v_add3_u32 v18, v18, v32, s37
	v_add3_u32 v6, v6, v66, s37
	v_add3_u32 v20, v7, v67, s37
	v_add3_u32 v7, v22, v68, s37
	v_lshrrev_b32_e32 v1, 16, v1
	v_lshrrev_b32_e32 v8, 16, v8
	v_lshrrev_b32_e32 v10, 16, v10
	v_lshrrev_b32_e32 v12, 16, v12
	v_add3_u32 v17, v21, v31, s37
	v_add3_u32 v19, v19, v33, s37
	v_add3_u32 v21, v23, v69, s37
	v_lshrrev_b32_e32 v16, 16, v16
	v_lshrrev_b32_e32 v18, 16, v18
	v_lshrrev_b32_e32 v22, 16, v6
	v_lshrrev_b32_e32 v23, 16, v7
	v_and_or_b32 v6, v5, s33, v1
	v_and_or_b32 v7, v9, s33, v8
	v_and_or_b32 v8, v11, s33, v10
	v_and_or_b32 v9, v13, s33, v12
	v_and_or_b32 v10, v17, s33, v16
	v_and_or_b32 v11, v19, s33, v18
	v_and_or_b32 v12, v20, s33, v22
	v_and_or_b32 v13, v21, s33, v23
	global_store_dwordx4 v[14:15], v[6:9], off sc1
	global_store_dwordx4 v[14:15], v[10:13], off offset:256 sc1
	global_load_dword v1, v4, s[16:17] offset:640
	v_add_co_u32_e32 v14, vcc, s11, v2
	s_mov_b32 s11, 0xb0000
	s_nop 0
	v_addc_co_u32_e32 v15, vcc, 0, v3, vcc
	s_waitcnt vmcnt(0)
	v_mul_f32_e32 v6, 0x3c800000, v1
	v_pk_mul_f32 v[8:9], v[64:65], v[6:7] op_sel_hi:[1,0]
	v_pk_mul_f32 v[10:11], v[62:63], v[6:7] op_sel_hi:[1,0]
	v_pk_mul_f32 v[12:13], v[60:61], v[6:7] op_sel_hi:[1,0]
	v_pk_mul_f32 v[16:17], v[58:59], v[6:7] op_sel_hi:[1,0]
	v_pk_mul_f32 v[18:19], v[56:57], v[6:7] op_sel_hi:[1,0]
	v_pk_mul_f32 v[20:21], v[54:55], v[6:7] op_sel_hi:[1,0]
	v_pk_mul_f32 v[22:23], v[52:53], v[6:7] op_sel_hi:[1,0]
	v_pk_mul_f32 v[6:7], v[50:51], v[6:7] op_sel_hi:[1,0]
	v_bfe_u32 v1, v10, 16, 1
	v_bfe_u32 v24, v8, 16, 1
	v_bfe_u32 v26, v16, 16, 1
	v_bfe_u32 v28, v12, 16, 1
	v_bfe_u32 v5, v11, 16, 1
	v_bfe_u32 v25, v9, 16, 1
	v_bfe_u32 v27, v17, 16, 1
	v_bfe_u32 v29, v13, 16, 1
	v_bfe_u32 v30, v20, 16, 1
	v_bfe_u32 v32, v18, 16, 1
	v_bfe_u32 v50, v6, 16, 1
	v_bfe_u32 v51, v7, 16, 1
	v_bfe_u32 v52, v22, 16, 1
	v_add3_u32 v1, v10, v1, s37
	v_add3_u32 v8, v8, v24, s37
	v_add3_u32 v10, v16, v26, s37
	v_add3_u32 v12, v12, v28, s37
	v_bfe_u32 v31, v21, 16, 1
	v_bfe_u32 v33, v19, 16, 1
	v_bfe_u32 v53, v23, 16, 1
	v_add3_u32 v5, v11, v5, s37
	v_add3_u32 v9, v9, v25, s37
	v_add3_u32 v11, v17, v27, s37
	v_add3_u32 v13, v13, v29, s37
	v_add3_u32 v16, v20, v30, s37
	v_add3_u32 v18, v18, v32, s37
	v_add3_u32 v6, v6, v50, s37
	v_add3_u32 v20, v7, v51, s37
	v_add3_u32 v7, v22, v52, s37
	v_lshrrev_b32_e32 v1, 16, v1
	v_lshrrev_b32_e32 v8, 16, v8
	v_lshrrev_b32_e32 v10, 16, v10
	v_lshrrev_b32_e32 v12, 16, v12
	v_add3_u32 v17, v21, v31, s37
	v_add3_u32 v19, v19, v33, s37
	v_add3_u32 v21, v23, v53, s37
	v_lshrrev_b32_e32 v16, 16, v16
	v_lshrrev_b32_e32 v18, 16, v18
	v_lshrrev_b32_e32 v22, 16, v6
	v_lshrrev_b32_e32 v23, 16, v7
	v_and_or_b32 v6, v5, s33, v1
	v_and_or_b32 v7, v9, s33, v8
	v_and_or_b32 v8, v11, s33, v10
	v_and_or_b32 v9, v13, s33, v12
	v_and_or_b32 v10, v17, s33, v16
	v_and_or_b32 v11, v19, s33, v18
	v_and_or_b32 v12, v20, s33, v22
	v_and_or_b32 v13, v21, s33, v23
	global_store_dwordx4 v[14:15], v[6:9], off sc1
	global_store_dwordx4 v[14:15], v[10:13], off offset:256 sc1
	global_load_dword v1, v4, s[16:17] offset:704
	s_mov_b64 s[16:17], -1
	v_add_co_u32_e32 v10, vcc, s11, v2
	s_waitcnt vmcnt(0)
	v_mul_f32_e32 v2, 0x3c800000, v1
	v_pk_mul_f32 v[4:5], v[48:49], v[2:3] op_sel_hi:[1,0]
	v_pk_mul_f32 v[6:7], v[46:47], v[2:3] op_sel_hi:[1,0]
	v_pk_mul_f32 v[8:9], v[44:45], v[2:3] op_sel_hi:[1,0]
	v_pk_mul_f32 v[12:13], v[42:43], v[2:3] op_sel_hi:[1,0]
	v_addc_co_u32_e32 v11, vcc, 0, v3, vcc
	v_pk_mul_f32 v[14:15], v[40:41], v[2:3] op_sel_hi:[1,0]
	v_pk_mul_f32 v[16:17], v[38:39], v[2:3] op_sel_hi:[1,0]
	v_pk_mul_f32 v[18:19], v[36:37], v[2:3] op_sel_hi:[1,0]
	v_pk_mul_f32 v[2:3], v[34:35], v[2:3] op_sel_hi:[1,0]
	v_bfe_u32 v1, v6, 16, 1
	v_bfe_u32 v20, v7, 16, 1
	v_bfe_u32 v21, v4, 16, 1
	v_bfe_u32 v23, v12, 16, 1
	v_bfe_u32 v25, v8, 16, 1
	v_bfe_u32 v22, v5, 16, 1
	v_bfe_u32 v24, v13, 16, 1
	v_bfe_u32 v26, v9, 16, 1
	v_bfe_u32 v27, v16, 16, 1
	v_bfe_u32 v28, v17, 16, 1
	v_bfe_u32 v29, v14, 16, 1
	v_bfe_u32 v31, v2, 16, 1
	v_bfe_u32 v32, v3, 16, 1
	v_bfe_u32 v33, v18, 16, 1
	v_add3_u32 v1, v6, v1, s37
	v_add3_u32 v6, v7, v20, s37
	v_add3_u32 v4, v4, v21, s37
	v_add3_u32 v7, v12, v23, s37
	v_add3_u32 v8, v8, v25, s37
	v_bfe_u32 v30, v15, 16, 1
	v_bfe_u32 v34, v19, 16, 1
	v_add3_u32 v5, v5, v22, s37
	v_add3_u32 v12, v13, v24, s37
	v_add3_u32 v9, v9, v26, s37
	v_add3_u32 v13, v16, v27, s37
	v_add3_u32 v16, v17, v28, s37
	v_add3_u32 v14, v14, v29, s37
	v_add3_u32 v2, v2, v31, s37
	v_add3_u32 v17, v3, v32, s37
	v_add3_u32 v3, v18, v33, s37
	v_lshrrev_b32_e32 v1, 16, v1
	v_lshrrev_b32_e32 v4, 16, v4
	v_lshrrev_b32_e32 v7, 16, v7
	v_lshrrev_b32_e32 v8, 16, v8
	s_and_b64 vcc, exec, s[38:39]
	v_add3_u32 v15, v15, v30, s37
	v_add3_u32 v18, v19, v34, s37
	v_lshrrev_b32_e32 v13, 16, v13
	v_lshrrev_b32_e32 v14, 16, v14
	v_lshrrev_b32_e32 v19, 16, v2
	v_lshrrev_b32_e32 v20, 16, v3
	v_and_or_b32 v2, v6, s33, v1
	v_and_or_b32 v3, v5, s33, v4
	v_and_or_b32 v4, v12, s33, v7
	v_and_or_b32 v5, v9, s33, v8
	v_and_or_b32 v6, v16, s33, v13
	v_and_or_b32 v7, v15, s33, v14
	v_and_or_b32 v8, v17, s33, v19
	v_and_or_b32 v9, v18, s33, v20
	global_store_dwordx4 v[10:11], v[2:5], off sc1
	global_store_dwordx4 v[10:11], v[6:9], off offset:256 sc1
	s_cbranch_vccnz .LBB0_2656
	s_andn2_b64 vcc, exec, s[4:5]
	s_cbranch_vccnz .LBB0_2655
	s_barrier
	s_branch .LBB0_2655

; __device__ __forceinline__ unsigned pk2(float lo, float hi) { return f2bf(lo) | (f2bf(hi) << 16); }
; __device__ __forceinline__ float dot4(f32x4 a, f32x4 b) { return (a.x * b.x + a.y * b.y) + (a.z * b.z + a.w * b.w); }
; __device__ __forceinline__ void phase_combine(const Args& a, const Ctx& c0, int l, bool last_in) {
;     ...
;         for (int j = 0; j < 4; ++j) { const int idx = (lane + 64 * j) * 8; const u32x4 xw = *(const u32x4*)(XM + (size_t)row * DM + idx);
;             xv[j][0] = (f32x4){bflo(xw.x), bfhi(xw.x), bflo(xw.y), bfhi(xw.y)}; xv[j][1] = (f32x4){bflo(xw.z), bfhi(xw.z), bflo(xw.w), bfhi(xw.w)};
; #pragma unroll
;             for (int hlf = 0; hlf < 2; ++hlf) gv[j][hlf] = *(const f32x4*)(g2 + idx + hlf * 4); }
;         f32x4 acc[4][2];
; #pragma unroll
;         for (int j = 0; j < 4; ++j) { acc[j][0] = (f32x4){0.f, 0.f, 0.f, 0.f}; acc[j][1] = (f32x4){0.f, 0.f, 0.f, 0.f}; }
;         unsigned long long m = __ballot(myslot >= 0);
;         while (m) { const int e = __builtin_ctzll(m); m &= m - 1; const int sl = __shfl(myslot, e);
;             const u32x4* y = (const u32x4*)(YE + ((size_t)e * EROWS + sl) * DM);
; #pragma unroll
;             for (int j = 0; j < 4; ++j) { const u32x4 w = y[lane + 64 * j];
;                 acc[j][0] += (f32x4){bflo(w.x), bfhi(w.x), bflo(w.y), bfhi(w.y)}; acc[j][1] += (f32x4){bflo(w.z), bfhi(w.z), bflo(w.w), bfhi(w.w)}; } }
;         float ssn = 0.f;
; #pragma unroll
;         for (int j = 0; j < 4; ++j) { const int idx = (lane + 64 * j) * 8;
; #pragma unroll
;             for (int hlf = 0; hlf < 2; ++hlf) { xv[j][hlf] = xv[j][hlf] + gv[j][hlf] * acc[j][hlf]; ssn += dot4(xv[j][hlf], xv[j][hlf]); }
;             if (last) { *(f32x4*)(out + (size_t)row * DM + idx) = xv[j][0]; *(f32x4*)(out + (size_t)row * DM + idx + 4) = xv[j][1]; }
;             else { u32x4 w; w.x = pk2(xv[j][0].x, xv[j][0].y); w.y = pk2(xv[j][0].z, xv[j][0].w); w.z = pk2(xv[j][1].x, xv[j][1].y); w.w = pk2(xv[j][1].z, xv[j][1].w); *(u32x4*)(x1o + (size_t)row * DM + idx) = w; } }
.LBB0_2734:
	s_add_u32 s20, s27, s14
	s_addc_u32 s21, s31, s15
	s_lshl_b64 s[2:3], s[10:11], 13
	v_readlane_b32 s44, v254, 21
	v_readlane_b32 s22, v254, 59
	v_lshlrev_b32_e32 v50, 16, v46
	v_and_b32_e32 v51, 0xffff0000, v46
	v_lshlrev_b32_e32 v46, 16, v47
	v_and_b32_e32 v47, 0xffff0000, v47
	v_lshlrev_b32_e32 v52, 16, v48
	v_and_b32_e32 v53, 0xffff0000, v48
	v_lshlrev_b32_e32 v48, 16, v49
	v_and_b32_e32 v49, 0xffff0000, v49
	v_readlane_b32 s45, v254, 22
	s_add_u32 s18, s44, s2
	v_readlane_b32 s23, v254, 60
	s_addc_u32 s19, s45, s3
	v_pk_fma_f32 v[40:41], v[40:41], v[102:103], v[46:47]
	v_pk_fma_f32 v[38:39], v[38:39], v[100:101], v[50:51]
	v_pk_fma_f32 v[36:37], v[36:37], v[98:99], v[48:49]
	v_pk_fma_f32 v[34:35], v[34:35], v[96:97], v[52:53]
	s_mov_b64 s[2:3], -1
	s_and_b64 vcc, exec, s[22:23]
	v_lshlrev_b32_e32 v46, 1, v56
	v_readlane_b32 s46, v254, 23
	v_readlane_b32 s47, v254, 24
	s_cbranch_vccz .LBB0_2736
	v_cvt_pk_bf16_f32 v48, v38, v39
	v_cvt_pk_bf16_f32 v49, v40, v41
	v_cvt_pk_bf16_f32 v50, v34, v35
	v_cvt_pk_bf16_f32 v51, v36, v37
	global_store_dwordx4 v46, v[48:51], s[20:21] sc1
	s_mov_b64 s[2:3], 0
.LBB0_2736:
	s_andn2_b64 vcc, exec, s[2:3]
	s_cbranch_vccnz .LBB0_2738
	global_store_dwordx4 v57, v[38:41], s[18:19] sc1
	global_store_dwordx4 v57, v[34:37], s[18:19] offset:16 sc1
.LBB0_2738:
	v_readlane_b32 s22, v254, 59
	v_readlane_b32 s23, v254, 60
	v_lshlrev_b32_e32 v48, 16, v42
	v_and_b32_e32 v49, 0xffff0000, v42
	v_lshlrev_b32_e32 v42, 16, v43
	v_and_b32_e32 v43, 0xffff0000, v43
	v_lshlrev_b32_e32 v50, 16, v44
	v_and_b32_e32 v51, 0xffff0000, v44
	v_lshlrev_b32_e32 v44, 16, v45
	v_and_b32_e32 v45, 0xffff0000, v45
	v_cndmask_b32_e64 v1, 0, 1, s[22:23]
	v_pk_fma_f32 v[32:33], v[32:33], v[94:95], v[42:43]
	v_pk_fma_f32 v[30:31], v[30:31], v[92:93], v[48:49]
	v_pk_fma_f32 v[24:25], v[24:25], v[90:91], v[44:45]
	v_pk_fma_f32 v[22:23], v[22:23], v[88:89], v[50:51]
	v_cmp_ne_u32_e64 s[2:3], 1, v1
	s_andn2_b64 vcc, exec, s[22:23]
	s_mov_b64 s[22:23], -1
	s_cbranch_vccnz .LBB0_2740
	v_cvt_pk_bf16_f32 v42, v30, v31
	v_cvt_pk_bf16_f32 v43, v32, v33
	v_cvt_pk_bf16_f32 v44, v22, v23
	v_cvt_pk_bf16_f32 v45, v24, v25
	s_mov_b64 s[22:23], 0
	global_store_dwordx4 v46, v[42:45], s[20:21] offset:1024 sc1
.LBB0_2740:
	s_andn2_b64 vcc, exec, s[22:23]
	s_cbranch_vccnz .LBB0_2742
	global_store_dwordx4 v57, v[30:33], s[18:19] offset:2048 sc1
	global_store_dwordx4 v57, v[22:25], s[18:19] offset:2064 sc1
.LBB0_2742:
	v_lshlrev_b32_e32 v42, 16, v26
	v_and_b32_e32 v43, 0xffff0000, v26
	v_lshlrev_b32_e32 v26, 16, v27
	v_and_b32_e32 v27, 0xffff0000, v27
	v_lshlrev_b32_e32 v44, 16, v28
	v_and_b32_e32 v45, 0xffff0000, v28
	v_lshlrev_b32_e32 v28, 16, v29
	v_and_b32_e32 v29, 0xffff0000, v29
	v_pk_fma_f32 v[16:17], v[16:17], v[86:87], v[26:27]
	v_pk_fma_f32 v[14:15], v[14:15], v[84:85], v[42:43]
	v_pk_fma_f32 v[12:13], v[12:13], v[82:83], v[28:29]
	v_pk_fma_f32 v[10:11], v[10:11], v[80:81], v[44:45]
	s_and_b64 vcc, exec, s[2:3]
	s_mov_b64 s[22:23], -1
	s_cbranch_vccnz .LBB0_2744
	v_cvt_pk_bf16_f32 v26, v14, v15
	v_cvt_pk_bf16_f32 v27, v16, v17
	v_cvt_pk_bf16_f32 v28, v10, v11
	v_cvt_pk_bf16_f32 v29, v12, v13
	s_mov_b64 s[22:23], 0
	global_store_dwordx4 v46, v[26:29], s[20:21] offset:2048 sc1
.LBB0_2744:
	s_andn2_b64 vcc, exec, s[22:23]
	s_cbranch_vccnz .LBB0_2746
	global_store_dwordx4 v105, v[14:17], s[18:19] sc1
	global_store_dwordx4 v105, v[10:13], s[18:19] offset:16 sc1
.LBB0_2746:
	v_lshlrev_b32_e32 v26, 16, v18
	v_and_b32_e32 v27, 0xffff0000, v18
	v_lshlrev_b32_e32 v18, 16, v19
	v_and_b32_e32 v19, 0xffff0000, v19
	v_lshlrev_b32_e32 v28, 16, v20
	v_and_b32_e32 v29, 0xffff0000, v20
	v_lshlrev_b32_e32 v20, 16, v21
	v_and_b32_e32 v21, 0xffff0000, v21
	v_pk_fma_f32 v[8:9], v[8:9], v[78:79], v[18:19]
	v_pk_fma_f32 v[6:7], v[6:7], v[76:77], v[26:27]
	v_pk_fma_f32 v[4:5], v[4:5], v[74:75], v[20:21]
	v_pk_fma_f32 v[2:3], v[2:3], v[72:73], v[28:29]
	s_and_b64 vcc, exec, s[2:3]
	s_mov_b64 s[22:23], -1
	s_cbranch_vccnz .LBB0_2749
	v_cvt_pk_bf16_f32 v18, v6, v7
	v_cvt_pk_bf16_f32 v19, v8, v9
	v_cvt_pk_bf16_f32 v20, v2, v3
	v_cvt_pk_bf16_f32 v21, v4, v5
	global_store_dwordx4 v46, v[18:21], s[20:21] offset:3072 sc1
	s_cbranch_execz .LBB0_2750

; __device__ __forceinline__ unsigned pk2(float lo, float hi) { return f2bf(lo) | (f2bf(hi) << 16); }
; __device__ __forceinline__ float dot4(f32x4 a, f32x4 b) { return (a.x * b.x + a.y * b.y) + (a.z * b.z + a.w * b.w); }
; __device__ __forceinline__ float wave_sum(float v) {
; #pragma unroll
;     for (int o = 1; o < 64; o <<= 1) v += __shfl_xor(v, o);
;     return v;
; __device__ __forceinline__ void phase_combine(const Args& a, const Ctx& c0, int l, bool last_in) {
;     ...
;         float ssn = 0.f;
; #pragma unroll
;         for (int j = 0; j < 4; ++j) { const int idx = (lane + 64 * j) * 8;
; #pragma unroll
;             for (int hlf = 0; hlf < 2; ++hlf) { xv[j][hlf] = xv[j][hlf] + gv[j][hlf] * acc[j][hlf]; ssn += dot4(xv[j][hlf], xv[j][hlf]); }
;             if (last) { *(f32x4*)(out + (size_t)row * DM + idx) = xv[j][0]; *(f32x4*)(out + (size_t)row * DM + idx + 4) = xv[j][1]; }
;             else { u32x4 w; w.x = pk2(xv[j][0].x, xv[j][0].y); w.y = pk2(xv[j][0].z, xv[j][0].w); w.z = pk2(xv[j][1].x, xv[j][1].y); w.w = pk2(xv[j][1].z, xv[j][1].w); *(u32x4*)(x1o + (size_t)row * DM + idx) = w; } }
;         if (!last) {
;             const float* mv1 = modv + (size_t)5 * NMODW + (size_t)mb * NMODW; const float* g1n = INP(6) + (size_t)(l + 1) * DM;
;             const float rstd = rsqrtf(wave_sum(ssn) * (1.f / DM) + EPS); bf16* hrow = WSP(bf16, WS_H) + (size_t)row * DM;
.LBB0_2750:
	global_store_dwordx4 v106, v[6:9], s[18:19] sc1
	global_store_dwordx4 v106, v[2:5], s[18:19] offset:16 sc1
	s_and_b64 vcc, exec, s[2:3]
	s_mov_b64 s[20:21], 0x2000
	s_cbranch_vccnz .LBB0_2727
.LBB0_2751:
	v_mul_f32_e32 v1, v39, v39
	v_mul_f32_e32 v18, v41, v41
	v_fmac_f32_e32 v1, v38, v38
	v_fmac_f32_e32 v18, v40, v40
	v_add_f32_e32 v1, v1, v18
	v_mul_f32_e32 v18, v35, v35
	v_mul_f32_e32 v19, v37, v37
	v_fmac_f32_e32 v18, v34, v34
	v_fmac_f32_e32 v19, v36, v36
	v_add_f32_e32 v18, v18, v19
	v_add_f32_e32 v1, v18, v1
	v_mul_f32_e32 v18, v31, v31
	v_mul_f32_e32 v19, v33, v33
	v_fmac_f32_e32 v18, v30, v30
	v_fmac_f32_e32 v19, v32, v32
	v_add_f32_e32 v18, v18, v19
	v_add_f32_e32 v1, v18, v1
	v_mul_f32_e32 v18, v23, v23
	v_mul_f32_e32 v19, v25, v25
	v_fmac_f32_e32 v18, v22, v22
	v_fmac_f32_e32 v19, v24, v24
	v_add_f32_e32 v18, v18, v19
	v_add_f32_e32 v1, v18, v1
	v_mul_f32_e32 v18, v15, v15
	v_mul_f32_e32 v19, v17, v17
	v_fmac_f32_e32 v18, v14, v14
	v_fmac_f32_e32 v19, v16, v16
	v_add_f32_e32 v18, v18, v19
	v_add_f32_e32 v1, v18, v1
	v_mul_f32_e32 v18, v11, v11
	v_mul_f32_e32 v19, v13, v13
	v_fmac_f32_e32 v18, v10, v10
	v_fmac_f32_e32 v19, v12, v12
	v_add_f32_e32 v18, v18, v19
	v_add_f32_e32 v1, v18, v1
	v_mul_f32_e32 v18, v7, v7
	v_mul_f32_e32 v19, v9, v9
	v_fmac_f32_e32 v18, v6, v6
	v_fmac_f32_e32 v19, v8, v8
	v_add_f32_e32 v18, v18, v19
	v_add_f32_e32 v1, v18, v1
	v_mul_f32_e32 v18, v3, v3
	v_mul_f32_e32 v19, v5, v5
	v_fmac_f32_e32 v18, v2, v2
	v_fmac_f32_e32 v19, v4, v4
	v_add_f32_e32 v18, v18, v19
	v_add_f32_e32 v1, v18, v1
	v_xor_b32_e32 v18, 1, v210
	v_cmp_lt_i32_e32 vcc, v18, v215
	s_add_u32 s2, s36, s16
	s_addc_u32 s3, s40, s17
	v_cndmask_b32_e32 v18, v210, v18, vcc
	v_lshlrev_b32_e32 v18, 2, v18
	ds_bpermute_b32 v18, v18, v1
	s_add_u32 s16, s2, 0x2000
	s_addc_u32 s17, s3, 0
	s_waitcnt lgkmcnt(0)
	v_add_f32_e32 v1, v1, v18
	v_xor_b32_e32 v18, 2, v210
	v_cmp_lt_i32_e32 vcc, v18, v215
	s_nop 1
	v_cndmask_b32_e32 v18, v210, v18, vcc
	v_lshlrev_b32_e32 v18, 2, v18
	ds_bpermute_b32 v18, v18, v1
	s_waitcnt lgkmcnt(0)
	v_add_f32_e32 v1, v1, v18
	v_xor_b32_e32 v18, 4, v210
	v_cmp_lt_i32_e32 vcc, v18, v215
	s_nop 1
	v_cndmask_b32_e32 v18, v210, v18, vcc
	v_lshlrev_b32_e32 v18, 2, v18
	ds_bpermute_b32 v18, v18, v1
	s_waitcnt lgkmcnt(0)
	v_add_f32_e32 v1, v1, v18
	v_xor_b32_e32 v18, 8, v210
	v_cmp_lt_i32_e32 vcc, v18, v215
	s_nop 1
	v_cndmask_b32_e32 v18, v210, v18, vcc
	v_lshlrev_b32_e32 v18, 2, v18
	ds_bpermute_b32 v18, v18, v1
	v_cmp_lt_i32_e32 vcc, v220, v215
	s_waitcnt lgkmcnt(0)
	v_add_f32_e32 v1, v1, v18
	v_cndmask_b32_e32 v18, v210, v220, vcc
	v_lshlrev_b32_e32 v18, 2, v18
	ds_bpermute_b32 v18, v18, v1
	v_cmp_lt_i32_e32 vcc, v221, v215
	s_waitcnt lgkmcnt(0)
	v_add_f32_e32 v1, v1, v18
	v_cndmask_b32_e32 v18, v210, v221, vcc
	v_lshlrev_b32_e32 v18, 2, v18
	ds_bpermute_b32 v18, v18, v1
	s_waitcnt lgkmcnt(0)
	v_add_f32_e32 v1, v1, v18
	v_fmamk_f32 v1, v1, 0x3a000000, v180
	v_cmp_gt_f32_e32 vcc, s79, v1
	v_mul_f32_e32 v18, 0x4b800000, v1
	s_nop 0
	v_cndmask_b32_e32 v1, v1, v18, vcc
	v_rsq_f32_e32 v1, v1
	s_nop 0
	v_mul_f32_e32 v18, 0x45800000, v1
	v_cndmask_b32_e32 v72, v1, v18, vcc
	global_load_dwordx4 v[18:21], v57, s[2:3] offset:16
	global_load_dwordx4 v[46:49], v57, s[2:3]
	global_load_dwordx4 v[26:29], v[60:61], off offset:16
	global_load_dwordx4 v[50:53], v[60:61], off
	global_load_dwordx4 v[42:45], v57, s[16:17] offset:16
	global_load_dwordx4 v[74:77], v57, s[16:17]
	v_pk_mul_f32 v[38:39], v[38:39], v[72:73] op_sel_hi:[1,0]
	v_pk_mul_f32 v[40:41], v[40:41], v[72:73] op_sel_hi:[1,0]
	v_pk_mul_f32 v[34:35], v[34:35], v[72:73] op_sel_hi:[1,0]
	v_pk_mul_f32 v[36:37], v[36:37], v[72:73] op_sel_hi:[1,0]
	v_pk_mul_f32 v[30:31], v[30:31], v[72:73] op_sel_hi:[1,0]
	v_pk_mul_f32 v[32:33], v[32:33], v[72:73] op_sel_hi:[1,0]
	v_pk_mul_f32 v[22:23], v[22:23], v[72:73] op_sel_hi:[1,0]
	v_pk_mul_f32 v[24:25], v[24:25], v[72:73] op_sel_hi:[1,0]
	v_pk_mul_f32 v[14:15], v[14:15], v[72:73] op_sel_hi:[1,0]
	v_pk_mul_f32 v[16:17], v[16:17], v[72:73] op_sel_hi:[1,0]
	v_pk_mul_f32 v[10:11], v[10:11], v[72:73] op_sel_hi:[1,0]
	v_pk_mul_f32 v[12:13], v[12:13], v[72:73] op_sel_hi:[1,0]
	v_pk_mul_f32 v[6:7], v[6:7], v[72:73] op_sel_hi:[1,0]
	v_pk_mul_f32 v[8:9], v[8:9], v[72:73] op_sel_hi:[1,0]
	v_pk_mul_f32 v[2:3], v[2:3], v[72:73] op_sel_hi:[1,0]
	v_pk_mul_f32 v[4:5], v[4:5], v[72:73] op_sel_hi:[1,0]
	s_waitcnt vmcnt(1)
	v_pk_add_f32 v[42:43], v[42:43], 1.0 op_sel_hi:[1,0]
	s_waitcnt vmcnt(0)
; __device__ __forceinline__ unsigned pk2(float lo, float hi) { return f2bf(lo) | (f2bf(hi) << 16); }
; __device__ __forceinline__ void phase_combine(const Args& a, const Ctx& c0, int l, bool last_in) {
;     ...
; #pragma unroll
;             for (int j = 0; j < 4; ++j) { const int idx = (lane + 64 * j) * 8; u32x4 w;
; #pragma unroll
;                 for (int hlf = 0; hlf < 2; ++hlf) { const int ix = idx + hlf * 4; const f32x4 gsv = *(const f32x4*)(g1n + ix) * (1.f + *(const f32x4*)(mv1 + DM + ix)), shv = *(const f32x4*)(mv1 + ix);
;                     const f32x4 o = (xv[j][hlf] * rstd) * gsv + shv;
;                     if (hlf == 0) { w.x = pk2(o.x, o.y); w.y = pk2(o.z, o.w); } else { w.z = pk2(o.x, o.y); w.w = pk2(o.z, o.w); } }
;                 *(u32x4*)(hrow + idx) = w; } }
	v_pk_add_f32 v[74:75], v[74:75], 1.0 op_sel_hi:[1,0]
	v_pk_add_f32 v[76:77], v[76:77], 1.0 op_sel_hi:[1,0]
	v_pk_mul_f32 v[50:51], v[50:51], v[74:75]
	v_pk_mul_f32 v[52:53], v[52:53], v[76:77]
	v_pk_fma_f32 v[38:39], v[50:51], v[38:39], v[46:47]
	v_pk_fma_f32 v[40:41], v[52:53], v[40:41], v[48:49]
	v_bfe_u32 v1, v38, 16, 1
	v_add3_u32 v1, v38, v1, s37
	v_bfe_u32 v38, v39, 16, 1
	v_lshrrev_b32_e32 v1, 16, v1
	v_add3_u32 v38, v39, v38, s37
	v_and_or_b32 v38, v38, s33, v1
	v_pk_mul_f32 v[26:27], v[26:27], v[42:43]
	v_pk_fma_f32 v[18:19], v[26:27], v[34:35], v[18:19]
	v_cvt_pk_bf16_f32 v39, v40, v41
	v_bfe_u32 v1, v19, 16, 1
	v_pk_add_f32 v[40:41], v[44:45], 1.0 op_sel_hi:[1,0]
	v_add3_u32 v1, v19, v1, s37
	v_bfe_u32 v19, v18, 16, 1
	v_pk_mul_f32 v[28:29], v[28:29], v[40:41]
	v_add3_u32 v18, v18, v19, s37
	v_pk_fma_f32 v[20:21], v[28:29], v[36:37], v[20:21]
	v_lshrrev_b32_e32 v18, 16, v18
	v_and_or_b32 v40, v1, s33, v18
	v_cvt_pk_bf16_f32 v41, v20, v21
	v_lshl_add_u64 v[18:19], v[70:71], 0, s[14:15]
	global_store_dwordx4 v[18:19], v[38:41], off sc1
	global_load_dwordx4 v[26:29], v57, s[2:3] offset:2064
	global_load_dwordx4 v[34:37], v57, s[2:3] offset:2048
	s_nop 0
	global_load_dwordx4 v[38:41], v[62:63], off offset:16
	global_load_dwordx4 v[42:45], v[62:63], off
	global_load_dwordx4 v[46:49], v104, s[16:17] offset:16
	global_load_dwordx4 v[50:53], v104, s[16:17]
	s_waitcnt vmcnt(0)
	v_pk_add_f32 v[20:21], v[52:53], 1.0 op_sel_hi:[1,0]
	v_pk_add_f32 v[50:51], v[50:51], 1.0 op_sel_hi:[1,0]
	v_pk_mul_f32 v[20:21], v[44:45], v[20:21]
	v_pk_mul_f32 v[42:43], v[42:43], v[50:51]
	v_pk_fma_f32 v[32:33], v[20:21], v[32:33], v[36:37]
	v_pk_fma_f32 v[20:21], v[42:43], v[30:31], v[34:35]
	v_pk_add_f32 v[30:31], v[48:49], 1.0 op_sel_hi:[1,0]
	v_bfe_u32 v1, v20, 16, 1
	v_add3_u32 v1, v20, v1, s37
	v_bfe_u32 v20, v21, 16, 1
	v_lshrrev_b32_e32 v1, 16, v1
	v_add3_u32 v20, v21, v20, s37
	v_and_or_b32 v20, v20, s33, v1
	v_bfe_u32 v1, v32, 16, 1
	v_bfe_u32 v21, v33, 16, 1
	v_add3_u32 v1, v32, v1, s37
	v_add3_u32 v21, v33, v21, s37
	v_pk_add_f32 v[32:33], v[46:47], 1.0 op_sel_hi:[1,0]
	v_lshrrev_b32_e32 v1, 16, v1
	v_pk_mul_f32 v[32:33], v[38:39], v[32:33]
	v_and_or_b32 v21, v21, s33, v1
	v_pk_fma_f32 v[22:23], v[22:23], v[32:33], v[26:27]
	v_pk_mul_f32 v[30:31], v[40:41], v[30:31]
	v_bfe_u32 v1, v23, 16, 1
	v_add3_u32 v1, v23, v1, s37
	v_bfe_u32 v23, v22, 16, 1
	v_pk_fma_f32 v[24:25], v[24:25], v[30:31], v[28:29]
	v_add3_u32 v22, v22, v23, s37
	v_lshrrev_b32_e32 v22, 16, v22
	v_and_or_b32 v22, v1, s33, v22
	v_cvt_pk_bf16_f32 v23, v24, v25
	global_store_dwordx4 v[18:19], v[20:23], off offset:1024 sc1
	global_load_dwordx4 v[20:23], v105, s[2:3] offset:16
	s_nop 0
	global_load_dwordx4 v[24:27], v105, s[2:3]
	global_load_dwordx4 v[28:31], v[64:65], off offset:16
	global_load_dwordx4 v[32:35], v[64:65], off
	global_load_dwordx4 v[36:39], v105, s[16:17] offset:16
	global_load_dwordx4 v[40:43], v105, s[16:17]
	s_waitcnt vmcnt(0)
	v_pk_add_f32 v[40:41], v[40:41], 1.0 op_sel_hi:[1,0]
	s_nop 0
	v_pk_mul_f32 v[32:33], v[32:33], v[40:41]
	v_pk_add_f32 v[42:43], v[42:43], 1.0 op_sel_hi:[1,0]
	v_pk_fma_f32 v[14:15], v[14:15], v[32:33], v[24:25]
	v_pk_mul_f32 v[34:35], v[34:35], v[42:43]
	v_bfe_u32 v1, v14, 16, 1
	v_add3_u32 v1, v14, v1, s37
	v_bfe_u32 v14, v15, 16, 1
	v_pk_fma_f32 v[16:17], v[16:17], v[34:35], v[26:27]
	v_lshrrev_b32_e32 v1, 16, v1
	v_add3_u32 v14, v15, v14, s37
	v_and_or_b32 v14, v14, s33, v1
	v_pk_add_f32 v[24:25], v[36:37], 1.0 op_sel_hi:[1,0]
	v_pk_mul_f32 v[24:25], v[28:29], v[24:25]
	v_pk_fma_f32 v[10:11], v[10:11], v[24:25], v[20:21]
	v_cvt_pk_bf16_f32 v15, v16, v17
	v_bfe_u32 v1, v11, 16, 1
	v_pk_add_f32 v[16:17], v[38:39], 1.0 op_sel_hi:[1,0]
	v_add3_u32 v1, v11, v1, s37
	v_bfe_u32 v11, v10, 16, 1
	v_pk_mul_f32 v[16:17], v[30:31], v[16:17]
	v_add3_u32 v10, v10, v11, s37
	v_pk_fma_f32 v[12:13], v[12:13], v[16:17], v[22:23]
	v_lshrrev_b32_e32 v10, 16, v10
	v_and_or_b32 v16, v1, s33, v10
	v_cvt_pk_bf16_f32 v17, v12, v13
	global_store_dwordx4 v[18:19], v[14:17], off offset:2048 sc1
	global_load_dwordx4 v[10:13], v106, s[2:3] offset:16
	s_nop 0
	global_load_dwordx4 v[14:17], v106, s[2:3]
	global_load_dwordx4 v[20:23], v[66:67], off offset:16
	global_load_dwordx4 v[24:27], v[66:67], off
	global_load_dwordx4 v[28:31], v106, s[16:17] offset:16
	global_load_dwordx4 v[32:35], v106, s[16:17]
	s_waitcnt vmcnt(0)
	v_pk_add_f32 v[32:33], v[32:33], 1.0 op_sel_hi:[1,0]
	s_nop 0
	v_pk_mul_f32 v[24:25], v[24:25], v[32:33]
	v_pk_add_f32 v[34:35], v[34:35], 1.0 op_sel_hi:[1,0]
	v_pk_fma_f32 v[6:7], v[6:7], v[24:25], v[14:15]
	v_pk_mul_f32 v[26:27], v[26:27], v[34:35]
	v_bfe_u32 v1, v6, 16, 1
	v_add3_u32 v1, v6, v1, s37
	v_bfe_u32 v6, v7, 16, 1
	v_pk_fma_f32 v[8:9], v[8:9], v[26:27], v[16:17]
	v_lshrrev_b32_e32 v1, 16, v1
	v_add3_u32 v6, v7, v6, s37
	v_and_or_b32 v6, v6, s33, v1
	v_pk_add_f32 v[14:15], v[28:29], 1.0 op_sel_hi:[1,0]
	v_pk_mul_f32 v[14:15], v[20:21], v[14:15]
	v_pk_fma_f32 v[2:3], v[2:3], v[14:15], v[10:11]
	v_cvt_pk_bf16_f32 v7, v8, v9
	v_bfe_u32 v1, v3, 16, 1
	v_pk_add_f32 v[8:9], v[30:31], 1.0 op_sel_hi:[1,0]
	v_add3_u32 v1, v3, v1, s37
	v_bfe_u32 v3, v2, 16, 1
	v_pk_mul_f32 v[8:9], v[22:23], v[8:9]
	v_add3_u32 v2, v2, v3, s37
	v_pk_fma_f32 v[4:5], v[4:5], v[8:9], v[12:13]
	v_lshrrev_b32_e32 v2, 16, v2
	v_and_or_b32 v8, v1, s33, v2
	v_cvt_pk_bf16_f32 v9, v4, v5
	global_store_dwordx4 v[18:19], v[6:9], off offset:3072 sc1
	s_branch .LBB0_2727
